# PEER gather V pass fully unrolled: constant lane indices, no index arithmetic or il/ih selects (on top of v43)
# speedup vs baseline: 1.0120x; 1.0008x over previous
.LBB0_1138:
	v_and_b32_e32 v4, 15, v148
	v_cmp_eq_u32_e32 vcc, 0, v4
	v_lshlrev_b32_e32 v5, 5, v40
	v_add_u32_e32 v10, 0x80, v148
	v_cndmask_b32_e32 v10, v10, v5, vcc
	v_cmp_gt_u32_e64 s[6:7], 8, v4
	v_lshl_add_u32 v32, v10, 2, v111
	v_and_b32_e32 v36, 12, v148
	v_cndmask_b32_e64 v10, 0, v252, s[6:7]
	v_cmp_lt_u32_e64 s[6:7], 3, v4
	v_lshl_or_b32 v4, v41, 3, v5
	v_add_u32_e32 v34, 0x400, v4
	v_lshlrev_b32_e32 v4, 4, v41
	v_lshl_or_b32 v35, v40, 6, v4
	ds_bpermute_b32 v4, v36, v130
	v_cmp_eq_u32_e32 vcc, 3, v41
	v_cmp_eq_u32_e64 s[2:3], 2, v41
	v_cmp_eq_u32_e64 s[4:5], 1, v41
	v_lshlrev_b32_e32 v129, 4, v148
	s_waitcnt lgkmcnt(0)
	v_mul_lo_u32 v4, v4, s43
	v_add_u32_e32 v5, v4, v35
	v_add_u32_e32 v4, v4, v34
	buffer_load_dwordx4 v[38:41], v5, s[44:47], 0 offen
	buffer_load_dwordx2 v[42:43], v4, s[44:47], 0 offen
	buffer_load_dwordx4 v[44:47], v5, s[44:47], s21 offen
	buffer_load_dwordx2 v[48:49], v4, s[44:47], s33 offen
	buffer_load_dwordx4 v[50:53], v5, s[44:47], s20 offen
	buffer_load_dwordx2 v[54:55], v4, s[44:47], s21 offen
	buffer_load_dwordx4 v[56:59], v5, s[44:47], s23 offen
	buffer_load_dwordx2 v[60:61], v4, s[44:47], s94 offen
	s_mov_b32 s0, 0
	v_cndmask_b32_e64 v33, 1.0, v10, s[6:7]
	ds_bpermute_b32 v4, v36, v130 offset:16
	s_waitcnt lgkmcnt(0)
	v_mul_lo_u32 v4, v4, s43
	v_add_u32_e32 v5, v4, v35
	v_add_u32_e32 v4, v4, v34
	buffer_load_dwordx4 v[62:65], v5, s[44:47], 0 offen
	buffer_load_dwordx4 v[68:71], v5, s[44:47], s20 offen
	buffer_load_dwordx4 v[74:77], v5, s[44:47], s21 offen
	buffer_load_dwordx4 v[86:89], v5, s[44:47], s23 offen
	buffer_load_dwordx2 v[66:67], v4, s[44:47], 0 offen
	buffer_load_dwordx2 v[78:79], v4, s[44:47], s33 offen
	buffer_load_dwordx2 v[72:73], v4, s[44:47], s21 offen
	buffer_load_dwordx2 v[90:91], v4, s[44:47], s94 offen
	ds_bpermute_b32 v4, v36, v130 offset:32
	s_waitcnt lgkmcnt(0)
	v_mul_lo_u32 v4, v4, s43
	v_add_u32_e32 v5, v4, v35
	v_add_u32_e32 v4, v4, v34
	buffer_load_dwordx4 v[92:95], v5, s[44:47], 0 offen
	buffer_load_dwordx4 v[98:101], v5, s[44:47], s20 offen
	buffer_load_dwordx4 v[150:153], v5, s[44:47], s21 offen
	buffer_load_dwordx4 v[156:159], v5, s[44:47], s23 offen
	buffer_load_dwordx2 v[96:97], v4, s[44:47], 0 offen
	buffer_load_dwordx2 v[154:155], v4, s[44:47], s33 offen
	buffer_load_dwordx2 v[102:103], v4, s[44:47], s21 offen
	buffer_load_dwordx2 v[160:161], v4, s[44:47], s94 offen
	ds_bpermute_b32 v4, v36, v130 offset:48
	s_waitcnt lgkmcnt(0)
	v_mul_lo_u32 v4, v4, s43
	v_add_u32_e32 v5, v4, v35
	v_add_u32_e32 v4, v4, v34
	buffer_load_dwordx4 v[162:165], v5, s[44:47], 0 offen
	buffer_load_dwordx4 v[168:171], v5, s[44:47], s20 offen
	buffer_load_dwordx4 v[174:177], v5, s[44:47], s21 offen
	buffer_load_dwordx4 v[216:219], v5, s[44:47], s23 offen
	buffer_load_dwordx2 v[166:167], v4, s[44:47], 0 offen
	buffer_load_dwordx2 v[178:179], v4, s[44:47], s33 offen
	buffer_load_dwordx2 v[172:173], v4, s[44:47], s21 offen
	buffer_load_dwordx2 v[220:221], v4, s[44:47], s94 offen
	v_mov_b32_e32 v22, v28
	v_mov_b32_e32 v23, v29
	v_mov_b32_e32 v16, v30
	v_mov_b32_e32 v17, v31
	s_waitcnt vmcnt(30)
	v_mfma_f32_16x16x128_f8f6f4 v[38:41], v[38:43], v[18:23], 0 cbsz:2 blgp:2
	v_mov_b32_e32 v10, v24
	v_mov_b32_e32 v11, v25
	v_mov_b32_e32 v4, v26
	s_waitcnt vmcnt(28)
	v_mfma_f32_16x16x128_f8f6f4 v[28:31], v[44:49], v[12:17], v[38:41] cbsz:2 blgp:2
	v_mov_b32_e32 v5, v27
	s_waitcnt vmcnt(26)
	v_mfma_f32_16x16x128_f8f6f4 v[28:31], v[50:55], v[6:11], v[28:31] cbsz:2 blgp:2
	s_waitcnt vmcnt(24)
	v_mfma_f32_16x16x128_f8f6f4 v[24:27], v[56:61], v[0:5], v[28:31] cbsz:2 blgp:2
	s_nop 7
	v_cndmask_b32_e64 v24, v24, v25, s[4:5]
	v_cndmask_b32_e64 v24, v24, v26, s[2:3]
	v_cndmask_b32_e32 v24, v24, v27, vcc
	v_mul_f32_e32 v25, v33, v24
	s_nop 1
	v_mov_b32_dpp v25, v25 quad_perm:[1,0,3,2] row_mask:0xf bank_mask:0xf bound_ctrl:1
	v_fmac_f32_e32 v25, v33, v24
	s_nop 1
	v_add_f32_dpp v24, v25, v25 quad_perm:[2,3,0,1] row_mask:0xf bank_mask:0xf bound_ctrl:1
	s_nop 1
	v_add_f32_dpp v24, v24, v24 row_half_mirror row_mask:0xf bank_mask:0xf bound_ctrl:1
	ds_write_b32 v32, v24 offset:49152
	ds_bpermute_b32 v24, v36, v130 offset:64
	s_waitcnt lgkmcnt(0)
	v_mul_lo_u32 v24, v24, s43
	v_add_u32_e32 v28, v24, v35
	v_add_u32_e32 v30, v24, v34
	buffer_load_dwordx4 v[24:27], v28, s[44:47], 0 offen
	buffer_load_dwordx4 v[38:41], v28, s[44:47], s20 offen
	buffer_load_dwordx4 v[44:47], v28, s[44:47], s21 offen
	buffer_load_dwordx4 v[50:53], v28, s[44:47], s23 offen
	s_nop 0
	buffer_load_dwordx2 v[28:29], v30, s[44:47], 0 offen
	buffer_load_dwordx2 v[48:49], v30, s[44:47], s33 offen
	buffer_load_dwordx2 v[42:43], v30, s[44:47], s21 offen
	buffer_load_dwordx2 v[54:55], v30, s[44:47], s94 offen
	s_waitcnt vmcnt(27)
	v_mfma_f32_16x16x128_f8f6f4 v[56:59], v[62:67], v[18:23], 0 cbsz:2 blgp:2
	s_waitcnt vmcnt(26)
	v_mfma_f32_16x16x128_f8f6f4 v[56:59], v[74:79], v[12:17], v[56:59] cbsz:2 blgp:2
	s_waitcnt vmcnt(25)
	v_mfma_f32_16x16x128_f8f6f4 v[56:59], v[68:73], v[6:11], v[56:59] cbsz:2 blgp:2
	s_waitcnt vmcnt(24)
	v_mfma_f32_16x16x128_f8f6f4 v[56:59], v[86:91], v[0:5], v[56:59] cbsz:2 blgp:2
	s_nop 7
	v_cndmask_b32_e64 v30, v56, v57, s[4:5]
	v_cndmask_b32_e64 v30, v30, v58, s[2:3]
	v_cndmask_b32_e32 v30, v30, v59, vcc
	v_mul_f32_e32 v31, v33, v30
	s_nop 1
	v_mov_b32_dpp v31, v31 quad_perm:[1,0,3,2] row_mask:0xf bank_mask:0xf bound_ctrl:1
	v_fmac_f32_e32 v31, v33, v30
	s_nop 1
	v_add_f32_dpp v30, v31, v31 quad_perm:[2,3,0,1] row_mask:0xf bank_mask:0xf bound_ctrl:1
	s_nop 1
	v_add_f32_dpp v30, v30, v30 row_half_mirror row_mask:0xf bank_mask:0xf bound_ctrl:1
	ds_write_b32 v32, v30 offset:49156
	ds_bpermute_b32 v30, v36, v130 offset:80
	s_waitcnt lgkmcnt(0)
	v_mul_lo_u32 v30, v30, s43
	v_add_u32_e32 v31, v30, v35
	v_add_u32_e32 v30, v30, v34
	buffer_load_dwordx4 v[56:59], v31, s[44:47], 0 offen
	buffer_load_dwordx4 v[62:65], v31, s[44:47], s20 offen
	buffer_load_dwordx4 v[68:71], v31, s[44:47], s21 offen
	buffer_load_dwordx4 v[74:77], v31, s[44:47], s23 offen
	buffer_load_dwordx2 v[60:61], v30, s[44:47], 0 offen
	buffer_load_dwordx2 v[72:73], v30, s[44:47], s33 offen
	buffer_load_dwordx2 v[66:67], v30, s[44:47], s21 offen
	buffer_load_dwordx2 v[78:79], v30, s[44:47], s94 offen
	s_waitcnt vmcnt(27)
	v_mfma_f32_16x16x128_f8f6f4 v[86:89], v[92:97], v[18:23], 0 cbsz:2 blgp:2
	s_waitcnt vmcnt(26)
	v_mfma_f32_16x16x128_f8f6f4 v[86:89], v[150:155], v[12:17], v[86:89] cbsz:2 blgp:2
	s_waitcnt vmcnt(25)
	v_mfma_f32_16x16x128_f8f6f4 v[86:89], v[98:103], v[6:11], v[86:89] cbsz:2 blgp:2
	s_waitcnt vmcnt(24)
	v_mfma_f32_16x16x128_f8f6f4 v[86:89], v[156:161], v[0:5], v[86:89] cbsz:2 blgp:2
	s_nop 7
	v_cndmask_b32_e64 v30, v86, v87, s[4:5]
	v_cndmask_b32_e64 v30, v30, v88, s[2:3]
	v_cndmask_b32_e32 v30, v30, v89, vcc
	v_mul_f32_e32 v31, v33, v30
	s_nop 1
	v_mov_b32_dpp v31, v31 quad_perm:[1,0,3,2] row_mask:0xf bank_mask:0xf bound_ctrl:1
	v_fmac_f32_e32 v31, v33, v30
	s_nop 1
	v_add_f32_dpp v30, v31, v31 quad_perm:[2,3,0,1] row_mask:0xf bank_mask:0xf bound_ctrl:1
	s_nop 1
	v_add_f32_dpp v30, v30, v30 row_half_mirror row_mask:0xf bank_mask:0xf bound_ctrl:1
	ds_write_b32 v32, v30 offset:49160
	ds_bpermute_b32 v30, v36, v130 offset:96
	s_waitcnt lgkmcnt(0)
	v_mul_lo_u32 v30, v30, s43
	v_add_u32_e32 v31, v30, v35
	v_add_u32_e32 v30, v30, v34
	buffer_load_dwordx4 v[86:89], v31, s[44:47], 0 offen
	buffer_load_dwordx4 v[92:95], v31, s[44:47], s20 offen
	buffer_load_dwordx4 v[98:101], v31, s[44:47], s21 offen
	buffer_load_dwordx4 v[150:153], v31, s[44:47], s23 offen
	buffer_load_dwordx2 v[90:91], v30, s[44:47], 0 offen
	buffer_load_dwordx2 v[102:103], v30, s[44:47], s33 offen
	buffer_load_dwordx2 v[96:97], v30, s[44:47], s21 offen
	buffer_load_dwordx2 v[154:155], v30, s[44:47], s94 offen
	s_waitcnt vmcnt(27)
	v_mfma_f32_16x16x128_f8f6f4 v[156:159], v[162:167], v[18:23], 0 cbsz:2 blgp:2
	s_waitcnt vmcnt(26)
	v_mfma_f32_16x16x128_f8f6f4 v[156:159], v[174:179], v[12:17], v[156:159] cbsz:2 blgp:2
	s_waitcnt vmcnt(25)
	v_mfma_f32_16x16x128_f8f6f4 v[156:159], v[168:173], v[6:11], v[156:159] cbsz:2 blgp:2
	s_waitcnt vmcnt(24)
	v_mfma_f32_16x16x128_f8f6f4 v[156:159], v[216:221], v[0:5], v[156:159] cbsz:2 blgp:2
	s_nop 7
	v_cndmask_b32_e64 v30, v156, v157, s[4:5]
	v_cndmask_b32_e64 v30, v30, v158, s[2:3]
	v_cndmask_b32_e32 v30, v30, v159, vcc
	v_mul_f32_e32 v31, v33, v30
	s_nop 1
	v_mov_b32_dpp v31, v31 quad_perm:[1,0,3,2] row_mask:0xf bank_mask:0xf bound_ctrl:1
	v_fmac_f32_e32 v31, v33, v30
	s_nop 1
	v_add_f32_dpp v30, v31, v31 quad_perm:[2,3,0,1] row_mask:0xf bank_mask:0xf bound_ctrl:1
	s_nop 1
	v_add_f32_dpp v30, v30, v30 row_half_mirror row_mask:0xf bank_mask:0xf bound_ctrl:1
	ds_write_b32 v32, v30 offset:49164
	ds_bpermute_b32 v30, v36, v130 offset:112
	s_waitcnt lgkmcnt(0)
	v_mul_lo_u32 v30, v30, s43
	v_add_u32_e32 v31, v30, v35
	v_add_u32_e32 v30, v30, v34
	buffer_load_dwordx4 v[156:159], v31, s[44:47], 0 offen
	buffer_load_dwordx4 v[162:165], v31, s[44:47], s20 offen
	buffer_load_dwordx4 v[168:171], v31, s[44:47], s21 offen
	buffer_load_dwordx4 v[174:177], v31, s[44:47], s23 offen
	buffer_load_dwordx2 v[160:161], v30, s[44:47], 0 offen
	buffer_load_dwordx2 v[172:173], v30, s[44:47], s33 offen
	buffer_load_dwordx2 v[166:167], v30, s[44:47], s21 offen
	buffer_load_dwordx2 v[178:179], v30, s[44:47], s94 offen
	s_waitcnt vmcnt(27)
	v_mfma_f32_16x16x128_f8f6f4 v[24:27], v[24:29], v[18:23], 0 cbsz:2 blgp:2
	s_waitcnt vmcnt(26)
	v_mfma_f32_16x16x128_f8f6f4 v[24:27], v[44:49], v[12:17], v[24:27] cbsz:2 blgp:2
	s_waitcnt vmcnt(25)
	v_mfma_f32_16x16x128_f8f6f4 v[24:27], v[38:43], v[6:11], v[24:27] cbsz:2 blgp:2
	s_waitcnt vmcnt(24)
	v_mfma_f32_16x16x128_f8f6f4 v[24:27], v[50:55], v[0:5], v[24:27] cbsz:2 blgp:2
	s_nop 7
	v_cndmask_b32_e64 v24, v24, v25, s[4:5]
	v_cndmask_b32_e64 v24, v24, v26, s[2:3]
	v_cndmask_b32_e32 v24, v24, v27, vcc
	v_mul_f32_e32 v25, v33, v24
	s_nop 1
	v_mov_b32_dpp v25, v25 quad_perm:[1,0,3,2] row_mask:0xf bank_mask:0xf bound_ctrl:1
	v_fmac_f32_e32 v25, v33, v24
	s_nop 1
	v_add_f32_dpp v24, v25, v25 quad_perm:[2,3,0,1] row_mask:0xf bank_mask:0xf bound_ctrl:1
	s_nop 1
	v_add_f32_dpp v24, v24, v24 row_half_mirror row_mask:0xf bank_mask:0xf bound_ctrl:1
	ds_write_b32 v32, v24 offset:49168
	ds_bpermute_b32 v24, v36, v130 offset:128
	s_waitcnt lgkmcnt(0)
	v_mul_lo_u32 v24, v24, s43
	v_add_u32_e32 v28, v24, v35
	v_add_u32_e32 v30, v24, v34
	buffer_load_dwordx4 v[24:27], v28, s[44:47], 0 offen
	buffer_load_dwordx4 v[38:41], v28, s[44:47], s20 offen
	buffer_load_dwordx4 v[44:47], v28, s[44:47], s21 offen
	buffer_load_dwordx4 v[50:53], v28, s[44:47], s23 offen
	s_nop 0
	buffer_load_dwordx2 v[28:29], v30, s[44:47], 0 offen
	buffer_load_dwordx2 v[48:49], v30, s[44:47], s33 offen
	buffer_load_dwordx2 v[42:43], v30, s[44:47], s21 offen
	buffer_load_dwordx2 v[54:55], v30, s[44:47], s94 offen
	s_waitcnt vmcnt(27)
	v_mfma_f32_16x16x128_f8f6f4 v[56:59], v[56:61], v[18:23], 0 cbsz:2 blgp:2
	s_waitcnt vmcnt(26)
	v_mfma_f32_16x16x128_f8f6f4 v[56:59], v[68:73], v[12:17], v[56:59] cbsz:2 blgp:2
	s_waitcnt vmcnt(25)
	v_mfma_f32_16x16x128_f8f6f4 v[56:59], v[62:67], v[6:11], v[56:59] cbsz:2 blgp:2
	s_waitcnt vmcnt(24)
	v_mfma_f32_16x16x128_f8f6f4 v[56:59], v[74:79], v[0:5], v[56:59] cbsz:2 blgp:2
	s_nop 7
	v_cndmask_b32_e64 v30, v56, v57, s[4:5]
	v_cndmask_b32_e64 v30, v30, v58, s[2:3]
	v_cndmask_b32_e32 v30, v30, v59, vcc
	v_mul_f32_e32 v31, v33, v30
	s_nop 1
	v_mov_b32_dpp v31, v31 quad_perm:[1,0,3,2] row_mask:0xf bank_mask:0xf bound_ctrl:1
	v_fmac_f32_e32 v31, v33, v30
	s_nop 1
	v_add_f32_dpp v30, v31, v31 quad_perm:[2,3,0,1] row_mask:0xf bank_mask:0xf bound_ctrl:1
	s_nop 1
	v_add_f32_dpp v30, v30, v30 row_half_mirror row_mask:0xf bank_mask:0xf bound_ctrl:1
	ds_write_b32 v32, v30 offset:49172
	ds_bpermute_b32 v30, v36, v130 offset:144
	s_waitcnt lgkmcnt(0)
	v_mul_lo_u32 v30, v30, s43
	v_add_u32_e32 v31, v30, v35
	v_add_u32_e32 v30, v30, v34
	buffer_load_dwordx4 v[56:59], v31, s[44:47], 0 offen
	buffer_load_dwordx4 v[62:65], v31, s[44:47], s20 offen
	buffer_load_dwordx4 v[68:71], v31, s[44:47], s21 offen
	buffer_load_dwordx4 v[74:77], v31, s[44:47], s23 offen
	buffer_load_dwordx2 v[60:61], v30, s[44:47], 0 offen
	buffer_load_dwordx2 v[72:73], v30, s[44:47], s33 offen
	buffer_load_dwordx2 v[66:67], v30, s[44:47], s21 offen
	buffer_load_dwordx2 v[78:79], v30, s[44:47], s94 offen
	s_waitcnt vmcnt(27)
	v_mfma_f32_16x16x128_f8f6f4 v[86:89], v[86:91], v[18:23], 0 cbsz:2 blgp:2
	s_waitcnt vmcnt(26)
	v_mfma_f32_16x16x128_f8f6f4 v[86:89], v[98:103], v[12:17], v[86:89] cbsz:2 blgp:2
	s_waitcnt vmcnt(25)
	v_mfma_f32_16x16x128_f8f6f4 v[86:89], v[92:97], v[6:11], v[86:89] cbsz:2 blgp:2
	s_waitcnt vmcnt(24)
	v_mfma_f32_16x16x128_f8f6f4 v[86:89], v[150:155], v[0:5], v[86:89] cbsz:2 blgp:2
	s_nop 7
	v_cndmask_b32_e64 v30, v86, v87, s[4:5]
	v_cndmask_b32_e64 v30, v30, v88, s[2:3]
	v_cndmask_b32_e32 v30, v30, v89, vcc
	v_mul_f32_e32 v31, v33, v30
	s_nop 1
	v_mov_b32_dpp v31, v31 quad_perm:[1,0,3,2] row_mask:0xf bank_mask:0xf bound_ctrl:1
	v_fmac_f32_e32 v31, v33, v30
	s_nop 1
	v_add_f32_dpp v30, v31, v31 quad_perm:[2,3,0,1] row_mask:0xf bank_mask:0xf bound_ctrl:1
	s_nop 1
	v_add_f32_dpp v30, v30, v30 row_half_mirror row_mask:0xf bank_mask:0xf bound_ctrl:1
	ds_write_b32 v32, v30 offset:49176
	ds_bpermute_b32 v30, v36, v130 offset:160
	s_waitcnt lgkmcnt(0)
	v_mul_lo_u32 v30, v30, s43
	v_add_u32_e32 v31, v30, v35
	v_add_u32_e32 v30, v30, v34
	buffer_load_dwordx4 v[86:89], v31, s[44:47], 0 offen
	buffer_load_dwordx4 v[92:95], v31, s[44:47], s20 offen
	buffer_load_dwordx4 v[98:101], v31, s[44:47], s21 offen
	buffer_load_dwordx4 v[150:153], v31, s[44:47], s23 offen
	buffer_load_dwordx2 v[90:91], v30, s[44:47], 0 offen
	buffer_load_dwordx2 v[102:103], v30, s[44:47], s33 offen
	buffer_load_dwordx2 v[96:97], v30, s[44:47], s21 offen
	buffer_load_dwordx2 v[154:155], v30, s[44:47], s94 offen
	s_waitcnt vmcnt(27)
	v_mfma_f32_16x16x128_f8f6f4 v[156:159], v[156:161], v[18:23], 0 cbsz:2 blgp:2
	s_waitcnt vmcnt(26)
	v_mfma_f32_16x16x128_f8f6f4 v[156:159], v[168:173], v[12:17], v[156:159] cbsz:2 blgp:2
	s_waitcnt vmcnt(25)
	v_mfma_f32_16x16x128_f8f6f4 v[156:159], v[162:167], v[6:11], v[156:159] cbsz:2 blgp:2
	s_waitcnt vmcnt(24)
	v_mfma_f32_16x16x128_f8f6f4 v[156:159], v[174:179], v[0:5], v[156:159] cbsz:2 blgp:2
	s_nop 7
	v_cndmask_b32_e64 v30, v156, v157, s[4:5]
	v_cndmask_b32_e64 v30, v30, v158, s[2:3]
	v_cndmask_b32_e32 v30, v30, v159, vcc
	v_mul_f32_e32 v31, v33, v30
	s_nop 1
	v_mov_b32_dpp v31, v31 quad_perm:[1,0,3,2] row_mask:0xf bank_mask:0xf bound_ctrl:1
	v_fmac_f32_e32 v31, v33, v30
	s_nop 1
	v_add_f32_dpp v30, v31, v31 quad_perm:[2,3,0,1] row_mask:0xf bank_mask:0xf bound_ctrl:1
	s_nop 1
	v_add_f32_dpp v30, v30, v30 row_half_mirror row_mask:0xf bank_mask:0xf bound_ctrl:1
	ds_write_b32 v32, v30 offset:49180
	ds_bpermute_b32 v30, v36, v130 offset:176
	s_waitcnt lgkmcnt(0)
	v_mul_lo_u32 v30, v30, s43
	v_add_u32_e32 v31, v30, v35
	v_add_u32_e32 v30, v30, v34
	buffer_load_dwordx4 v[156:159], v31, s[44:47], 0 offen
	buffer_load_dwordx4 v[162:165], v31, s[44:47], s20 offen
	buffer_load_dwordx4 v[168:171], v31, s[44:47], s21 offen
	buffer_load_dwordx4 v[174:177], v31, s[44:47], s23 offen
	buffer_load_dwordx2 v[160:161], v30, s[44:47], 0 offen
	buffer_load_dwordx2 v[172:173], v30, s[44:47], s33 offen
	buffer_load_dwordx2 v[166:167], v30, s[44:47], s21 offen
	buffer_load_dwordx2 v[178:179], v30, s[44:47], s94 offen
	s_waitcnt vmcnt(27)
	v_mfma_f32_16x16x128_f8f6f4 v[24:27], v[24:29], v[18:23], 0 cbsz:2 blgp:2
	s_waitcnt vmcnt(26)
	v_mfma_f32_16x16x128_f8f6f4 v[24:27], v[44:49], v[12:17], v[24:27] cbsz:2 blgp:2
	s_waitcnt vmcnt(25)
	v_mfma_f32_16x16x128_f8f6f4 v[24:27], v[38:43], v[6:11], v[24:27] cbsz:2 blgp:2
	s_waitcnt vmcnt(24)
	v_mfma_f32_16x16x128_f8f6f4 v[24:27], v[50:55], v[0:5], v[24:27] cbsz:2 blgp:2
	s_nop 7
	v_cndmask_b32_e64 v24, v24, v25, s[4:5]
	v_cndmask_b32_e64 v24, v24, v26, s[2:3]
	v_cndmask_b32_e32 v24, v24, v27, vcc
	v_mul_f32_e32 v25, v33, v24
	s_nop 1
	v_mov_b32_dpp v25, v25 quad_perm:[1,0,3,2] row_mask:0xf bank_mask:0xf bound_ctrl:1
	v_fmac_f32_e32 v25, v33, v24
	s_nop 1
	v_add_f32_dpp v24, v25, v25 quad_perm:[2,3,0,1] row_mask:0xf bank_mask:0xf bound_ctrl:1
	s_nop 1
	v_add_f32_dpp v24, v24, v24 row_half_mirror row_mask:0xf bank_mask:0xf bound_ctrl:1
	ds_write_b32 v32, v24 offset:49184
	ds_bpermute_b32 v24, v36, v130 offset:192
	s_waitcnt lgkmcnt(0)
	v_mul_lo_u32 v24, v24, s43
	v_add_u32_e32 v28, v24, v35
	v_add_u32_e32 v30, v24, v34
	buffer_load_dwordx4 v[24:27], v28, s[44:47], 0 offen
	buffer_load_dwordx4 v[38:41], v28, s[44:47], s20 offen
	buffer_load_dwordx4 v[44:47], v28, s[44:47], s21 offen
	buffer_load_dwordx4 v[50:53], v28, s[44:47], s23 offen
	s_nop 0
	buffer_load_dwordx2 v[28:29], v30, s[44:47], 0 offen
	buffer_load_dwordx2 v[48:49], v30, s[44:47], s33 offen
	buffer_load_dwordx2 v[42:43], v30, s[44:47], s21 offen
	buffer_load_dwordx2 v[54:55], v30, s[44:47], s94 offen
	s_waitcnt vmcnt(27)
	v_mfma_f32_16x16x128_f8f6f4 v[56:59], v[56:61], v[18:23], 0 cbsz:2 blgp:2
	s_waitcnt vmcnt(26)
	v_mfma_f32_16x16x128_f8f6f4 v[56:59], v[68:73], v[12:17], v[56:59] cbsz:2 blgp:2
	s_waitcnt vmcnt(25)
	v_mfma_f32_16x16x128_f8f6f4 v[56:59], v[62:67], v[6:11], v[56:59] cbsz:2 blgp:2
	s_waitcnt vmcnt(24)
	v_mfma_f32_16x16x128_f8f6f4 v[56:59], v[74:79], v[0:5], v[56:59] cbsz:2 blgp:2
	s_nop 7
	v_cndmask_b32_e64 v30, v56, v57, s[4:5]
	v_cndmask_b32_e64 v30, v30, v58, s[2:3]
	v_cndmask_b32_e32 v30, v30, v59, vcc
	v_mul_f32_e32 v31, v33, v30
	s_nop 1
	v_mov_b32_dpp v31, v31 quad_perm:[1,0,3,2] row_mask:0xf bank_mask:0xf bound_ctrl:1
	v_fmac_f32_e32 v31, v33, v30
	s_nop 1
	v_add_f32_dpp v30, v31, v31 quad_perm:[2,3,0,1] row_mask:0xf bank_mask:0xf bound_ctrl:1
	s_nop 1
	v_add_f32_dpp v30, v30, v30 row_half_mirror row_mask:0xf bank_mask:0xf bound_ctrl:1
	ds_write_b32 v32, v30 offset:49188
	ds_bpermute_b32 v30, v36, v130 offset:208
	s_waitcnt lgkmcnt(0)
	v_mul_lo_u32 v30, v30, s43
	v_add_u32_e32 v31, v30, v35
	v_add_u32_e32 v30, v30, v34
	buffer_load_dwordx4 v[56:59], v31, s[44:47], 0 offen
	buffer_load_dwordx4 v[62:65], v31, s[44:47], s20 offen
	buffer_load_dwordx4 v[68:71], v31, s[44:47], s21 offen
	buffer_load_dwordx4 v[74:77], v31, s[44:47], s23 offen
	buffer_load_dwordx2 v[60:61], v30, s[44:47], 0 offen
	buffer_load_dwordx2 v[72:73], v30, s[44:47], s33 offen
	buffer_load_dwordx2 v[66:67], v30, s[44:47], s21 offen
	buffer_load_dwordx2 v[78:79], v30, s[44:47], s94 offen
	s_waitcnt vmcnt(27)
	v_mfma_f32_16x16x128_f8f6f4 v[86:89], v[86:91], v[18:23], 0 cbsz:2 blgp:2
	s_waitcnt vmcnt(26)
	v_mfma_f32_16x16x128_f8f6f4 v[86:89], v[98:103], v[12:17], v[86:89] cbsz:2 blgp:2
	s_waitcnt vmcnt(25)
	v_mfma_f32_16x16x128_f8f6f4 v[86:89], v[92:97], v[6:11], v[86:89] cbsz:2 blgp:2
	s_waitcnt vmcnt(24)
	v_mfma_f32_16x16x128_f8f6f4 v[86:89], v[150:155], v[0:5], v[86:89] cbsz:2 blgp:2
	s_nop 7
	v_cndmask_b32_e64 v30, v86, v87, s[4:5]
	v_cndmask_b32_e64 v30, v30, v88, s[2:3]
	v_cndmask_b32_e32 v30, v30, v89, vcc
	v_mul_f32_e32 v31, v33, v30
	s_nop 1
	v_mov_b32_dpp v31, v31 quad_perm:[1,0,3,2] row_mask:0xf bank_mask:0xf bound_ctrl:1
	v_fmac_f32_e32 v31, v33, v30
	s_nop 1
	v_add_f32_dpp v30, v31, v31 quad_perm:[2,3,0,1] row_mask:0xf bank_mask:0xf bound_ctrl:1
	s_nop 1
	v_add_f32_dpp v30, v30, v30 row_half_mirror row_mask:0xf bank_mask:0xf bound_ctrl:1
	ds_write_b32 v32, v30 offset:49192
	ds_bpermute_b32 v30, v36, v130 offset:224
	s_waitcnt lgkmcnt(0)
	v_mul_lo_u32 v30, v30, s43
	v_add_u32_e32 v31, v30, v35
	v_add_u32_e32 v30, v30, v34
	buffer_load_dwordx4 v[86:89], v31, s[44:47], 0 offen
	buffer_load_dwordx4 v[92:95], v31, s[44:47], s20 offen
	buffer_load_dwordx4 v[98:101], v31, s[44:47], s21 offen
	buffer_load_dwordx4 v[150:153], v31, s[44:47], s23 offen
	buffer_load_dwordx2 v[90:91], v30, s[44:47], 0 offen
	buffer_load_dwordx2 v[102:103], v30, s[44:47], s33 offen
	buffer_load_dwordx2 v[96:97], v30, s[44:47], s21 offen
	buffer_load_dwordx2 v[154:155], v30, s[44:47], s94 offen
	s_waitcnt vmcnt(27)
	v_mfma_f32_16x16x128_f8f6f4 v[156:159], v[156:161], v[18:23], 0 cbsz:2 blgp:2
	s_waitcnt vmcnt(26)
	v_mfma_f32_16x16x128_f8f6f4 v[156:159], v[168:173], v[12:17], v[156:159] cbsz:2 blgp:2
	s_waitcnt vmcnt(25)
	v_mfma_f32_16x16x128_f8f6f4 v[156:159], v[162:167], v[6:11], v[156:159] cbsz:2 blgp:2
	s_waitcnt vmcnt(24)
	v_mfma_f32_16x16x128_f8f6f4 v[156:159], v[174:179], v[0:5], v[156:159] cbsz:2 blgp:2
	s_nop 7
	v_cndmask_b32_e64 v30, v156, v157, s[4:5]
	v_cndmask_b32_e64 v30, v30, v158, s[2:3]
	v_cndmask_b32_e32 v30, v30, v159, vcc
	v_mul_f32_e32 v31, v33, v30
	s_nop 1
	v_mov_b32_dpp v31, v31 quad_perm:[1,0,3,2] row_mask:0xf bank_mask:0xf bound_ctrl:1
	v_fmac_f32_e32 v31, v33, v30
	s_nop 1
	v_add_f32_dpp v30, v31, v31 quad_perm:[2,3,0,1] row_mask:0xf bank_mask:0xf bound_ctrl:1
	s_nop 1
	v_add_f32_dpp v30, v30, v30 row_half_mirror row_mask:0xf bank_mask:0xf bound_ctrl:1
	ds_write_b32 v32, v30 offset:49196
	ds_bpermute_b32 v30, v36, v130 offset:240
	s_waitcnt lgkmcnt(0)
	v_mul_lo_u32 v30, v30, s43
	v_add_u32_e32 v31, v30, v35
	v_add_u32_e32 v30, v30, v34
	buffer_load_dwordx4 v[156:159], v31, s[44:47], 0 offen
	buffer_load_dwordx4 v[162:165], v31, s[44:47], s20 offen
	buffer_load_dwordx4 v[168:171], v31, s[44:47], s21 offen
	buffer_load_dwordx4 v[174:177], v31, s[44:47], s23 offen
	buffer_load_dwordx2 v[160:161], v30, s[44:47], 0 offen
	buffer_load_dwordx2 v[172:173], v30, s[44:47], s33 offen
	buffer_load_dwordx2 v[166:167], v30, s[44:47], s21 offen
	buffer_load_dwordx2 v[178:179], v30, s[44:47], s94 offen
	s_waitcnt vmcnt(27)
	v_mfma_f32_16x16x128_f8f6f4 v[24:27], v[24:29], v[18:23], 0 cbsz:2 blgp:2
	s_waitcnt vmcnt(26)
	v_mfma_f32_16x16x128_f8f6f4 v[24:27], v[44:49], v[12:17], v[24:27] cbsz:2 blgp:2
	s_waitcnt vmcnt(25)
	v_mfma_f32_16x16x128_f8f6f4 v[24:27], v[38:43], v[6:11], v[24:27] cbsz:2 blgp:2
	s_waitcnt vmcnt(24)
	v_mfma_f32_16x16x128_f8f6f4 v[24:27], v[50:55], v[0:5], v[24:27] cbsz:2 blgp:2
	s_nop 7
	v_cndmask_b32_e64 v24, v24, v25, s[4:5]
	v_cndmask_b32_e64 v24, v24, v26, s[2:3]
	v_cndmask_b32_e32 v24, v24, v27, vcc
	v_mul_f32_e32 v25, v33, v24
	s_nop 1
	v_mov_b32_dpp v25, v25 quad_perm:[1,0,3,2] row_mask:0xf bank_mask:0xf bound_ctrl:1
	v_fmac_f32_e32 v25, v33, v24
	s_nop 1
	v_add_f32_dpp v24, v25, v25 quad_perm:[2,3,0,1] row_mask:0xf bank_mask:0xf bound_ctrl:1
	s_nop 1
	v_add_f32_dpp v24, v24, v24 row_half_mirror row_mask:0xf bank_mask:0xf bound_ctrl:1
	ds_write_b32 v32, v24 offset:49200
	ds_bpermute_b32 v24, v36, v128
	s_waitcnt lgkmcnt(0)
	v_mul_lo_u32 v24, v24, s43
	v_add_u32_e32 v28, v24, v35
	v_add_u32_e32 v30, v24, v34
	buffer_load_dwordx4 v[24:27], v28, s[44:47], 0 offen
	buffer_load_dwordx4 v[38:41], v28, s[44:47], s20 offen
	buffer_load_dwordx4 v[44:47], v28, s[44:47], s21 offen
	buffer_load_dwordx4 v[50:53], v28, s[44:47], s23 offen
	s_nop 0
	buffer_load_dwordx2 v[28:29], v30, s[44:47], 0 offen
	buffer_load_dwordx2 v[48:49], v30, s[44:47], s33 offen
	buffer_load_dwordx2 v[42:43], v30, s[44:47], s21 offen
	buffer_load_dwordx2 v[54:55], v30, s[44:47], s94 offen
	s_waitcnt vmcnt(27)
	v_mfma_f32_16x16x128_f8f6f4 v[56:59], v[56:61], v[18:23], 0 cbsz:2 blgp:2
	s_waitcnt vmcnt(26)
	v_mfma_f32_16x16x128_f8f6f4 v[56:59], v[68:73], v[12:17], v[56:59] cbsz:2 blgp:2
	s_waitcnt vmcnt(25)
	v_mfma_f32_16x16x128_f8f6f4 v[56:59], v[62:67], v[6:11], v[56:59] cbsz:2 blgp:2
	s_waitcnt vmcnt(24)
	v_mfma_f32_16x16x128_f8f6f4 v[56:59], v[74:79], v[0:5], v[56:59] cbsz:2 blgp:2
	s_nop 7
	v_cndmask_b32_e64 v30, v56, v57, s[4:5]
	v_cndmask_b32_e64 v30, v30, v58, s[2:3]
	v_cndmask_b32_e32 v30, v30, v59, vcc
	v_mul_f32_e32 v31, v33, v30
	s_nop 1
	v_mov_b32_dpp v31, v31 quad_perm:[1,0,3,2] row_mask:0xf bank_mask:0xf bound_ctrl:1
	v_fmac_f32_e32 v31, v33, v30
	s_nop 1
	v_add_f32_dpp v30, v31, v31 quad_perm:[2,3,0,1] row_mask:0xf bank_mask:0xf bound_ctrl:1
	s_nop 1
	v_add_f32_dpp v30, v30, v30 row_half_mirror row_mask:0xf bank_mask:0xf bound_ctrl:1
	ds_write_b32 v32, v30 offset:49204
	ds_bpermute_b32 v30, v36, v128 offset:16
	s_waitcnt lgkmcnt(0)
	v_mul_lo_u32 v30, v30, s43
	v_add_u32_e32 v31, v30, v35
	v_add_u32_e32 v30, v30, v34
	buffer_load_dwordx4 v[56:59], v31, s[44:47], 0 offen
	buffer_load_dwordx4 v[62:65], v31, s[44:47], s20 offen
	buffer_load_dwordx4 v[68:71], v31, s[44:47], s21 offen
	buffer_load_dwordx4 v[74:77], v31, s[44:47], s23 offen
	buffer_load_dwordx2 v[60:61], v30, s[44:47], 0 offen
	buffer_load_dwordx2 v[72:73], v30, s[44:47], s33 offen
	buffer_load_dwordx2 v[66:67], v30, s[44:47], s21 offen
	buffer_load_dwordx2 v[78:79], v30, s[44:47], s94 offen
	s_waitcnt vmcnt(27)
	v_mfma_f32_16x16x128_f8f6f4 v[86:89], v[86:91], v[18:23], 0 cbsz:2 blgp:2
	s_waitcnt vmcnt(26)
	v_mfma_f32_16x16x128_f8f6f4 v[86:89], v[98:103], v[12:17], v[86:89] cbsz:2 blgp:2
	s_waitcnt vmcnt(25)
	v_mfma_f32_16x16x128_f8f6f4 v[86:89], v[92:97], v[6:11], v[86:89] cbsz:2 blgp:2
	s_waitcnt vmcnt(24)
	v_mfma_f32_16x16x128_f8f6f4 v[86:89], v[150:155], v[0:5], v[86:89] cbsz:2 blgp:2
	s_nop 7
	v_cndmask_b32_e64 v30, v86, v87, s[4:5]
	v_cndmask_b32_e64 v30, v30, v88, s[2:3]
	v_cndmask_b32_e32 v30, v30, v89, vcc
	v_mul_f32_e32 v31, v33, v30
	s_nop 1
	v_mov_b32_dpp v31, v31 quad_perm:[1,0,3,2] row_mask:0xf bank_mask:0xf bound_ctrl:1
	v_fmac_f32_e32 v31, v33, v30
	s_nop 1
	v_add_f32_dpp v30, v31, v31 quad_perm:[2,3,0,1] row_mask:0xf bank_mask:0xf bound_ctrl:1
	s_nop 1
	v_add_f32_dpp v30, v30, v30 row_half_mirror row_mask:0xf bank_mask:0xf bound_ctrl:1
	ds_write_b32 v32, v30 offset:49208
	ds_bpermute_b32 v30, v36, v128 offset:32
	s_waitcnt lgkmcnt(0)
	v_mul_lo_u32 v30, v30, s43
	v_add_u32_e32 v31, v30, v35
	v_add_u32_e32 v30, v30, v34
	buffer_load_dwordx4 v[86:89], v31, s[44:47], 0 offen
	buffer_load_dwordx4 v[92:95], v31, s[44:47], s20 offen
	buffer_load_dwordx4 v[98:101], v31, s[44:47], s21 offen
	buffer_load_dwordx4 v[150:153], v31, s[44:47], s23 offen
	buffer_load_dwordx2 v[90:91], v30, s[44:47], 0 offen
	buffer_load_dwordx2 v[102:103], v30, s[44:47], s33 offen
	buffer_load_dwordx2 v[96:97], v30, s[44:47], s21 offen
	buffer_load_dwordx2 v[154:155], v30, s[44:47], s94 offen
	s_waitcnt vmcnt(27)
	v_mfma_f32_16x16x128_f8f6f4 v[156:159], v[156:161], v[18:23], 0 cbsz:2 blgp:2
	s_waitcnt vmcnt(26)
	v_mfma_f32_16x16x128_f8f6f4 v[156:159], v[168:173], v[12:17], v[156:159] cbsz:2 blgp:2
	s_waitcnt vmcnt(25)
	v_mfma_f32_16x16x128_f8f6f4 v[156:159], v[162:167], v[6:11], v[156:159] cbsz:2 blgp:2
	s_waitcnt vmcnt(24)
	v_mfma_f32_16x16x128_f8f6f4 v[156:159], v[174:179], v[0:5], v[156:159] cbsz:2 blgp:2
	s_nop 7
	v_cndmask_b32_e64 v30, v156, v157, s[4:5]
	v_cndmask_b32_e64 v30, v30, v158, s[2:3]
	v_cndmask_b32_e32 v30, v30, v159, vcc
	v_mul_f32_e32 v31, v33, v30
	s_nop 1
	v_mov_b32_dpp v31, v31 quad_perm:[1,0,3,2] row_mask:0xf bank_mask:0xf bound_ctrl:1
	v_fmac_f32_e32 v31, v33, v30
	s_nop 1
	v_add_f32_dpp v30, v31, v31 quad_perm:[2,3,0,1] row_mask:0xf bank_mask:0xf bound_ctrl:1
	s_nop 1
	v_add_f32_dpp v30, v30, v30 row_half_mirror row_mask:0xf bank_mask:0xf bound_ctrl:1
	ds_write_b32 v32, v30 offset:49212
	ds_bpermute_b32 v30, v36, v128 offset:48
	s_waitcnt lgkmcnt(0)
	v_mul_lo_u32 v30, v30, s43
	v_add_u32_e32 v31, v30, v35
	v_add_u32_e32 v30, v30, v34
	buffer_load_dwordx4 v[156:159], v31, s[44:47], 0 offen
	buffer_load_dwordx4 v[162:165], v31, s[44:47], s20 offen
	buffer_load_dwordx4 v[168:171], v31, s[44:47], s21 offen
	buffer_load_dwordx4 v[174:177], v31, s[44:47], s23 offen
	buffer_load_dwordx2 v[160:161], v30, s[44:47], 0 offen
	buffer_load_dwordx2 v[172:173], v30, s[44:47], s33 offen
	buffer_load_dwordx2 v[166:167], v30, s[44:47], s21 offen
	buffer_load_dwordx2 v[178:179], v30, s[44:47], s94 offen
	s_waitcnt vmcnt(27)
	v_mfma_f32_16x16x128_f8f6f4 v[24:27], v[24:29], v[18:23], 0 cbsz:2 blgp:2
	s_waitcnt vmcnt(26)
	v_mfma_f32_16x16x128_f8f6f4 v[24:27], v[44:49], v[12:17], v[24:27] cbsz:2 blgp:2
	s_waitcnt vmcnt(25)
	v_mfma_f32_16x16x128_f8f6f4 v[24:27], v[38:43], v[6:11], v[24:27] cbsz:2 blgp:2
	s_waitcnt vmcnt(24)
	v_mfma_f32_16x16x128_f8f6f4 v[24:27], v[50:55], v[0:5], v[24:27] cbsz:2 blgp:2
	s_nop 7
	v_cndmask_b32_e64 v24, v24, v25, s[4:5]
	v_cndmask_b32_e64 v24, v24, v26, s[2:3]
	v_cndmask_b32_e32 v24, v24, v27, vcc
	v_mul_f32_e32 v25, v33, v24
	s_nop 1
	v_mov_b32_dpp v25, v25 quad_perm:[1,0,3,2] row_mask:0xf bank_mask:0xf bound_ctrl:1
	v_fmac_f32_e32 v25, v33, v24
	s_nop 1
	v_add_f32_dpp v24, v25, v25 quad_perm:[2,3,0,1] row_mask:0xf bank_mask:0xf bound_ctrl:1
	s_nop 1
	v_add_f32_dpp v24, v24, v24 row_half_mirror row_mask:0xf bank_mask:0xf bound_ctrl:1
	ds_write_b32 v32, v24 offset:49216
	ds_bpermute_b32 v24, v36, v128 offset:64
	s_waitcnt lgkmcnt(0)
	v_mul_lo_u32 v24, v24, s43
	v_add_u32_e32 v28, v24, v35
	v_add_u32_e32 v30, v24, v34
	buffer_load_dwordx4 v[24:27], v28, s[44:47], 0 offen
	buffer_load_dwordx4 v[38:41], v28, s[44:47], s20 offen
	buffer_load_dwordx4 v[44:47], v28, s[44:47], s21 offen
	buffer_load_dwordx4 v[50:53], v28, s[44:47], s23 offen
	s_nop 0
	buffer_load_dwordx2 v[28:29], v30, s[44:47], 0 offen
	buffer_load_dwordx2 v[48:49], v30, s[44:47], s33 offen
	buffer_load_dwordx2 v[42:43], v30, s[44:47], s21 offen
	buffer_load_dwordx2 v[54:55], v30, s[44:47], s94 offen
	s_waitcnt vmcnt(27)
	v_mfma_f32_16x16x128_f8f6f4 v[56:59], v[56:61], v[18:23], 0 cbsz:2 blgp:2
	s_waitcnt vmcnt(26)
	v_mfma_f32_16x16x128_f8f6f4 v[56:59], v[68:73], v[12:17], v[56:59] cbsz:2 blgp:2
	s_waitcnt vmcnt(25)
	v_mfma_f32_16x16x128_f8f6f4 v[56:59], v[62:67], v[6:11], v[56:59] cbsz:2 blgp:2
	s_waitcnt vmcnt(24)
	v_mfma_f32_16x16x128_f8f6f4 v[56:59], v[74:79], v[0:5], v[56:59] cbsz:2 blgp:2
	s_nop 7
	v_cndmask_b32_e64 v30, v56, v57, s[4:5]
	v_cndmask_b32_e64 v30, v30, v58, s[2:3]
	v_cndmask_b32_e32 v30, v30, v59, vcc
	v_mul_f32_e32 v31, v33, v30
	s_nop 1
	v_mov_b32_dpp v31, v31 quad_perm:[1,0,3,2] row_mask:0xf bank_mask:0xf bound_ctrl:1
	v_fmac_f32_e32 v31, v33, v30
	s_nop 1
	v_add_f32_dpp v30, v31, v31 quad_perm:[2,3,0,1] row_mask:0xf bank_mask:0xf bound_ctrl:1
	s_nop 1
	v_add_f32_dpp v30, v30, v30 row_half_mirror row_mask:0xf bank_mask:0xf bound_ctrl:1
	ds_write_b32 v32, v30 offset:49220
	ds_bpermute_b32 v30, v36, v128 offset:80
	s_waitcnt lgkmcnt(0)
	v_mul_lo_u32 v30, v30, s43
	v_add_u32_e32 v31, v30, v35
	v_add_u32_e32 v30, v30, v34
	buffer_load_dwordx4 v[56:59], v31, s[44:47], 0 offen
	buffer_load_dwordx4 v[62:65], v31, s[44:47], s20 offen
	buffer_load_dwordx4 v[68:71], v31, s[44:47], s21 offen
	buffer_load_dwordx4 v[74:77], v31, s[44:47], s23 offen
	buffer_load_dwordx2 v[60:61], v30, s[44:47], 0 offen
	buffer_load_dwordx2 v[72:73], v30, s[44:47], s33 offen
	buffer_load_dwordx2 v[66:67], v30, s[44:47], s21 offen
	buffer_load_dwordx2 v[78:79], v30, s[44:47], s94 offen
	s_waitcnt vmcnt(27)
	v_mfma_f32_16x16x128_f8f6f4 v[86:89], v[86:91], v[18:23], 0 cbsz:2 blgp:2
	s_waitcnt vmcnt(26)
	v_mfma_f32_16x16x128_f8f6f4 v[86:89], v[98:103], v[12:17], v[86:89] cbsz:2 blgp:2
	s_waitcnt vmcnt(25)
	v_mfma_f32_16x16x128_f8f6f4 v[86:89], v[92:97], v[6:11], v[86:89] cbsz:2 blgp:2
	s_waitcnt vmcnt(24)
	v_mfma_f32_16x16x128_f8f6f4 v[86:89], v[150:155], v[0:5], v[86:89] cbsz:2 blgp:2
	s_nop 7
	v_cndmask_b32_e64 v30, v86, v87, s[4:5]
	v_cndmask_b32_e64 v30, v30, v88, s[2:3]
	v_cndmask_b32_e32 v30, v30, v89, vcc
	v_mul_f32_e32 v31, v33, v30
	s_nop 1
	v_mov_b32_dpp v31, v31 quad_perm:[1,0,3,2] row_mask:0xf bank_mask:0xf bound_ctrl:1
	v_fmac_f32_e32 v31, v33, v30
	s_nop 1
	v_add_f32_dpp v30, v31, v31 quad_perm:[2,3,0,1] row_mask:0xf bank_mask:0xf bound_ctrl:1
	s_nop 1
	v_add_f32_dpp v30, v30, v30 row_half_mirror row_mask:0xf bank_mask:0xf bound_ctrl:1
	ds_write_b32 v32, v30 offset:49224
	ds_bpermute_b32 v30, v36, v128 offset:96
	s_waitcnt lgkmcnt(0)
	v_mul_lo_u32 v30, v30, s43
	v_add_u32_e32 v31, v30, v35
	v_add_u32_e32 v30, v30, v34
	buffer_load_dwordx4 v[86:89], v31, s[44:47], 0 offen
	buffer_load_dwordx4 v[92:95], v31, s[44:47], s20 offen
	buffer_load_dwordx4 v[98:101], v31, s[44:47], s21 offen
	buffer_load_dwordx4 v[150:153], v31, s[44:47], s23 offen
	buffer_load_dwordx2 v[90:91], v30, s[44:47], 0 offen
	buffer_load_dwordx2 v[102:103], v30, s[44:47], s33 offen
	buffer_load_dwordx2 v[96:97], v30, s[44:47], s21 offen
	buffer_load_dwordx2 v[154:155], v30, s[44:47], s94 offen
	s_waitcnt vmcnt(27)
	v_mfma_f32_16x16x128_f8f6f4 v[156:159], v[156:161], v[18:23], 0 cbsz:2 blgp:2
	s_waitcnt vmcnt(26)
	v_mfma_f32_16x16x128_f8f6f4 v[156:159], v[168:173], v[12:17], v[156:159] cbsz:2 blgp:2
	s_waitcnt vmcnt(25)
	v_mfma_f32_16x16x128_f8f6f4 v[156:159], v[162:167], v[6:11], v[156:159] cbsz:2 blgp:2
	s_waitcnt vmcnt(24)
	v_mfma_f32_16x16x128_f8f6f4 v[156:159], v[174:179], v[0:5], v[156:159] cbsz:2 blgp:2
	s_nop 7
	v_cndmask_b32_e64 v30, v156, v157, s[4:5]
	v_cndmask_b32_e64 v30, v30, v158, s[2:3]
	v_cndmask_b32_e32 v30, v30, v159, vcc
	v_mul_f32_e32 v31, v33, v30
	s_nop 1
	v_mov_b32_dpp v31, v31 quad_perm:[1,0,3,2] row_mask:0xf bank_mask:0xf bound_ctrl:1
	v_fmac_f32_e32 v31, v33, v30
	s_nop 1
	v_add_f32_dpp v30, v31, v31 quad_perm:[2,3,0,1] row_mask:0xf bank_mask:0xf bound_ctrl:1
	s_nop 1
	v_add_f32_dpp v30, v30, v30 row_half_mirror row_mask:0xf bank_mask:0xf bound_ctrl:1
	ds_write_b32 v32, v30 offset:49228
	ds_bpermute_b32 v30, v36, v128 offset:112
	s_waitcnt lgkmcnt(0)
	v_mul_lo_u32 v30, v30, s43
	v_add_u32_e32 v31, v30, v35
	v_add_u32_e32 v30, v30, v34
	buffer_load_dwordx4 v[156:159], v31, s[44:47], 0 offen
	buffer_load_dwordx4 v[162:165], v31, s[44:47], s20 offen
	buffer_load_dwordx4 v[168:171], v31, s[44:47], s21 offen
	buffer_load_dwordx4 v[174:177], v31, s[44:47], s23 offen
	buffer_load_dwordx2 v[160:161], v30, s[44:47], 0 offen
	buffer_load_dwordx2 v[172:173], v30, s[44:47], s33 offen
	buffer_load_dwordx2 v[166:167], v30, s[44:47], s21 offen
	buffer_load_dwordx2 v[178:179], v30, s[44:47], s94 offen
	s_waitcnt vmcnt(27)
	v_mfma_f32_16x16x128_f8f6f4 v[24:27], v[24:29], v[18:23], 0 cbsz:2 blgp:2
	s_waitcnt vmcnt(26)
	v_mfma_f32_16x16x128_f8f6f4 v[24:27], v[44:49], v[12:17], v[24:27] cbsz:2 blgp:2
	s_waitcnt vmcnt(25)
	v_mfma_f32_16x16x128_f8f6f4 v[24:27], v[38:43], v[6:11], v[24:27] cbsz:2 blgp:2
	s_waitcnt vmcnt(24)
	v_mfma_f32_16x16x128_f8f6f4 v[24:27], v[50:55], v[0:5], v[24:27] cbsz:2 blgp:2
	s_nop 7
	v_cndmask_b32_e64 v24, v24, v25, s[4:5]
	v_cndmask_b32_e64 v24, v24, v26, s[2:3]
	v_cndmask_b32_e32 v24, v24, v27, vcc
	v_mul_f32_e32 v25, v33, v24
	s_nop 1
	v_mov_b32_dpp v25, v25 quad_perm:[1,0,3,2] row_mask:0xf bank_mask:0xf bound_ctrl:1
	v_fmac_f32_e32 v25, v33, v24
	s_nop 1
	v_add_f32_dpp v24, v25, v25 quad_perm:[2,3,0,1] row_mask:0xf bank_mask:0xf bound_ctrl:1
	s_nop 1
	v_add_f32_dpp v24, v24, v24 row_half_mirror row_mask:0xf bank_mask:0xf bound_ctrl:1
	ds_write_b32 v32, v24 offset:49232
	ds_bpermute_b32 v24, v36, v128 offset:128
	s_waitcnt lgkmcnt(0)
	v_mul_lo_u32 v24, v24, s43
	v_add_u32_e32 v28, v24, v35
	v_add_u32_e32 v30, v24, v34
	buffer_load_dwordx4 v[24:27], v28, s[44:47], 0 offen
	buffer_load_dwordx4 v[38:41], v28, s[44:47], s20 offen
	buffer_load_dwordx4 v[44:47], v28, s[44:47], s21 offen
	buffer_load_dwordx4 v[50:53], v28, s[44:47], s23 offen
	s_nop 0
	buffer_load_dwordx2 v[28:29], v30, s[44:47], 0 offen
	buffer_load_dwordx2 v[48:49], v30, s[44:47], s33 offen
	buffer_load_dwordx2 v[42:43], v30, s[44:47], s21 offen
	buffer_load_dwordx2 v[54:55], v30, s[44:47], s94 offen
	s_waitcnt vmcnt(27)
	v_mfma_f32_16x16x128_f8f6f4 v[56:59], v[56:61], v[18:23], 0 cbsz:2 blgp:2
	s_waitcnt vmcnt(26)
	v_mfma_f32_16x16x128_f8f6f4 v[56:59], v[68:73], v[12:17], v[56:59] cbsz:2 blgp:2
	s_waitcnt vmcnt(25)
	v_mfma_f32_16x16x128_f8f6f4 v[56:59], v[62:67], v[6:11], v[56:59] cbsz:2 blgp:2
	s_waitcnt vmcnt(24)
	v_mfma_f32_16x16x128_f8f6f4 v[56:59], v[74:79], v[0:5], v[56:59] cbsz:2 blgp:2
	s_nop 7
	v_cndmask_b32_e64 v30, v56, v57, s[4:5]
	v_cndmask_b32_e64 v30, v30, v58, s[2:3]
	v_cndmask_b32_e32 v30, v30, v59, vcc
	v_mul_f32_e32 v31, v33, v30
	s_nop 1
	v_mov_b32_dpp v31, v31 quad_perm:[1,0,3,2] row_mask:0xf bank_mask:0xf bound_ctrl:1
	v_fmac_f32_e32 v31, v33, v30
	s_nop 1
	v_add_f32_dpp v30, v31, v31 quad_perm:[2,3,0,1] row_mask:0xf bank_mask:0xf bound_ctrl:1
	s_nop 1
	v_add_f32_dpp v30, v30, v30 row_half_mirror row_mask:0xf bank_mask:0xf bound_ctrl:1
	ds_write_b32 v32, v30 offset:49236
	ds_bpermute_b32 v30, v36, v128 offset:144
	s_waitcnt lgkmcnt(0)
	v_mul_lo_u32 v30, v30, s43
	v_add_u32_e32 v31, v30, v35
	v_add_u32_e32 v30, v30, v34
	buffer_load_dwordx4 v[56:59], v31, s[44:47], 0 offen
	buffer_load_dwordx4 v[62:65], v31, s[44:47], s20 offen
	buffer_load_dwordx4 v[68:71], v31, s[44:47], s21 offen
	buffer_load_dwordx4 v[74:77], v31, s[44:47], s23 offen
	buffer_load_dwordx2 v[60:61], v30, s[44:47], 0 offen
	buffer_load_dwordx2 v[72:73], v30, s[44:47], s33 offen
	buffer_load_dwordx2 v[66:67], v30, s[44:47], s21 offen
	buffer_load_dwordx2 v[78:79], v30, s[44:47], s94 offen
	s_waitcnt vmcnt(27)
	v_mfma_f32_16x16x128_f8f6f4 v[86:89], v[86:91], v[18:23], 0 cbsz:2 blgp:2
	s_waitcnt vmcnt(26)
	v_mfma_f32_16x16x128_f8f6f4 v[86:89], v[98:103], v[12:17], v[86:89] cbsz:2 blgp:2
	s_waitcnt vmcnt(25)
	v_mfma_f32_16x16x128_f8f6f4 v[86:89], v[92:97], v[6:11], v[86:89] cbsz:2 blgp:2
	s_waitcnt vmcnt(24)
	v_mfma_f32_16x16x128_f8f6f4 v[86:89], v[150:155], v[0:5], v[86:89] cbsz:2 blgp:2
	s_nop 7
	v_cndmask_b32_e64 v30, v86, v87, s[4:5]
	v_cndmask_b32_e64 v30, v30, v88, s[2:3]
	v_cndmask_b32_e32 v30, v30, v89, vcc
	v_mul_f32_e32 v31, v33, v30
	s_nop 1
	v_mov_b32_dpp v31, v31 quad_perm:[1,0,3,2] row_mask:0xf bank_mask:0xf bound_ctrl:1
	v_fmac_f32_e32 v31, v33, v30
	s_nop 1
	v_add_f32_dpp v30, v31, v31 quad_perm:[2,3,0,1] row_mask:0xf bank_mask:0xf bound_ctrl:1
	s_nop 1
	v_add_f32_dpp v30, v30, v30 row_half_mirror row_mask:0xf bank_mask:0xf bound_ctrl:1
	ds_write_b32 v32, v30 offset:49240
	ds_bpermute_b32 v30, v36, v128 offset:160
	s_waitcnt lgkmcnt(0)
	v_mul_lo_u32 v30, v30, s43
	v_add_u32_e32 v31, v30, v35
	v_add_u32_e32 v30, v30, v34
	buffer_load_dwordx4 v[86:89], v31, s[44:47], 0 offen
	buffer_load_dwordx4 v[92:95], v31, s[44:47], s20 offen
	buffer_load_dwordx4 v[98:101], v31, s[44:47], s21 offen
	buffer_load_dwordx4 v[150:153], v31, s[44:47], s23 offen
	buffer_load_dwordx2 v[90:91], v30, s[44:47], 0 offen
	buffer_load_dwordx2 v[102:103], v30, s[44:47], s33 offen
	buffer_load_dwordx2 v[96:97], v30, s[44:47], s21 offen
	buffer_load_dwordx2 v[154:155], v30, s[44:47], s94 offen
	s_waitcnt vmcnt(27)
	v_mfma_f32_16x16x128_f8f6f4 v[156:159], v[156:161], v[18:23], 0 cbsz:2 blgp:2
	s_waitcnt vmcnt(26)
	v_mfma_f32_16x16x128_f8f6f4 v[156:159], v[168:173], v[12:17], v[156:159] cbsz:2 blgp:2
	s_waitcnt vmcnt(25)
	v_mfma_f32_16x16x128_f8f6f4 v[156:159], v[162:167], v[6:11], v[156:159] cbsz:2 blgp:2
	s_waitcnt vmcnt(24)
	v_mfma_f32_16x16x128_f8f6f4 v[156:159], v[174:179], v[0:5], v[156:159] cbsz:2 blgp:2
	s_nop 7
	v_cndmask_b32_e64 v30, v156, v157, s[4:5]
	v_cndmask_b32_e64 v30, v30, v158, s[2:3]
	v_cndmask_b32_e32 v30, v30, v159, vcc
	v_mul_f32_e32 v31, v33, v30
	s_nop 1
	v_mov_b32_dpp v31, v31 quad_perm:[1,0,3,2] row_mask:0xf bank_mask:0xf bound_ctrl:1
	v_fmac_f32_e32 v31, v33, v30
	s_nop 1
	v_add_f32_dpp v30, v31, v31 quad_perm:[2,3,0,1] row_mask:0xf bank_mask:0xf bound_ctrl:1
	s_nop 1
	v_add_f32_dpp v30, v30, v30 row_half_mirror row_mask:0xf bank_mask:0xf bound_ctrl:1
	ds_write_b32 v32, v30 offset:49244
	ds_bpermute_b32 v30, v36, v128 offset:176
	s_waitcnt lgkmcnt(0)
	v_mul_lo_u32 v30, v30, s43
	v_add_u32_e32 v31, v30, v35
	v_add_u32_e32 v30, v30, v34
	buffer_load_dwordx4 v[156:159], v31, s[44:47], 0 offen
	buffer_load_dwordx4 v[162:165], v31, s[44:47], s20 offen
	buffer_load_dwordx4 v[168:171], v31, s[44:47], s21 offen
	buffer_load_dwordx4 v[174:177], v31, s[44:47], s23 offen
	buffer_load_dwordx2 v[160:161], v30, s[44:47], 0 offen
	buffer_load_dwordx2 v[172:173], v30, s[44:47], s33 offen
	buffer_load_dwordx2 v[166:167], v30, s[44:47], s21 offen
	buffer_load_dwordx2 v[178:179], v30, s[44:47], s94 offen
	s_waitcnt vmcnt(27)
	v_mfma_f32_16x16x128_f8f6f4 v[24:27], v[24:29], v[18:23], 0 cbsz:2 blgp:2
	s_waitcnt vmcnt(26)
	v_mfma_f32_16x16x128_f8f6f4 v[24:27], v[44:49], v[12:17], v[24:27] cbsz:2 blgp:2
	s_waitcnt vmcnt(25)
	v_mfma_f32_16x16x128_f8f6f4 v[24:27], v[38:43], v[6:11], v[24:27] cbsz:2 blgp:2
	s_waitcnt vmcnt(24)
	v_mfma_f32_16x16x128_f8f6f4 v[24:27], v[50:55], v[0:5], v[24:27] cbsz:2 blgp:2
	s_nop 7
	v_cndmask_b32_e64 v24, v24, v25, s[4:5]
	v_cndmask_b32_e64 v24, v24, v26, s[2:3]
	v_cndmask_b32_e32 v24, v24, v27, vcc
	v_mul_f32_e32 v25, v33, v24
	s_nop 1
	v_mov_b32_dpp v25, v25 quad_perm:[1,0,3,2] row_mask:0xf bank_mask:0xf bound_ctrl:1
	v_fmac_f32_e32 v25, v33, v24
	s_nop 1
	v_add_f32_dpp v24, v25, v25 quad_perm:[2,3,0,1] row_mask:0xf bank_mask:0xf bound_ctrl:1
	s_nop 1
	v_add_f32_dpp v24, v24, v24 row_half_mirror row_mask:0xf bank_mask:0xf bound_ctrl:1
	ds_write_b32 v32, v24 offset:49248
	ds_bpermute_b32 v24, v36, v128 offset:192
	s_waitcnt lgkmcnt(0)
	v_mul_lo_u32 v24, v24, s43
	v_add_u32_e32 v28, v24, v35
	v_add_u32_e32 v30, v24, v34
	buffer_load_dwordx4 v[24:27], v28, s[44:47], 0 offen
	buffer_load_dwordx4 v[38:41], v28, s[44:47], s20 offen
	buffer_load_dwordx4 v[44:47], v28, s[44:47], s21 offen
	buffer_load_dwordx4 v[50:53], v28, s[44:47], s23 offen
	s_nop 0
	buffer_load_dwordx2 v[28:29], v30, s[44:47], 0 offen
	buffer_load_dwordx2 v[48:49], v30, s[44:47], s33 offen
	buffer_load_dwordx2 v[42:43], v30, s[44:47], s21 offen
	buffer_load_dwordx2 v[54:55], v30, s[44:47], s94 offen
	s_waitcnt vmcnt(27)
	v_mfma_f32_16x16x128_f8f6f4 v[56:59], v[56:61], v[18:23], 0 cbsz:2 blgp:2
	s_waitcnt vmcnt(26)
	v_mfma_f32_16x16x128_f8f6f4 v[56:59], v[68:73], v[12:17], v[56:59] cbsz:2 blgp:2
	s_waitcnt vmcnt(25)
	v_mfma_f32_16x16x128_f8f6f4 v[56:59], v[62:67], v[6:11], v[56:59] cbsz:2 blgp:2
	s_waitcnt vmcnt(24)
	v_mfma_f32_16x16x128_f8f6f4 v[56:59], v[74:79], v[0:5], v[56:59] cbsz:2 blgp:2
	s_nop 7
	v_cndmask_b32_e64 v30, v56, v57, s[4:5]
	v_cndmask_b32_e64 v30, v30, v58, s[2:3]
	v_cndmask_b32_e32 v30, v30, v59, vcc
	v_mul_f32_e32 v31, v33, v30
	s_nop 1
	v_mov_b32_dpp v31, v31 quad_perm:[1,0,3,2] row_mask:0xf bank_mask:0xf bound_ctrl:1
	v_fmac_f32_e32 v31, v33, v30
	s_nop 1
	v_add_f32_dpp v30, v31, v31 quad_perm:[2,3,0,1] row_mask:0xf bank_mask:0xf bound_ctrl:1
	s_nop 1
	v_add_f32_dpp v30, v30, v30 row_half_mirror row_mask:0xf bank_mask:0xf bound_ctrl:1
	ds_write_b32 v32, v30 offset:49252
	ds_bpermute_b32 v30, v36, v128 offset:208
	s_waitcnt lgkmcnt(0)
	v_mul_lo_u32 v30, v30, s43
	v_add_u32_e32 v31, v30, v35
	v_add_u32_e32 v30, v30, v34
	buffer_load_dwordx4 v[56:59], v31, s[44:47], 0 offen
	buffer_load_dwordx4 v[62:65], v31, s[44:47], s20 offen
	buffer_load_dwordx4 v[68:71], v31, s[44:47], s21 offen
	buffer_load_dwordx4 v[74:77], v31, s[44:47], s23 offen
	buffer_load_dwordx2 v[60:61], v30, s[44:47], 0 offen
	buffer_load_dwordx2 v[72:73], v30, s[44:47], s33 offen
	buffer_load_dwordx2 v[66:67], v30, s[44:47], s21 offen
	buffer_load_dwordx2 v[78:79], v30, s[44:47], s94 offen
	s_waitcnt vmcnt(27)
	v_mfma_f32_16x16x128_f8f6f4 v[86:89], v[86:91], v[18:23], 0 cbsz:2 blgp:2
	s_waitcnt vmcnt(26)
	v_mfma_f32_16x16x128_f8f6f4 v[86:89], v[98:103], v[12:17], v[86:89] cbsz:2 blgp:2
	s_waitcnt vmcnt(25)
	v_mfma_f32_16x16x128_f8f6f4 v[86:89], v[92:97], v[6:11], v[86:89] cbsz:2 blgp:2
	s_waitcnt vmcnt(24)
	v_mfma_f32_16x16x128_f8f6f4 v[86:89], v[150:155], v[0:5], v[86:89] cbsz:2 blgp:2
	s_nop 7
	v_cndmask_b32_e64 v30, v86, v87, s[4:5]
	v_cndmask_b32_e64 v30, v30, v88, s[2:3]
	v_cndmask_b32_e32 v30, v30, v89, vcc
	v_mul_f32_e32 v31, v33, v30
	s_nop 1
	v_mov_b32_dpp v31, v31 quad_perm:[1,0,3,2] row_mask:0xf bank_mask:0xf bound_ctrl:1
	v_fmac_f32_e32 v31, v33, v30
	s_nop 1
	v_add_f32_dpp v30, v31, v31 quad_perm:[2,3,0,1] row_mask:0xf bank_mask:0xf bound_ctrl:1
	s_nop 1
	v_add_f32_dpp v30, v30, v30 row_half_mirror row_mask:0xf bank_mask:0xf bound_ctrl:1
	ds_write_b32 v32, v30 offset:49256
	ds_bpermute_b32 v30, v36, v128 offset:224
	s_waitcnt lgkmcnt(0)
	v_mul_lo_u32 v30, v30, s43
	v_add_u32_e32 v31, v30, v35
	v_add_u32_e32 v30, v30, v34
	buffer_load_dwordx4 v[86:89], v31, s[44:47], 0 offen
	buffer_load_dwordx4 v[92:95], v31, s[44:47], s20 offen
	buffer_load_dwordx4 v[98:101], v31, s[44:47], s21 offen
	buffer_load_dwordx4 v[150:153], v31, s[44:47], s23 offen
	buffer_load_dwordx2 v[90:91], v30, s[44:47], 0 offen
	buffer_load_dwordx2 v[102:103], v30, s[44:47], s33 offen
	buffer_load_dwordx2 v[96:97], v30, s[44:47], s21 offen
	buffer_load_dwordx2 v[154:155], v30, s[44:47], s94 offen
	s_waitcnt vmcnt(27)
	v_mfma_f32_16x16x128_f8f6f4 v[156:159], v[156:161], v[18:23], 0 cbsz:2 blgp:2
	s_waitcnt vmcnt(26)
	v_mfma_f32_16x16x128_f8f6f4 v[156:159], v[168:173], v[12:17], v[156:159] cbsz:2 blgp:2
	s_waitcnt vmcnt(25)
	v_mfma_f32_16x16x128_f8f6f4 v[156:159], v[162:167], v[6:11], v[156:159] cbsz:2 blgp:2
	s_waitcnt vmcnt(24)
	v_mfma_f32_16x16x128_f8f6f4 v[156:159], v[174:179], v[0:5], v[156:159] cbsz:2 blgp:2
	s_nop 7
	v_cndmask_b32_e64 v30, v156, v157, s[4:5]
	v_cndmask_b32_e64 v30, v30, v158, s[2:3]
	v_cndmask_b32_e32 v30, v30, v159, vcc
	v_mul_f32_e32 v31, v33, v30
	s_nop 1
	v_mov_b32_dpp v31, v31 quad_perm:[1,0,3,2] row_mask:0xf bank_mask:0xf bound_ctrl:1
	v_fmac_f32_e32 v31, v33, v30
	s_nop 1
	v_add_f32_dpp v30, v31, v31 quad_perm:[2,3,0,1] row_mask:0xf bank_mask:0xf bound_ctrl:1
	s_nop 1
	v_add_f32_dpp v30, v30, v30 row_half_mirror row_mask:0xf bank_mask:0xf bound_ctrl:1
	ds_write_b32 v32, v30 offset:49260
	ds_bpermute_b32 v30, v36, v128 offset:240
	s_waitcnt lgkmcnt(0)
	v_mul_lo_u32 v30, v30, s43
	v_add_u32_e32 v31, v30, v35
	v_add_u32_e32 v30, v30, v34
	buffer_load_dwordx4 v[156:159], v31, s[44:47], 0 offen
	buffer_load_dwordx4 v[162:165], v31, s[44:47], s20 offen
	buffer_load_dwordx4 v[168:171], v31, s[44:47], s21 offen
	buffer_load_dwordx4 v[174:177], v31, s[44:47], s23 offen
	buffer_load_dwordx2 v[160:161], v30, s[44:47], 0 offen
	buffer_load_dwordx2 v[172:173], v30, s[44:47], s33 offen
	buffer_load_dwordx2 v[166:167], v30, s[44:47], s21 offen
	buffer_load_dwordx2 v[178:179], v30, s[44:47], s94 offen
	s_waitcnt vmcnt(27)
	v_mfma_f32_16x16x128_f8f6f4 v[24:27], v[24:29], v[18:23], 0 cbsz:2 blgp:2
	s_waitcnt vmcnt(26)
	v_mfma_f32_16x16x128_f8f6f4 v[24:27], v[44:49], v[12:17], v[24:27] cbsz:2 blgp:2
	s_waitcnt vmcnt(25)
	v_mfma_f32_16x16x128_f8f6f4 v[24:27], v[38:43], v[6:11], v[24:27] cbsz:2 blgp:2
	s_waitcnt vmcnt(24)
	v_mfma_f32_16x16x128_f8f6f4 v[24:27], v[50:55], v[0:5], v[24:27] cbsz:2 blgp:2
	s_nop 7
	v_cndmask_b32_e64 v24, v24, v25, s[4:5]
	v_cndmask_b32_e64 v24, v24, v26, s[2:3]
	v_cndmask_b32_e32 v24, v24, v27, vcc
	v_mul_f32_e32 v25, v33, v24
	s_nop 1
	v_mov_b32_dpp v25, v25 quad_perm:[1,0,3,2] row_mask:0xf bank_mask:0xf bound_ctrl:1
	v_fmac_f32_e32 v25, v33, v24
	s_nop 1
	v_add_f32_dpp v24, v25, v25 quad_perm:[2,3,0,1] row_mask:0xf bank_mask:0xf bound_ctrl:1
	s_nop 1
	v_add_f32_dpp v24, v24, v24 row_half_mirror row_mask:0xf bank_mask:0xf bound_ctrl:1
	ds_write_b32 v32, v24 offset:49264
	s_waitcnt vmcnt(19)
	v_mfma_f32_16x16x128_f8f6f4 v[24:27], v[56:61], v[18:23], 0 cbsz:2 blgp:2
	s_waitcnt vmcnt(18)
	v_mfma_f32_16x16x128_f8f6f4 v[24:27], v[68:73], v[12:17], v[24:27] cbsz:2 blgp:2
	s_waitcnt vmcnt(17)
	v_mfma_f32_16x16x128_f8f6f4 v[24:27], v[62:67], v[6:11], v[24:27] cbsz:2 blgp:2
	s_waitcnt vmcnt(16)
	v_mfma_f32_16x16x128_f8f6f4 v[24:27], v[74:79], v[0:5], v[24:27] cbsz:2 blgp:2
	s_nop 7
	v_cndmask_b32_e64 v24, v24, v25, s[4:5]
	v_cndmask_b32_e64 v24, v24, v26, s[2:3]
	v_cndmask_b32_e32 v24, v24, v27, vcc
	v_mul_f32_e32 v25, v33, v24
	s_nop 1
	v_mov_b32_dpp v25, v25 quad_perm:[1,0,3,2] row_mask:0xf bank_mask:0xf bound_ctrl:1
	v_fmac_f32_e32 v25, v33, v24
	s_nop 1
	v_add_f32_dpp v24, v25, v25 quad_perm:[2,3,0,1] row_mask:0xf bank_mask:0xf bound_ctrl:1
	s_nop 1
	v_add_f32_dpp v24, v24, v24 row_half_mirror row_mask:0xf bank_mask:0xf bound_ctrl:1
	ds_write_b32 v32, v24 offset:49268
	s_waitcnt vmcnt(11)
	v_mfma_f32_16x16x128_f8f6f4 v[24:27], v[86:91], v[18:23], 0 cbsz:2 blgp:2
	s_waitcnt vmcnt(10)
	v_mfma_f32_16x16x128_f8f6f4 v[24:27], v[98:103], v[12:17], v[24:27] cbsz:2 blgp:2
	s_waitcnt vmcnt(9)
	v_mfma_f32_16x16x128_f8f6f4 v[24:27], v[92:97], v[6:11], v[24:27] cbsz:2 blgp:2
	s_waitcnt vmcnt(8)
	v_mfma_f32_16x16x128_f8f6f4 v[24:27], v[150:155], v[0:5], v[24:27] cbsz:2 blgp:2
	s_nop 7
	v_cndmask_b32_e64 v24, v24, v25, s[4:5]
	v_cndmask_b32_e64 v24, v24, v26, s[2:3]
	v_cndmask_b32_e32 v24, v24, v27, vcc
	v_mul_f32_e32 v25, v33, v24
	s_nop 1
	v_mov_b32_dpp v25, v25 quad_perm:[1,0,3,2] row_mask:0xf bank_mask:0xf bound_ctrl:1
	v_fmac_f32_e32 v25, v33, v24
	s_nop 1
	v_add_f32_dpp v24, v25, v25 quad_perm:[2,3,0,1] row_mask:0xf bank_mask:0xf bound_ctrl:1
	s_nop 1
	v_add_f32_dpp v24, v24, v24 row_half_mirror row_mask:0xf bank_mask:0xf bound_ctrl:1
	ds_write_b32 v32, v24 offset:49272
	s_waitcnt vmcnt(3)
	v_mfma_f32_16x16x128_f8f6f4 v[18:21], v[156:161], v[18:23], 0 cbsz:2 blgp:2
	s_waitcnt vmcnt(2)
	v_mfma_f32_16x16x128_f8f6f4 v[12:15], v[168:173], v[12:17], v[18:21] cbsz:2 blgp:2
	s_waitcnt vmcnt(1)
	v_mfma_f32_16x16x128_f8f6f4 v[6:9], v[162:167], v[6:11], v[12:15] cbsz:2 blgp:2
	s_waitcnt vmcnt(0)
	v_mfma_f32_16x16x128_f8f6f4 v[0:3], v[174:179], v[0:5], v[6:9] cbsz:2 blgp:2
	s_nop 7
	v_cndmask_b32_e64 v0, v0, v1, s[4:5]
	v_cndmask_b32_e64 v0, v0, v2, s[2:3]
	v_cndmask_b32_e32 v0, v0, v3, vcc
	v_mul_f32_e32 v1, v33, v0
	s_nop 1
	v_mov_b32_dpp v1, v1 quad_perm:[1,0,3,2] row_mask:0xf bank_mask:0xf bound_ctrl:1
	v_fmac_f32_e32 v1, v33, v0
	s_nop 1
	v_add_f32_dpp v0, v1, v1 quad_perm:[2,3,0,1] row_mask:0xf bank_mask:0xf bound_ctrl:1
	s_nop 1
	v_add_f32_dpp v0, v0, v0 row_half_mirror row_mask:0xf bank_mask:0xf bound_ctrl:1
	ds_write_b32 v32, v0 offset:49276
	v_mul_u32_u24_e32 v240, 0x600, v130
	v_mul_u32_u24_e32 v241, 0x600, v128
	v_add_u32_e32 v240, 0x8000000, v240
	v_add_u32_e32 v241, 0x8000000, v241
	v_lshrrev_b32_e32 v0, 1, v129
	v_readlane_b32 s100, v240, 0
	v_readlane_b32 s101, v240, 1
	v_readlane_b32 s2, v240, 2
	v_readlane_b32 s3, v240, 3
	s_nop 1
	buffer_load_dwordx4 v[74:77], v129, s[44:47], s100 offen
	buffer_load_dwordx2 v[78:79], v0, s[44:47], s100 offen offset:1024
	buffer_load_dwordx4 v[68:71], v129, s[44:47], s101 offen
	buffer_load_dwordx2 v[72:73], v0, s[44:47], s101 offen offset:1024
	buffer_load_dwordx4 v[56:59], v129, s[44:47], s2 offen
	buffer_load_dwordx2 v[60:61], v0, s[44:47], s2 offen offset:1024
	buffer_load_dwordx4 v[44:47], v129, s[44:47], s3 offen
	buffer_load_dwordx2 v[48:49], v0, s[44:47], s3 offen offset:1024
	v_add_u32_e32 v210, 0x400, v0
	v_readlane_b32 s100, v240, 4
	v_readlane_b32 s101, v240, 5
	v_readlane_b32 s2, v240, 6
	v_readlane_b32 s3, v240, 7
	s_nop 1
	buffer_load_dwordx4 v[62:65], v129, s[44:47], s100 offen
	buffer_load_dwordx2 v[66:67], v0, s[44:47], s100 offen offset:1024
	buffer_load_dwordx4 v[50:53], v129, s[44:47], s101 offen
	buffer_load_dwordx2 v[54:55], v0, s[44:47], s101 offen offset:1024
	buffer_load_dwordx4 v[38:41], v129, s[44:47], s2 offen
	buffer_load_dwordx2 v[42:43], v0, s[44:47], s2 offen offset:1024
	buffer_load_dwordx4 v[32:35], v129, s[44:47], s3 offen
	buffer_load_dwordx2 v[36:37], v0, s[44:47], s3 offen offset:1024
	v_div_scale_f32 v2, s[2:3], v80, v80, 1.0
	v_rcp_f32_e32 v3, v2
	v_div_scale_f32 v4, vcc, 1.0, v80, 1.0
	v_and_b32_e32 v1, -4, v148
	v_fma_f32 v0, -v2, v3, 1.0
	v_fmac_f32_e32 v3, v0, v3
	v_mul_f32_e32 v5, v4, v3
	v_fma_f32 v0, -v2, v5, v4
	v_fmac_f32_e32 v5, v0, v3
	v_lshlrev_b32_e32 v0, 7, v148
	v_and_b32_e32 v0, 0x180, v0
	v_add3_u32 v0, v111, v0, v1
	v_add_u32_e32 v0, 0xc000, v0
	ds_read2_b32 v[0:1], v0 offset1:16
	v_fma_f32 v2, -v2, v5, v4
	v_div_fmas_f32 v2, v2, v3, v5
	v_div_fixup_f32 v2, v2, v80, 1.0
	s_mov_b32 s1, 0x3e6d3388
	s_waitcnt lgkmcnt(0)
	v_mul_f32_e32 v0, v2, v0
	v_mul_f32_e32 v0, v83, v0
	v_fma_f32 v3, |v0|, s1, 1.0
	v_rcp_f32_e32 v3, v3
	v_mul_f32_e32 v5, v0, v0
	v_mul_f32_e32 v5, 0xbf38aa3b, v5
	v_exp_f32_e32 v5, v5
	v_fmamk_f32 v4, v3, 0x3f07dc22, v184
	v_fmaak_f32 v4, v3, v4, 0x3f35f0e3
	v_fmaak_f32 v4, v3, v4, 0xbe11a98e
	v_mul_f32_e32 v1, v2, v1
	v_fmaak_f32 v4, v3, v4, 0x3e027906
	v_mul_f32_e32 v3, v3, v4
	v_mul_f32_e32 v1, v82, v1
	v_mul_f32_e32 v3, v5, v3
	v_fma_f32 v5, |v1|, s1, 1.0
	v_rcp_f32_e32 v5, v5
	v_mul_f32_e32 v4, v0, v3
	v_fma_f32 v3, -v0, v3, v0
	v_cmp_gt_f32_e32 vcc, 0, v0
	v_mul_f32_e32 v2, v206, v84
	v_mov_b32_e32 v180, 0
	v_cndmask_b32_e32 v0, v3, v4, vcc
	v_mul_f32_e32 v211, v2, v0
	v_mul_f32_e32 v2, v1, v1
	v_fmamk_f32 v0, v5, 0x3f07dc22, v184
	v_mul_f32_e32 v2, 0xbf38aa3b, v2
	v_fmaak_f32 v0, v5, v0, 0x3f35f0e3
	v_exp_f32_e32 v2, v2
	v_fmaak_f32 v0, v5, v0, 0xbe11a98e
	v_fmaak_f32 v0, v5, v0, 0x3e027906
	v_mul_f32_e32 v0, v5, v0
	v_mul_f32_e32 v0, v2, v0
	v_mul_f32_e32 v2, v1, v0
	v_fma_f32 v0, -v1, v0, v1
	v_cmp_gt_f32_e32 vcc, 0, v1
	v_mul_f32_e32 v1, v205, v81
	v_mov_b32_e32 v181, v180
	v_cndmask_b32_e32 v0, v0, v2, vcc
	v_mul_f32_e32 v131, v1, v0
	v_mov_b32_e32 v178, v180
	v_mov_b32_e32 v179, v180
	v_mov_b32_e32 v176, v180
	v_mov_b32_e32 v177, v180
	v_mov_b32_e32 v174, v180
	v_mov_b32_e32 v175, v180
	v_mov_b32_e32 v172, v180
	v_mov_b32_e32 v173, v180
	v_mov_b32_e32 v170, v180
	v_mov_b32_e32 v171, v180
	v_mov_b32_e32 v168, v180
	v_mov_b32_e32 v169, v180
	v_mov_b32_e32 v166, v180
	v_mov_b32_e32 v167, v180
	v_mov_b32_e32 v164, v180
	v_mov_b32_e32 v165, v180
	v_mov_b32_e32 v162, v180
	v_mov_b32_e32 v163, v180
	v_mov_b32_e32 v160, v180
	v_mov_b32_e32 v161, v180
	v_mov_b32_e32 v158, v180
	v_mov_b32_e32 v159, v180
	v_mov_b32_e32 v156, v180
	v_mov_b32_e32 v157, v180
	v_mov_b32_e32 v154, v180
	v_mov_b32_e32 v155, v180
	v_mov_b32_e32 v152, v180
	v_mov_b32_e32 v153, v180
	v_mov_b32_e32 v150, v180
	v_mov_b32_e32 v151, v180
	v_readlane_b32 s2, v240, 8
	v_readlane_b32 s3, v240, 9
	v_readlane_b32 s100, v240, 10
	v_readlane_b32 s101, v240, 11
	s_nop 1
	buffer_load_dwordx4 v[98:101], v129, s[44:47], s2 offen
	buffer_load_dwordx2 v[102:103], v210, s[44:47], s2 offen
	buffer_load_dwordx4 v[92:95], v129, s[44:47], s3 offen
	buffer_load_dwordx2 v[96:97], v210, s[44:47], s3 offen
	buffer_load_dwordx4 v[86:89], v129, s[44:47], s100 offen
	buffer_load_dwordx2 v[90:91], v210, s[44:47], s100 offen
	buffer_load_dwordx4 v[80:83], v129, s[44:47], s101 offen
	buffer_load_dwordx2 v[84:85], v210, s[44:47], s101 offen
	v_readlane_b32 s2, v211, 0
	s_waitcnt vmcnt(22)
	v_cvt_scalef32_pk32_f32_fp6 v[0:31], v[74:79], 1.0
	v_pk_fma_f32 v[74:75], v[0:1], s[2:3], v[180:181] op_sel_hi:[1,0,1]
	v_pk_fma_f32 v[76:77], v[2:3], s[2:3], v[178:179] op_sel_hi:[1,0,1]
	v_pk_fma_f32 v[78:79], v[4:5], s[2:3], v[176:177] op_sel_hi:[1,0,1]
	v_pk_fma_f32 v[174:175], v[6:7], s[2:3], v[174:175] op_sel_hi:[1,0,1]
	v_pk_fma_f32 v[172:173], v[8:9], s[2:3], v[172:173] op_sel_hi:[1,0,1]
	v_pk_fma_f32 v[170:171], v[10:11], s[2:3], v[170:171] op_sel_hi:[1,0,1]
	v_pk_fma_f32 v[168:169], v[12:13], s[2:3], v[168:169] op_sel_hi:[1,0,1]
	v_pk_fma_f32 v[166:167], v[14:15], s[2:3], v[166:167] op_sel_hi:[1,0,1]
	v_pk_fma_f32 v[164:165], v[16:17], s[2:3], v[164:165] op_sel_hi:[1,0,1]
	v_pk_fma_f32 v[162:163], v[18:19], s[2:3], v[162:163] op_sel_hi:[1,0,1]
	v_pk_fma_f32 v[160:161], v[20:21], s[2:3], v[160:161] op_sel_hi:[1,0,1]
	v_pk_fma_f32 v[158:159], v[22:23], s[2:3], v[158:159] op_sel_hi:[1,0,1]
	v_pk_fma_f32 v[156:157], v[24:25], s[2:3], v[156:157] op_sel_hi:[1,0,1]
	v_pk_fma_f32 v[154:155], v[26:27], s[2:3], v[154:155] op_sel_hi:[1,0,1]
	v_pk_fma_f32 v[152:153], v[28:29], s[2:3], v[152:153] op_sel_hi:[1,0,1]
	v_pk_fma_f32 v[150:151], v[30:31], s[2:3], v[150:151] op_sel_hi:[1,0,1]
	v_readlane_b32 s2, v211, 1
	s_waitcnt vmcnt(20)
	v_cvt_scalef32_pk32_f32_fp6 v[0:31], v[68:73], 1.0
	v_pk_fma_f32 v[68:69], v[0:1], s[2:3], v[74:75] op_sel_hi:[1,0,1]
	v_pk_fma_f32 v[70:71], v[2:3], s[2:3], v[76:77] op_sel_hi:[1,0,1]
	v_pk_fma_f32 v[72:73], v[4:5], s[2:3], v[78:79] op_sel_hi:[1,0,1]
	v_pk_fma_f32 v[74:75], v[6:7], s[2:3], v[174:175] op_sel_hi:[1,0,1]
	v_pk_fma_f32 v[76:77], v[8:9], s[2:3], v[172:173] op_sel_hi:[1,0,1]
	v_pk_fma_f32 v[78:79], v[10:11], s[2:3], v[170:171] op_sel_hi:[1,0,1]
	v_pk_fma_f32 v[168:169], v[12:13], s[2:3], v[168:169] op_sel_hi:[1,0,1]
	v_pk_fma_f32 v[166:167], v[14:15], s[2:3], v[166:167] op_sel_hi:[1,0,1]
	v_pk_fma_f32 v[164:165], v[16:17], s[2:3], v[164:165] op_sel_hi:[1,0,1]
	v_pk_fma_f32 v[162:163], v[18:19], s[2:3], v[162:163] op_sel_hi:[1,0,1]
	v_pk_fma_f32 v[160:161], v[20:21], s[2:3], v[160:161] op_sel_hi:[1,0,1]
	v_pk_fma_f32 v[158:159], v[22:23], s[2:3], v[158:159] op_sel_hi:[1,0,1]
	v_pk_fma_f32 v[156:157], v[24:25], s[2:3], v[156:157] op_sel_hi:[1,0,1]
	v_pk_fma_f32 v[154:155], v[26:27], s[2:3], v[154:155] op_sel_hi:[1,0,1]
	v_pk_fma_f32 v[152:153], v[28:29], s[2:3], v[152:153] op_sel_hi:[1,0,1]
	v_pk_fma_f32 v[150:151], v[30:31], s[2:3], v[150:151] op_sel_hi:[1,0,1]
	v_readlane_b32 s2, v211, 2
	s_waitcnt vmcnt(18)
	v_cvt_scalef32_pk32_f32_fp6 v[0:31], v[56:61], 1.0
	v_pk_fma_f32 v[56:57], v[0:1], s[2:3], v[68:69] op_sel_hi:[1,0,1]
	v_pk_fma_f32 v[58:59], v[2:3], s[2:3], v[70:71] op_sel_hi:[1,0,1]
	v_pk_fma_f32 v[60:61], v[4:5], s[2:3], v[72:73] op_sel_hi:[1,0,1]
	v_pk_fma_f32 v[68:69], v[6:7], s[2:3], v[74:75] op_sel_hi:[1,0,1]
	v_pk_fma_f32 v[70:71], v[8:9], s[2:3], v[76:77] op_sel_hi:[1,0,1]
	v_pk_fma_f32 v[72:73], v[10:11], s[2:3], v[78:79] op_sel_hi:[1,0,1]
	v_pk_fma_f32 v[74:75], v[12:13], s[2:3], v[168:169] op_sel_hi:[1,0,1]
	v_pk_fma_f32 v[76:77], v[14:15], s[2:3], v[166:167] op_sel_hi:[1,0,1]
	v_pk_fma_f32 v[78:79], v[16:17], s[2:3], v[164:165] op_sel_hi:[1,0,1]
	v_pk_fma_f32 v[162:163], v[18:19], s[2:3], v[162:163] op_sel_hi:[1,0,1]
	v_pk_fma_f32 v[160:161], v[20:21], s[2:3], v[160:161] op_sel_hi:[1,0,1]
	v_pk_fma_f32 v[158:159], v[22:23], s[2:3], v[158:159] op_sel_hi:[1,0,1]
	v_pk_fma_f32 v[156:157], v[24:25], s[2:3], v[156:157] op_sel_hi:[1,0,1]
	v_pk_fma_f32 v[154:155], v[26:27], s[2:3], v[154:155] op_sel_hi:[1,0,1]
	v_pk_fma_f32 v[152:153], v[28:29], s[2:3], v[152:153] op_sel_hi:[1,0,1]
	v_pk_fma_f32 v[150:151], v[30:31], s[2:3], v[150:151] op_sel_hi:[1,0,1]
	v_readlane_b32 s2, v211, 3
	s_waitcnt vmcnt(16)
	v_cvt_scalef32_pk32_f32_fp6 v[0:31], v[44:49], 1.0
	v_pk_fma_f32 v[164:165], v[0:1], s[2:3], v[56:57] op_sel_hi:[1,0,1]
	v_pk_fma_f32 v[166:167], v[2:3], s[2:3], v[58:59] op_sel_hi:[1,0,1]
	v_pk_fma_f32 v[168:169], v[4:5], s[2:3], v[60:61] op_sel_hi:[1,0,1]
	v_pk_fma_f32 v[170:171], v[6:7], s[2:3], v[68:69] op_sel_hi:[1,0,1]
	v_pk_fma_f32 v[172:173], v[8:9], s[2:3], v[70:71] op_sel_hi:[1,0,1]
	v_pk_fma_f32 v[174:175], v[10:11], s[2:3], v[72:73] op_sel_hi:[1,0,1]
	v_pk_fma_f32 v[176:177], v[12:13], s[2:3], v[74:75] op_sel_hi:[1,0,1]
	v_pk_fma_f32 v[178:179], v[14:15], s[2:3], v[76:77] op_sel_hi:[1,0,1]
	v_pk_fma_f32 v[180:181], v[16:17], s[2:3], v[78:79] op_sel_hi:[1,0,1]
	v_pk_fma_f32 v[162:163], v[18:19], s[2:3], v[162:163] op_sel_hi:[1,0,1]
	v_pk_fma_f32 v[160:161], v[20:21], s[2:3], v[160:161] op_sel_hi:[1,0,1]
	v_pk_fma_f32 v[158:159], v[22:23], s[2:3], v[158:159] op_sel_hi:[1,0,1]
	v_pk_fma_f32 v[156:157], v[24:25], s[2:3], v[156:157] op_sel_hi:[1,0,1]
	v_pk_fma_f32 v[154:155], v[26:27], s[2:3], v[154:155] op_sel_hi:[1,0,1]
	v_pk_fma_f32 v[152:153], v[28:29], s[2:3], v[152:153] op_sel_hi:[1,0,1]
	v_pk_fma_f32 v[150:151], v[30:31], s[2:3], v[150:151] op_sel_hi:[1,0,1]
	v_readlane_b32 s2, v240, 12
	v_readlane_b32 s3, v240, 13
	v_readlane_b32 s100, v240, 14
	v_readlane_b32 s101, v240, 15
	s_nop 1
	buffer_load_dwordx4 v[74:77], v129, s[44:47], s2 offen
	buffer_load_dwordx2 v[78:79], v210, s[44:47], s2 offen
	buffer_load_dwordx4 v[68:71], v129, s[44:47], s3 offen
	buffer_load_dwordx2 v[72:73], v210, s[44:47], s3 offen
	buffer_load_dwordx4 v[56:59], v129, s[44:47], s100 offen
	buffer_load_dwordx2 v[60:61], v210, s[44:47], s100 offen
	buffer_load_dwordx4 v[44:47], v129, s[44:47], s101 offen
	buffer_load_dwordx2 v[48:49], v210, s[44:47], s101 offen
	v_readlane_b32 s2, v211, 4
	s_waitcnt vmcnt(22)
	v_cvt_scalef32_pk32_f32_fp6 v[0:31], v[62:67], 1.0
	v_pk_fma_f32 v[62:63], v[0:1], s[2:3], v[164:165] op_sel_hi:[1,0,1]
	v_pk_fma_f32 v[64:65], v[2:3], s[2:3], v[166:167] op_sel_hi:[1,0,1]
	v_pk_fma_f32 v[66:67], v[4:5], s[2:3], v[168:169] op_sel_hi:[1,0,1]
	v_pk_fma_f32 v[164:165], v[6:7], s[2:3], v[170:171] op_sel_hi:[1,0,1]
	v_pk_fma_f32 v[166:167], v[8:9], s[2:3], v[172:173] op_sel_hi:[1,0,1]
	v_pk_fma_f32 v[168:169], v[10:11], s[2:3], v[174:175] op_sel_hi:[1,0,1]
	v_pk_fma_f32 v[170:171], v[12:13], s[2:3], v[176:177] op_sel_hi:[1,0,1]
	v_pk_fma_f32 v[172:173], v[14:15], s[2:3], v[178:179] op_sel_hi:[1,0,1]
	v_pk_fma_f32 v[174:175], v[16:17], s[2:3], v[180:181] op_sel_hi:[1,0,1]
	v_pk_fma_f32 v[162:163], v[18:19], s[2:3], v[162:163] op_sel_hi:[1,0,1]
	v_pk_fma_f32 v[160:161], v[20:21], s[2:3], v[160:161] op_sel_hi:[1,0,1]
	v_pk_fma_f32 v[158:159], v[22:23], s[2:3], v[158:159] op_sel_hi:[1,0,1]
	v_pk_fma_f32 v[156:157], v[24:25], s[2:3], v[156:157] op_sel_hi:[1,0,1]
	v_pk_fma_f32 v[154:155], v[26:27], s[2:3], v[154:155] op_sel_hi:[1,0,1]
	v_pk_fma_f32 v[152:153], v[28:29], s[2:3], v[152:153] op_sel_hi:[1,0,1]
	v_pk_fma_f32 v[150:151], v[30:31], s[2:3], v[150:151] op_sel_hi:[1,0,1]
	v_readlane_b32 s2, v211, 5
	s_waitcnt vmcnt(20)
	v_cvt_scalef32_pk32_f32_fp6 v[0:31], v[50:55], 1.0
	v_pk_fma_f32 v[50:51], v[0:1], s[2:3], v[62:63] op_sel_hi:[1,0,1]
	v_pk_fma_f32 v[52:53], v[2:3], s[2:3], v[64:65] op_sel_hi:[1,0,1]
	v_pk_fma_f32 v[54:55], v[4:5], s[2:3], v[66:67] op_sel_hi:[1,0,1]
	v_pk_fma_f32 v[62:63], v[6:7], s[2:3], v[164:165] op_sel_hi:[1,0,1]
	v_pk_fma_f32 v[64:65], v[8:9], s[2:3], v[166:167] op_sel_hi:[1,0,1]
	v_pk_fma_f32 v[66:67], v[10:11], s[2:3], v[168:169] op_sel_hi:[1,0,1]
	v_pk_fma_f32 v[164:165], v[12:13], s[2:3], v[170:171] op_sel_hi:[1,0,1]
	v_pk_fma_f32 v[166:167], v[14:15], s[2:3], v[172:173] op_sel_hi:[1,0,1]
	v_pk_fma_f32 v[168:169], v[16:17], s[2:3], v[174:175] op_sel_hi:[1,0,1]
	v_pk_fma_f32 v[162:163], v[18:19], s[2:3], v[162:163] op_sel_hi:[1,0,1]
	v_pk_fma_f32 v[160:161], v[20:21], s[2:3], v[160:161] op_sel_hi:[1,0,1]
	v_pk_fma_f32 v[158:159], v[22:23], s[2:3], v[158:159] op_sel_hi:[1,0,1]
	v_pk_fma_f32 v[156:157], v[24:25], s[2:3], v[156:157] op_sel_hi:[1,0,1]
	v_pk_fma_f32 v[154:155], v[26:27], s[2:3], v[154:155] op_sel_hi:[1,0,1]
	v_pk_fma_f32 v[152:153], v[28:29], s[2:3], v[152:153] op_sel_hi:[1,0,1]
	v_pk_fma_f32 v[150:151], v[30:31], s[2:3], v[150:151] op_sel_hi:[1,0,1]
	v_readlane_b32 s2, v211, 6
	s_waitcnt vmcnt(18)
	v_cvt_scalef32_pk32_f32_fp6 v[0:31], v[38:43], 1.0
	v_pk_fma_f32 v[38:39], v[0:1], s[2:3], v[50:51] op_sel_hi:[1,0,1]
	v_pk_fma_f32 v[40:41], v[2:3], s[2:3], v[52:53] op_sel_hi:[1,0,1]
	v_pk_fma_f32 v[42:43], v[4:5], s[2:3], v[54:55] op_sel_hi:[1,0,1]
	v_pk_fma_f32 v[50:51], v[6:7], s[2:3], v[62:63] op_sel_hi:[1,0,1]
	v_pk_fma_f32 v[52:53], v[8:9], s[2:3], v[64:65] op_sel_hi:[1,0,1]
	v_pk_fma_f32 v[54:55], v[10:11], s[2:3], v[66:67] op_sel_hi:[1,0,1]
	v_pk_fma_f32 v[62:63], v[12:13], s[2:3], v[164:165] op_sel_hi:[1,0,1]
	v_pk_fma_f32 v[64:65], v[14:15], s[2:3], v[166:167] op_sel_hi:[1,0,1]
	v_pk_fma_f32 v[66:67], v[16:17], s[2:3], v[168:169] op_sel_hi:[1,0,1]
	v_pk_fma_f32 v[162:163], v[18:19], s[2:3], v[162:163] op_sel_hi:[1,0,1]
	v_pk_fma_f32 v[160:161], v[20:21], s[2:3], v[160:161] op_sel_hi:[1,0,1]
	v_pk_fma_f32 v[158:159], v[22:23], s[2:3], v[158:159] op_sel_hi:[1,0,1]
	v_pk_fma_f32 v[156:157], v[24:25], s[2:3], v[156:157] op_sel_hi:[1,0,1]
	v_pk_fma_f32 v[154:155], v[26:27], s[2:3], v[154:155] op_sel_hi:[1,0,1]
	v_pk_fma_f32 v[152:153], v[28:29], s[2:3], v[152:153] op_sel_hi:[1,0,1]
	v_pk_fma_f32 v[150:151], v[30:31], s[2:3], v[150:151] op_sel_hi:[1,0,1]
	v_readlane_b32 s2, v211, 7
	s_waitcnt vmcnt(16)
	v_cvt_scalef32_pk32_f32_fp6 v[0:31], v[32:37], 1.0
	v_pk_fma_f32 v[164:165], v[0:1], s[2:3], v[38:39] op_sel_hi:[1,0,1]
	v_pk_fma_f32 v[166:167], v[2:3], s[2:3], v[40:41] op_sel_hi:[1,0,1]
	v_pk_fma_f32 v[168:169], v[4:5], s[2:3], v[42:43] op_sel_hi:[1,0,1]
	v_pk_fma_f32 v[170:171], v[6:7], s[2:3], v[50:51] op_sel_hi:[1,0,1]
	v_pk_fma_f32 v[172:173], v[8:9], s[2:3], v[52:53] op_sel_hi:[1,0,1]
	v_pk_fma_f32 v[174:175], v[10:11], s[2:3], v[54:55] op_sel_hi:[1,0,1]
	v_pk_fma_f32 v[176:177], v[12:13], s[2:3], v[62:63] op_sel_hi:[1,0,1]
	v_pk_fma_f32 v[178:179], v[14:15], s[2:3], v[64:65] op_sel_hi:[1,0,1]
	v_pk_fma_f32 v[180:181], v[16:17], s[2:3], v[66:67] op_sel_hi:[1,0,1]
	v_pk_fma_f32 v[162:163], v[18:19], s[2:3], v[162:163] op_sel_hi:[1,0,1]
	v_pk_fma_f32 v[160:161], v[20:21], s[2:3], v[160:161] op_sel_hi:[1,0,1]
	v_pk_fma_f32 v[158:159], v[22:23], s[2:3], v[158:159] op_sel_hi:[1,0,1]
	v_pk_fma_f32 v[156:157], v[24:25], s[2:3], v[156:157] op_sel_hi:[1,0,1]
	v_pk_fma_f32 v[154:155], v[26:27], s[2:3], v[154:155] op_sel_hi:[1,0,1]
	v_pk_fma_f32 v[152:153], v[28:29], s[2:3], v[152:153] op_sel_hi:[1,0,1]
	v_pk_fma_f32 v[150:151], v[30:31], s[2:3], v[150:151] op_sel_hi:[1,0,1]
	v_readlane_b32 s2, v240, 16
	v_readlane_b32 s3, v240, 17
	v_readlane_b32 s100, v240, 18
	v_readlane_b32 s101, v240, 19
	s_nop 1
	buffer_load_dwordx4 v[62:65], v129, s[44:47], s2 offen
	buffer_load_dwordx2 v[66:67], v210, s[44:47], s2 offen
	buffer_load_dwordx4 v[50:53], v129, s[44:47], s3 offen
	buffer_load_dwordx2 v[54:55], v210, s[44:47], s3 offen
	buffer_load_dwordx4 v[38:41], v129, s[44:47], s100 offen
	buffer_load_dwordx2 v[42:43], v210, s[44:47], s100 offen
	buffer_load_dwordx4 v[32:35], v129, s[44:47], s101 offen
	buffer_load_dwordx2 v[36:37], v210, s[44:47], s101 offen
	v_readlane_b32 s2, v211, 8
	s_waitcnt vmcnt(22)
	v_cvt_scalef32_pk32_f32_fp6 v[0:31], v[98:103], 1.0
	v_pk_fma_f32 v[98:99], v[0:1], s[2:3], v[164:165] op_sel_hi:[1,0,1]
	v_pk_fma_f32 v[100:101], v[2:3], s[2:3], v[166:167] op_sel_hi:[1,0,1]
	v_pk_fma_f32 v[102:103], v[4:5], s[2:3], v[168:169] op_sel_hi:[1,0,1]
	v_pk_fma_f32 v[164:165], v[6:7], s[2:3], v[170:171] op_sel_hi:[1,0,1]
	v_pk_fma_f32 v[166:167], v[8:9], s[2:3], v[172:173] op_sel_hi:[1,0,1]
	v_pk_fma_f32 v[168:169], v[10:11], s[2:3], v[174:175] op_sel_hi:[1,0,1]
	v_pk_fma_f32 v[170:171], v[12:13], s[2:3], v[176:177] op_sel_hi:[1,0,1]
	v_pk_fma_f32 v[172:173], v[14:15], s[2:3], v[178:179] op_sel_hi:[1,0,1]
	v_pk_fma_f32 v[174:175], v[16:17], s[2:3], v[180:181] op_sel_hi:[1,0,1]
	v_pk_fma_f32 v[162:163], v[18:19], s[2:3], v[162:163] op_sel_hi:[1,0,1]
	v_pk_fma_f32 v[160:161], v[20:21], s[2:3], v[160:161] op_sel_hi:[1,0,1]
	v_pk_fma_f32 v[158:159], v[22:23], s[2:3], v[158:159] op_sel_hi:[1,0,1]
	v_pk_fma_f32 v[156:157], v[24:25], s[2:3], v[156:157] op_sel_hi:[1,0,1]
	v_pk_fma_f32 v[154:155], v[26:27], s[2:3], v[154:155] op_sel_hi:[1,0,1]
	v_pk_fma_f32 v[152:153], v[28:29], s[2:3], v[152:153] op_sel_hi:[1,0,1]
	v_pk_fma_f32 v[150:151], v[30:31], s[2:3], v[150:151] op_sel_hi:[1,0,1]
	v_readlane_b32 s2, v211, 9
	s_waitcnt vmcnt(20)
	v_cvt_scalef32_pk32_f32_fp6 v[0:31], v[92:97], 1.0
	v_pk_fma_f32 v[92:93], v[0:1], s[2:3], v[98:99] op_sel_hi:[1,0,1]
	v_pk_fma_f32 v[94:95], v[2:3], s[2:3], v[100:101] op_sel_hi:[1,0,1]
	v_pk_fma_f32 v[96:97], v[4:5], s[2:3], v[102:103] op_sel_hi:[1,0,1]
	v_pk_fma_f32 v[98:99], v[6:7], s[2:3], v[164:165] op_sel_hi:[1,0,1]
	v_pk_fma_f32 v[100:101], v[8:9], s[2:3], v[166:167] op_sel_hi:[1,0,1]
	v_pk_fma_f32 v[102:103], v[10:11], s[2:3], v[168:169] op_sel_hi:[1,0,1]
	v_pk_fma_f32 v[164:165], v[12:13], s[2:3], v[170:171] op_sel_hi:[1,0,1]
	v_pk_fma_f32 v[166:167], v[14:15], s[2:3], v[172:173] op_sel_hi:[1,0,1]
	v_pk_fma_f32 v[168:169], v[16:17], s[2:3], v[174:175] op_sel_hi:[1,0,1]
	v_pk_fma_f32 v[162:163], v[18:19], s[2:3], v[162:163] op_sel_hi:[1,0,1]
	v_pk_fma_f32 v[160:161], v[20:21], s[2:3], v[160:161] op_sel_hi:[1,0,1]
	v_pk_fma_f32 v[158:159], v[22:23], s[2:3], v[158:159] op_sel_hi:[1,0,1]
	v_pk_fma_f32 v[156:157], v[24:25], s[2:3], v[156:157] op_sel_hi:[1,0,1]
	v_pk_fma_f32 v[154:155], v[26:27], s[2:3], v[154:155] op_sel_hi:[1,0,1]
	v_pk_fma_f32 v[152:153], v[28:29], s[2:3], v[152:153] op_sel_hi:[1,0,1]
	v_pk_fma_f32 v[150:151], v[30:31], s[2:3], v[150:151] op_sel_hi:[1,0,1]
	v_readlane_b32 s2, v211, 10
	s_waitcnt vmcnt(18)
	v_cvt_scalef32_pk32_f32_fp6 v[0:31], v[86:91], 1.0
	v_pk_fma_f32 v[86:87], v[0:1], s[2:3], v[92:93] op_sel_hi:[1,0,1]
	v_pk_fma_f32 v[88:89], v[2:3], s[2:3], v[94:95] op_sel_hi:[1,0,1]
	v_pk_fma_f32 v[90:91], v[4:5], s[2:3], v[96:97] op_sel_hi:[1,0,1]
	v_pk_fma_f32 v[92:93], v[6:7], s[2:3], v[98:99] op_sel_hi:[1,0,1]
	v_pk_fma_f32 v[94:95], v[8:9], s[2:3], v[100:101] op_sel_hi:[1,0,1]
	v_pk_fma_f32 v[96:97], v[10:11], s[2:3], v[102:103] op_sel_hi:[1,0,1]
	v_pk_fma_f32 v[98:99], v[12:13], s[2:3], v[164:165] op_sel_hi:[1,0,1]
	v_pk_fma_f32 v[100:101], v[14:15], s[2:3], v[166:167] op_sel_hi:[1,0,1]
	v_pk_fma_f32 v[102:103], v[16:17], s[2:3], v[168:169] op_sel_hi:[1,0,1]
	v_pk_fma_f32 v[162:163], v[18:19], s[2:3], v[162:163] op_sel_hi:[1,0,1]
	v_pk_fma_f32 v[160:161], v[20:21], s[2:3], v[160:161] op_sel_hi:[1,0,1]
	v_pk_fma_f32 v[158:159], v[22:23], s[2:3], v[158:159] op_sel_hi:[1,0,1]
	v_pk_fma_f32 v[156:157], v[24:25], s[2:3], v[156:157] op_sel_hi:[1,0,1]
	v_pk_fma_f32 v[154:155], v[26:27], s[2:3], v[154:155] op_sel_hi:[1,0,1]
	v_pk_fma_f32 v[152:153], v[28:29], s[2:3], v[152:153] op_sel_hi:[1,0,1]
	v_pk_fma_f32 v[150:151], v[30:31], s[2:3], v[150:151] op_sel_hi:[1,0,1]
	v_readlane_b32 s2, v211, 11
	s_waitcnt vmcnt(16)
	v_cvt_scalef32_pk32_f32_fp6 v[0:31], v[80:85], 1.0
	v_pk_fma_f32 v[180:181], v[0:1], s[2:3], v[86:87] op_sel_hi:[1,0,1]
	v_pk_fma_f32 v[178:179], v[2:3], s[2:3], v[88:89] op_sel_hi:[1,0,1]
	v_pk_fma_f32 v[176:177], v[4:5], s[2:3], v[90:91] op_sel_hi:[1,0,1]
	v_pk_fma_f32 v[174:175], v[6:7], s[2:3], v[92:93] op_sel_hi:[1,0,1]
	v_pk_fma_f32 v[172:173], v[8:9], s[2:3], v[94:95] op_sel_hi:[1,0,1]
	v_pk_fma_f32 v[170:171], v[10:11], s[2:3], v[96:97] op_sel_hi:[1,0,1]
	v_pk_fma_f32 v[168:169], v[12:13], s[2:3], v[98:99] op_sel_hi:[1,0,1]
	v_pk_fma_f32 v[166:167], v[14:15], s[2:3], v[100:101] op_sel_hi:[1,0,1]
	v_pk_fma_f32 v[164:165], v[16:17], s[2:3], v[102:103] op_sel_hi:[1,0,1]
	v_pk_fma_f32 v[162:163], v[18:19], s[2:3], v[162:163] op_sel_hi:[1,0,1]
	v_pk_fma_f32 v[160:161], v[20:21], s[2:3], v[160:161] op_sel_hi:[1,0,1]
	v_pk_fma_f32 v[158:159], v[22:23], s[2:3], v[158:159] op_sel_hi:[1,0,1]
	v_pk_fma_f32 v[156:157], v[24:25], s[2:3], v[156:157] op_sel_hi:[1,0,1]
	v_pk_fma_f32 v[154:155], v[26:27], s[2:3], v[154:155] op_sel_hi:[1,0,1]
	v_pk_fma_f32 v[152:153], v[28:29], s[2:3], v[152:153] op_sel_hi:[1,0,1]
	v_pk_fma_f32 v[150:151], v[30:31], s[2:3], v[150:151] op_sel_hi:[1,0,1]
	v_readlane_b32 s2, v240, 20
	v_readlane_b32 s3, v240, 21
	v_readlane_b32 s100, v240, 22
	v_readlane_b32 s101, v240, 23
	s_nop 1
	buffer_load_dwordx4 v[98:101], v129, s[44:47], s2 offen
	buffer_load_dwordx2 v[102:103], v210, s[44:47], s2 offen
	buffer_load_dwordx4 v[92:95], v129, s[44:47], s3 offen
	buffer_load_dwordx2 v[96:97], v210, s[44:47], s3 offen
	buffer_load_dwordx4 v[86:89], v129, s[44:47], s100 offen
	buffer_load_dwordx2 v[90:91], v210, s[44:47], s100 offen
	buffer_load_dwordx4 v[80:83], v129, s[44:47], s101 offen
	buffer_load_dwordx2 v[84:85], v210, s[44:47], s101 offen
	v_readlane_b32 s2, v211, 12
	s_waitcnt vmcnt(22)
	v_cvt_scalef32_pk32_f32_fp6 v[0:31], v[74:79], 1.0
	v_pk_fma_f32 v[74:75], v[0:1], s[2:3], v[180:181] op_sel_hi:[1,0,1]
	v_pk_fma_f32 v[76:77], v[2:3], s[2:3], v[178:179] op_sel_hi:[1,0,1]
	v_pk_fma_f32 v[78:79], v[4:5], s[2:3], v[176:177] op_sel_hi:[1,0,1]
	v_pk_fma_f32 v[174:175], v[6:7], s[2:3], v[174:175] op_sel_hi:[1,0,1]
	v_pk_fma_f32 v[172:173], v[8:9], s[2:3], v[172:173] op_sel_hi:[1,0,1]
	v_pk_fma_f32 v[170:171], v[10:11], s[2:3], v[170:171] op_sel_hi:[1,0,1]
	v_pk_fma_f32 v[168:169], v[12:13], s[2:3], v[168:169] op_sel_hi:[1,0,1]
	v_pk_fma_f32 v[166:167], v[14:15], s[2:3], v[166:167] op_sel_hi:[1,0,1]
	v_pk_fma_f32 v[164:165], v[16:17], s[2:3], v[164:165] op_sel_hi:[1,0,1]
	v_pk_fma_f32 v[162:163], v[18:19], s[2:3], v[162:163] op_sel_hi:[1,0,1]
	v_pk_fma_f32 v[160:161], v[20:21], s[2:3], v[160:161] op_sel_hi:[1,0,1]
	v_pk_fma_f32 v[158:159], v[22:23], s[2:3], v[158:159] op_sel_hi:[1,0,1]
	v_pk_fma_f32 v[156:157], v[24:25], s[2:3], v[156:157] op_sel_hi:[1,0,1]
	v_pk_fma_f32 v[154:155], v[26:27], s[2:3], v[154:155] op_sel_hi:[1,0,1]
	v_pk_fma_f32 v[152:153], v[28:29], s[2:3], v[152:153] op_sel_hi:[1,0,1]
	v_pk_fma_f32 v[150:151], v[30:31], s[2:3], v[150:151] op_sel_hi:[1,0,1]
	v_readlane_b32 s2, v211, 13
	s_waitcnt vmcnt(20)
	v_cvt_scalef32_pk32_f32_fp6 v[0:31], v[68:73], 1.0
	v_pk_fma_f32 v[68:69], v[0:1], s[2:3], v[74:75] op_sel_hi:[1,0,1]
	v_pk_fma_f32 v[70:71], v[2:3], s[2:3], v[76:77] op_sel_hi:[1,0,1]
	v_pk_fma_f32 v[72:73], v[4:5], s[2:3], v[78:79] op_sel_hi:[1,0,1]
	v_pk_fma_f32 v[74:75], v[6:7], s[2:3], v[174:175] op_sel_hi:[1,0,1]
	v_pk_fma_f32 v[76:77], v[8:9], s[2:3], v[172:173] op_sel_hi:[1,0,1]
	v_pk_fma_f32 v[78:79], v[10:11], s[2:3], v[170:171] op_sel_hi:[1,0,1]
	v_pk_fma_f32 v[168:169], v[12:13], s[2:3], v[168:169] op_sel_hi:[1,0,1]
	v_pk_fma_f32 v[166:167], v[14:15], s[2:3], v[166:167] op_sel_hi:[1,0,1]
	v_pk_fma_f32 v[164:165], v[16:17], s[2:3], v[164:165] op_sel_hi:[1,0,1]
	v_pk_fma_f32 v[162:163], v[18:19], s[2:3], v[162:163] op_sel_hi:[1,0,1]
	v_pk_fma_f32 v[160:161], v[20:21], s[2:3], v[160:161] op_sel_hi:[1,0,1]
	v_pk_fma_f32 v[158:159], v[22:23], s[2:3], v[158:159] op_sel_hi:[1,0,1]
	v_pk_fma_f32 v[156:157], v[24:25], s[2:3], v[156:157] op_sel_hi:[1,0,1]
	v_pk_fma_f32 v[154:155], v[26:27], s[2:3], v[154:155] op_sel_hi:[1,0,1]
	v_pk_fma_f32 v[152:153], v[28:29], s[2:3], v[152:153] op_sel_hi:[1,0,1]
	v_pk_fma_f32 v[150:151], v[30:31], s[2:3], v[150:151] op_sel_hi:[1,0,1]
	v_readlane_b32 s2, v211, 14
	s_waitcnt vmcnt(18)
	v_cvt_scalef32_pk32_f32_fp6 v[0:31], v[56:61], 1.0
	v_pk_fma_f32 v[56:57], v[0:1], s[2:3], v[68:69] op_sel_hi:[1,0,1]
	v_pk_fma_f32 v[58:59], v[2:3], s[2:3], v[70:71] op_sel_hi:[1,0,1]
	v_pk_fma_f32 v[60:61], v[4:5], s[2:3], v[72:73] op_sel_hi:[1,0,1]
	v_pk_fma_f32 v[68:69], v[6:7], s[2:3], v[74:75] op_sel_hi:[1,0,1]
	v_pk_fma_f32 v[70:71], v[8:9], s[2:3], v[76:77] op_sel_hi:[1,0,1]
	v_pk_fma_f32 v[72:73], v[10:11], s[2:3], v[78:79] op_sel_hi:[1,0,1]
	v_pk_fma_f32 v[74:75], v[12:13], s[2:3], v[168:169] op_sel_hi:[1,0,1]
	v_pk_fma_f32 v[76:77], v[14:15], s[2:3], v[166:167] op_sel_hi:[1,0,1]
	v_pk_fma_f32 v[78:79], v[16:17], s[2:3], v[164:165] op_sel_hi:[1,0,1]
	v_pk_fma_f32 v[162:163], v[18:19], s[2:3], v[162:163] op_sel_hi:[1,0,1]
	v_pk_fma_f32 v[160:161], v[20:21], s[2:3], v[160:161] op_sel_hi:[1,0,1]
	v_pk_fma_f32 v[158:159], v[22:23], s[2:3], v[158:159] op_sel_hi:[1,0,1]
	v_pk_fma_f32 v[156:157], v[24:25], s[2:3], v[156:157] op_sel_hi:[1,0,1]
	v_pk_fma_f32 v[154:155], v[26:27], s[2:3], v[154:155] op_sel_hi:[1,0,1]
	v_pk_fma_f32 v[152:153], v[28:29], s[2:3], v[152:153] op_sel_hi:[1,0,1]
	v_pk_fma_f32 v[150:151], v[30:31], s[2:3], v[150:151] op_sel_hi:[1,0,1]
	v_readlane_b32 s2, v211, 15
	s_waitcnt vmcnt(16)
	v_cvt_scalef32_pk32_f32_fp6 v[0:31], v[44:49], 1.0
	v_pk_fma_f32 v[164:165], v[0:1], s[2:3], v[56:57] op_sel_hi:[1,0,1]
	v_pk_fma_f32 v[166:167], v[2:3], s[2:3], v[58:59] op_sel_hi:[1,0,1]
	v_pk_fma_f32 v[168:169], v[4:5], s[2:3], v[60:61] op_sel_hi:[1,0,1]
	v_pk_fma_f32 v[170:171], v[6:7], s[2:3], v[68:69] op_sel_hi:[1,0,1]
	v_pk_fma_f32 v[172:173], v[8:9], s[2:3], v[70:71] op_sel_hi:[1,0,1]
	v_pk_fma_f32 v[174:175], v[10:11], s[2:3], v[72:73] op_sel_hi:[1,0,1]
	v_pk_fma_f32 v[176:177], v[12:13], s[2:3], v[74:75] op_sel_hi:[1,0,1]
	v_pk_fma_f32 v[178:179], v[14:15], s[2:3], v[76:77] op_sel_hi:[1,0,1]
	v_pk_fma_f32 v[180:181], v[16:17], s[2:3], v[78:79] op_sel_hi:[1,0,1]
	v_pk_fma_f32 v[162:163], v[18:19], s[2:3], v[162:163] op_sel_hi:[1,0,1]
	v_pk_fma_f32 v[160:161], v[20:21], s[2:3], v[160:161] op_sel_hi:[1,0,1]
	v_pk_fma_f32 v[158:159], v[22:23], s[2:3], v[158:159] op_sel_hi:[1,0,1]
	v_pk_fma_f32 v[156:157], v[24:25], s[2:3], v[156:157] op_sel_hi:[1,0,1]
	v_pk_fma_f32 v[154:155], v[26:27], s[2:3], v[154:155] op_sel_hi:[1,0,1]
	v_pk_fma_f32 v[152:153], v[28:29], s[2:3], v[152:153] op_sel_hi:[1,0,1]
	v_pk_fma_f32 v[150:151], v[30:31], s[2:3], v[150:151] op_sel_hi:[1,0,1]
	v_readlane_b32 s2, v240, 24
	v_readlane_b32 s3, v240, 25
	v_readlane_b32 s100, v240, 26
	v_readlane_b32 s101, v240, 27
	s_nop 1
	buffer_load_dwordx4 v[74:77], v129, s[44:47], s2 offen
	buffer_load_dwordx2 v[78:79], v210, s[44:47], s2 offen
	buffer_load_dwordx4 v[68:71], v129, s[44:47], s3 offen
	buffer_load_dwordx2 v[72:73], v210, s[44:47], s3 offen
	buffer_load_dwordx4 v[56:59], v129, s[44:47], s100 offen
	buffer_load_dwordx2 v[60:61], v210, s[44:47], s100 offen
	buffer_load_dwordx4 v[44:47], v129, s[44:47], s101 offen
	buffer_load_dwordx2 v[48:49], v210, s[44:47], s101 offen
	v_readlane_b32 s2, v211, 16
	s_waitcnt vmcnt(22)
	v_cvt_scalef32_pk32_f32_fp6 v[0:31], v[62:67], 1.0
	v_pk_fma_f32 v[62:63], v[0:1], s[2:3], v[164:165] op_sel_hi:[1,0,1]
	v_pk_fma_f32 v[64:65], v[2:3], s[2:3], v[166:167] op_sel_hi:[1,0,1]
	v_pk_fma_f32 v[66:67], v[4:5], s[2:3], v[168:169] op_sel_hi:[1,0,1]
	v_pk_fma_f32 v[164:165], v[6:7], s[2:3], v[170:171] op_sel_hi:[1,0,1]
	v_pk_fma_f32 v[166:167], v[8:9], s[2:3], v[172:173] op_sel_hi:[1,0,1]
	v_pk_fma_f32 v[168:169], v[10:11], s[2:3], v[174:175] op_sel_hi:[1,0,1]
	v_pk_fma_f32 v[170:171], v[12:13], s[2:3], v[176:177] op_sel_hi:[1,0,1]
	v_pk_fma_f32 v[172:173], v[14:15], s[2:3], v[178:179] op_sel_hi:[1,0,1]
	v_pk_fma_f32 v[174:175], v[16:17], s[2:3], v[180:181] op_sel_hi:[1,0,1]
	v_pk_fma_f32 v[162:163], v[18:19], s[2:3], v[162:163] op_sel_hi:[1,0,1]
	v_pk_fma_f32 v[160:161], v[20:21], s[2:3], v[160:161] op_sel_hi:[1,0,1]
	v_pk_fma_f32 v[158:159], v[22:23], s[2:3], v[158:159] op_sel_hi:[1,0,1]
	v_pk_fma_f32 v[156:157], v[24:25], s[2:3], v[156:157] op_sel_hi:[1,0,1]
	v_pk_fma_f32 v[154:155], v[26:27], s[2:3], v[154:155] op_sel_hi:[1,0,1]
	v_pk_fma_f32 v[152:153], v[28:29], s[2:3], v[152:153] op_sel_hi:[1,0,1]
	v_pk_fma_f32 v[150:151], v[30:31], s[2:3], v[150:151] op_sel_hi:[1,0,1]
	v_readlane_b32 s2, v211, 17
	s_waitcnt vmcnt(20)
	v_cvt_scalef32_pk32_f32_fp6 v[0:31], v[50:55], 1.0
	v_pk_fma_f32 v[50:51], v[0:1], s[2:3], v[62:63] op_sel_hi:[1,0,1]
	v_pk_fma_f32 v[52:53], v[2:3], s[2:3], v[64:65] op_sel_hi:[1,0,1]
	v_pk_fma_f32 v[54:55], v[4:5], s[2:3], v[66:67] op_sel_hi:[1,0,1]
	v_pk_fma_f32 v[62:63], v[6:7], s[2:3], v[164:165] op_sel_hi:[1,0,1]
	v_pk_fma_f32 v[64:65], v[8:9], s[2:3], v[166:167] op_sel_hi:[1,0,1]
	v_pk_fma_f32 v[66:67], v[10:11], s[2:3], v[168:169] op_sel_hi:[1,0,1]
	v_pk_fma_f32 v[164:165], v[12:13], s[2:3], v[170:171] op_sel_hi:[1,0,1]
	v_pk_fma_f32 v[166:167], v[14:15], s[2:3], v[172:173] op_sel_hi:[1,0,1]
	v_pk_fma_f32 v[168:169], v[16:17], s[2:3], v[174:175] op_sel_hi:[1,0,1]
	v_pk_fma_f32 v[162:163], v[18:19], s[2:3], v[162:163] op_sel_hi:[1,0,1]
	v_pk_fma_f32 v[160:161], v[20:21], s[2:3], v[160:161] op_sel_hi:[1,0,1]
	v_pk_fma_f32 v[158:159], v[22:23], s[2:3], v[158:159] op_sel_hi:[1,0,1]
	v_pk_fma_f32 v[156:157], v[24:25], s[2:3], v[156:157] op_sel_hi:[1,0,1]
	v_pk_fma_f32 v[154:155], v[26:27], s[2:3], v[154:155] op_sel_hi:[1,0,1]
	v_pk_fma_f32 v[152:153], v[28:29], s[2:3], v[152:153] op_sel_hi:[1,0,1]
	v_pk_fma_f32 v[150:151], v[30:31], s[2:3], v[150:151] op_sel_hi:[1,0,1]
	v_readlane_b32 s2, v211, 18
	s_waitcnt vmcnt(18)
	v_cvt_scalef32_pk32_f32_fp6 v[0:31], v[38:43], 1.0
	v_pk_fma_f32 v[38:39], v[0:1], s[2:3], v[50:51] op_sel_hi:[1,0,1]
	v_pk_fma_f32 v[40:41], v[2:3], s[2:3], v[52:53] op_sel_hi:[1,0,1]
	v_pk_fma_f32 v[42:43], v[4:5], s[2:3], v[54:55] op_sel_hi:[1,0,1]
	v_pk_fma_f32 v[50:51], v[6:7], s[2:3], v[62:63] op_sel_hi:[1,0,1]
	v_pk_fma_f32 v[52:53], v[8:9], s[2:3], v[64:65] op_sel_hi:[1,0,1]
	v_pk_fma_f32 v[54:55], v[10:11], s[2:3], v[66:67] op_sel_hi:[1,0,1]
	v_pk_fma_f32 v[62:63], v[12:13], s[2:3], v[164:165] op_sel_hi:[1,0,1]
	v_pk_fma_f32 v[64:65], v[14:15], s[2:3], v[166:167] op_sel_hi:[1,0,1]
	v_pk_fma_f32 v[66:67], v[16:17], s[2:3], v[168:169] op_sel_hi:[1,0,1]
	v_pk_fma_f32 v[162:163], v[18:19], s[2:3], v[162:163] op_sel_hi:[1,0,1]
	v_pk_fma_f32 v[160:161], v[20:21], s[2:3], v[160:161] op_sel_hi:[1,0,1]
	v_pk_fma_f32 v[158:159], v[22:23], s[2:3], v[158:159] op_sel_hi:[1,0,1]
	v_pk_fma_f32 v[156:157], v[24:25], s[2:3], v[156:157] op_sel_hi:[1,0,1]
	v_pk_fma_f32 v[154:155], v[26:27], s[2:3], v[154:155] op_sel_hi:[1,0,1]
	v_pk_fma_f32 v[152:153], v[28:29], s[2:3], v[152:153] op_sel_hi:[1,0,1]
	v_pk_fma_f32 v[150:151], v[30:31], s[2:3], v[150:151] op_sel_hi:[1,0,1]
	v_readlane_b32 s2, v211, 19
	s_waitcnt vmcnt(16)
	v_cvt_scalef32_pk32_f32_fp6 v[0:31], v[32:37], 1.0
	v_pk_fma_f32 v[164:165], v[0:1], s[2:3], v[38:39] op_sel_hi:[1,0,1]
	v_pk_fma_f32 v[166:167], v[2:3], s[2:3], v[40:41] op_sel_hi:[1,0,1]
	v_pk_fma_f32 v[168:169], v[4:5], s[2:3], v[42:43] op_sel_hi:[1,0,1]
	v_pk_fma_f32 v[170:171], v[6:7], s[2:3], v[50:51] op_sel_hi:[1,0,1]
	v_pk_fma_f32 v[172:173], v[8:9], s[2:3], v[52:53] op_sel_hi:[1,0,1]
	v_pk_fma_f32 v[174:175], v[10:11], s[2:3], v[54:55] op_sel_hi:[1,0,1]
	v_pk_fma_f32 v[176:177], v[12:13], s[2:3], v[62:63] op_sel_hi:[1,0,1]
	v_pk_fma_f32 v[178:179], v[14:15], s[2:3], v[64:65] op_sel_hi:[1,0,1]
	v_pk_fma_f32 v[180:181], v[16:17], s[2:3], v[66:67] op_sel_hi:[1,0,1]
	v_pk_fma_f32 v[162:163], v[18:19], s[2:3], v[162:163] op_sel_hi:[1,0,1]
	v_pk_fma_f32 v[160:161], v[20:21], s[2:3], v[160:161] op_sel_hi:[1,0,1]
	v_pk_fma_f32 v[158:159], v[22:23], s[2:3], v[158:159] op_sel_hi:[1,0,1]
	v_pk_fma_f32 v[156:157], v[24:25], s[2:3], v[156:157] op_sel_hi:[1,0,1]
	v_pk_fma_f32 v[154:155], v[26:27], s[2:3], v[154:155] op_sel_hi:[1,0,1]
	v_pk_fma_f32 v[152:153], v[28:29], s[2:3], v[152:153] op_sel_hi:[1,0,1]
	v_pk_fma_f32 v[150:151], v[30:31], s[2:3], v[150:151] op_sel_hi:[1,0,1]
	v_readlane_b32 s2, v240, 28
	v_readlane_b32 s3, v240, 29
	v_readlane_b32 s100, v240, 30
	v_readlane_b32 s101, v240, 31
	s_nop 1
	buffer_load_dwordx4 v[62:65], v129, s[44:47], s2 offen
	buffer_load_dwordx2 v[66:67], v210, s[44:47], s2 offen
	buffer_load_dwordx4 v[50:53], v129, s[44:47], s3 offen
	buffer_load_dwordx2 v[54:55], v210, s[44:47], s3 offen
	buffer_load_dwordx4 v[38:41], v129, s[44:47], s100 offen
	buffer_load_dwordx2 v[42:43], v210, s[44:47], s100 offen
	buffer_load_dwordx4 v[32:35], v129, s[44:47], s101 offen
	buffer_load_dwordx2 v[36:37], v210, s[44:47], s101 offen
	v_readlane_b32 s2, v211, 20
	s_waitcnt vmcnt(22)
	v_cvt_scalef32_pk32_f32_fp6 v[0:31], v[98:103], 1.0
	v_pk_fma_f32 v[98:99], v[0:1], s[2:3], v[164:165] op_sel_hi:[1,0,1]
	v_pk_fma_f32 v[100:101], v[2:3], s[2:3], v[166:167] op_sel_hi:[1,0,1]
	v_pk_fma_f32 v[102:103], v[4:5], s[2:3], v[168:169] op_sel_hi:[1,0,1]
	v_pk_fma_f32 v[164:165], v[6:7], s[2:3], v[170:171] op_sel_hi:[1,0,1]
	v_pk_fma_f32 v[166:167], v[8:9], s[2:3], v[172:173] op_sel_hi:[1,0,1]
	v_pk_fma_f32 v[168:169], v[10:11], s[2:3], v[174:175] op_sel_hi:[1,0,1]
	v_pk_fma_f32 v[170:171], v[12:13], s[2:3], v[176:177] op_sel_hi:[1,0,1]
	v_pk_fma_f32 v[172:173], v[14:15], s[2:3], v[178:179] op_sel_hi:[1,0,1]
	v_pk_fma_f32 v[174:175], v[16:17], s[2:3], v[180:181] op_sel_hi:[1,0,1]
	v_pk_fma_f32 v[162:163], v[18:19], s[2:3], v[162:163] op_sel_hi:[1,0,1]
	v_pk_fma_f32 v[160:161], v[20:21], s[2:3], v[160:161] op_sel_hi:[1,0,1]
	v_pk_fma_f32 v[158:159], v[22:23], s[2:3], v[158:159] op_sel_hi:[1,0,1]
	v_pk_fma_f32 v[156:157], v[24:25], s[2:3], v[156:157] op_sel_hi:[1,0,1]
	v_pk_fma_f32 v[154:155], v[26:27], s[2:3], v[154:155] op_sel_hi:[1,0,1]
	v_pk_fma_f32 v[152:153], v[28:29], s[2:3], v[152:153] op_sel_hi:[1,0,1]
	v_pk_fma_f32 v[150:151], v[30:31], s[2:3], v[150:151] op_sel_hi:[1,0,1]
	v_readlane_b32 s2, v211, 21
	s_waitcnt vmcnt(20)
	v_cvt_scalef32_pk32_f32_fp6 v[0:31], v[92:97], 1.0
	v_pk_fma_f32 v[92:93], v[0:1], s[2:3], v[98:99] op_sel_hi:[1,0,1]
	v_pk_fma_f32 v[94:95], v[2:3], s[2:3], v[100:101] op_sel_hi:[1,0,1]
	v_pk_fma_f32 v[96:97], v[4:5], s[2:3], v[102:103] op_sel_hi:[1,0,1]
	v_pk_fma_f32 v[98:99], v[6:7], s[2:3], v[164:165] op_sel_hi:[1,0,1]
	v_pk_fma_f32 v[100:101], v[8:9], s[2:3], v[166:167] op_sel_hi:[1,0,1]
	v_pk_fma_f32 v[102:103], v[10:11], s[2:3], v[168:169] op_sel_hi:[1,0,1]
	v_pk_fma_f32 v[164:165], v[12:13], s[2:3], v[170:171] op_sel_hi:[1,0,1]
	v_pk_fma_f32 v[166:167], v[14:15], s[2:3], v[172:173] op_sel_hi:[1,0,1]
	v_pk_fma_f32 v[168:169], v[16:17], s[2:3], v[174:175] op_sel_hi:[1,0,1]
	v_pk_fma_f32 v[162:163], v[18:19], s[2:3], v[162:163] op_sel_hi:[1,0,1]
	v_pk_fma_f32 v[160:161], v[20:21], s[2:3], v[160:161] op_sel_hi:[1,0,1]
	v_pk_fma_f32 v[158:159], v[22:23], s[2:3], v[158:159] op_sel_hi:[1,0,1]
	v_pk_fma_f32 v[156:157], v[24:25], s[2:3], v[156:157] op_sel_hi:[1,0,1]
	v_pk_fma_f32 v[154:155], v[26:27], s[2:3], v[154:155] op_sel_hi:[1,0,1]
	v_pk_fma_f32 v[152:153], v[28:29], s[2:3], v[152:153] op_sel_hi:[1,0,1]
	v_pk_fma_f32 v[150:151], v[30:31], s[2:3], v[150:151] op_sel_hi:[1,0,1]
	v_readlane_b32 s2, v211, 22
	s_waitcnt vmcnt(18)
	v_cvt_scalef32_pk32_f32_fp6 v[0:31], v[86:91], 1.0
	v_pk_fma_f32 v[86:87], v[0:1], s[2:3], v[92:93] op_sel_hi:[1,0,1]
	v_pk_fma_f32 v[88:89], v[2:3], s[2:3], v[94:95] op_sel_hi:[1,0,1]
	v_pk_fma_f32 v[90:91], v[4:5], s[2:3], v[96:97] op_sel_hi:[1,0,1]
	v_pk_fma_f32 v[92:93], v[6:7], s[2:3], v[98:99] op_sel_hi:[1,0,1]
	v_pk_fma_f32 v[94:95], v[8:9], s[2:3], v[100:101] op_sel_hi:[1,0,1]
	v_pk_fma_f32 v[96:97], v[10:11], s[2:3], v[102:103] op_sel_hi:[1,0,1]
	v_pk_fma_f32 v[98:99], v[12:13], s[2:3], v[164:165] op_sel_hi:[1,0,1]
	v_pk_fma_f32 v[100:101], v[14:15], s[2:3], v[166:167] op_sel_hi:[1,0,1]
	v_pk_fma_f32 v[102:103], v[16:17], s[2:3], v[168:169] op_sel_hi:[1,0,1]
	v_pk_fma_f32 v[162:163], v[18:19], s[2:3], v[162:163] op_sel_hi:[1,0,1]
	v_pk_fma_f32 v[160:161], v[20:21], s[2:3], v[160:161] op_sel_hi:[1,0,1]
	v_pk_fma_f32 v[158:159], v[22:23], s[2:3], v[158:159] op_sel_hi:[1,0,1]
	v_pk_fma_f32 v[156:157], v[24:25], s[2:3], v[156:157] op_sel_hi:[1,0,1]
	v_pk_fma_f32 v[154:155], v[26:27], s[2:3], v[154:155] op_sel_hi:[1,0,1]
	v_pk_fma_f32 v[152:153], v[28:29], s[2:3], v[152:153] op_sel_hi:[1,0,1]
	v_pk_fma_f32 v[150:151], v[30:31], s[2:3], v[150:151] op_sel_hi:[1,0,1]
	v_readlane_b32 s2, v211, 23
	s_waitcnt vmcnt(16)
	v_cvt_scalef32_pk32_f32_fp6 v[0:31], v[80:85], 1.0
	v_pk_fma_f32 v[180:181], v[0:1], s[2:3], v[86:87] op_sel_hi:[1,0,1]
	v_pk_fma_f32 v[178:179], v[2:3], s[2:3], v[88:89] op_sel_hi:[1,0,1]
	v_pk_fma_f32 v[176:177], v[4:5], s[2:3], v[90:91] op_sel_hi:[1,0,1]
	v_pk_fma_f32 v[174:175], v[6:7], s[2:3], v[92:93] op_sel_hi:[1,0,1]
	v_pk_fma_f32 v[172:173], v[8:9], s[2:3], v[94:95] op_sel_hi:[1,0,1]
	v_pk_fma_f32 v[170:171], v[10:11], s[2:3], v[96:97] op_sel_hi:[1,0,1]
	v_pk_fma_f32 v[168:169], v[12:13], s[2:3], v[98:99] op_sel_hi:[1,0,1]
	v_pk_fma_f32 v[166:167], v[14:15], s[2:3], v[100:101] op_sel_hi:[1,0,1]
	v_pk_fma_f32 v[164:165], v[16:17], s[2:3], v[102:103] op_sel_hi:[1,0,1]
	v_pk_fma_f32 v[162:163], v[18:19], s[2:3], v[162:163] op_sel_hi:[1,0,1]
	v_pk_fma_f32 v[160:161], v[20:21], s[2:3], v[160:161] op_sel_hi:[1,0,1]
	v_pk_fma_f32 v[158:159], v[22:23], s[2:3], v[158:159] op_sel_hi:[1,0,1]
	v_pk_fma_f32 v[156:157], v[24:25], s[2:3], v[156:157] op_sel_hi:[1,0,1]
	v_pk_fma_f32 v[154:155], v[26:27], s[2:3], v[154:155] op_sel_hi:[1,0,1]
	v_pk_fma_f32 v[152:153], v[28:29], s[2:3], v[152:153] op_sel_hi:[1,0,1]
	v_pk_fma_f32 v[150:151], v[30:31], s[2:3], v[150:151] op_sel_hi:[1,0,1]
	v_readlane_b32 s2, v240, 32
	v_readlane_b32 s3, v240, 33
	v_readlane_b32 s100, v240, 34
	v_readlane_b32 s101, v240, 35
	s_nop 1
	buffer_load_dwordx4 v[98:101], v129, s[44:47], s2 offen
	buffer_load_dwordx2 v[102:103], v210, s[44:47], s2 offen
	buffer_load_dwordx4 v[92:95], v129, s[44:47], s3 offen
	buffer_load_dwordx2 v[96:97], v210, s[44:47], s3 offen
	buffer_load_dwordx4 v[86:89], v129, s[44:47], s100 offen
	buffer_load_dwordx2 v[90:91], v210, s[44:47], s100 offen
	buffer_load_dwordx4 v[80:83], v129, s[44:47], s101 offen
	buffer_load_dwordx2 v[84:85], v210, s[44:47], s101 offen
	v_readlane_b32 s2, v211, 24
	s_waitcnt vmcnt(22)
	v_cvt_scalef32_pk32_f32_fp6 v[0:31], v[74:79], 1.0
	v_pk_fma_f32 v[74:75], v[0:1], s[2:3], v[180:181] op_sel_hi:[1,0,1]
	v_pk_fma_f32 v[76:77], v[2:3], s[2:3], v[178:179] op_sel_hi:[1,0,1]
	v_pk_fma_f32 v[78:79], v[4:5], s[2:3], v[176:177] op_sel_hi:[1,0,1]
	v_pk_fma_f32 v[174:175], v[6:7], s[2:3], v[174:175] op_sel_hi:[1,0,1]
	v_pk_fma_f32 v[172:173], v[8:9], s[2:3], v[172:173] op_sel_hi:[1,0,1]
	v_pk_fma_f32 v[170:171], v[10:11], s[2:3], v[170:171] op_sel_hi:[1,0,1]
	v_pk_fma_f32 v[168:169], v[12:13], s[2:3], v[168:169] op_sel_hi:[1,0,1]
	v_pk_fma_f32 v[166:167], v[14:15], s[2:3], v[166:167] op_sel_hi:[1,0,1]
	v_pk_fma_f32 v[164:165], v[16:17], s[2:3], v[164:165] op_sel_hi:[1,0,1]
	v_pk_fma_f32 v[162:163], v[18:19], s[2:3], v[162:163] op_sel_hi:[1,0,1]
	v_pk_fma_f32 v[160:161], v[20:21], s[2:3], v[160:161] op_sel_hi:[1,0,1]
	v_pk_fma_f32 v[158:159], v[22:23], s[2:3], v[158:159] op_sel_hi:[1,0,1]
	v_pk_fma_f32 v[156:157], v[24:25], s[2:3], v[156:157] op_sel_hi:[1,0,1]
	v_pk_fma_f32 v[154:155], v[26:27], s[2:3], v[154:155] op_sel_hi:[1,0,1]
	v_pk_fma_f32 v[152:153], v[28:29], s[2:3], v[152:153] op_sel_hi:[1,0,1]
	v_pk_fma_f32 v[150:151], v[30:31], s[2:3], v[150:151] op_sel_hi:[1,0,1]
	v_readlane_b32 s2, v211, 25
	s_waitcnt vmcnt(20)
	v_cvt_scalef32_pk32_f32_fp6 v[0:31], v[68:73], 1.0
	v_pk_fma_f32 v[68:69], v[0:1], s[2:3], v[74:75] op_sel_hi:[1,0,1]
	v_pk_fma_f32 v[70:71], v[2:3], s[2:3], v[76:77] op_sel_hi:[1,0,1]
	v_pk_fma_f32 v[72:73], v[4:5], s[2:3], v[78:79] op_sel_hi:[1,0,1]
	v_pk_fma_f32 v[74:75], v[6:7], s[2:3], v[174:175] op_sel_hi:[1,0,1]
	v_pk_fma_f32 v[76:77], v[8:9], s[2:3], v[172:173] op_sel_hi:[1,0,1]
	v_pk_fma_f32 v[78:79], v[10:11], s[2:3], v[170:171] op_sel_hi:[1,0,1]
	v_pk_fma_f32 v[168:169], v[12:13], s[2:3], v[168:169] op_sel_hi:[1,0,1]
	v_pk_fma_f32 v[166:167], v[14:15], s[2:3], v[166:167] op_sel_hi:[1,0,1]
	v_pk_fma_f32 v[164:165], v[16:17], s[2:3], v[164:165] op_sel_hi:[1,0,1]
	v_pk_fma_f32 v[162:163], v[18:19], s[2:3], v[162:163] op_sel_hi:[1,0,1]
	v_pk_fma_f32 v[160:161], v[20:21], s[2:3], v[160:161] op_sel_hi:[1,0,1]
	v_pk_fma_f32 v[158:159], v[22:23], s[2:3], v[158:159] op_sel_hi:[1,0,1]
	v_pk_fma_f32 v[156:157], v[24:25], s[2:3], v[156:157] op_sel_hi:[1,0,1]
	v_pk_fma_f32 v[154:155], v[26:27], s[2:3], v[154:155] op_sel_hi:[1,0,1]
	v_pk_fma_f32 v[152:153], v[28:29], s[2:3], v[152:153] op_sel_hi:[1,0,1]
	v_pk_fma_f32 v[150:151], v[30:31], s[2:3], v[150:151] op_sel_hi:[1,0,1]
	v_readlane_b32 s2, v211, 26
	s_waitcnt vmcnt(18)
	v_cvt_scalef32_pk32_f32_fp6 v[0:31], v[56:61], 1.0
	v_pk_fma_f32 v[56:57], v[0:1], s[2:3], v[68:69] op_sel_hi:[1,0,1]
	v_pk_fma_f32 v[58:59], v[2:3], s[2:3], v[70:71] op_sel_hi:[1,0,1]
	v_pk_fma_f32 v[60:61], v[4:5], s[2:3], v[72:73] op_sel_hi:[1,0,1]
	v_pk_fma_f32 v[68:69], v[6:7], s[2:3], v[74:75] op_sel_hi:[1,0,1]
	v_pk_fma_f32 v[70:71], v[8:9], s[2:3], v[76:77] op_sel_hi:[1,0,1]
	v_pk_fma_f32 v[72:73], v[10:11], s[2:3], v[78:79] op_sel_hi:[1,0,1]
	v_pk_fma_f32 v[74:75], v[12:13], s[2:3], v[168:169] op_sel_hi:[1,0,1]
	v_pk_fma_f32 v[76:77], v[14:15], s[2:3], v[166:167] op_sel_hi:[1,0,1]
	v_pk_fma_f32 v[78:79], v[16:17], s[2:3], v[164:165] op_sel_hi:[1,0,1]
	v_pk_fma_f32 v[162:163], v[18:19], s[2:3], v[162:163] op_sel_hi:[1,0,1]
	v_pk_fma_f32 v[160:161], v[20:21], s[2:3], v[160:161] op_sel_hi:[1,0,1]
	v_pk_fma_f32 v[158:159], v[22:23], s[2:3], v[158:159] op_sel_hi:[1,0,1]
	v_pk_fma_f32 v[156:157], v[24:25], s[2:3], v[156:157] op_sel_hi:[1,0,1]
	v_pk_fma_f32 v[154:155], v[26:27], s[2:3], v[154:155] op_sel_hi:[1,0,1]
	v_pk_fma_f32 v[152:153], v[28:29], s[2:3], v[152:153] op_sel_hi:[1,0,1]
	v_pk_fma_f32 v[150:151], v[30:31], s[2:3], v[150:151] op_sel_hi:[1,0,1]
	v_readlane_b32 s2, v211, 27
	s_waitcnt vmcnt(16)
	v_cvt_scalef32_pk32_f32_fp6 v[0:31], v[44:49], 1.0
	v_pk_fma_f32 v[164:165], v[0:1], s[2:3], v[56:57] op_sel_hi:[1,0,1]
	v_pk_fma_f32 v[166:167], v[2:3], s[2:3], v[58:59] op_sel_hi:[1,0,1]
	v_pk_fma_f32 v[168:169], v[4:5], s[2:3], v[60:61] op_sel_hi:[1,0,1]
	v_pk_fma_f32 v[170:171], v[6:7], s[2:3], v[68:69] op_sel_hi:[1,0,1]
	v_pk_fma_f32 v[172:173], v[8:9], s[2:3], v[70:71] op_sel_hi:[1,0,1]
	v_pk_fma_f32 v[174:175], v[10:11], s[2:3], v[72:73] op_sel_hi:[1,0,1]
	v_pk_fma_f32 v[176:177], v[12:13], s[2:3], v[74:75] op_sel_hi:[1,0,1]
	v_pk_fma_f32 v[178:179], v[14:15], s[2:3], v[76:77] op_sel_hi:[1,0,1]
	v_pk_fma_f32 v[180:181], v[16:17], s[2:3], v[78:79] op_sel_hi:[1,0,1]
	v_pk_fma_f32 v[162:163], v[18:19], s[2:3], v[162:163] op_sel_hi:[1,0,1]
	v_pk_fma_f32 v[160:161], v[20:21], s[2:3], v[160:161] op_sel_hi:[1,0,1]
	v_pk_fma_f32 v[158:159], v[22:23], s[2:3], v[158:159] op_sel_hi:[1,0,1]
	v_pk_fma_f32 v[156:157], v[24:25], s[2:3], v[156:157] op_sel_hi:[1,0,1]
	v_pk_fma_f32 v[154:155], v[26:27], s[2:3], v[154:155] op_sel_hi:[1,0,1]
	v_pk_fma_f32 v[152:153], v[28:29], s[2:3], v[152:153] op_sel_hi:[1,0,1]
	v_pk_fma_f32 v[150:151], v[30:31], s[2:3], v[150:151] op_sel_hi:[1,0,1]
	v_readlane_b32 s2, v240, 36
	v_readlane_b32 s3, v240, 37
	v_readlane_b32 s100, v240, 38
	v_readlane_b32 s101, v240, 39
	s_nop 1
	buffer_load_dwordx4 v[74:77], v129, s[44:47], s2 offen
	buffer_load_dwordx2 v[78:79], v210, s[44:47], s2 offen
	buffer_load_dwordx4 v[68:71], v129, s[44:47], s3 offen
	buffer_load_dwordx2 v[72:73], v210, s[44:47], s3 offen
	buffer_load_dwordx4 v[56:59], v129, s[44:47], s100 offen
	buffer_load_dwordx2 v[60:61], v210, s[44:47], s100 offen
	buffer_load_dwordx4 v[44:47], v129, s[44:47], s101 offen
	buffer_load_dwordx2 v[48:49], v210, s[44:47], s101 offen
	v_readlane_b32 s2, v211, 28
	s_waitcnt vmcnt(22)
	v_cvt_scalef32_pk32_f32_fp6 v[0:31], v[62:67], 1.0
	v_pk_fma_f32 v[62:63], v[0:1], s[2:3], v[164:165] op_sel_hi:[1,0,1]
	v_pk_fma_f32 v[64:65], v[2:3], s[2:3], v[166:167] op_sel_hi:[1,0,1]
	v_pk_fma_f32 v[66:67], v[4:5], s[2:3], v[168:169] op_sel_hi:[1,0,1]
	v_pk_fma_f32 v[164:165], v[6:7], s[2:3], v[170:171] op_sel_hi:[1,0,1]
	v_pk_fma_f32 v[166:167], v[8:9], s[2:3], v[172:173] op_sel_hi:[1,0,1]
	v_pk_fma_f32 v[168:169], v[10:11], s[2:3], v[174:175] op_sel_hi:[1,0,1]
	v_pk_fma_f32 v[170:171], v[12:13], s[2:3], v[176:177] op_sel_hi:[1,0,1]
	v_pk_fma_f32 v[172:173], v[14:15], s[2:3], v[178:179] op_sel_hi:[1,0,1]
	v_pk_fma_f32 v[174:175], v[16:17], s[2:3], v[180:181] op_sel_hi:[1,0,1]
	v_pk_fma_f32 v[162:163], v[18:19], s[2:3], v[162:163] op_sel_hi:[1,0,1]
	v_pk_fma_f32 v[160:161], v[20:21], s[2:3], v[160:161] op_sel_hi:[1,0,1]
	v_pk_fma_f32 v[158:159], v[22:23], s[2:3], v[158:159] op_sel_hi:[1,0,1]
	v_pk_fma_f32 v[156:157], v[24:25], s[2:3], v[156:157] op_sel_hi:[1,0,1]
	v_pk_fma_f32 v[154:155], v[26:27], s[2:3], v[154:155] op_sel_hi:[1,0,1]
	v_pk_fma_f32 v[152:153], v[28:29], s[2:3], v[152:153] op_sel_hi:[1,0,1]
	v_pk_fma_f32 v[150:151], v[30:31], s[2:3], v[150:151] op_sel_hi:[1,0,1]
	v_readlane_b32 s2, v211, 29
	s_waitcnt vmcnt(20)
	v_cvt_scalef32_pk32_f32_fp6 v[0:31], v[50:55], 1.0
	v_pk_fma_f32 v[50:51], v[0:1], s[2:3], v[62:63] op_sel_hi:[1,0,1]
	v_pk_fma_f32 v[52:53], v[2:3], s[2:3], v[64:65] op_sel_hi:[1,0,1]
	v_pk_fma_f32 v[54:55], v[4:5], s[2:3], v[66:67] op_sel_hi:[1,0,1]
	v_pk_fma_f32 v[62:63], v[6:7], s[2:3], v[164:165] op_sel_hi:[1,0,1]
	v_pk_fma_f32 v[64:65], v[8:9], s[2:3], v[166:167] op_sel_hi:[1,0,1]
	v_pk_fma_f32 v[66:67], v[10:11], s[2:3], v[168:169] op_sel_hi:[1,0,1]
	v_pk_fma_f32 v[164:165], v[12:13], s[2:3], v[170:171] op_sel_hi:[1,0,1]
	v_pk_fma_f32 v[166:167], v[14:15], s[2:3], v[172:173] op_sel_hi:[1,0,1]
	v_pk_fma_f32 v[168:169], v[16:17], s[2:3], v[174:175] op_sel_hi:[1,0,1]
	v_pk_fma_f32 v[162:163], v[18:19], s[2:3], v[162:163] op_sel_hi:[1,0,1]
	v_pk_fma_f32 v[160:161], v[20:21], s[2:3], v[160:161] op_sel_hi:[1,0,1]
	v_pk_fma_f32 v[158:159], v[22:23], s[2:3], v[158:159] op_sel_hi:[1,0,1]
	v_pk_fma_f32 v[156:157], v[24:25], s[2:3], v[156:157] op_sel_hi:[1,0,1]
	v_pk_fma_f32 v[154:155], v[26:27], s[2:3], v[154:155] op_sel_hi:[1,0,1]
	v_pk_fma_f32 v[152:153], v[28:29], s[2:3], v[152:153] op_sel_hi:[1,0,1]
	v_pk_fma_f32 v[150:151], v[30:31], s[2:3], v[150:151] op_sel_hi:[1,0,1]
	v_readlane_b32 s2, v211, 30
	s_waitcnt vmcnt(18)
	v_cvt_scalef32_pk32_f32_fp6 v[0:31], v[38:43], 1.0
	v_pk_fma_f32 v[38:39], v[0:1], s[2:3], v[50:51] op_sel_hi:[1,0,1]
	v_pk_fma_f32 v[40:41], v[2:3], s[2:3], v[52:53] op_sel_hi:[1,0,1]
	v_pk_fma_f32 v[42:43], v[4:5], s[2:3], v[54:55] op_sel_hi:[1,0,1]
	v_pk_fma_f32 v[50:51], v[6:7], s[2:3], v[62:63] op_sel_hi:[1,0,1]
	v_pk_fma_f32 v[52:53], v[8:9], s[2:3], v[64:65] op_sel_hi:[1,0,1]
	v_pk_fma_f32 v[54:55], v[10:11], s[2:3], v[66:67] op_sel_hi:[1,0,1]
	v_pk_fma_f32 v[62:63], v[12:13], s[2:3], v[164:165] op_sel_hi:[1,0,1]
	v_pk_fma_f32 v[64:65], v[14:15], s[2:3], v[166:167] op_sel_hi:[1,0,1]
	v_pk_fma_f32 v[66:67], v[16:17], s[2:3], v[168:169] op_sel_hi:[1,0,1]
	v_pk_fma_f32 v[162:163], v[18:19], s[2:3], v[162:163] op_sel_hi:[1,0,1]
	v_pk_fma_f32 v[160:161], v[20:21], s[2:3], v[160:161] op_sel_hi:[1,0,1]
	v_pk_fma_f32 v[158:159], v[22:23], s[2:3], v[158:159] op_sel_hi:[1,0,1]
	v_pk_fma_f32 v[156:157], v[24:25], s[2:3], v[156:157] op_sel_hi:[1,0,1]
	v_pk_fma_f32 v[154:155], v[26:27], s[2:3], v[154:155] op_sel_hi:[1,0,1]
	v_pk_fma_f32 v[152:153], v[28:29], s[2:3], v[152:153] op_sel_hi:[1,0,1]
	v_pk_fma_f32 v[150:151], v[30:31], s[2:3], v[150:151] op_sel_hi:[1,0,1]
	v_readlane_b32 s2, v211, 31
	s_waitcnt vmcnt(16)
	v_cvt_scalef32_pk32_f32_fp6 v[0:31], v[32:37], 1.0
	v_pk_fma_f32 v[164:165], v[0:1], s[2:3], v[38:39] op_sel_hi:[1,0,1]
	v_pk_fma_f32 v[166:167], v[2:3], s[2:3], v[40:41] op_sel_hi:[1,0,1]
	v_pk_fma_f32 v[168:169], v[4:5], s[2:3], v[42:43] op_sel_hi:[1,0,1]
	v_pk_fma_f32 v[170:171], v[6:7], s[2:3], v[50:51] op_sel_hi:[1,0,1]
	v_pk_fma_f32 v[172:173], v[8:9], s[2:3], v[52:53] op_sel_hi:[1,0,1]
	v_pk_fma_f32 v[174:175], v[10:11], s[2:3], v[54:55] op_sel_hi:[1,0,1]
	v_pk_fma_f32 v[176:177], v[12:13], s[2:3], v[62:63] op_sel_hi:[1,0,1]
	v_pk_fma_f32 v[178:179], v[14:15], s[2:3], v[64:65] op_sel_hi:[1,0,1]
	v_pk_fma_f32 v[180:181], v[16:17], s[2:3], v[66:67] op_sel_hi:[1,0,1]
	v_pk_fma_f32 v[162:163], v[18:19], s[2:3], v[162:163] op_sel_hi:[1,0,1]
	v_pk_fma_f32 v[160:161], v[20:21], s[2:3], v[160:161] op_sel_hi:[1,0,1]
	v_pk_fma_f32 v[158:159], v[22:23], s[2:3], v[158:159] op_sel_hi:[1,0,1]
	v_pk_fma_f32 v[156:157], v[24:25], s[2:3], v[156:157] op_sel_hi:[1,0,1]
	v_pk_fma_f32 v[154:155], v[26:27], s[2:3], v[154:155] op_sel_hi:[1,0,1]
	v_pk_fma_f32 v[152:153], v[28:29], s[2:3], v[152:153] op_sel_hi:[1,0,1]
	v_pk_fma_f32 v[150:151], v[30:31], s[2:3], v[150:151] op_sel_hi:[1,0,1]
	v_readlane_b32 s2, v240, 40
	v_readlane_b32 s3, v240, 41
	v_readlane_b32 s100, v240, 42
	v_readlane_b32 s101, v240, 43
	s_nop 1
	buffer_load_dwordx4 v[62:65], v129, s[44:47], s2 offen
	buffer_load_dwordx2 v[66:67], v210, s[44:47], s2 offen
	buffer_load_dwordx4 v[50:53], v129, s[44:47], s3 offen
	buffer_load_dwordx2 v[54:55], v210, s[44:47], s3 offen
	buffer_load_dwordx4 v[38:41], v129, s[44:47], s100 offen
	buffer_load_dwordx2 v[42:43], v210, s[44:47], s100 offen
	buffer_load_dwordx4 v[32:35], v129, s[44:47], s101 offen
	buffer_load_dwordx2 v[36:37], v210, s[44:47], s101 offen
	v_readlane_b32 s2, v211, 32
	s_waitcnt vmcnt(22)
	v_cvt_scalef32_pk32_f32_fp6 v[0:31], v[98:103], 1.0
	v_pk_fma_f32 v[98:99], v[0:1], s[2:3], v[164:165] op_sel_hi:[1,0,1]
	v_pk_fma_f32 v[100:101], v[2:3], s[2:3], v[166:167] op_sel_hi:[1,0,1]
	v_pk_fma_f32 v[102:103], v[4:5], s[2:3], v[168:169] op_sel_hi:[1,0,1]
	v_pk_fma_f32 v[164:165], v[6:7], s[2:3], v[170:171] op_sel_hi:[1,0,1]
	v_pk_fma_f32 v[166:167], v[8:9], s[2:3], v[172:173] op_sel_hi:[1,0,1]
	v_pk_fma_f32 v[168:169], v[10:11], s[2:3], v[174:175] op_sel_hi:[1,0,1]
	v_pk_fma_f32 v[170:171], v[12:13], s[2:3], v[176:177] op_sel_hi:[1,0,1]
	v_pk_fma_f32 v[172:173], v[14:15], s[2:3], v[178:179] op_sel_hi:[1,0,1]
	v_pk_fma_f32 v[174:175], v[16:17], s[2:3], v[180:181] op_sel_hi:[1,0,1]
	v_pk_fma_f32 v[162:163], v[18:19], s[2:3], v[162:163] op_sel_hi:[1,0,1]
	v_pk_fma_f32 v[160:161], v[20:21], s[2:3], v[160:161] op_sel_hi:[1,0,1]
	v_pk_fma_f32 v[158:159], v[22:23], s[2:3], v[158:159] op_sel_hi:[1,0,1]
	v_pk_fma_f32 v[156:157], v[24:25], s[2:3], v[156:157] op_sel_hi:[1,0,1]
	v_pk_fma_f32 v[154:155], v[26:27], s[2:3], v[154:155] op_sel_hi:[1,0,1]
	v_pk_fma_f32 v[152:153], v[28:29], s[2:3], v[152:153] op_sel_hi:[1,0,1]
	v_pk_fma_f32 v[150:151], v[30:31], s[2:3], v[150:151] op_sel_hi:[1,0,1]
	v_readlane_b32 s2, v211, 33
	s_waitcnt vmcnt(20)
	v_cvt_scalef32_pk32_f32_fp6 v[0:31], v[92:97], 1.0
	v_pk_fma_f32 v[92:93], v[0:1], s[2:3], v[98:99] op_sel_hi:[1,0,1]
	v_pk_fma_f32 v[94:95], v[2:3], s[2:3], v[100:101] op_sel_hi:[1,0,1]
	v_pk_fma_f32 v[96:97], v[4:5], s[2:3], v[102:103] op_sel_hi:[1,0,1]
	v_pk_fma_f32 v[98:99], v[6:7], s[2:3], v[164:165] op_sel_hi:[1,0,1]
	v_pk_fma_f32 v[100:101], v[8:9], s[2:3], v[166:167] op_sel_hi:[1,0,1]
	v_pk_fma_f32 v[102:103], v[10:11], s[2:3], v[168:169] op_sel_hi:[1,0,1]
	v_pk_fma_f32 v[164:165], v[12:13], s[2:3], v[170:171] op_sel_hi:[1,0,1]
	v_pk_fma_f32 v[166:167], v[14:15], s[2:3], v[172:173] op_sel_hi:[1,0,1]
	v_pk_fma_f32 v[168:169], v[16:17], s[2:3], v[174:175] op_sel_hi:[1,0,1]
	v_pk_fma_f32 v[162:163], v[18:19], s[2:3], v[162:163] op_sel_hi:[1,0,1]
	v_pk_fma_f32 v[160:161], v[20:21], s[2:3], v[160:161] op_sel_hi:[1,0,1]
	v_pk_fma_f32 v[158:159], v[22:23], s[2:3], v[158:159] op_sel_hi:[1,0,1]
	v_pk_fma_f32 v[156:157], v[24:25], s[2:3], v[156:157] op_sel_hi:[1,0,1]
	v_pk_fma_f32 v[154:155], v[26:27], s[2:3], v[154:155] op_sel_hi:[1,0,1]
	v_pk_fma_f32 v[152:153], v[28:29], s[2:3], v[152:153] op_sel_hi:[1,0,1]
	v_pk_fma_f32 v[150:151], v[30:31], s[2:3], v[150:151] op_sel_hi:[1,0,1]
	v_readlane_b32 s2, v211, 34
	s_waitcnt vmcnt(18)
	v_cvt_scalef32_pk32_f32_fp6 v[0:31], v[86:91], 1.0
	v_pk_fma_f32 v[86:87], v[0:1], s[2:3], v[92:93] op_sel_hi:[1,0,1]
	v_pk_fma_f32 v[88:89], v[2:3], s[2:3], v[94:95] op_sel_hi:[1,0,1]
	v_pk_fma_f32 v[90:91], v[4:5], s[2:3], v[96:97] op_sel_hi:[1,0,1]
	v_pk_fma_f32 v[92:93], v[6:7], s[2:3], v[98:99] op_sel_hi:[1,0,1]
	v_pk_fma_f32 v[94:95], v[8:9], s[2:3], v[100:101] op_sel_hi:[1,0,1]
	v_pk_fma_f32 v[96:97], v[10:11], s[2:3], v[102:103] op_sel_hi:[1,0,1]
	v_pk_fma_f32 v[98:99], v[12:13], s[2:3], v[164:165] op_sel_hi:[1,0,1]
	v_pk_fma_f32 v[100:101], v[14:15], s[2:3], v[166:167] op_sel_hi:[1,0,1]
	v_pk_fma_f32 v[102:103], v[16:17], s[2:3], v[168:169] op_sel_hi:[1,0,1]
	v_pk_fma_f32 v[162:163], v[18:19], s[2:3], v[162:163] op_sel_hi:[1,0,1]
	v_pk_fma_f32 v[160:161], v[20:21], s[2:3], v[160:161] op_sel_hi:[1,0,1]
	v_pk_fma_f32 v[158:159], v[22:23], s[2:3], v[158:159] op_sel_hi:[1,0,1]
	v_pk_fma_f32 v[156:157], v[24:25], s[2:3], v[156:157] op_sel_hi:[1,0,1]
	v_pk_fma_f32 v[154:155], v[26:27], s[2:3], v[154:155] op_sel_hi:[1,0,1]
	v_pk_fma_f32 v[152:153], v[28:29], s[2:3], v[152:153] op_sel_hi:[1,0,1]
	v_pk_fma_f32 v[150:151], v[30:31], s[2:3], v[150:151] op_sel_hi:[1,0,1]
	v_readlane_b32 s2, v211, 35
	s_waitcnt vmcnt(16)
	v_cvt_scalef32_pk32_f32_fp6 v[0:31], v[80:85], 1.0
	v_pk_fma_f32 v[180:181], v[0:1], s[2:3], v[86:87] op_sel_hi:[1,0,1]
	v_pk_fma_f32 v[178:179], v[2:3], s[2:3], v[88:89] op_sel_hi:[1,0,1]
	v_pk_fma_f32 v[176:177], v[4:5], s[2:3], v[90:91] op_sel_hi:[1,0,1]
	v_pk_fma_f32 v[174:175], v[6:7], s[2:3], v[92:93] op_sel_hi:[1,0,1]
	v_pk_fma_f32 v[172:173], v[8:9], s[2:3], v[94:95] op_sel_hi:[1,0,1]
	v_pk_fma_f32 v[170:171], v[10:11], s[2:3], v[96:97] op_sel_hi:[1,0,1]
	v_pk_fma_f32 v[168:169], v[12:13], s[2:3], v[98:99] op_sel_hi:[1,0,1]
	v_pk_fma_f32 v[166:167], v[14:15], s[2:3], v[100:101] op_sel_hi:[1,0,1]
	v_pk_fma_f32 v[164:165], v[16:17], s[2:3], v[102:103] op_sel_hi:[1,0,1]
	v_pk_fma_f32 v[162:163], v[18:19], s[2:3], v[162:163] op_sel_hi:[1,0,1]
	v_pk_fma_f32 v[160:161], v[20:21], s[2:3], v[160:161] op_sel_hi:[1,0,1]
	v_pk_fma_f32 v[158:159], v[22:23], s[2:3], v[158:159] op_sel_hi:[1,0,1]
	v_pk_fma_f32 v[156:157], v[24:25], s[2:3], v[156:157] op_sel_hi:[1,0,1]
	v_pk_fma_f32 v[154:155], v[26:27], s[2:3], v[154:155] op_sel_hi:[1,0,1]
	v_pk_fma_f32 v[152:153], v[28:29], s[2:3], v[152:153] op_sel_hi:[1,0,1]
	v_pk_fma_f32 v[150:151], v[30:31], s[2:3], v[150:151] op_sel_hi:[1,0,1]
	v_readlane_b32 s2, v240, 44
	v_readlane_b32 s3, v240, 45
	v_readlane_b32 s100, v240, 46
	v_readlane_b32 s101, v240, 47
	s_nop 1
	buffer_load_dwordx4 v[98:101], v129, s[44:47], s2 offen
	buffer_load_dwordx2 v[102:103], v210, s[44:47], s2 offen
	buffer_load_dwordx4 v[92:95], v129, s[44:47], s3 offen
	buffer_load_dwordx2 v[96:97], v210, s[44:47], s3 offen
	buffer_load_dwordx4 v[86:89], v129, s[44:47], s100 offen
	buffer_load_dwordx2 v[90:91], v210, s[44:47], s100 offen
	buffer_load_dwordx4 v[80:83], v129, s[44:47], s101 offen
	buffer_load_dwordx2 v[84:85], v210, s[44:47], s101 offen
	v_readlane_b32 s2, v211, 36
	s_waitcnt vmcnt(22)
	v_cvt_scalef32_pk32_f32_fp6 v[0:31], v[74:79], 1.0
	v_pk_fma_f32 v[74:75], v[0:1], s[2:3], v[180:181] op_sel_hi:[1,0,1]
	v_pk_fma_f32 v[76:77], v[2:3], s[2:3], v[178:179] op_sel_hi:[1,0,1]
	v_pk_fma_f32 v[78:79], v[4:5], s[2:3], v[176:177] op_sel_hi:[1,0,1]
	v_pk_fma_f32 v[174:175], v[6:7], s[2:3], v[174:175] op_sel_hi:[1,0,1]
	v_pk_fma_f32 v[172:173], v[8:9], s[2:3], v[172:173] op_sel_hi:[1,0,1]
	v_pk_fma_f32 v[170:171], v[10:11], s[2:3], v[170:171] op_sel_hi:[1,0,1]
	v_pk_fma_f32 v[168:169], v[12:13], s[2:3], v[168:169] op_sel_hi:[1,0,1]
	v_pk_fma_f32 v[166:167], v[14:15], s[2:3], v[166:167] op_sel_hi:[1,0,1]
	v_pk_fma_f32 v[164:165], v[16:17], s[2:3], v[164:165] op_sel_hi:[1,0,1]
	v_pk_fma_f32 v[162:163], v[18:19], s[2:3], v[162:163] op_sel_hi:[1,0,1]
	v_pk_fma_f32 v[160:161], v[20:21], s[2:3], v[160:161] op_sel_hi:[1,0,1]
	v_pk_fma_f32 v[158:159], v[22:23], s[2:3], v[158:159] op_sel_hi:[1,0,1]
	v_pk_fma_f32 v[156:157], v[24:25], s[2:3], v[156:157] op_sel_hi:[1,0,1]
	v_pk_fma_f32 v[154:155], v[26:27], s[2:3], v[154:155] op_sel_hi:[1,0,1]
	v_pk_fma_f32 v[152:153], v[28:29], s[2:3], v[152:153] op_sel_hi:[1,0,1]
	v_pk_fma_f32 v[150:151], v[30:31], s[2:3], v[150:151] op_sel_hi:[1,0,1]
	v_readlane_b32 s2, v211, 37
	s_waitcnt vmcnt(20)
	v_cvt_scalef32_pk32_f32_fp6 v[0:31], v[68:73], 1.0
	v_pk_fma_f32 v[68:69], v[0:1], s[2:3], v[74:75] op_sel_hi:[1,0,1]
	v_pk_fma_f32 v[70:71], v[2:3], s[2:3], v[76:77] op_sel_hi:[1,0,1]
	v_pk_fma_f32 v[72:73], v[4:5], s[2:3], v[78:79] op_sel_hi:[1,0,1]
	v_pk_fma_f32 v[74:75], v[6:7], s[2:3], v[174:175] op_sel_hi:[1,0,1]
	v_pk_fma_f32 v[76:77], v[8:9], s[2:3], v[172:173] op_sel_hi:[1,0,1]
	v_pk_fma_f32 v[78:79], v[10:11], s[2:3], v[170:171] op_sel_hi:[1,0,1]
	v_pk_fma_f32 v[168:169], v[12:13], s[2:3], v[168:169] op_sel_hi:[1,0,1]
	v_pk_fma_f32 v[166:167], v[14:15], s[2:3], v[166:167] op_sel_hi:[1,0,1]
	v_pk_fma_f32 v[164:165], v[16:17], s[2:3], v[164:165] op_sel_hi:[1,0,1]
	v_pk_fma_f32 v[162:163], v[18:19], s[2:3], v[162:163] op_sel_hi:[1,0,1]
	v_pk_fma_f32 v[160:161], v[20:21], s[2:3], v[160:161] op_sel_hi:[1,0,1]
	v_pk_fma_f32 v[158:159], v[22:23], s[2:3], v[158:159] op_sel_hi:[1,0,1]
	v_pk_fma_f32 v[156:157], v[24:25], s[2:3], v[156:157] op_sel_hi:[1,0,1]
	v_pk_fma_f32 v[154:155], v[26:27], s[2:3], v[154:155] op_sel_hi:[1,0,1]
	v_pk_fma_f32 v[152:153], v[28:29], s[2:3], v[152:153] op_sel_hi:[1,0,1]
	v_pk_fma_f32 v[150:151], v[30:31], s[2:3], v[150:151] op_sel_hi:[1,0,1]
	v_readlane_b32 s2, v211, 38
	s_waitcnt vmcnt(18)
	v_cvt_scalef32_pk32_f32_fp6 v[0:31], v[56:61], 1.0
	v_pk_fma_f32 v[56:57], v[0:1], s[2:3], v[68:69] op_sel_hi:[1,0,1]
	v_pk_fma_f32 v[58:59], v[2:3], s[2:3], v[70:71] op_sel_hi:[1,0,1]
	v_pk_fma_f32 v[60:61], v[4:5], s[2:3], v[72:73] op_sel_hi:[1,0,1]
	v_pk_fma_f32 v[68:69], v[6:7], s[2:3], v[74:75] op_sel_hi:[1,0,1]
	v_pk_fma_f32 v[70:71], v[8:9], s[2:3], v[76:77] op_sel_hi:[1,0,1]
	v_pk_fma_f32 v[72:73], v[10:11], s[2:3], v[78:79] op_sel_hi:[1,0,1]
	v_pk_fma_f32 v[74:75], v[12:13], s[2:3], v[168:169] op_sel_hi:[1,0,1]
	v_pk_fma_f32 v[76:77], v[14:15], s[2:3], v[166:167] op_sel_hi:[1,0,1]
	v_pk_fma_f32 v[78:79], v[16:17], s[2:3], v[164:165] op_sel_hi:[1,0,1]
	v_pk_fma_f32 v[162:163], v[18:19], s[2:3], v[162:163] op_sel_hi:[1,0,1]
	v_pk_fma_f32 v[160:161], v[20:21], s[2:3], v[160:161] op_sel_hi:[1,0,1]
	v_pk_fma_f32 v[158:159], v[22:23], s[2:3], v[158:159] op_sel_hi:[1,0,1]
	v_pk_fma_f32 v[156:157], v[24:25], s[2:3], v[156:157] op_sel_hi:[1,0,1]
	v_pk_fma_f32 v[154:155], v[26:27], s[2:3], v[154:155] op_sel_hi:[1,0,1]
	v_pk_fma_f32 v[152:153], v[28:29], s[2:3], v[152:153] op_sel_hi:[1,0,1]
	v_pk_fma_f32 v[150:151], v[30:31], s[2:3], v[150:151] op_sel_hi:[1,0,1]
	v_readlane_b32 s2, v211, 39
	s_waitcnt vmcnt(16)
	v_cvt_scalef32_pk32_f32_fp6 v[0:31], v[44:49], 1.0
	v_pk_fma_f32 v[164:165], v[0:1], s[2:3], v[56:57] op_sel_hi:[1,0,1]
	v_pk_fma_f32 v[166:167], v[2:3], s[2:3], v[58:59] op_sel_hi:[1,0,1]
	v_pk_fma_f32 v[168:169], v[4:5], s[2:3], v[60:61] op_sel_hi:[1,0,1]
	v_pk_fma_f32 v[170:171], v[6:7], s[2:3], v[68:69] op_sel_hi:[1,0,1]
	v_pk_fma_f32 v[172:173], v[8:9], s[2:3], v[70:71] op_sel_hi:[1,0,1]
	v_pk_fma_f32 v[174:175], v[10:11], s[2:3], v[72:73] op_sel_hi:[1,0,1]
	v_pk_fma_f32 v[176:177], v[12:13], s[2:3], v[74:75] op_sel_hi:[1,0,1]
	v_pk_fma_f32 v[178:179], v[14:15], s[2:3], v[76:77] op_sel_hi:[1,0,1]
	v_pk_fma_f32 v[180:181], v[16:17], s[2:3], v[78:79] op_sel_hi:[1,0,1]
	v_pk_fma_f32 v[162:163], v[18:19], s[2:3], v[162:163] op_sel_hi:[1,0,1]
	v_pk_fma_f32 v[160:161], v[20:21], s[2:3], v[160:161] op_sel_hi:[1,0,1]
	v_pk_fma_f32 v[158:159], v[22:23], s[2:3], v[158:159] op_sel_hi:[1,0,1]
	v_pk_fma_f32 v[156:157], v[24:25], s[2:3], v[156:157] op_sel_hi:[1,0,1]
	v_pk_fma_f32 v[154:155], v[26:27], s[2:3], v[154:155] op_sel_hi:[1,0,1]
	v_pk_fma_f32 v[152:153], v[28:29], s[2:3], v[152:153] op_sel_hi:[1,0,1]
	v_pk_fma_f32 v[150:151], v[30:31], s[2:3], v[150:151] op_sel_hi:[1,0,1]
	v_readlane_b32 s2, v240, 48
	v_readlane_b32 s3, v240, 49
	v_readlane_b32 s100, v240, 50
	v_readlane_b32 s101, v240, 51
	s_nop 1
	buffer_load_dwordx4 v[74:77], v129, s[44:47], s2 offen
	buffer_load_dwordx2 v[78:79], v210, s[44:47], s2 offen
	buffer_load_dwordx4 v[68:71], v129, s[44:47], s3 offen
	buffer_load_dwordx2 v[72:73], v210, s[44:47], s3 offen
	buffer_load_dwordx4 v[56:59], v129, s[44:47], s100 offen
	buffer_load_dwordx2 v[60:61], v210, s[44:47], s100 offen
	buffer_load_dwordx4 v[44:47], v129, s[44:47], s101 offen
	buffer_load_dwordx2 v[48:49], v210, s[44:47], s101 offen
	v_readlane_b32 s2, v211, 40
	s_waitcnt vmcnt(22)
	v_cvt_scalef32_pk32_f32_fp6 v[0:31], v[62:67], 1.0
	v_pk_fma_f32 v[62:63], v[0:1], s[2:3], v[164:165] op_sel_hi:[1,0,1]
	v_pk_fma_f32 v[64:65], v[2:3], s[2:3], v[166:167] op_sel_hi:[1,0,1]
	v_pk_fma_f32 v[66:67], v[4:5], s[2:3], v[168:169] op_sel_hi:[1,0,1]
	v_pk_fma_f32 v[164:165], v[6:7], s[2:3], v[170:171] op_sel_hi:[1,0,1]
	v_pk_fma_f32 v[166:167], v[8:9], s[2:3], v[172:173] op_sel_hi:[1,0,1]
	v_pk_fma_f32 v[168:169], v[10:11], s[2:3], v[174:175] op_sel_hi:[1,0,1]
	v_pk_fma_f32 v[170:171], v[12:13], s[2:3], v[176:177] op_sel_hi:[1,0,1]
	v_pk_fma_f32 v[172:173], v[14:15], s[2:3], v[178:179] op_sel_hi:[1,0,1]
	v_pk_fma_f32 v[174:175], v[16:17], s[2:3], v[180:181] op_sel_hi:[1,0,1]
	v_pk_fma_f32 v[162:163], v[18:19], s[2:3], v[162:163] op_sel_hi:[1,0,1]
	v_pk_fma_f32 v[160:161], v[20:21], s[2:3], v[160:161] op_sel_hi:[1,0,1]
	v_pk_fma_f32 v[158:159], v[22:23], s[2:3], v[158:159] op_sel_hi:[1,0,1]
	v_pk_fma_f32 v[156:157], v[24:25], s[2:3], v[156:157] op_sel_hi:[1,0,1]
	v_pk_fma_f32 v[154:155], v[26:27], s[2:3], v[154:155] op_sel_hi:[1,0,1]
	v_pk_fma_f32 v[152:153], v[28:29], s[2:3], v[152:153] op_sel_hi:[1,0,1]
	v_pk_fma_f32 v[150:151], v[30:31], s[2:3], v[150:151] op_sel_hi:[1,0,1]
	v_readlane_b32 s2, v211, 41
	s_waitcnt vmcnt(20)
	v_cvt_scalef32_pk32_f32_fp6 v[0:31], v[50:55], 1.0
	v_pk_fma_f32 v[50:51], v[0:1], s[2:3], v[62:63] op_sel_hi:[1,0,1]
	v_pk_fma_f32 v[52:53], v[2:3], s[2:3], v[64:65] op_sel_hi:[1,0,1]
	v_pk_fma_f32 v[54:55], v[4:5], s[2:3], v[66:67] op_sel_hi:[1,0,1]
	v_pk_fma_f32 v[62:63], v[6:7], s[2:3], v[164:165] op_sel_hi:[1,0,1]
	v_pk_fma_f32 v[64:65], v[8:9], s[2:3], v[166:167] op_sel_hi:[1,0,1]
	v_pk_fma_f32 v[66:67], v[10:11], s[2:3], v[168:169] op_sel_hi:[1,0,1]
	v_pk_fma_f32 v[164:165], v[12:13], s[2:3], v[170:171] op_sel_hi:[1,0,1]
	v_pk_fma_f32 v[166:167], v[14:15], s[2:3], v[172:173] op_sel_hi:[1,0,1]
	v_pk_fma_f32 v[168:169], v[16:17], s[2:3], v[174:175] op_sel_hi:[1,0,1]
	v_pk_fma_f32 v[162:163], v[18:19], s[2:3], v[162:163] op_sel_hi:[1,0,1]
	v_pk_fma_f32 v[160:161], v[20:21], s[2:3], v[160:161] op_sel_hi:[1,0,1]
	v_pk_fma_f32 v[158:159], v[22:23], s[2:3], v[158:159] op_sel_hi:[1,0,1]
	v_pk_fma_f32 v[156:157], v[24:25], s[2:3], v[156:157] op_sel_hi:[1,0,1]
	v_pk_fma_f32 v[154:155], v[26:27], s[2:3], v[154:155] op_sel_hi:[1,0,1]
	v_pk_fma_f32 v[152:153], v[28:29], s[2:3], v[152:153] op_sel_hi:[1,0,1]
	v_pk_fma_f32 v[150:151], v[30:31], s[2:3], v[150:151] op_sel_hi:[1,0,1]
	v_readlane_b32 s2, v211, 42
	s_waitcnt vmcnt(18)
	v_cvt_scalef32_pk32_f32_fp6 v[0:31], v[38:43], 1.0
	v_pk_fma_f32 v[38:39], v[0:1], s[2:3], v[50:51] op_sel_hi:[1,0,1]
	v_pk_fma_f32 v[40:41], v[2:3], s[2:3], v[52:53] op_sel_hi:[1,0,1]
	v_pk_fma_f32 v[42:43], v[4:5], s[2:3], v[54:55] op_sel_hi:[1,0,1]
	v_pk_fma_f32 v[50:51], v[6:7], s[2:3], v[62:63] op_sel_hi:[1,0,1]
	v_pk_fma_f32 v[52:53], v[8:9], s[2:3], v[64:65] op_sel_hi:[1,0,1]
	v_pk_fma_f32 v[54:55], v[10:11], s[2:3], v[66:67] op_sel_hi:[1,0,1]
	v_pk_fma_f32 v[62:63], v[12:13], s[2:3], v[164:165] op_sel_hi:[1,0,1]
	v_pk_fma_f32 v[64:65], v[14:15], s[2:3], v[166:167] op_sel_hi:[1,0,1]
	v_pk_fma_f32 v[66:67], v[16:17], s[2:3], v[168:169] op_sel_hi:[1,0,1]
	v_pk_fma_f32 v[162:163], v[18:19], s[2:3], v[162:163] op_sel_hi:[1,0,1]
	v_pk_fma_f32 v[160:161], v[20:21], s[2:3], v[160:161] op_sel_hi:[1,0,1]
	v_pk_fma_f32 v[158:159], v[22:23], s[2:3], v[158:159] op_sel_hi:[1,0,1]
	v_pk_fma_f32 v[156:157], v[24:25], s[2:3], v[156:157] op_sel_hi:[1,0,1]
	v_pk_fma_f32 v[154:155], v[26:27], s[2:3], v[154:155] op_sel_hi:[1,0,1]
	v_pk_fma_f32 v[152:153], v[28:29], s[2:3], v[152:153] op_sel_hi:[1,0,1]
	v_pk_fma_f32 v[150:151], v[30:31], s[2:3], v[150:151] op_sel_hi:[1,0,1]
	v_readlane_b32 s2, v211, 43
	s_waitcnt vmcnt(16)
	v_cvt_scalef32_pk32_f32_fp6 v[0:31], v[32:37], 1.0
	v_pk_fma_f32 v[164:165], v[0:1], s[2:3], v[38:39] op_sel_hi:[1,0,1]
	v_pk_fma_f32 v[166:167], v[2:3], s[2:3], v[40:41] op_sel_hi:[1,0,1]
	v_pk_fma_f32 v[168:169], v[4:5], s[2:3], v[42:43] op_sel_hi:[1,0,1]
	v_pk_fma_f32 v[170:171], v[6:7], s[2:3], v[50:51] op_sel_hi:[1,0,1]
	v_pk_fma_f32 v[172:173], v[8:9], s[2:3], v[52:53] op_sel_hi:[1,0,1]
	v_pk_fma_f32 v[174:175], v[10:11], s[2:3], v[54:55] op_sel_hi:[1,0,1]
	v_pk_fma_f32 v[176:177], v[12:13], s[2:3], v[62:63] op_sel_hi:[1,0,1]
	v_pk_fma_f32 v[178:179], v[14:15], s[2:3], v[64:65] op_sel_hi:[1,0,1]
	v_pk_fma_f32 v[180:181], v[16:17], s[2:3], v[66:67] op_sel_hi:[1,0,1]
	v_pk_fma_f32 v[162:163], v[18:19], s[2:3], v[162:163] op_sel_hi:[1,0,1]
	v_pk_fma_f32 v[160:161], v[20:21], s[2:3], v[160:161] op_sel_hi:[1,0,1]
	v_pk_fma_f32 v[158:159], v[22:23], s[2:3], v[158:159] op_sel_hi:[1,0,1]
	v_pk_fma_f32 v[156:157], v[24:25], s[2:3], v[156:157] op_sel_hi:[1,0,1]
	v_pk_fma_f32 v[154:155], v[26:27], s[2:3], v[154:155] op_sel_hi:[1,0,1]
	v_pk_fma_f32 v[152:153], v[28:29], s[2:3], v[152:153] op_sel_hi:[1,0,1]
	v_pk_fma_f32 v[150:151], v[30:31], s[2:3], v[150:151] op_sel_hi:[1,0,1]
	v_readlane_b32 s2, v240, 52
	v_readlane_b32 s3, v240, 53
	v_readlane_b32 s100, v240, 54
	v_readlane_b32 s101, v240, 55
	s_nop 1
	buffer_load_dwordx4 v[62:65], v129, s[44:47], s2 offen
	buffer_load_dwordx2 v[66:67], v210, s[44:47], s2 offen
	buffer_load_dwordx4 v[50:53], v129, s[44:47], s3 offen
	buffer_load_dwordx2 v[54:55], v210, s[44:47], s3 offen
	buffer_load_dwordx4 v[38:41], v129, s[44:47], s100 offen
	buffer_load_dwordx2 v[42:43], v210, s[44:47], s100 offen
	buffer_load_dwordx4 v[32:35], v129, s[44:47], s101 offen
	buffer_load_dwordx2 v[36:37], v210, s[44:47], s101 offen
	v_readlane_b32 s2, v211, 44
	s_waitcnt vmcnt(22)
	v_cvt_scalef32_pk32_f32_fp6 v[0:31], v[98:103], 1.0
	v_pk_fma_f32 v[98:99], v[0:1], s[2:3], v[164:165] op_sel_hi:[1,0,1]
	v_pk_fma_f32 v[100:101], v[2:3], s[2:3], v[166:167] op_sel_hi:[1,0,1]
	v_pk_fma_f32 v[102:103], v[4:5], s[2:3], v[168:169] op_sel_hi:[1,0,1]
	v_pk_fma_f32 v[164:165], v[6:7], s[2:3], v[170:171] op_sel_hi:[1,0,1]
	v_pk_fma_f32 v[166:167], v[8:9], s[2:3], v[172:173] op_sel_hi:[1,0,1]
	v_pk_fma_f32 v[168:169], v[10:11], s[2:3], v[174:175] op_sel_hi:[1,0,1]
	v_pk_fma_f32 v[170:171], v[12:13], s[2:3], v[176:177] op_sel_hi:[1,0,1]
	v_pk_fma_f32 v[172:173], v[14:15], s[2:3], v[178:179] op_sel_hi:[1,0,1]
	v_pk_fma_f32 v[174:175], v[16:17], s[2:3], v[180:181] op_sel_hi:[1,0,1]
	v_pk_fma_f32 v[162:163], v[18:19], s[2:3], v[162:163] op_sel_hi:[1,0,1]
	v_pk_fma_f32 v[160:161], v[20:21], s[2:3], v[160:161] op_sel_hi:[1,0,1]
	v_pk_fma_f32 v[158:159], v[22:23], s[2:3], v[158:159] op_sel_hi:[1,0,1]
	v_pk_fma_f32 v[156:157], v[24:25], s[2:3], v[156:157] op_sel_hi:[1,0,1]
	v_pk_fma_f32 v[154:155], v[26:27], s[2:3], v[154:155] op_sel_hi:[1,0,1]
	v_pk_fma_f32 v[152:153], v[28:29], s[2:3], v[152:153] op_sel_hi:[1,0,1]
	v_pk_fma_f32 v[150:151], v[30:31], s[2:3], v[150:151] op_sel_hi:[1,0,1]
	v_readlane_b32 s2, v211, 45
	s_waitcnt vmcnt(20)
	v_cvt_scalef32_pk32_f32_fp6 v[0:31], v[92:97], 1.0
	v_pk_fma_f32 v[92:93], v[0:1], s[2:3], v[98:99] op_sel_hi:[1,0,1]
	v_pk_fma_f32 v[94:95], v[2:3], s[2:3], v[100:101] op_sel_hi:[1,0,1]
	v_pk_fma_f32 v[96:97], v[4:5], s[2:3], v[102:103] op_sel_hi:[1,0,1]
	v_pk_fma_f32 v[98:99], v[6:7], s[2:3], v[164:165] op_sel_hi:[1,0,1]
	v_pk_fma_f32 v[100:101], v[8:9], s[2:3], v[166:167] op_sel_hi:[1,0,1]
	v_pk_fma_f32 v[102:103], v[10:11], s[2:3], v[168:169] op_sel_hi:[1,0,1]
	v_pk_fma_f32 v[164:165], v[12:13], s[2:3], v[170:171] op_sel_hi:[1,0,1]
	v_pk_fma_f32 v[166:167], v[14:15], s[2:3], v[172:173] op_sel_hi:[1,0,1]
	v_pk_fma_f32 v[168:169], v[16:17], s[2:3], v[174:175] op_sel_hi:[1,0,1]
	v_pk_fma_f32 v[162:163], v[18:19], s[2:3], v[162:163] op_sel_hi:[1,0,1]
	v_pk_fma_f32 v[160:161], v[20:21], s[2:3], v[160:161] op_sel_hi:[1,0,1]
	v_pk_fma_f32 v[158:159], v[22:23], s[2:3], v[158:159] op_sel_hi:[1,0,1]
	v_pk_fma_f32 v[156:157], v[24:25], s[2:3], v[156:157] op_sel_hi:[1,0,1]
	v_pk_fma_f32 v[154:155], v[26:27], s[2:3], v[154:155] op_sel_hi:[1,0,1]
	v_pk_fma_f32 v[152:153], v[28:29], s[2:3], v[152:153] op_sel_hi:[1,0,1]
	v_pk_fma_f32 v[150:151], v[30:31], s[2:3], v[150:151] op_sel_hi:[1,0,1]
	v_readlane_b32 s2, v211, 46
	s_waitcnt vmcnt(18)
	v_cvt_scalef32_pk32_f32_fp6 v[0:31], v[86:91], 1.0
	v_pk_fma_f32 v[86:87], v[0:1], s[2:3], v[92:93] op_sel_hi:[1,0,1]
	v_pk_fma_f32 v[88:89], v[2:3], s[2:3], v[94:95] op_sel_hi:[1,0,1]
	v_pk_fma_f32 v[90:91], v[4:5], s[2:3], v[96:97] op_sel_hi:[1,0,1]
	v_pk_fma_f32 v[92:93], v[6:7], s[2:3], v[98:99] op_sel_hi:[1,0,1]
	v_pk_fma_f32 v[94:95], v[8:9], s[2:3], v[100:101] op_sel_hi:[1,0,1]
	v_pk_fma_f32 v[96:97], v[10:11], s[2:3], v[102:103] op_sel_hi:[1,0,1]
	v_pk_fma_f32 v[98:99], v[12:13], s[2:3], v[164:165] op_sel_hi:[1,0,1]
	v_pk_fma_f32 v[100:101], v[14:15], s[2:3], v[166:167] op_sel_hi:[1,0,1]
	v_pk_fma_f32 v[102:103], v[16:17], s[2:3], v[168:169] op_sel_hi:[1,0,1]
	v_pk_fma_f32 v[162:163], v[18:19], s[2:3], v[162:163] op_sel_hi:[1,0,1]
	v_pk_fma_f32 v[160:161], v[20:21], s[2:3], v[160:161] op_sel_hi:[1,0,1]
	v_pk_fma_f32 v[158:159], v[22:23], s[2:3], v[158:159] op_sel_hi:[1,0,1]
	v_pk_fma_f32 v[156:157], v[24:25], s[2:3], v[156:157] op_sel_hi:[1,0,1]
	v_pk_fma_f32 v[154:155], v[26:27], s[2:3], v[154:155] op_sel_hi:[1,0,1]
	v_pk_fma_f32 v[152:153], v[28:29], s[2:3], v[152:153] op_sel_hi:[1,0,1]
	v_pk_fma_f32 v[150:151], v[30:31], s[2:3], v[150:151] op_sel_hi:[1,0,1]
	v_readlane_b32 s2, v211, 47
	s_waitcnt vmcnt(16)
	v_cvt_scalef32_pk32_f32_fp6 v[0:31], v[80:85], 1.0
	v_pk_fma_f32 v[180:181], v[0:1], s[2:3], v[86:87] op_sel_hi:[1,0,1]
	v_pk_fma_f32 v[178:179], v[2:3], s[2:3], v[88:89] op_sel_hi:[1,0,1]
	v_pk_fma_f32 v[176:177], v[4:5], s[2:3], v[90:91] op_sel_hi:[1,0,1]
	v_pk_fma_f32 v[174:175], v[6:7], s[2:3], v[92:93] op_sel_hi:[1,0,1]
	v_pk_fma_f32 v[172:173], v[8:9], s[2:3], v[94:95] op_sel_hi:[1,0,1]
	v_pk_fma_f32 v[170:171], v[10:11], s[2:3], v[96:97] op_sel_hi:[1,0,1]
	v_pk_fma_f32 v[168:169], v[12:13], s[2:3], v[98:99] op_sel_hi:[1,0,1]
	v_pk_fma_f32 v[166:167], v[14:15], s[2:3], v[100:101] op_sel_hi:[1,0,1]
	v_pk_fma_f32 v[164:165], v[16:17], s[2:3], v[102:103] op_sel_hi:[1,0,1]
	v_pk_fma_f32 v[162:163], v[18:19], s[2:3], v[162:163] op_sel_hi:[1,0,1]
	v_pk_fma_f32 v[160:161], v[20:21], s[2:3], v[160:161] op_sel_hi:[1,0,1]
	v_pk_fma_f32 v[158:159], v[22:23], s[2:3], v[158:159] op_sel_hi:[1,0,1]
	v_pk_fma_f32 v[156:157], v[24:25], s[2:3], v[156:157] op_sel_hi:[1,0,1]
	v_pk_fma_f32 v[154:155], v[26:27], s[2:3], v[154:155] op_sel_hi:[1,0,1]
	v_pk_fma_f32 v[152:153], v[28:29], s[2:3], v[152:153] op_sel_hi:[1,0,1]
	v_pk_fma_f32 v[150:151], v[30:31], s[2:3], v[150:151] op_sel_hi:[1,0,1]
	v_readlane_b32 s2, v240, 56
	v_readlane_b32 s3, v240, 57
	v_readlane_b32 s100, v240, 58
	v_readlane_b32 s101, v240, 59
	s_nop 1
	buffer_load_dwordx4 v[98:101], v129, s[44:47], s2 offen
	buffer_load_dwordx2 v[102:103], v210, s[44:47], s2 offen
	buffer_load_dwordx4 v[92:95], v129, s[44:47], s3 offen
	buffer_load_dwordx2 v[96:97], v210, s[44:47], s3 offen
	buffer_load_dwordx4 v[86:89], v129, s[44:47], s100 offen
	buffer_load_dwordx2 v[90:91], v210, s[44:47], s100 offen
	buffer_load_dwordx4 v[80:83], v129, s[44:47], s101 offen
	buffer_load_dwordx2 v[84:85], v210, s[44:47], s101 offen
	v_readlane_b32 s2, v211, 48
	s_waitcnt vmcnt(22)
	v_cvt_scalef32_pk32_f32_fp6 v[0:31], v[74:79], 1.0
	v_pk_fma_f32 v[74:75], v[0:1], s[2:3], v[180:181] op_sel_hi:[1,0,1]
	v_pk_fma_f32 v[76:77], v[2:3], s[2:3], v[178:179] op_sel_hi:[1,0,1]
	v_pk_fma_f32 v[78:79], v[4:5], s[2:3], v[176:177] op_sel_hi:[1,0,1]
	v_pk_fma_f32 v[174:175], v[6:7], s[2:3], v[174:175] op_sel_hi:[1,0,1]
	v_pk_fma_f32 v[172:173], v[8:9], s[2:3], v[172:173] op_sel_hi:[1,0,1]
	v_pk_fma_f32 v[170:171], v[10:11], s[2:3], v[170:171] op_sel_hi:[1,0,1]
	v_pk_fma_f32 v[168:169], v[12:13], s[2:3], v[168:169] op_sel_hi:[1,0,1]
	v_pk_fma_f32 v[166:167], v[14:15], s[2:3], v[166:167] op_sel_hi:[1,0,1]
	v_pk_fma_f32 v[164:165], v[16:17], s[2:3], v[164:165] op_sel_hi:[1,0,1]
	v_pk_fma_f32 v[162:163], v[18:19], s[2:3], v[162:163] op_sel_hi:[1,0,1]
	v_pk_fma_f32 v[160:161], v[20:21], s[2:3], v[160:161] op_sel_hi:[1,0,1]
	v_pk_fma_f32 v[158:159], v[22:23], s[2:3], v[158:159] op_sel_hi:[1,0,1]
	v_pk_fma_f32 v[156:157], v[24:25], s[2:3], v[156:157] op_sel_hi:[1,0,1]
	v_pk_fma_f32 v[154:155], v[26:27], s[2:3], v[154:155] op_sel_hi:[1,0,1]
	v_pk_fma_f32 v[152:153], v[28:29], s[2:3], v[152:153] op_sel_hi:[1,0,1]
	v_pk_fma_f32 v[150:151], v[30:31], s[2:3], v[150:151] op_sel_hi:[1,0,1]
	v_readlane_b32 s2, v211, 49
	s_waitcnt vmcnt(20)
	v_cvt_scalef32_pk32_f32_fp6 v[0:31], v[68:73], 1.0
	v_pk_fma_f32 v[68:69], v[0:1], s[2:3], v[74:75] op_sel_hi:[1,0,1]
	v_pk_fma_f32 v[70:71], v[2:3], s[2:3], v[76:77] op_sel_hi:[1,0,1]
	v_pk_fma_f32 v[72:73], v[4:5], s[2:3], v[78:79] op_sel_hi:[1,0,1]
	v_pk_fma_f32 v[74:75], v[6:7], s[2:3], v[174:175] op_sel_hi:[1,0,1]
	v_pk_fma_f32 v[76:77], v[8:9], s[2:3], v[172:173] op_sel_hi:[1,0,1]
	v_pk_fma_f32 v[78:79], v[10:11], s[2:3], v[170:171] op_sel_hi:[1,0,1]
	v_pk_fma_f32 v[168:169], v[12:13], s[2:3], v[168:169] op_sel_hi:[1,0,1]
	v_pk_fma_f32 v[166:167], v[14:15], s[2:3], v[166:167] op_sel_hi:[1,0,1]
	v_pk_fma_f32 v[164:165], v[16:17], s[2:3], v[164:165] op_sel_hi:[1,0,1]
	v_pk_fma_f32 v[162:163], v[18:19], s[2:3], v[162:163] op_sel_hi:[1,0,1]
	v_pk_fma_f32 v[160:161], v[20:21], s[2:3], v[160:161] op_sel_hi:[1,0,1]
	v_pk_fma_f32 v[158:159], v[22:23], s[2:3], v[158:159] op_sel_hi:[1,0,1]
	v_pk_fma_f32 v[156:157], v[24:25], s[2:3], v[156:157] op_sel_hi:[1,0,1]
	v_pk_fma_f32 v[154:155], v[26:27], s[2:3], v[154:155] op_sel_hi:[1,0,1]
	v_pk_fma_f32 v[152:153], v[28:29], s[2:3], v[152:153] op_sel_hi:[1,0,1]
	v_pk_fma_f32 v[150:151], v[30:31], s[2:3], v[150:151] op_sel_hi:[1,0,1]
	v_readlane_b32 s2, v211, 50
	s_waitcnt vmcnt(18)
	v_cvt_scalef32_pk32_f32_fp6 v[0:31], v[56:61], 1.0
	v_pk_fma_f32 v[56:57], v[0:1], s[2:3], v[68:69] op_sel_hi:[1,0,1]
	v_pk_fma_f32 v[58:59], v[2:3], s[2:3], v[70:71] op_sel_hi:[1,0,1]
	v_pk_fma_f32 v[60:61], v[4:5], s[2:3], v[72:73] op_sel_hi:[1,0,1]
	v_pk_fma_f32 v[68:69], v[6:7], s[2:3], v[74:75] op_sel_hi:[1,0,1]
	v_pk_fma_f32 v[70:71], v[8:9], s[2:3], v[76:77] op_sel_hi:[1,0,1]
	v_pk_fma_f32 v[72:73], v[10:11], s[2:3], v[78:79] op_sel_hi:[1,0,1]
	v_pk_fma_f32 v[74:75], v[12:13], s[2:3], v[168:169] op_sel_hi:[1,0,1]
	v_pk_fma_f32 v[76:77], v[14:15], s[2:3], v[166:167] op_sel_hi:[1,0,1]
	v_pk_fma_f32 v[78:79], v[16:17], s[2:3], v[164:165] op_sel_hi:[1,0,1]
	v_pk_fma_f32 v[162:163], v[18:19], s[2:3], v[162:163] op_sel_hi:[1,0,1]
	v_pk_fma_f32 v[160:161], v[20:21], s[2:3], v[160:161] op_sel_hi:[1,0,1]
	v_pk_fma_f32 v[158:159], v[22:23], s[2:3], v[158:159] op_sel_hi:[1,0,1]
	v_pk_fma_f32 v[156:157], v[24:25], s[2:3], v[156:157] op_sel_hi:[1,0,1]
	v_pk_fma_f32 v[154:155], v[26:27], s[2:3], v[154:155] op_sel_hi:[1,0,1]
	v_pk_fma_f32 v[152:153], v[28:29], s[2:3], v[152:153] op_sel_hi:[1,0,1]
	v_pk_fma_f32 v[150:151], v[30:31], s[2:3], v[150:151] op_sel_hi:[1,0,1]
	v_readlane_b32 s2, v211, 51
	s_waitcnt vmcnt(16)
	v_cvt_scalef32_pk32_f32_fp6 v[0:31], v[44:49], 1.0
	v_pk_fma_f32 v[164:165], v[0:1], s[2:3], v[56:57] op_sel_hi:[1,0,1]
	v_pk_fma_f32 v[166:167], v[2:3], s[2:3], v[58:59] op_sel_hi:[1,0,1]
	v_pk_fma_f32 v[168:169], v[4:5], s[2:3], v[60:61] op_sel_hi:[1,0,1]
	v_pk_fma_f32 v[170:171], v[6:7], s[2:3], v[68:69] op_sel_hi:[1,0,1]
	v_pk_fma_f32 v[172:173], v[8:9], s[2:3], v[70:71] op_sel_hi:[1,0,1]
	v_pk_fma_f32 v[174:175], v[10:11], s[2:3], v[72:73] op_sel_hi:[1,0,1]
	v_pk_fma_f32 v[176:177], v[12:13], s[2:3], v[74:75] op_sel_hi:[1,0,1]
	v_pk_fma_f32 v[178:179], v[14:15], s[2:3], v[76:77] op_sel_hi:[1,0,1]
	v_pk_fma_f32 v[180:181], v[16:17], s[2:3], v[78:79] op_sel_hi:[1,0,1]
	v_pk_fma_f32 v[162:163], v[18:19], s[2:3], v[162:163] op_sel_hi:[1,0,1]
	v_pk_fma_f32 v[160:161], v[20:21], s[2:3], v[160:161] op_sel_hi:[1,0,1]
	v_pk_fma_f32 v[158:159], v[22:23], s[2:3], v[158:159] op_sel_hi:[1,0,1]
	v_pk_fma_f32 v[156:157], v[24:25], s[2:3], v[156:157] op_sel_hi:[1,0,1]
	v_pk_fma_f32 v[154:155], v[26:27], s[2:3], v[154:155] op_sel_hi:[1,0,1]
	v_pk_fma_f32 v[152:153], v[28:29], s[2:3], v[152:153] op_sel_hi:[1,0,1]
	v_pk_fma_f32 v[150:151], v[30:31], s[2:3], v[150:151] op_sel_hi:[1,0,1]
	v_readlane_b32 s2, v240, 60
	v_readlane_b32 s3, v240, 61
	v_readlane_b32 s100, v240, 62
	v_readlane_b32 s101, v240, 63
	s_nop 1
	buffer_load_dwordx4 v[74:77], v129, s[44:47], s2 offen
	buffer_load_dwordx2 v[78:79], v210, s[44:47], s2 offen
	buffer_load_dwordx4 v[68:71], v129, s[44:47], s3 offen
	buffer_load_dwordx2 v[72:73], v210, s[44:47], s3 offen
	buffer_load_dwordx4 v[56:59], v129, s[44:47], s100 offen
	buffer_load_dwordx2 v[60:61], v210, s[44:47], s100 offen
	buffer_load_dwordx4 v[44:47], v129, s[44:47], s101 offen
	buffer_load_dwordx2 v[48:49], v210, s[44:47], s101 offen
	v_readlane_b32 s2, v211, 52
	s_waitcnt vmcnt(22)
	v_cvt_scalef32_pk32_f32_fp6 v[0:31], v[62:67], 1.0
	v_pk_fma_f32 v[62:63], v[0:1], s[2:3], v[164:165] op_sel_hi:[1,0,1]
	v_pk_fma_f32 v[64:65], v[2:3], s[2:3], v[166:167] op_sel_hi:[1,0,1]
	v_pk_fma_f32 v[66:67], v[4:5], s[2:3], v[168:169] op_sel_hi:[1,0,1]
	v_pk_fma_f32 v[164:165], v[6:7], s[2:3], v[170:171] op_sel_hi:[1,0,1]
	v_pk_fma_f32 v[166:167], v[8:9], s[2:3], v[172:173] op_sel_hi:[1,0,1]
	v_pk_fma_f32 v[168:169], v[10:11], s[2:3], v[174:175] op_sel_hi:[1,0,1]
	v_pk_fma_f32 v[170:171], v[12:13], s[2:3], v[176:177] op_sel_hi:[1,0,1]
	v_pk_fma_f32 v[172:173], v[14:15], s[2:3], v[178:179] op_sel_hi:[1,0,1]
	v_pk_fma_f32 v[174:175], v[16:17], s[2:3], v[180:181] op_sel_hi:[1,0,1]
	v_pk_fma_f32 v[162:163], v[18:19], s[2:3], v[162:163] op_sel_hi:[1,0,1]
	v_pk_fma_f32 v[160:161], v[20:21], s[2:3], v[160:161] op_sel_hi:[1,0,1]
	v_pk_fma_f32 v[158:159], v[22:23], s[2:3], v[158:159] op_sel_hi:[1,0,1]
	v_pk_fma_f32 v[156:157], v[24:25], s[2:3], v[156:157] op_sel_hi:[1,0,1]
	v_pk_fma_f32 v[154:155], v[26:27], s[2:3], v[154:155] op_sel_hi:[1,0,1]
	v_pk_fma_f32 v[152:153], v[28:29], s[2:3], v[152:153] op_sel_hi:[1,0,1]
	v_pk_fma_f32 v[150:151], v[30:31], s[2:3], v[150:151] op_sel_hi:[1,0,1]
	v_readlane_b32 s2, v211, 53
	s_waitcnt vmcnt(20)
	v_cvt_scalef32_pk32_f32_fp6 v[0:31], v[50:55], 1.0
	v_pk_fma_f32 v[50:51], v[0:1], s[2:3], v[62:63] op_sel_hi:[1,0,1]
	v_pk_fma_f32 v[52:53], v[2:3], s[2:3], v[64:65] op_sel_hi:[1,0,1]
	v_pk_fma_f32 v[54:55], v[4:5], s[2:3], v[66:67] op_sel_hi:[1,0,1]
	v_pk_fma_f32 v[62:63], v[6:7], s[2:3], v[164:165] op_sel_hi:[1,0,1]
	v_pk_fma_f32 v[64:65], v[8:9], s[2:3], v[166:167] op_sel_hi:[1,0,1]
	v_pk_fma_f32 v[66:67], v[10:11], s[2:3], v[168:169] op_sel_hi:[1,0,1]
	v_pk_fma_f32 v[164:165], v[12:13], s[2:3], v[170:171] op_sel_hi:[1,0,1]
	v_pk_fma_f32 v[166:167], v[14:15], s[2:3], v[172:173] op_sel_hi:[1,0,1]
	v_pk_fma_f32 v[168:169], v[16:17], s[2:3], v[174:175] op_sel_hi:[1,0,1]
	v_pk_fma_f32 v[162:163], v[18:19], s[2:3], v[162:163] op_sel_hi:[1,0,1]
	v_pk_fma_f32 v[160:161], v[20:21], s[2:3], v[160:161] op_sel_hi:[1,0,1]
	v_pk_fma_f32 v[158:159], v[22:23], s[2:3], v[158:159] op_sel_hi:[1,0,1]
	v_pk_fma_f32 v[156:157], v[24:25], s[2:3], v[156:157] op_sel_hi:[1,0,1]
	v_pk_fma_f32 v[154:155], v[26:27], s[2:3], v[154:155] op_sel_hi:[1,0,1]
	v_pk_fma_f32 v[152:153], v[28:29], s[2:3], v[152:153] op_sel_hi:[1,0,1]
	v_pk_fma_f32 v[150:151], v[30:31], s[2:3], v[150:151] op_sel_hi:[1,0,1]
	v_readlane_b32 s2, v211, 54
	s_waitcnt vmcnt(18)
	v_cvt_scalef32_pk32_f32_fp6 v[0:31], v[38:43], 1.0
	v_pk_fma_f32 v[38:39], v[0:1], s[2:3], v[50:51] op_sel_hi:[1,0,1]
	v_pk_fma_f32 v[40:41], v[2:3], s[2:3], v[52:53] op_sel_hi:[1,0,1]
	v_pk_fma_f32 v[42:43], v[4:5], s[2:3], v[54:55] op_sel_hi:[1,0,1]
	v_pk_fma_f32 v[50:51], v[6:7], s[2:3], v[62:63] op_sel_hi:[1,0,1]
	v_pk_fma_f32 v[52:53], v[8:9], s[2:3], v[64:65] op_sel_hi:[1,0,1]
	v_pk_fma_f32 v[54:55], v[10:11], s[2:3], v[66:67] op_sel_hi:[1,0,1]
	v_pk_fma_f32 v[62:63], v[12:13], s[2:3], v[164:165] op_sel_hi:[1,0,1]
	v_pk_fma_f32 v[64:65], v[14:15], s[2:3], v[166:167] op_sel_hi:[1,0,1]
	v_pk_fma_f32 v[66:67], v[16:17], s[2:3], v[168:169] op_sel_hi:[1,0,1]
	v_pk_fma_f32 v[162:163], v[18:19], s[2:3], v[162:163] op_sel_hi:[1,0,1]
	v_pk_fma_f32 v[160:161], v[20:21], s[2:3], v[160:161] op_sel_hi:[1,0,1]
	v_pk_fma_f32 v[158:159], v[22:23], s[2:3], v[158:159] op_sel_hi:[1,0,1]
	v_pk_fma_f32 v[156:157], v[24:25], s[2:3], v[156:157] op_sel_hi:[1,0,1]
	v_pk_fma_f32 v[154:155], v[26:27], s[2:3], v[154:155] op_sel_hi:[1,0,1]
	v_pk_fma_f32 v[152:153], v[28:29], s[2:3], v[152:153] op_sel_hi:[1,0,1]
	v_pk_fma_f32 v[150:151], v[30:31], s[2:3], v[150:151] op_sel_hi:[1,0,1]
	v_readlane_b32 s2, v211, 55
	s_waitcnt vmcnt(16)
	v_cvt_scalef32_pk32_f32_fp6 v[0:31], v[32:37], 1.0
	v_pk_fma_f32 v[164:165], v[0:1], s[2:3], v[38:39] op_sel_hi:[1,0,1]
	v_pk_fma_f32 v[166:167], v[2:3], s[2:3], v[40:41] op_sel_hi:[1,0,1]
	v_pk_fma_f32 v[168:169], v[4:5], s[2:3], v[42:43] op_sel_hi:[1,0,1]
	v_pk_fma_f32 v[170:171], v[6:7], s[2:3], v[50:51] op_sel_hi:[1,0,1]
	v_pk_fma_f32 v[172:173], v[8:9], s[2:3], v[52:53] op_sel_hi:[1,0,1]
	v_pk_fma_f32 v[174:175], v[10:11], s[2:3], v[54:55] op_sel_hi:[1,0,1]
	v_pk_fma_f32 v[176:177], v[12:13], s[2:3], v[62:63] op_sel_hi:[1,0,1]
	v_pk_fma_f32 v[178:179], v[14:15], s[2:3], v[64:65] op_sel_hi:[1,0,1]
	v_pk_fma_f32 v[180:181], v[16:17], s[2:3], v[66:67] op_sel_hi:[1,0,1]
	v_pk_fma_f32 v[162:163], v[18:19], s[2:3], v[162:163] op_sel_hi:[1,0,1]
	v_pk_fma_f32 v[160:161], v[20:21], s[2:3], v[160:161] op_sel_hi:[1,0,1]
	v_pk_fma_f32 v[158:159], v[22:23], s[2:3], v[158:159] op_sel_hi:[1,0,1]
	v_pk_fma_f32 v[156:157], v[24:25], s[2:3], v[156:157] op_sel_hi:[1,0,1]
	v_pk_fma_f32 v[154:155], v[26:27], s[2:3], v[154:155] op_sel_hi:[1,0,1]
	v_pk_fma_f32 v[152:153], v[28:29], s[2:3], v[152:153] op_sel_hi:[1,0,1]
	v_pk_fma_f32 v[150:151], v[30:31], s[2:3], v[150:151] op_sel_hi:[1,0,1]
	v_readlane_b32 s2, v241, 0
	v_readlane_b32 s3, v241, 1
	v_readlane_b32 s100, v241, 2
	v_readlane_b32 s101, v241, 3
	s_nop 1
	buffer_load_dwordx4 v[62:65], v129, s[44:47], s2 offen
	buffer_load_dwordx2 v[66:67], v210, s[44:47], s2 offen
	buffer_load_dwordx4 v[50:53], v129, s[44:47], s3 offen
	buffer_load_dwordx2 v[54:55], v210, s[44:47], s3 offen
	buffer_load_dwordx4 v[38:41], v129, s[44:47], s100 offen
	buffer_load_dwordx2 v[42:43], v210, s[44:47], s100 offen
	buffer_load_dwordx4 v[32:35], v129, s[44:47], s101 offen
	buffer_load_dwordx2 v[36:37], v210, s[44:47], s101 offen
	v_readlane_b32 s2, v211, 56
	s_waitcnt vmcnt(22)
	v_cvt_scalef32_pk32_f32_fp6 v[0:31], v[98:103], 1.0
	v_pk_fma_f32 v[98:99], v[0:1], s[2:3], v[164:165] op_sel_hi:[1,0,1]
	v_pk_fma_f32 v[100:101], v[2:3], s[2:3], v[166:167] op_sel_hi:[1,0,1]
	v_pk_fma_f32 v[102:103], v[4:5], s[2:3], v[168:169] op_sel_hi:[1,0,1]
	v_pk_fma_f32 v[164:165], v[6:7], s[2:3], v[170:171] op_sel_hi:[1,0,1]
	v_pk_fma_f32 v[166:167], v[8:9], s[2:3], v[172:173] op_sel_hi:[1,0,1]
	v_pk_fma_f32 v[168:169], v[10:11], s[2:3], v[174:175] op_sel_hi:[1,0,1]
	v_pk_fma_f32 v[170:171], v[12:13], s[2:3], v[176:177] op_sel_hi:[1,0,1]
	v_pk_fma_f32 v[172:173], v[14:15], s[2:3], v[178:179] op_sel_hi:[1,0,1]
	v_pk_fma_f32 v[174:175], v[16:17], s[2:3], v[180:181] op_sel_hi:[1,0,1]
	v_pk_fma_f32 v[162:163], v[18:19], s[2:3], v[162:163] op_sel_hi:[1,0,1]
	v_pk_fma_f32 v[160:161], v[20:21], s[2:3], v[160:161] op_sel_hi:[1,0,1]
	v_pk_fma_f32 v[158:159], v[22:23], s[2:3], v[158:159] op_sel_hi:[1,0,1]
	v_pk_fma_f32 v[156:157], v[24:25], s[2:3], v[156:157] op_sel_hi:[1,0,1]
	v_pk_fma_f32 v[154:155], v[26:27], s[2:3], v[154:155] op_sel_hi:[1,0,1]
	v_pk_fma_f32 v[152:153], v[28:29], s[2:3], v[152:153] op_sel_hi:[1,0,1]
	v_pk_fma_f32 v[150:151], v[30:31], s[2:3], v[150:151] op_sel_hi:[1,0,1]
	v_readlane_b32 s2, v211, 57
	s_waitcnt vmcnt(20)
	v_cvt_scalef32_pk32_f32_fp6 v[0:31], v[92:97], 1.0
	v_pk_fma_f32 v[92:93], v[0:1], s[2:3], v[98:99] op_sel_hi:[1,0,1]
	v_pk_fma_f32 v[94:95], v[2:3], s[2:3], v[100:101] op_sel_hi:[1,0,1]
	v_pk_fma_f32 v[96:97], v[4:5], s[2:3], v[102:103] op_sel_hi:[1,0,1]
	v_pk_fma_f32 v[98:99], v[6:7], s[2:3], v[164:165] op_sel_hi:[1,0,1]
	v_pk_fma_f32 v[100:101], v[8:9], s[2:3], v[166:167] op_sel_hi:[1,0,1]
	v_pk_fma_f32 v[102:103], v[10:11], s[2:3], v[168:169] op_sel_hi:[1,0,1]
	v_pk_fma_f32 v[164:165], v[12:13], s[2:3], v[170:171] op_sel_hi:[1,0,1]
	v_pk_fma_f32 v[166:167], v[14:15], s[2:3], v[172:173] op_sel_hi:[1,0,1]
	v_pk_fma_f32 v[168:169], v[16:17], s[2:3], v[174:175] op_sel_hi:[1,0,1]
	v_pk_fma_f32 v[162:163], v[18:19], s[2:3], v[162:163] op_sel_hi:[1,0,1]
	v_pk_fma_f32 v[160:161], v[20:21], s[2:3], v[160:161] op_sel_hi:[1,0,1]
	v_pk_fma_f32 v[158:159], v[22:23], s[2:3], v[158:159] op_sel_hi:[1,0,1]
	v_pk_fma_f32 v[156:157], v[24:25], s[2:3], v[156:157] op_sel_hi:[1,0,1]
	v_pk_fma_f32 v[154:155], v[26:27], s[2:3], v[154:155] op_sel_hi:[1,0,1]
	v_pk_fma_f32 v[152:153], v[28:29], s[2:3], v[152:153] op_sel_hi:[1,0,1]
	v_pk_fma_f32 v[150:151], v[30:31], s[2:3], v[150:151] op_sel_hi:[1,0,1]
	v_readlane_b32 s2, v211, 58
	s_waitcnt vmcnt(18)
	v_cvt_scalef32_pk32_f32_fp6 v[0:31], v[86:91], 1.0
	v_pk_fma_f32 v[86:87], v[0:1], s[2:3], v[92:93] op_sel_hi:[1,0,1]
	v_pk_fma_f32 v[88:89], v[2:3], s[2:3], v[94:95] op_sel_hi:[1,0,1]
	v_pk_fma_f32 v[90:91], v[4:5], s[2:3], v[96:97] op_sel_hi:[1,0,1]
	v_pk_fma_f32 v[92:93], v[6:7], s[2:3], v[98:99] op_sel_hi:[1,0,1]
	v_pk_fma_f32 v[94:95], v[8:9], s[2:3], v[100:101] op_sel_hi:[1,0,1]
	v_pk_fma_f32 v[96:97], v[10:11], s[2:3], v[102:103] op_sel_hi:[1,0,1]
	v_pk_fma_f32 v[98:99], v[12:13], s[2:3], v[164:165] op_sel_hi:[1,0,1]
	v_pk_fma_f32 v[100:101], v[14:15], s[2:3], v[166:167] op_sel_hi:[1,0,1]
	v_pk_fma_f32 v[102:103], v[16:17], s[2:3], v[168:169] op_sel_hi:[1,0,1]
	v_pk_fma_f32 v[162:163], v[18:19], s[2:3], v[162:163] op_sel_hi:[1,0,1]
	v_pk_fma_f32 v[160:161], v[20:21], s[2:3], v[160:161] op_sel_hi:[1,0,1]
	v_pk_fma_f32 v[158:159], v[22:23], s[2:3], v[158:159] op_sel_hi:[1,0,1]
	v_pk_fma_f32 v[156:157], v[24:25], s[2:3], v[156:157] op_sel_hi:[1,0,1]
	v_pk_fma_f32 v[154:155], v[26:27], s[2:3], v[154:155] op_sel_hi:[1,0,1]
	v_pk_fma_f32 v[152:153], v[28:29], s[2:3], v[152:153] op_sel_hi:[1,0,1]
	v_pk_fma_f32 v[150:151], v[30:31], s[2:3], v[150:151] op_sel_hi:[1,0,1]
	v_readlane_b32 s2, v211, 59
	s_waitcnt vmcnt(16)
	v_cvt_scalef32_pk32_f32_fp6 v[0:31], v[80:85], 1.0
	v_pk_fma_f32 v[180:181], v[0:1], s[2:3], v[86:87] op_sel_hi:[1,0,1]
	v_pk_fma_f32 v[178:179], v[2:3], s[2:3], v[88:89] op_sel_hi:[1,0,1]
	v_pk_fma_f32 v[176:177], v[4:5], s[2:3], v[90:91] op_sel_hi:[1,0,1]
	v_pk_fma_f32 v[174:175], v[6:7], s[2:3], v[92:93] op_sel_hi:[1,0,1]
	v_pk_fma_f32 v[172:173], v[8:9], s[2:3], v[94:95] op_sel_hi:[1,0,1]
	v_pk_fma_f32 v[170:171], v[10:11], s[2:3], v[96:97] op_sel_hi:[1,0,1]
	v_pk_fma_f32 v[168:169], v[12:13], s[2:3], v[98:99] op_sel_hi:[1,0,1]
	v_pk_fma_f32 v[166:167], v[14:15], s[2:3], v[100:101] op_sel_hi:[1,0,1]
	v_pk_fma_f32 v[164:165], v[16:17], s[2:3], v[102:103] op_sel_hi:[1,0,1]
	v_pk_fma_f32 v[162:163], v[18:19], s[2:3], v[162:163] op_sel_hi:[1,0,1]
	v_pk_fma_f32 v[160:161], v[20:21], s[2:3], v[160:161] op_sel_hi:[1,0,1]
	v_pk_fma_f32 v[158:159], v[22:23], s[2:3], v[158:159] op_sel_hi:[1,0,1]
	v_pk_fma_f32 v[156:157], v[24:25], s[2:3], v[156:157] op_sel_hi:[1,0,1]
	v_pk_fma_f32 v[154:155], v[26:27], s[2:3], v[154:155] op_sel_hi:[1,0,1]
	v_pk_fma_f32 v[152:153], v[28:29], s[2:3], v[152:153] op_sel_hi:[1,0,1]
	v_pk_fma_f32 v[150:151], v[30:31], s[2:3], v[150:151] op_sel_hi:[1,0,1]
	v_readlane_b32 s2, v241, 4
	v_readlane_b32 s3, v241, 5
	v_readlane_b32 s100, v241, 6
	v_readlane_b32 s101, v241, 7
	s_nop 1
	buffer_load_dwordx4 v[98:101], v129, s[44:47], s2 offen
	buffer_load_dwordx2 v[102:103], v210, s[44:47], s2 offen
	buffer_load_dwordx4 v[92:95], v129, s[44:47], s3 offen
	buffer_load_dwordx2 v[96:97], v210, s[44:47], s3 offen
	buffer_load_dwordx4 v[86:89], v129, s[44:47], s100 offen
	buffer_load_dwordx2 v[90:91], v210, s[44:47], s100 offen
	buffer_load_dwordx4 v[80:83], v129, s[44:47], s101 offen
	buffer_load_dwordx2 v[84:85], v210, s[44:47], s101 offen
	v_readlane_b32 s2, v211, 60
	s_waitcnt vmcnt(22)
	v_cvt_scalef32_pk32_f32_fp6 v[0:31], v[74:79], 1.0
	v_pk_fma_f32 v[74:75], v[0:1], s[2:3], v[180:181] op_sel_hi:[1,0,1]
	v_pk_fma_f32 v[76:77], v[2:3], s[2:3], v[178:179] op_sel_hi:[1,0,1]
	v_pk_fma_f32 v[78:79], v[4:5], s[2:3], v[176:177] op_sel_hi:[1,0,1]
	v_pk_fma_f32 v[174:175], v[6:7], s[2:3], v[174:175] op_sel_hi:[1,0,1]
	v_pk_fma_f32 v[172:173], v[8:9], s[2:3], v[172:173] op_sel_hi:[1,0,1]
	v_pk_fma_f32 v[170:171], v[10:11], s[2:3], v[170:171] op_sel_hi:[1,0,1]
	v_pk_fma_f32 v[168:169], v[12:13], s[2:3], v[168:169] op_sel_hi:[1,0,1]
	v_pk_fma_f32 v[166:167], v[14:15], s[2:3], v[166:167] op_sel_hi:[1,0,1]
	v_pk_fma_f32 v[164:165], v[16:17], s[2:3], v[164:165] op_sel_hi:[1,0,1]
	v_pk_fma_f32 v[162:163], v[18:19], s[2:3], v[162:163] op_sel_hi:[1,0,1]
	v_pk_fma_f32 v[160:161], v[20:21], s[2:3], v[160:161] op_sel_hi:[1,0,1]
	v_pk_fma_f32 v[158:159], v[22:23], s[2:3], v[158:159] op_sel_hi:[1,0,1]
	v_pk_fma_f32 v[156:157], v[24:25], s[2:3], v[156:157] op_sel_hi:[1,0,1]
	v_pk_fma_f32 v[154:155], v[26:27], s[2:3], v[154:155] op_sel_hi:[1,0,1]
	v_pk_fma_f32 v[152:153], v[28:29], s[2:3], v[152:153] op_sel_hi:[1,0,1]
	v_pk_fma_f32 v[150:151], v[30:31], s[2:3], v[150:151] op_sel_hi:[1,0,1]
	v_readlane_b32 s2, v211, 61
	s_waitcnt vmcnt(20)
	v_cvt_scalef32_pk32_f32_fp6 v[0:31], v[68:73], 1.0
	v_pk_fma_f32 v[68:69], v[0:1], s[2:3], v[74:75] op_sel_hi:[1,0,1]
	v_pk_fma_f32 v[70:71], v[2:3], s[2:3], v[76:77] op_sel_hi:[1,0,1]
	v_pk_fma_f32 v[72:73], v[4:5], s[2:3], v[78:79] op_sel_hi:[1,0,1]
	v_pk_fma_f32 v[74:75], v[6:7], s[2:3], v[174:175] op_sel_hi:[1,0,1]
	v_pk_fma_f32 v[76:77], v[8:9], s[2:3], v[172:173] op_sel_hi:[1,0,1]
	v_pk_fma_f32 v[78:79], v[10:11], s[2:3], v[170:171] op_sel_hi:[1,0,1]
	v_pk_fma_f32 v[168:169], v[12:13], s[2:3], v[168:169] op_sel_hi:[1,0,1]
	v_pk_fma_f32 v[166:167], v[14:15], s[2:3], v[166:167] op_sel_hi:[1,0,1]
	v_pk_fma_f32 v[164:165], v[16:17], s[2:3], v[164:165] op_sel_hi:[1,0,1]
	v_pk_fma_f32 v[162:163], v[18:19], s[2:3], v[162:163] op_sel_hi:[1,0,1]
	v_pk_fma_f32 v[160:161], v[20:21], s[2:3], v[160:161] op_sel_hi:[1,0,1]
	v_pk_fma_f32 v[158:159], v[22:23], s[2:3], v[158:159] op_sel_hi:[1,0,1]
	v_pk_fma_f32 v[156:157], v[24:25], s[2:3], v[156:157] op_sel_hi:[1,0,1]
	v_pk_fma_f32 v[154:155], v[26:27], s[2:3], v[154:155] op_sel_hi:[1,0,1]
	v_pk_fma_f32 v[152:153], v[28:29], s[2:3], v[152:153] op_sel_hi:[1,0,1]
	v_pk_fma_f32 v[150:151], v[30:31], s[2:3], v[150:151] op_sel_hi:[1,0,1]
	v_readlane_b32 s2, v211, 62
	s_waitcnt vmcnt(18)
	v_cvt_scalef32_pk32_f32_fp6 v[0:31], v[56:61], 1.0
	v_pk_fma_f32 v[56:57], v[0:1], s[2:3], v[68:69] op_sel_hi:[1,0,1]
	v_pk_fma_f32 v[58:59], v[2:3], s[2:3], v[70:71] op_sel_hi:[1,0,1]
	v_pk_fma_f32 v[60:61], v[4:5], s[2:3], v[72:73] op_sel_hi:[1,0,1]
	v_pk_fma_f32 v[68:69], v[6:7], s[2:3], v[74:75] op_sel_hi:[1,0,1]
	v_pk_fma_f32 v[70:71], v[8:9], s[2:3], v[76:77] op_sel_hi:[1,0,1]
	v_pk_fma_f32 v[72:73], v[10:11], s[2:3], v[78:79] op_sel_hi:[1,0,1]
	v_pk_fma_f32 v[74:75], v[12:13], s[2:3], v[168:169] op_sel_hi:[1,0,1]
	v_pk_fma_f32 v[76:77], v[14:15], s[2:3], v[166:167] op_sel_hi:[1,0,1]
	v_pk_fma_f32 v[78:79], v[16:17], s[2:3], v[164:165] op_sel_hi:[1,0,1]
	v_pk_fma_f32 v[162:163], v[18:19], s[2:3], v[162:163] op_sel_hi:[1,0,1]
	v_pk_fma_f32 v[160:161], v[20:21], s[2:3], v[160:161] op_sel_hi:[1,0,1]
	v_pk_fma_f32 v[158:159], v[22:23], s[2:3], v[158:159] op_sel_hi:[1,0,1]
	v_pk_fma_f32 v[156:157], v[24:25], s[2:3], v[156:157] op_sel_hi:[1,0,1]
	v_pk_fma_f32 v[154:155], v[26:27], s[2:3], v[154:155] op_sel_hi:[1,0,1]
	v_pk_fma_f32 v[152:153], v[28:29], s[2:3], v[152:153] op_sel_hi:[1,0,1]
	v_pk_fma_f32 v[150:151], v[30:31], s[2:3], v[150:151] op_sel_hi:[1,0,1]
	v_readlane_b32 s2, v211, 63
	s_waitcnt vmcnt(16)
	v_cvt_scalef32_pk32_f32_fp6 v[0:31], v[44:49], 1.0
	v_pk_fma_f32 v[164:165], v[0:1], s[2:3], v[56:57] op_sel_hi:[1,0,1]
	v_pk_fma_f32 v[166:167], v[2:3], s[2:3], v[58:59] op_sel_hi:[1,0,1]
	v_pk_fma_f32 v[168:169], v[4:5], s[2:3], v[60:61] op_sel_hi:[1,0,1]
	v_pk_fma_f32 v[170:171], v[6:7], s[2:3], v[68:69] op_sel_hi:[1,0,1]
	v_pk_fma_f32 v[172:173], v[8:9], s[2:3], v[70:71] op_sel_hi:[1,0,1]
	v_pk_fma_f32 v[174:175], v[10:11], s[2:3], v[72:73] op_sel_hi:[1,0,1]
	v_pk_fma_f32 v[176:177], v[12:13], s[2:3], v[74:75] op_sel_hi:[1,0,1]
	v_pk_fma_f32 v[178:179], v[14:15], s[2:3], v[76:77] op_sel_hi:[1,0,1]
	v_pk_fma_f32 v[180:181], v[16:17], s[2:3], v[78:79] op_sel_hi:[1,0,1]
	v_pk_fma_f32 v[162:163], v[18:19], s[2:3], v[162:163] op_sel_hi:[1,0,1]
	v_pk_fma_f32 v[160:161], v[20:21], s[2:3], v[160:161] op_sel_hi:[1,0,1]
	v_pk_fma_f32 v[158:159], v[22:23], s[2:3], v[158:159] op_sel_hi:[1,0,1]
	v_pk_fma_f32 v[156:157], v[24:25], s[2:3], v[156:157] op_sel_hi:[1,0,1]
	v_pk_fma_f32 v[154:155], v[26:27], s[2:3], v[154:155] op_sel_hi:[1,0,1]
	v_pk_fma_f32 v[152:153], v[28:29], s[2:3], v[152:153] op_sel_hi:[1,0,1]
	v_pk_fma_f32 v[150:151], v[30:31], s[2:3], v[150:151] op_sel_hi:[1,0,1]
	v_readlane_b32 s2, v241, 8
	v_readlane_b32 s3, v241, 9
	v_readlane_b32 s100, v241, 10
	v_readlane_b32 s101, v241, 11
	s_nop 1
	buffer_load_dwordx4 v[74:77], v129, s[44:47], s2 offen
	buffer_load_dwordx2 v[78:79], v210, s[44:47], s2 offen
	buffer_load_dwordx4 v[68:71], v129, s[44:47], s3 offen
	buffer_load_dwordx2 v[72:73], v210, s[44:47], s3 offen
	buffer_load_dwordx4 v[56:59], v129, s[44:47], s100 offen
	buffer_load_dwordx2 v[60:61], v210, s[44:47], s100 offen
	buffer_load_dwordx4 v[44:47], v129, s[44:47], s101 offen
	buffer_load_dwordx2 v[48:49], v210, s[44:47], s101 offen
	v_readlane_b32 s2, v131, 0
	s_waitcnt vmcnt(22)
	v_cvt_scalef32_pk32_f32_fp6 v[0:31], v[62:67], 1.0
	v_pk_fma_f32 v[62:63], v[0:1], s[2:3], v[164:165] op_sel_hi:[1,0,1]
	v_pk_fma_f32 v[64:65], v[2:3], s[2:3], v[166:167] op_sel_hi:[1,0,1]
	v_pk_fma_f32 v[66:67], v[4:5], s[2:3], v[168:169] op_sel_hi:[1,0,1]
	v_pk_fma_f32 v[164:165], v[6:7], s[2:3], v[170:171] op_sel_hi:[1,0,1]
	v_pk_fma_f32 v[166:167], v[8:9], s[2:3], v[172:173] op_sel_hi:[1,0,1]
	v_pk_fma_f32 v[168:169], v[10:11], s[2:3], v[174:175] op_sel_hi:[1,0,1]
	v_pk_fma_f32 v[170:171], v[12:13], s[2:3], v[176:177] op_sel_hi:[1,0,1]
	v_pk_fma_f32 v[172:173], v[14:15], s[2:3], v[178:179] op_sel_hi:[1,0,1]
	v_pk_fma_f32 v[174:175], v[16:17], s[2:3], v[180:181] op_sel_hi:[1,0,1]
	v_pk_fma_f32 v[162:163], v[18:19], s[2:3], v[162:163] op_sel_hi:[1,0,1]
	v_pk_fma_f32 v[160:161], v[20:21], s[2:3], v[160:161] op_sel_hi:[1,0,1]
	v_pk_fma_f32 v[158:159], v[22:23], s[2:3], v[158:159] op_sel_hi:[1,0,1]
	v_pk_fma_f32 v[156:157], v[24:25], s[2:3], v[156:157] op_sel_hi:[1,0,1]
	v_pk_fma_f32 v[154:155], v[26:27], s[2:3], v[154:155] op_sel_hi:[1,0,1]
	v_pk_fma_f32 v[152:153], v[28:29], s[2:3], v[152:153] op_sel_hi:[1,0,1]
	v_pk_fma_f32 v[150:151], v[30:31], s[2:3], v[150:151] op_sel_hi:[1,0,1]
	v_readlane_b32 s2, v131, 1
	s_waitcnt vmcnt(20)
	v_cvt_scalef32_pk32_f32_fp6 v[0:31], v[50:55], 1.0
	v_pk_fma_f32 v[50:51], v[0:1], s[2:3], v[62:63] op_sel_hi:[1,0,1]
	v_pk_fma_f32 v[52:53], v[2:3], s[2:3], v[64:65] op_sel_hi:[1,0,1]
	v_pk_fma_f32 v[54:55], v[4:5], s[2:3], v[66:67] op_sel_hi:[1,0,1]
	v_pk_fma_f32 v[62:63], v[6:7], s[2:3], v[164:165] op_sel_hi:[1,0,1]
	v_pk_fma_f32 v[64:65], v[8:9], s[2:3], v[166:167] op_sel_hi:[1,0,1]
	v_pk_fma_f32 v[66:67], v[10:11], s[2:3], v[168:169] op_sel_hi:[1,0,1]
	v_pk_fma_f32 v[164:165], v[12:13], s[2:3], v[170:171] op_sel_hi:[1,0,1]
	v_pk_fma_f32 v[166:167], v[14:15], s[2:3], v[172:173] op_sel_hi:[1,0,1]
	v_pk_fma_f32 v[168:169], v[16:17], s[2:3], v[174:175] op_sel_hi:[1,0,1]
	v_pk_fma_f32 v[162:163], v[18:19], s[2:3], v[162:163] op_sel_hi:[1,0,1]
	v_pk_fma_f32 v[160:161], v[20:21], s[2:3], v[160:161] op_sel_hi:[1,0,1]
	v_pk_fma_f32 v[158:159], v[22:23], s[2:3], v[158:159] op_sel_hi:[1,0,1]
	v_pk_fma_f32 v[156:157], v[24:25], s[2:3], v[156:157] op_sel_hi:[1,0,1]
	v_pk_fma_f32 v[154:155], v[26:27], s[2:3], v[154:155] op_sel_hi:[1,0,1]
	v_pk_fma_f32 v[152:153], v[28:29], s[2:3], v[152:153] op_sel_hi:[1,0,1]
	v_pk_fma_f32 v[150:151], v[30:31], s[2:3], v[150:151] op_sel_hi:[1,0,1]
	v_readlane_b32 s2, v131, 2
	s_waitcnt vmcnt(18)
	v_cvt_scalef32_pk32_f32_fp6 v[0:31], v[38:43], 1.0
	v_pk_fma_f32 v[38:39], v[0:1], s[2:3], v[50:51] op_sel_hi:[1,0,1]
	v_pk_fma_f32 v[40:41], v[2:3], s[2:3], v[52:53] op_sel_hi:[1,0,1]
	v_pk_fma_f32 v[42:43], v[4:5], s[2:3], v[54:55] op_sel_hi:[1,0,1]
	v_pk_fma_f32 v[50:51], v[6:7], s[2:3], v[62:63] op_sel_hi:[1,0,1]
	v_pk_fma_f32 v[52:53], v[8:9], s[2:3], v[64:65] op_sel_hi:[1,0,1]
	v_pk_fma_f32 v[54:55], v[10:11], s[2:3], v[66:67] op_sel_hi:[1,0,1]
	v_pk_fma_f32 v[62:63], v[12:13], s[2:3], v[164:165] op_sel_hi:[1,0,1]
	v_pk_fma_f32 v[64:65], v[14:15], s[2:3], v[166:167] op_sel_hi:[1,0,1]
	v_pk_fma_f32 v[66:67], v[16:17], s[2:3], v[168:169] op_sel_hi:[1,0,1]
	v_pk_fma_f32 v[162:163], v[18:19], s[2:3], v[162:163] op_sel_hi:[1,0,1]
	v_pk_fma_f32 v[160:161], v[20:21], s[2:3], v[160:161] op_sel_hi:[1,0,1]
	v_pk_fma_f32 v[158:159], v[22:23], s[2:3], v[158:159] op_sel_hi:[1,0,1]
	v_pk_fma_f32 v[156:157], v[24:25], s[2:3], v[156:157] op_sel_hi:[1,0,1]
	v_pk_fma_f32 v[154:155], v[26:27], s[2:3], v[154:155] op_sel_hi:[1,0,1]
	v_pk_fma_f32 v[152:153], v[28:29], s[2:3], v[152:153] op_sel_hi:[1,0,1]
	v_pk_fma_f32 v[150:151], v[30:31], s[2:3], v[150:151] op_sel_hi:[1,0,1]
	v_readlane_b32 s2, v131, 3
	s_waitcnt vmcnt(16)
	v_cvt_scalef32_pk32_f32_fp6 v[0:31], v[32:37], 1.0
	v_pk_fma_f32 v[164:165], v[0:1], s[2:3], v[38:39] op_sel_hi:[1,0,1]
	v_pk_fma_f32 v[166:167], v[2:3], s[2:3], v[40:41] op_sel_hi:[1,0,1]
	v_pk_fma_f32 v[168:169], v[4:5], s[2:3], v[42:43] op_sel_hi:[1,0,1]
	v_pk_fma_f32 v[170:171], v[6:7], s[2:3], v[50:51] op_sel_hi:[1,0,1]
	v_pk_fma_f32 v[172:173], v[8:9], s[2:3], v[52:53] op_sel_hi:[1,0,1]
	v_pk_fma_f32 v[174:175], v[10:11], s[2:3], v[54:55] op_sel_hi:[1,0,1]
	v_pk_fma_f32 v[176:177], v[12:13], s[2:3], v[62:63] op_sel_hi:[1,0,1]
	v_pk_fma_f32 v[178:179], v[14:15], s[2:3], v[64:65] op_sel_hi:[1,0,1]
	v_pk_fma_f32 v[180:181], v[16:17], s[2:3], v[66:67] op_sel_hi:[1,0,1]
	v_pk_fma_f32 v[162:163], v[18:19], s[2:3], v[162:163] op_sel_hi:[1,0,1]
	v_pk_fma_f32 v[160:161], v[20:21], s[2:3], v[160:161] op_sel_hi:[1,0,1]
	v_pk_fma_f32 v[158:159], v[22:23], s[2:3], v[158:159] op_sel_hi:[1,0,1]
	v_pk_fma_f32 v[156:157], v[24:25], s[2:3], v[156:157] op_sel_hi:[1,0,1]
	v_pk_fma_f32 v[154:155], v[26:27], s[2:3], v[154:155] op_sel_hi:[1,0,1]
	v_pk_fma_f32 v[152:153], v[28:29], s[2:3], v[152:153] op_sel_hi:[1,0,1]
	v_pk_fma_f32 v[150:151], v[30:31], s[2:3], v[150:151] op_sel_hi:[1,0,1]
	v_readlane_b32 s2, v241, 12
	v_readlane_b32 s3, v241, 13
	v_readlane_b32 s100, v241, 14
	v_readlane_b32 s101, v241, 15
	s_nop 1
	buffer_load_dwordx4 v[62:65], v129, s[44:47], s2 offen
	buffer_load_dwordx2 v[66:67], v210, s[44:47], s2 offen
	buffer_load_dwordx4 v[50:53], v129, s[44:47], s3 offen
	buffer_load_dwordx2 v[54:55], v210, s[44:47], s3 offen
	buffer_load_dwordx4 v[38:41], v129, s[44:47], s100 offen
	buffer_load_dwordx2 v[42:43], v210, s[44:47], s100 offen
	buffer_load_dwordx4 v[32:35], v129, s[44:47], s101 offen
	buffer_load_dwordx2 v[36:37], v210, s[44:47], s101 offen
	v_readlane_b32 s2, v131, 4
	s_waitcnt vmcnt(22)
	v_cvt_scalef32_pk32_f32_fp6 v[0:31], v[98:103], 1.0
	v_pk_fma_f32 v[98:99], v[0:1], s[2:3], v[164:165] op_sel_hi:[1,0,1]
	v_pk_fma_f32 v[100:101], v[2:3], s[2:3], v[166:167] op_sel_hi:[1,0,1]
	v_pk_fma_f32 v[102:103], v[4:5], s[2:3], v[168:169] op_sel_hi:[1,0,1]
	v_pk_fma_f32 v[164:165], v[6:7], s[2:3], v[170:171] op_sel_hi:[1,0,1]
	v_pk_fma_f32 v[166:167], v[8:9], s[2:3], v[172:173] op_sel_hi:[1,0,1]
	v_pk_fma_f32 v[168:169], v[10:11], s[2:3], v[174:175] op_sel_hi:[1,0,1]
	v_pk_fma_f32 v[170:171], v[12:13], s[2:3], v[176:177] op_sel_hi:[1,0,1]
	v_pk_fma_f32 v[172:173], v[14:15], s[2:3], v[178:179] op_sel_hi:[1,0,1]
	v_pk_fma_f32 v[174:175], v[16:17], s[2:3], v[180:181] op_sel_hi:[1,0,1]
	v_pk_fma_f32 v[162:163], v[18:19], s[2:3], v[162:163] op_sel_hi:[1,0,1]
	v_pk_fma_f32 v[160:161], v[20:21], s[2:3], v[160:161] op_sel_hi:[1,0,1]
	v_pk_fma_f32 v[158:159], v[22:23], s[2:3], v[158:159] op_sel_hi:[1,0,1]
	v_pk_fma_f32 v[156:157], v[24:25], s[2:3], v[156:157] op_sel_hi:[1,0,1]
	v_pk_fma_f32 v[154:155], v[26:27], s[2:3], v[154:155] op_sel_hi:[1,0,1]
	v_pk_fma_f32 v[152:153], v[28:29], s[2:3], v[152:153] op_sel_hi:[1,0,1]
	v_pk_fma_f32 v[150:151], v[30:31], s[2:3], v[150:151] op_sel_hi:[1,0,1]
	v_readlane_b32 s2, v131, 5
	s_waitcnt vmcnt(20)
	v_cvt_scalef32_pk32_f32_fp6 v[0:31], v[92:97], 1.0
	v_pk_fma_f32 v[92:93], v[0:1], s[2:3], v[98:99] op_sel_hi:[1,0,1]
	v_pk_fma_f32 v[94:95], v[2:3], s[2:3], v[100:101] op_sel_hi:[1,0,1]
	v_pk_fma_f32 v[96:97], v[4:5], s[2:3], v[102:103] op_sel_hi:[1,0,1]
	v_pk_fma_f32 v[98:99], v[6:7], s[2:3], v[164:165] op_sel_hi:[1,0,1]
	v_pk_fma_f32 v[100:101], v[8:9], s[2:3], v[166:167] op_sel_hi:[1,0,1]
	v_pk_fma_f32 v[102:103], v[10:11], s[2:3], v[168:169] op_sel_hi:[1,0,1]
	v_pk_fma_f32 v[164:165], v[12:13], s[2:3], v[170:171] op_sel_hi:[1,0,1]
	v_pk_fma_f32 v[166:167], v[14:15], s[2:3], v[172:173] op_sel_hi:[1,0,1]
	v_pk_fma_f32 v[168:169], v[16:17], s[2:3], v[174:175] op_sel_hi:[1,0,1]
	v_pk_fma_f32 v[162:163], v[18:19], s[2:3], v[162:163] op_sel_hi:[1,0,1]
	v_pk_fma_f32 v[160:161], v[20:21], s[2:3], v[160:161] op_sel_hi:[1,0,1]
	v_pk_fma_f32 v[158:159], v[22:23], s[2:3], v[158:159] op_sel_hi:[1,0,1]
	v_pk_fma_f32 v[156:157], v[24:25], s[2:3], v[156:157] op_sel_hi:[1,0,1]
	v_pk_fma_f32 v[154:155], v[26:27], s[2:3], v[154:155] op_sel_hi:[1,0,1]
	v_pk_fma_f32 v[152:153], v[28:29], s[2:3], v[152:153] op_sel_hi:[1,0,1]
	v_pk_fma_f32 v[150:151], v[30:31], s[2:3], v[150:151] op_sel_hi:[1,0,1]
	v_readlane_b32 s2, v131, 6
	s_waitcnt vmcnt(18)
	v_cvt_scalef32_pk32_f32_fp6 v[0:31], v[86:91], 1.0
	v_pk_fma_f32 v[86:87], v[0:1], s[2:3], v[92:93] op_sel_hi:[1,0,1]
	v_pk_fma_f32 v[88:89], v[2:3], s[2:3], v[94:95] op_sel_hi:[1,0,1]
	v_pk_fma_f32 v[90:91], v[4:5], s[2:3], v[96:97] op_sel_hi:[1,0,1]
	v_pk_fma_f32 v[92:93], v[6:7], s[2:3], v[98:99] op_sel_hi:[1,0,1]
	v_pk_fma_f32 v[94:95], v[8:9], s[2:3], v[100:101] op_sel_hi:[1,0,1]
	v_pk_fma_f32 v[96:97], v[10:11], s[2:3], v[102:103] op_sel_hi:[1,0,1]
	v_pk_fma_f32 v[98:99], v[12:13], s[2:3], v[164:165] op_sel_hi:[1,0,1]
	v_pk_fma_f32 v[100:101], v[14:15], s[2:3], v[166:167] op_sel_hi:[1,0,1]
	v_pk_fma_f32 v[102:103], v[16:17], s[2:3], v[168:169] op_sel_hi:[1,0,1]
	v_pk_fma_f32 v[162:163], v[18:19], s[2:3], v[162:163] op_sel_hi:[1,0,1]
	v_pk_fma_f32 v[160:161], v[20:21], s[2:3], v[160:161] op_sel_hi:[1,0,1]
	v_pk_fma_f32 v[158:159], v[22:23], s[2:3], v[158:159] op_sel_hi:[1,0,1]
	v_pk_fma_f32 v[156:157], v[24:25], s[2:3], v[156:157] op_sel_hi:[1,0,1]
	v_pk_fma_f32 v[154:155], v[26:27], s[2:3], v[154:155] op_sel_hi:[1,0,1]
	v_pk_fma_f32 v[152:153], v[28:29], s[2:3], v[152:153] op_sel_hi:[1,0,1]
	v_pk_fma_f32 v[150:151], v[30:31], s[2:3], v[150:151] op_sel_hi:[1,0,1]
	v_readlane_b32 s2, v131, 7
	s_waitcnt vmcnt(16)
	v_cvt_scalef32_pk32_f32_fp6 v[0:31], v[80:85], 1.0
	v_pk_fma_f32 v[180:181], v[0:1], s[2:3], v[86:87] op_sel_hi:[1,0,1]
	v_pk_fma_f32 v[178:179], v[2:3], s[2:3], v[88:89] op_sel_hi:[1,0,1]
	v_pk_fma_f32 v[176:177], v[4:5], s[2:3], v[90:91] op_sel_hi:[1,0,1]
	v_pk_fma_f32 v[174:175], v[6:7], s[2:3], v[92:93] op_sel_hi:[1,0,1]
	v_pk_fma_f32 v[172:173], v[8:9], s[2:3], v[94:95] op_sel_hi:[1,0,1]
	v_pk_fma_f32 v[170:171], v[10:11], s[2:3], v[96:97] op_sel_hi:[1,0,1]
	v_pk_fma_f32 v[168:169], v[12:13], s[2:3], v[98:99] op_sel_hi:[1,0,1]
	v_pk_fma_f32 v[166:167], v[14:15], s[2:3], v[100:101] op_sel_hi:[1,0,1]
	v_pk_fma_f32 v[164:165], v[16:17], s[2:3], v[102:103] op_sel_hi:[1,0,1]
	v_pk_fma_f32 v[162:163], v[18:19], s[2:3], v[162:163] op_sel_hi:[1,0,1]
	v_pk_fma_f32 v[160:161], v[20:21], s[2:3], v[160:161] op_sel_hi:[1,0,1]
	v_pk_fma_f32 v[158:159], v[22:23], s[2:3], v[158:159] op_sel_hi:[1,0,1]
	v_pk_fma_f32 v[156:157], v[24:25], s[2:3], v[156:157] op_sel_hi:[1,0,1]
	v_pk_fma_f32 v[154:155], v[26:27], s[2:3], v[154:155] op_sel_hi:[1,0,1]
	v_pk_fma_f32 v[152:153], v[28:29], s[2:3], v[152:153] op_sel_hi:[1,0,1]
	v_pk_fma_f32 v[150:151], v[30:31], s[2:3], v[150:151] op_sel_hi:[1,0,1]
	v_readlane_b32 s2, v241, 16
	v_readlane_b32 s3, v241, 17
	v_readlane_b32 s100, v241, 18
	v_readlane_b32 s101, v241, 19
	s_nop 1
	buffer_load_dwordx4 v[98:101], v129, s[44:47], s2 offen
	buffer_load_dwordx2 v[102:103], v210, s[44:47], s2 offen
	buffer_load_dwordx4 v[92:95], v129, s[44:47], s3 offen
	buffer_load_dwordx2 v[96:97], v210, s[44:47], s3 offen
	buffer_load_dwordx4 v[86:89], v129, s[44:47], s100 offen
	buffer_load_dwordx2 v[90:91], v210, s[44:47], s100 offen
	buffer_load_dwordx4 v[80:83], v129, s[44:47], s101 offen
	buffer_load_dwordx2 v[84:85], v210, s[44:47], s101 offen
	v_readlane_b32 s2, v131, 8
	s_waitcnt vmcnt(22)
	v_cvt_scalef32_pk32_f32_fp6 v[0:31], v[74:79], 1.0
	v_pk_fma_f32 v[74:75], v[0:1], s[2:3], v[180:181] op_sel_hi:[1,0,1]
	v_pk_fma_f32 v[76:77], v[2:3], s[2:3], v[178:179] op_sel_hi:[1,0,1]
	v_pk_fma_f32 v[78:79], v[4:5], s[2:3], v[176:177] op_sel_hi:[1,0,1]
	v_pk_fma_f32 v[174:175], v[6:7], s[2:3], v[174:175] op_sel_hi:[1,0,1]
	v_pk_fma_f32 v[172:173], v[8:9], s[2:3], v[172:173] op_sel_hi:[1,0,1]
	v_pk_fma_f32 v[170:171], v[10:11], s[2:3], v[170:171] op_sel_hi:[1,0,1]
	v_pk_fma_f32 v[168:169], v[12:13], s[2:3], v[168:169] op_sel_hi:[1,0,1]
	v_pk_fma_f32 v[166:167], v[14:15], s[2:3], v[166:167] op_sel_hi:[1,0,1]
	v_pk_fma_f32 v[164:165], v[16:17], s[2:3], v[164:165] op_sel_hi:[1,0,1]
	v_pk_fma_f32 v[162:163], v[18:19], s[2:3], v[162:163] op_sel_hi:[1,0,1]
	v_pk_fma_f32 v[160:161], v[20:21], s[2:3], v[160:161] op_sel_hi:[1,0,1]
	v_pk_fma_f32 v[158:159], v[22:23], s[2:3], v[158:159] op_sel_hi:[1,0,1]
	v_pk_fma_f32 v[156:157], v[24:25], s[2:3], v[156:157] op_sel_hi:[1,0,1]
	v_pk_fma_f32 v[154:155], v[26:27], s[2:3], v[154:155] op_sel_hi:[1,0,1]
	v_pk_fma_f32 v[152:153], v[28:29], s[2:3], v[152:153] op_sel_hi:[1,0,1]
	v_pk_fma_f32 v[150:151], v[30:31], s[2:3], v[150:151] op_sel_hi:[1,0,1]
	v_readlane_b32 s2, v131, 9
	s_waitcnt vmcnt(20)
	v_cvt_scalef32_pk32_f32_fp6 v[0:31], v[68:73], 1.0
	v_pk_fma_f32 v[68:69], v[0:1], s[2:3], v[74:75] op_sel_hi:[1,0,1]
	v_pk_fma_f32 v[70:71], v[2:3], s[2:3], v[76:77] op_sel_hi:[1,0,1]
	v_pk_fma_f32 v[72:73], v[4:5], s[2:3], v[78:79] op_sel_hi:[1,0,1]
	v_pk_fma_f32 v[74:75], v[6:7], s[2:3], v[174:175] op_sel_hi:[1,0,1]
	v_pk_fma_f32 v[76:77], v[8:9], s[2:3], v[172:173] op_sel_hi:[1,0,1]
	v_pk_fma_f32 v[78:79], v[10:11], s[2:3], v[170:171] op_sel_hi:[1,0,1]
	v_pk_fma_f32 v[168:169], v[12:13], s[2:3], v[168:169] op_sel_hi:[1,0,1]
	v_pk_fma_f32 v[166:167], v[14:15], s[2:3], v[166:167] op_sel_hi:[1,0,1]
	v_pk_fma_f32 v[164:165], v[16:17], s[2:3], v[164:165] op_sel_hi:[1,0,1]
	v_pk_fma_f32 v[162:163], v[18:19], s[2:3], v[162:163] op_sel_hi:[1,0,1]
	v_pk_fma_f32 v[160:161], v[20:21], s[2:3], v[160:161] op_sel_hi:[1,0,1]
	v_pk_fma_f32 v[158:159], v[22:23], s[2:3], v[158:159] op_sel_hi:[1,0,1]
	v_pk_fma_f32 v[156:157], v[24:25], s[2:3], v[156:157] op_sel_hi:[1,0,1]
	v_pk_fma_f32 v[154:155], v[26:27], s[2:3], v[154:155] op_sel_hi:[1,0,1]
	v_pk_fma_f32 v[152:153], v[28:29], s[2:3], v[152:153] op_sel_hi:[1,0,1]
	v_pk_fma_f32 v[150:151], v[30:31], s[2:3], v[150:151] op_sel_hi:[1,0,1]
	v_readlane_b32 s2, v131, 10
	s_waitcnt vmcnt(18)
	v_cvt_scalef32_pk32_f32_fp6 v[0:31], v[56:61], 1.0
	v_pk_fma_f32 v[56:57], v[0:1], s[2:3], v[68:69] op_sel_hi:[1,0,1]
	v_pk_fma_f32 v[58:59], v[2:3], s[2:3], v[70:71] op_sel_hi:[1,0,1]
	v_pk_fma_f32 v[60:61], v[4:5], s[2:3], v[72:73] op_sel_hi:[1,0,1]
	v_pk_fma_f32 v[68:69], v[6:7], s[2:3], v[74:75] op_sel_hi:[1,0,1]
	v_pk_fma_f32 v[70:71], v[8:9], s[2:3], v[76:77] op_sel_hi:[1,0,1]
	v_pk_fma_f32 v[72:73], v[10:11], s[2:3], v[78:79] op_sel_hi:[1,0,1]
	v_pk_fma_f32 v[74:75], v[12:13], s[2:3], v[168:169] op_sel_hi:[1,0,1]
	v_pk_fma_f32 v[76:77], v[14:15], s[2:3], v[166:167] op_sel_hi:[1,0,1]
	v_pk_fma_f32 v[78:79], v[16:17], s[2:3], v[164:165] op_sel_hi:[1,0,1]
	v_pk_fma_f32 v[162:163], v[18:19], s[2:3], v[162:163] op_sel_hi:[1,0,1]
	v_pk_fma_f32 v[160:161], v[20:21], s[2:3], v[160:161] op_sel_hi:[1,0,1]
	v_pk_fma_f32 v[158:159], v[22:23], s[2:3], v[158:159] op_sel_hi:[1,0,1]
	v_pk_fma_f32 v[156:157], v[24:25], s[2:3], v[156:157] op_sel_hi:[1,0,1]
	v_pk_fma_f32 v[154:155], v[26:27], s[2:3], v[154:155] op_sel_hi:[1,0,1]
	v_pk_fma_f32 v[152:153], v[28:29], s[2:3], v[152:153] op_sel_hi:[1,0,1]
	v_pk_fma_f32 v[150:151], v[30:31], s[2:3], v[150:151] op_sel_hi:[1,0,1]
	v_readlane_b32 s2, v131, 11
	s_waitcnt vmcnt(16)
	v_cvt_scalef32_pk32_f32_fp6 v[0:31], v[44:49], 1.0
	v_pk_fma_f32 v[164:165], v[0:1], s[2:3], v[56:57] op_sel_hi:[1,0,1]
	v_pk_fma_f32 v[166:167], v[2:3], s[2:3], v[58:59] op_sel_hi:[1,0,1]
	v_pk_fma_f32 v[168:169], v[4:5], s[2:3], v[60:61] op_sel_hi:[1,0,1]
	v_pk_fma_f32 v[170:171], v[6:7], s[2:3], v[68:69] op_sel_hi:[1,0,1]
	v_pk_fma_f32 v[172:173], v[8:9], s[2:3], v[70:71] op_sel_hi:[1,0,1]
	v_pk_fma_f32 v[174:175], v[10:11], s[2:3], v[72:73] op_sel_hi:[1,0,1]
	v_pk_fma_f32 v[176:177], v[12:13], s[2:3], v[74:75] op_sel_hi:[1,0,1]
	v_pk_fma_f32 v[178:179], v[14:15], s[2:3], v[76:77] op_sel_hi:[1,0,1]
	v_pk_fma_f32 v[180:181], v[16:17], s[2:3], v[78:79] op_sel_hi:[1,0,1]
	v_pk_fma_f32 v[162:163], v[18:19], s[2:3], v[162:163] op_sel_hi:[1,0,1]
	v_pk_fma_f32 v[160:161], v[20:21], s[2:3], v[160:161] op_sel_hi:[1,0,1]
	v_pk_fma_f32 v[158:159], v[22:23], s[2:3], v[158:159] op_sel_hi:[1,0,1]
	v_pk_fma_f32 v[156:157], v[24:25], s[2:3], v[156:157] op_sel_hi:[1,0,1]
	v_pk_fma_f32 v[154:155], v[26:27], s[2:3], v[154:155] op_sel_hi:[1,0,1]
	v_pk_fma_f32 v[152:153], v[28:29], s[2:3], v[152:153] op_sel_hi:[1,0,1]
	v_pk_fma_f32 v[150:151], v[30:31], s[2:3], v[150:151] op_sel_hi:[1,0,1]
	v_readlane_b32 s2, v241, 20
	v_readlane_b32 s3, v241, 21
	v_readlane_b32 s100, v241, 22
	v_readlane_b32 s101, v241, 23
	s_nop 1
	buffer_load_dwordx4 v[74:77], v129, s[44:47], s2 offen
	buffer_load_dwordx2 v[78:79], v210, s[44:47], s2 offen
	buffer_load_dwordx4 v[68:71], v129, s[44:47], s3 offen
	buffer_load_dwordx2 v[72:73], v210, s[44:47], s3 offen
	buffer_load_dwordx4 v[56:59], v129, s[44:47], s100 offen
	buffer_load_dwordx2 v[60:61], v210, s[44:47], s100 offen
	buffer_load_dwordx4 v[44:47], v129, s[44:47], s101 offen
	buffer_load_dwordx2 v[48:49], v210, s[44:47], s101 offen
	v_readlane_b32 s2, v131, 12
	s_waitcnt vmcnt(22)
	v_cvt_scalef32_pk32_f32_fp6 v[0:31], v[62:67], 1.0
	v_pk_fma_f32 v[62:63], v[0:1], s[2:3], v[164:165] op_sel_hi:[1,0,1]
	v_pk_fma_f32 v[64:65], v[2:3], s[2:3], v[166:167] op_sel_hi:[1,0,1]
	v_pk_fma_f32 v[66:67], v[4:5], s[2:3], v[168:169] op_sel_hi:[1,0,1]
	v_pk_fma_f32 v[164:165], v[6:7], s[2:3], v[170:171] op_sel_hi:[1,0,1]
	v_pk_fma_f32 v[166:167], v[8:9], s[2:3], v[172:173] op_sel_hi:[1,0,1]
	v_pk_fma_f32 v[168:169], v[10:11], s[2:3], v[174:175] op_sel_hi:[1,0,1]
	v_pk_fma_f32 v[170:171], v[12:13], s[2:3], v[176:177] op_sel_hi:[1,0,1]
	v_pk_fma_f32 v[172:173], v[14:15], s[2:3], v[178:179] op_sel_hi:[1,0,1]
	v_pk_fma_f32 v[174:175], v[16:17], s[2:3], v[180:181] op_sel_hi:[1,0,1]
	v_pk_fma_f32 v[162:163], v[18:19], s[2:3], v[162:163] op_sel_hi:[1,0,1]
	v_pk_fma_f32 v[160:161], v[20:21], s[2:3], v[160:161] op_sel_hi:[1,0,1]
	v_pk_fma_f32 v[158:159], v[22:23], s[2:3], v[158:159] op_sel_hi:[1,0,1]
	v_pk_fma_f32 v[156:157], v[24:25], s[2:3], v[156:157] op_sel_hi:[1,0,1]
	v_pk_fma_f32 v[154:155], v[26:27], s[2:3], v[154:155] op_sel_hi:[1,0,1]
	v_pk_fma_f32 v[152:153], v[28:29], s[2:3], v[152:153] op_sel_hi:[1,0,1]
	v_pk_fma_f32 v[150:151], v[30:31], s[2:3], v[150:151] op_sel_hi:[1,0,1]
	v_readlane_b32 s2, v131, 13
	s_waitcnt vmcnt(20)
	v_cvt_scalef32_pk32_f32_fp6 v[0:31], v[50:55], 1.0
	v_pk_fma_f32 v[50:51], v[0:1], s[2:3], v[62:63] op_sel_hi:[1,0,1]
	v_pk_fma_f32 v[52:53], v[2:3], s[2:3], v[64:65] op_sel_hi:[1,0,1]
	v_pk_fma_f32 v[54:55], v[4:5], s[2:3], v[66:67] op_sel_hi:[1,0,1]
	v_pk_fma_f32 v[62:63], v[6:7], s[2:3], v[164:165] op_sel_hi:[1,0,1]
	v_pk_fma_f32 v[64:65], v[8:9], s[2:3], v[166:167] op_sel_hi:[1,0,1]
	v_pk_fma_f32 v[66:67], v[10:11], s[2:3], v[168:169] op_sel_hi:[1,0,1]
	v_pk_fma_f32 v[164:165], v[12:13], s[2:3], v[170:171] op_sel_hi:[1,0,1]
	v_pk_fma_f32 v[166:167], v[14:15], s[2:3], v[172:173] op_sel_hi:[1,0,1]
	v_pk_fma_f32 v[168:169], v[16:17], s[2:3], v[174:175] op_sel_hi:[1,0,1]
	v_pk_fma_f32 v[162:163], v[18:19], s[2:3], v[162:163] op_sel_hi:[1,0,1]
	v_pk_fma_f32 v[160:161], v[20:21], s[2:3], v[160:161] op_sel_hi:[1,0,1]
	v_pk_fma_f32 v[158:159], v[22:23], s[2:3], v[158:159] op_sel_hi:[1,0,1]
	v_pk_fma_f32 v[156:157], v[24:25], s[2:3], v[156:157] op_sel_hi:[1,0,1]
	v_pk_fma_f32 v[154:155], v[26:27], s[2:3], v[154:155] op_sel_hi:[1,0,1]
	v_pk_fma_f32 v[152:153], v[28:29], s[2:3], v[152:153] op_sel_hi:[1,0,1]
	v_pk_fma_f32 v[150:151], v[30:31], s[2:3], v[150:151] op_sel_hi:[1,0,1]
	v_readlane_b32 s2, v131, 14
	s_waitcnt vmcnt(18)
	v_cvt_scalef32_pk32_f32_fp6 v[0:31], v[38:43], 1.0
	v_pk_fma_f32 v[38:39], v[0:1], s[2:3], v[50:51] op_sel_hi:[1,0,1]
	v_pk_fma_f32 v[40:41], v[2:3], s[2:3], v[52:53] op_sel_hi:[1,0,1]
	v_pk_fma_f32 v[42:43], v[4:5], s[2:3], v[54:55] op_sel_hi:[1,0,1]
	v_pk_fma_f32 v[50:51], v[6:7], s[2:3], v[62:63] op_sel_hi:[1,0,1]
	v_pk_fma_f32 v[52:53], v[8:9], s[2:3], v[64:65] op_sel_hi:[1,0,1]
	v_pk_fma_f32 v[54:55], v[10:11], s[2:3], v[66:67] op_sel_hi:[1,0,1]
	v_pk_fma_f32 v[62:63], v[12:13], s[2:3], v[164:165] op_sel_hi:[1,0,1]
	v_pk_fma_f32 v[64:65], v[14:15], s[2:3], v[166:167] op_sel_hi:[1,0,1]
	v_pk_fma_f32 v[66:67], v[16:17], s[2:3], v[168:169] op_sel_hi:[1,0,1]
	v_pk_fma_f32 v[162:163], v[18:19], s[2:3], v[162:163] op_sel_hi:[1,0,1]
	v_pk_fma_f32 v[160:161], v[20:21], s[2:3], v[160:161] op_sel_hi:[1,0,1]
	v_pk_fma_f32 v[158:159], v[22:23], s[2:3], v[158:159] op_sel_hi:[1,0,1]
	v_pk_fma_f32 v[156:157], v[24:25], s[2:3], v[156:157] op_sel_hi:[1,0,1]
	v_pk_fma_f32 v[154:155], v[26:27], s[2:3], v[154:155] op_sel_hi:[1,0,1]
	v_pk_fma_f32 v[152:153], v[28:29], s[2:3], v[152:153] op_sel_hi:[1,0,1]
	v_pk_fma_f32 v[150:151], v[30:31], s[2:3], v[150:151] op_sel_hi:[1,0,1]
	v_readlane_b32 s2, v131, 15
	s_waitcnt vmcnt(16)
	v_cvt_scalef32_pk32_f32_fp6 v[0:31], v[32:37], 1.0
	v_pk_fma_f32 v[164:165], v[0:1], s[2:3], v[38:39] op_sel_hi:[1,0,1]
	v_pk_fma_f32 v[166:167], v[2:3], s[2:3], v[40:41] op_sel_hi:[1,0,1]
	v_pk_fma_f32 v[168:169], v[4:5], s[2:3], v[42:43] op_sel_hi:[1,0,1]
	v_pk_fma_f32 v[170:171], v[6:7], s[2:3], v[50:51] op_sel_hi:[1,0,1]
	v_pk_fma_f32 v[172:173], v[8:9], s[2:3], v[52:53] op_sel_hi:[1,0,1]
	v_pk_fma_f32 v[174:175], v[10:11], s[2:3], v[54:55] op_sel_hi:[1,0,1]
	v_pk_fma_f32 v[176:177], v[12:13], s[2:3], v[62:63] op_sel_hi:[1,0,1]
	v_pk_fma_f32 v[178:179], v[14:15], s[2:3], v[64:65] op_sel_hi:[1,0,1]
	v_pk_fma_f32 v[180:181], v[16:17], s[2:3], v[66:67] op_sel_hi:[1,0,1]
	v_pk_fma_f32 v[162:163], v[18:19], s[2:3], v[162:163] op_sel_hi:[1,0,1]
	v_pk_fma_f32 v[160:161], v[20:21], s[2:3], v[160:161] op_sel_hi:[1,0,1]
	v_pk_fma_f32 v[158:159], v[22:23], s[2:3], v[158:159] op_sel_hi:[1,0,1]
	v_pk_fma_f32 v[156:157], v[24:25], s[2:3], v[156:157] op_sel_hi:[1,0,1]
	v_pk_fma_f32 v[154:155], v[26:27], s[2:3], v[154:155] op_sel_hi:[1,0,1]
	v_pk_fma_f32 v[152:153], v[28:29], s[2:3], v[152:153] op_sel_hi:[1,0,1]
	v_pk_fma_f32 v[150:151], v[30:31], s[2:3], v[150:151] op_sel_hi:[1,0,1]
	v_readlane_b32 s2, v241, 24
	v_readlane_b32 s3, v241, 25
	v_readlane_b32 s100, v241, 26
	v_readlane_b32 s101, v241, 27
	s_nop 1
	buffer_load_dwordx4 v[62:65], v129, s[44:47], s2 offen
	buffer_load_dwordx2 v[66:67], v210, s[44:47], s2 offen
	buffer_load_dwordx4 v[50:53], v129, s[44:47], s3 offen
	buffer_load_dwordx2 v[54:55], v210, s[44:47], s3 offen
	buffer_load_dwordx4 v[38:41], v129, s[44:47], s100 offen
	buffer_load_dwordx2 v[42:43], v210, s[44:47], s100 offen
	buffer_load_dwordx4 v[32:35], v129, s[44:47], s101 offen
	buffer_load_dwordx2 v[36:37], v210, s[44:47], s101 offen
	v_readlane_b32 s2, v131, 16
	s_waitcnt vmcnt(22)
	v_cvt_scalef32_pk32_f32_fp6 v[0:31], v[98:103], 1.0
	v_pk_fma_f32 v[98:99], v[0:1], s[2:3], v[164:165] op_sel_hi:[1,0,1]
	v_pk_fma_f32 v[100:101], v[2:3], s[2:3], v[166:167] op_sel_hi:[1,0,1]
	v_pk_fma_f32 v[102:103], v[4:5], s[2:3], v[168:169] op_sel_hi:[1,0,1]
	v_pk_fma_f32 v[164:165], v[6:7], s[2:3], v[170:171] op_sel_hi:[1,0,1]
	v_pk_fma_f32 v[166:167], v[8:9], s[2:3], v[172:173] op_sel_hi:[1,0,1]
	v_pk_fma_f32 v[168:169], v[10:11], s[2:3], v[174:175] op_sel_hi:[1,0,1]
	v_pk_fma_f32 v[170:171], v[12:13], s[2:3], v[176:177] op_sel_hi:[1,0,1]
	v_pk_fma_f32 v[172:173], v[14:15], s[2:3], v[178:179] op_sel_hi:[1,0,1]
	v_pk_fma_f32 v[174:175], v[16:17], s[2:3], v[180:181] op_sel_hi:[1,0,1]
	v_pk_fma_f32 v[162:163], v[18:19], s[2:3], v[162:163] op_sel_hi:[1,0,1]
	v_pk_fma_f32 v[160:161], v[20:21], s[2:3], v[160:161] op_sel_hi:[1,0,1]
	v_pk_fma_f32 v[158:159], v[22:23], s[2:3], v[158:159] op_sel_hi:[1,0,1]
	v_pk_fma_f32 v[156:157], v[24:25], s[2:3], v[156:157] op_sel_hi:[1,0,1]
	v_pk_fma_f32 v[154:155], v[26:27], s[2:3], v[154:155] op_sel_hi:[1,0,1]
	v_pk_fma_f32 v[152:153], v[28:29], s[2:3], v[152:153] op_sel_hi:[1,0,1]
	v_pk_fma_f32 v[150:151], v[30:31], s[2:3], v[150:151] op_sel_hi:[1,0,1]
	v_readlane_b32 s2, v131, 17
	s_waitcnt vmcnt(20)
	v_cvt_scalef32_pk32_f32_fp6 v[0:31], v[92:97], 1.0
	v_pk_fma_f32 v[92:93], v[0:1], s[2:3], v[98:99] op_sel_hi:[1,0,1]
	v_pk_fma_f32 v[94:95], v[2:3], s[2:3], v[100:101] op_sel_hi:[1,0,1]
	v_pk_fma_f32 v[96:97], v[4:5], s[2:3], v[102:103] op_sel_hi:[1,0,1]
	v_pk_fma_f32 v[98:99], v[6:7], s[2:3], v[164:165] op_sel_hi:[1,0,1]
	v_pk_fma_f32 v[100:101], v[8:9], s[2:3], v[166:167] op_sel_hi:[1,0,1]
	v_pk_fma_f32 v[102:103], v[10:11], s[2:3], v[168:169] op_sel_hi:[1,0,1]
	v_pk_fma_f32 v[164:165], v[12:13], s[2:3], v[170:171] op_sel_hi:[1,0,1]
	v_pk_fma_f32 v[166:167], v[14:15], s[2:3], v[172:173] op_sel_hi:[1,0,1]
	v_pk_fma_f32 v[168:169], v[16:17], s[2:3], v[174:175] op_sel_hi:[1,0,1]
	v_pk_fma_f32 v[162:163], v[18:19], s[2:3], v[162:163] op_sel_hi:[1,0,1]
	v_pk_fma_f32 v[160:161], v[20:21], s[2:3], v[160:161] op_sel_hi:[1,0,1]
	v_pk_fma_f32 v[158:159], v[22:23], s[2:3], v[158:159] op_sel_hi:[1,0,1]
	v_pk_fma_f32 v[156:157], v[24:25], s[2:3], v[156:157] op_sel_hi:[1,0,1]
	v_pk_fma_f32 v[154:155], v[26:27], s[2:3], v[154:155] op_sel_hi:[1,0,1]
	v_pk_fma_f32 v[152:153], v[28:29], s[2:3], v[152:153] op_sel_hi:[1,0,1]
	v_pk_fma_f32 v[150:151], v[30:31], s[2:3], v[150:151] op_sel_hi:[1,0,1]
	v_readlane_b32 s2, v131, 18
	s_waitcnt vmcnt(18)
	v_cvt_scalef32_pk32_f32_fp6 v[0:31], v[86:91], 1.0
	v_pk_fma_f32 v[86:87], v[0:1], s[2:3], v[92:93] op_sel_hi:[1,0,1]
	v_pk_fma_f32 v[88:89], v[2:3], s[2:3], v[94:95] op_sel_hi:[1,0,1]
	v_pk_fma_f32 v[90:91], v[4:5], s[2:3], v[96:97] op_sel_hi:[1,0,1]
	v_pk_fma_f32 v[92:93], v[6:7], s[2:3], v[98:99] op_sel_hi:[1,0,1]
	v_pk_fma_f32 v[94:95], v[8:9], s[2:3], v[100:101] op_sel_hi:[1,0,1]
	v_pk_fma_f32 v[96:97], v[10:11], s[2:3], v[102:103] op_sel_hi:[1,0,1]
	v_pk_fma_f32 v[98:99], v[12:13], s[2:3], v[164:165] op_sel_hi:[1,0,1]
	v_pk_fma_f32 v[100:101], v[14:15], s[2:3], v[166:167] op_sel_hi:[1,0,1]
	v_pk_fma_f32 v[102:103], v[16:17], s[2:3], v[168:169] op_sel_hi:[1,0,1]
	v_pk_fma_f32 v[162:163], v[18:19], s[2:3], v[162:163] op_sel_hi:[1,0,1]
	v_pk_fma_f32 v[160:161], v[20:21], s[2:3], v[160:161] op_sel_hi:[1,0,1]
	v_pk_fma_f32 v[158:159], v[22:23], s[2:3], v[158:159] op_sel_hi:[1,0,1]
	v_pk_fma_f32 v[156:157], v[24:25], s[2:3], v[156:157] op_sel_hi:[1,0,1]
	v_pk_fma_f32 v[154:155], v[26:27], s[2:3], v[154:155] op_sel_hi:[1,0,1]
	v_pk_fma_f32 v[152:153], v[28:29], s[2:3], v[152:153] op_sel_hi:[1,0,1]
	v_pk_fma_f32 v[150:151], v[30:31], s[2:3], v[150:151] op_sel_hi:[1,0,1]
	v_readlane_b32 s2, v131, 19
	s_waitcnt vmcnt(16)
	v_cvt_scalef32_pk32_f32_fp6 v[0:31], v[80:85], 1.0
	v_pk_fma_f32 v[180:181], v[0:1], s[2:3], v[86:87] op_sel_hi:[1,0,1]
	v_pk_fma_f32 v[178:179], v[2:3], s[2:3], v[88:89] op_sel_hi:[1,0,1]
	v_pk_fma_f32 v[176:177], v[4:5], s[2:3], v[90:91] op_sel_hi:[1,0,1]
	v_pk_fma_f32 v[174:175], v[6:7], s[2:3], v[92:93] op_sel_hi:[1,0,1]
	v_pk_fma_f32 v[172:173], v[8:9], s[2:3], v[94:95] op_sel_hi:[1,0,1]
	v_pk_fma_f32 v[170:171], v[10:11], s[2:3], v[96:97] op_sel_hi:[1,0,1]
	v_pk_fma_f32 v[168:169], v[12:13], s[2:3], v[98:99] op_sel_hi:[1,0,1]
	v_pk_fma_f32 v[166:167], v[14:15], s[2:3], v[100:101] op_sel_hi:[1,0,1]
	v_pk_fma_f32 v[164:165], v[16:17], s[2:3], v[102:103] op_sel_hi:[1,0,1]
	v_pk_fma_f32 v[162:163], v[18:19], s[2:3], v[162:163] op_sel_hi:[1,0,1]
	v_pk_fma_f32 v[160:161], v[20:21], s[2:3], v[160:161] op_sel_hi:[1,0,1]
	v_pk_fma_f32 v[158:159], v[22:23], s[2:3], v[158:159] op_sel_hi:[1,0,1]
	v_pk_fma_f32 v[156:157], v[24:25], s[2:3], v[156:157] op_sel_hi:[1,0,1]
	v_pk_fma_f32 v[154:155], v[26:27], s[2:3], v[154:155] op_sel_hi:[1,0,1]
	v_pk_fma_f32 v[152:153], v[28:29], s[2:3], v[152:153] op_sel_hi:[1,0,1]
	v_pk_fma_f32 v[150:151], v[30:31], s[2:3], v[150:151] op_sel_hi:[1,0,1]
	v_readlane_b32 s2, v241, 28
	v_readlane_b32 s3, v241, 29
	v_readlane_b32 s100, v241, 30
	v_readlane_b32 s101, v241, 31
	s_nop 1
	buffer_load_dwordx4 v[98:101], v129, s[44:47], s2 offen
	buffer_load_dwordx2 v[102:103], v210, s[44:47], s2 offen
	buffer_load_dwordx4 v[92:95], v129, s[44:47], s3 offen
	buffer_load_dwordx2 v[96:97], v210, s[44:47], s3 offen
	buffer_load_dwordx4 v[86:89], v129, s[44:47], s100 offen
	buffer_load_dwordx2 v[90:91], v210, s[44:47], s100 offen
	buffer_load_dwordx4 v[80:83], v129, s[44:47], s101 offen
	buffer_load_dwordx2 v[84:85], v210, s[44:47], s101 offen
	v_readlane_b32 s2, v131, 20
	s_waitcnt vmcnt(22)
	v_cvt_scalef32_pk32_f32_fp6 v[0:31], v[74:79], 1.0
	v_pk_fma_f32 v[74:75], v[0:1], s[2:3], v[180:181] op_sel_hi:[1,0,1]
	v_pk_fma_f32 v[76:77], v[2:3], s[2:3], v[178:179] op_sel_hi:[1,0,1]
	v_pk_fma_f32 v[78:79], v[4:5], s[2:3], v[176:177] op_sel_hi:[1,0,1]
	v_pk_fma_f32 v[174:175], v[6:7], s[2:3], v[174:175] op_sel_hi:[1,0,1]
	v_pk_fma_f32 v[172:173], v[8:9], s[2:3], v[172:173] op_sel_hi:[1,0,1]
	v_pk_fma_f32 v[170:171], v[10:11], s[2:3], v[170:171] op_sel_hi:[1,0,1]
	v_pk_fma_f32 v[168:169], v[12:13], s[2:3], v[168:169] op_sel_hi:[1,0,1]
	v_pk_fma_f32 v[166:167], v[14:15], s[2:3], v[166:167] op_sel_hi:[1,0,1]
	v_pk_fma_f32 v[164:165], v[16:17], s[2:3], v[164:165] op_sel_hi:[1,0,1]
	v_pk_fma_f32 v[162:163], v[18:19], s[2:3], v[162:163] op_sel_hi:[1,0,1]
	v_pk_fma_f32 v[160:161], v[20:21], s[2:3], v[160:161] op_sel_hi:[1,0,1]
	v_pk_fma_f32 v[158:159], v[22:23], s[2:3], v[158:159] op_sel_hi:[1,0,1]
	v_pk_fma_f32 v[156:157], v[24:25], s[2:3], v[156:157] op_sel_hi:[1,0,1]
	v_pk_fma_f32 v[154:155], v[26:27], s[2:3], v[154:155] op_sel_hi:[1,0,1]
	v_pk_fma_f32 v[152:153], v[28:29], s[2:3], v[152:153] op_sel_hi:[1,0,1]
	v_pk_fma_f32 v[150:151], v[30:31], s[2:3], v[150:151] op_sel_hi:[1,0,1]
	v_readlane_b32 s2, v131, 21
	s_waitcnt vmcnt(20)
	v_cvt_scalef32_pk32_f32_fp6 v[0:31], v[68:73], 1.0
	v_pk_fma_f32 v[68:69], v[0:1], s[2:3], v[74:75] op_sel_hi:[1,0,1]
	v_pk_fma_f32 v[70:71], v[2:3], s[2:3], v[76:77] op_sel_hi:[1,0,1]
	v_pk_fma_f32 v[72:73], v[4:5], s[2:3], v[78:79] op_sel_hi:[1,0,1]
	v_pk_fma_f32 v[74:75], v[6:7], s[2:3], v[174:175] op_sel_hi:[1,0,1]
	v_pk_fma_f32 v[76:77], v[8:9], s[2:3], v[172:173] op_sel_hi:[1,0,1]
	v_pk_fma_f32 v[78:79], v[10:11], s[2:3], v[170:171] op_sel_hi:[1,0,1]
	v_pk_fma_f32 v[168:169], v[12:13], s[2:3], v[168:169] op_sel_hi:[1,0,1]
	v_pk_fma_f32 v[166:167], v[14:15], s[2:3], v[166:167] op_sel_hi:[1,0,1]
	v_pk_fma_f32 v[164:165], v[16:17], s[2:3], v[164:165] op_sel_hi:[1,0,1]
	v_pk_fma_f32 v[162:163], v[18:19], s[2:3], v[162:163] op_sel_hi:[1,0,1]
	v_pk_fma_f32 v[160:161], v[20:21], s[2:3], v[160:161] op_sel_hi:[1,0,1]
	v_pk_fma_f32 v[158:159], v[22:23], s[2:3], v[158:159] op_sel_hi:[1,0,1]
	v_pk_fma_f32 v[156:157], v[24:25], s[2:3], v[156:157] op_sel_hi:[1,0,1]
	v_pk_fma_f32 v[154:155], v[26:27], s[2:3], v[154:155] op_sel_hi:[1,0,1]
	v_pk_fma_f32 v[152:153], v[28:29], s[2:3], v[152:153] op_sel_hi:[1,0,1]
	v_pk_fma_f32 v[150:151], v[30:31], s[2:3], v[150:151] op_sel_hi:[1,0,1]
	v_readlane_b32 s2, v131, 22
	s_waitcnt vmcnt(18)
	v_cvt_scalef32_pk32_f32_fp6 v[0:31], v[56:61], 1.0
	v_pk_fma_f32 v[56:57], v[0:1], s[2:3], v[68:69] op_sel_hi:[1,0,1]
	v_pk_fma_f32 v[58:59], v[2:3], s[2:3], v[70:71] op_sel_hi:[1,0,1]
	v_pk_fma_f32 v[60:61], v[4:5], s[2:3], v[72:73] op_sel_hi:[1,0,1]
	v_pk_fma_f32 v[68:69], v[6:7], s[2:3], v[74:75] op_sel_hi:[1,0,1]
	v_pk_fma_f32 v[70:71], v[8:9], s[2:3], v[76:77] op_sel_hi:[1,0,1]
	v_pk_fma_f32 v[72:73], v[10:11], s[2:3], v[78:79] op_sel_hi:[1,0,1]
	v_pk_fma_f32 v[74:75], v[12:13], s[2:3], v[168:169] op_sel_hi:[1,0,1]
	v_pk_fma_f32 v[76:77], v[14:15], s[2:3], v[166:167] op_sel_hi:[1,0,1]
	v_pk_fma_f32 v[78:79], v[16:17], s[2:3], v[164:165] op_sel_hi:[1,0,1]
	v_pk_fma_f32 v[162:163], v[18:19], s[2:3], v[162:163] op_sel_hi:[1,0,1]
	v_pk_fma_f32 v[160:161], v[20:21], s[2:3], v[160:161] op_sel_hi:[1,0,1]
	v_pk_fma_f32 v[158:159], v[22:23], s[2:3], v[158:159] op_sel_hi:[1,0,1]
	v_pk_fma_f32 v[156:157], v[24:25], s[2:3], v[156:157] op_sel_hi:[1,0,1]
	v_pk_fma_f32 v[154:155], v[26:27], s[2:3], v[154:155] op_sel_hi:[1,0,1]
	v_pk_fma_f32 v[152:153], v[28:29], s[2:3], v[152:153] op_sel_hi:[1,0,1]
	v_pk_fma_f32 v[150:151], v[30:31], s[2:3], v[150:151] op_sel_hi:[1,0,1]
	v_readlane_b32 s2, v131, 23
	s_waitcnt vmcnt(16)
	v_cvt_scalef32_pk32_f32_fp6 v[0:31], v[44:49], 1.0
	v_pk_fma_f32 v[164:165], v[0:1], s[2:3], v[56:57] op_sel_hi:[1,0,1]
	v_pk_fma_f32 v[166:167], v[2:3], s[2:3], v[58:59] op_sel_hi:[1,0,1]
	v_pk_fma_f32 v[168:169], v[4:5], s[2:3], v[60:61] op_sel_hi:[1,0,1]
	v_pk_fma_f32 v[170:171], v[6:7], s[2:3], v[68:69] op_sel_hi:[1,0,1]
	v_pk_fma_f32 v[172:173], v[8:9], s[2:3], v[70:71] op_sel_hi:[1,0,1]
	v_pk_fma_f32 v[174:175], v[10:11], s[2:3], v[72:73] op_sel_hi:[1,0,1]
	v_pk_fma_f32 v[176:177], v[12:13], s[2:3], v[74:75] op_sel_hi:[1,0,1]
	v_pk_fma_f32 v[178:179], v[14:15], s[2:3], v[76:77] op_sel_hi:[1,0,1]
	v_pk_fma_f32 v[180:181], v[16:17], s[2:3], v[78:79] op_sel_hi:[1,0,1]
	v_pk_fma_f32 v[162:163], v[18:19], s[2:3], v[162:163] op_sel_hi:[1,0,1]
	v_pk_fma_f32 v[160:161], v[20:21], s[2:3], v[160:161] op_sel_hi:[1,0,1]
	v_pk_fma_f32 v[158:159], v[22:23], s[2:3], v[158:159] op_sel_hi:[1,0,1]
	v_pk_fma_f32 v[156:157], v[24:25], s[2:3], v[156:157] op_sel_hi:[1,0,1]
	v_pk_fma_f32 v[154:155], v[26:27], s[2:3], v[154:155] op_sel_hi:[1,0,1]
	v_pk_fma_f32 v[152:153], v[28:29], s[2:3], v[152:153] op_sel_hi:[1,0,1]
	v_pk_fma_f32 v[150:151], v[30:31], s[2:3], v[150:151] op_sel_hi:[1,0,1]
	v_readlane_b32 s2, v241, 32
	v_readlane_b32 s3, v241, 33
	v_readlane_b32 s100, v241, 34
	v_readlane_b32 s101, v241, 35
	s_nop 1
	buffer_load_dwordx4 v[74:77], v129, s[44:47], s2 offen
	buffer_load_dwordx2 v[78:79], v210, s[44:47], s2 offen
	buffer_load_dwordx4 v[68:71], v129, s[44:47], s3 offen
	buffer_load_dwordx2 v[72:73], v210, s[44:47], s3 offen
	buffer_load_dwordx4 v[56:59], v129, s[44:47], s100 offen
	buffer_load_dwordx2 v[60:61], v210, s[44:47], s100 offen
	buffer_load_dwordx4 v[44:47], v129, s[44:47], s101 offen
	buffer_load_dwordx2 v[48:49], v210, s[44:47], s101 offen
	v_readlane_b32 s2, v131, 24
	s_waitcnt vmcnt(22)
	v_cvt_scalef32_pk32_f32_fp6 v[0:31], v[62:67], 1.0
	v_pk_fma_f32 v[62:63], v[0:1], s[2:3], v[164:165] op_sel_hi:[1,0,1]
	v_pk_fma_f32 v[64:65], v[2:3], s[2:3], v[166:167] op_sel_hi:[1,0,1]
	v_pk_fma_f32 v[66:67], v[4:5], s[2:3], v[168:169] op_sel_hi:[1,0,1]
	v_pk_fma_f32 v[164:165], v[6:7], s[2:3], v[170:171] op_sel_hi:[1,0,1]
	v_pk_fma_f32 v[166:167], v[8:9], s[2:3], v[172:173] op_sel_hi:[1,0,1]
	v_pk_fma_f32 v[168:169], v[10:11], s[2:3], v[174:175] op_sel_hi:[1,0,1]
	v_pk_fma_f32 v[170:171], v[12:13], s[2:3], v[176:177] op_sel_hi:[1,0,1]
	v_pk_fma_f32 v[172:173], v[14:15], s[2:3], v[178:179] op_sel_hi:[1,0,1]
	v_pk_fma_f32 v[174:175], v[16:17], s[2:3], v[180:181] op_sel_hi:[1,0,1]
	v_pk_fma_f32 v[162:163], v[18:19], s[2:3], v[162:163] op_sel_hi:[1,0,1]
	v_pk_fma_f32 v[160:161], v[20:21], s[2:3], v[160:161] op_sel_hi:[1,0,1]
	v_pk_fma_f32 v[158:159], v[22:23], s[2:3], v[158:159] op_sel_hi:[1,0,1]
	v_pk_fma_f32 v[156:157], v[24:25], s[2:3], v[156:157] op_sel_hi:[1,0,1]
	v_pk_fma_f32 v[154:155], v[26:27], s[2:3], v[154:155] op_sel_hi:[1,0,1]
	v_pk_fma_f32 v[152:153], v[28:29], s[2:3], v[152:153] op_sel_hi:[1,0,1]
	v_pk_fma_f32 v[150:151], v[30:31], s[2:3], v[150:151] op_sel_hi:[1,0,1]
	v_readlane_b32 s2, v131, 25
	s_waitcnt vmcnt(20)
	v_cvt_scalef32_pk32_f32_fp6 v[0:31], v[50:55], 1.0
	v_pk_fma_f32 v[50:51], v[0:1], s[2:3], v[62:63] op_sel_hi:[1,0,1]
	v_pk_fma_f32 v[52:53], v[2:3], s[2:3], v[64:65] op_sel_hi:[1,0,1]
	v_pk_fma_f32 v[54:55], v[4:5], s[2:3], v[66:67] op_sel_hi:[1,0,1]
	v_pk_fma_f32 v[62:63], v[6:7], s[2:3], v[164:165] op_sel_hi:[1,0,1]
	v_pk_fma_f32 v[64:65], v[8:9], s[2:3], v[166:167] op_sel_hi:[1,0,1]
	v_pk_fma_f32 v[66:67], v[10:11], s[2:3], v[168:169] op_sel_hi:[1,0,1]
	v_pk_fma_f32 v[164:165], v[12:13], s[2:3], v[170:171] op_sel_hi:[1,0,1]
	v_pk_fma_f32 v[166:167], v[14:15], s[2:3], v[172:173] op_sel_hi:[1,0,1]
	v_pk_fma_f32 v[168:169], v[16:17], s[2:3], v[174:175] op_sel_hi:[1,0,1]
	v_pk_fma_f32 v[162:163], v[18:19], s[2:3], v[162:163] op_sel_hi:[1,0,1]
	v_pk_fma_f32 v[160:161], v[20:21], s[2:3], v[160:161] op_sel_hi:[1,0,1]
	v_pk_fma_f32 v[158:159], v[22:23], s[2:3], v[158:159] op_sel_hi:[1,0,1]
	v_pk_fma_f32 v[156:157], v[24:25], s[2:3], v[156:157] op_sel_hi:[1,0,1]
	v_pk_fma_f32 v[154:155], v[26:27], s[2:3], v[154:155] op_sel_hi:[1,0,1]
	v_pk_fma_f32 v[152:153], v[28:29], s[2:3], v[152:153] op_sel_hi:[1,0,1]
	v_pk_fma_f32 v[150:151], v[30:31], s[2:3], v[150:151] op_sel_hi:[1,0,1]
	v_readlane_b32 s2, v131, 26
	s_waitcnt vmcnt(18)
	v_cvt_scalef32_pk32_f32_fp6 v[0:31], v[38:43], 1.0
	v_pk_fma_f32 v[38:39], v[0:1], s[2:3], v[50:51] op_sel_hi:[1,0,1]
	v_pk_fma_f32 v[40:41], v[2:3], s[2:3], v[52:53] op_sel_hi:[1,0,1]
	v_pk_fma_f32 v[42:43], v[4:5], s[2:3], v[54:55] op_sel_hi:[1,0,1]
	v_pk_fma_f32 v[50:51], v[6:7], s[2:3], v[62:63] op_sel_hi:[1,0,1]
	v_pk_fma_f32 v[52:53], v[8:9], s[2:3], v[64:65] op_sel_hi:[1,0,1]
	v_pk_fma_f32 v[54:55], v[10:11], s[2:3], v[66:67] op_sel_hi:[1,0,1]
	v_pk_fma_f32 v[62:63], v[12:13], s[2:3], v[164:165] op_sel_hi:[1,0,1]
	v_pk_fma_f32 v[64:65], v[14:15], s[2:3], v[166:167] op_sel_hi:[1,0,1]
	v_pk_fma_f32 v[66:67], v[16:17], s[2:3], v[168:169] op_sel_hi:[1,0,1]
	v_pk_fma_f32 v[162:163], v[18:19], s[2:3], v[162:163] op_sel_hi:[1,0,1]
	v_pk_fma_f32 v[160:161], v[20:21], s[2:3], v[160:161] op_sel_hi:[1,0,1]
	v_pk_fma_f32 v[158:159], v[22:23], s[2:3], v[158:159] op_sel_hi:[1,0,1]
	v_pk_fma_f32 v[156:157], v[24:25], s[2:3], v[156:157] op_sel_hi:[1,0,1]
	v_pk_fma_f32 v[154:155], v[26:27], s[2:3], v[154:155] op_sel_hi:[1,0,1]
	v_pk_fma_f32 v[152:153], v[28:29], s[2:3], v[152:153] op_sel_hi:[1,0,1]
	v_pk_fma_f32 v[150:151], v[30:31], s[2:3], v[150:151] op_sel_hi:[1,0,1]
	v_readlane_b32 s2, v131, 27
	s_waitcnt vmcnt(16)
	v_cvt_scalef32_pk32_f32_fp6 v[0:31], v[32:37], 1.0
	v_pk_fma_f32 v[164:165], v[0:1], s[2:3], v[38:39] op_sel_hi:[1,0,1]
	v_pk_fma_f32 v[166:167], v[2:3], s[2:3], v[40:41] op_sel_hi:[1,0,1]
	v_pk_fma_f32 v[168:169], v[4:5], s[2:3], v[42:43] op_sel_hi:[1,0,1]
	v_pk_fma_f32 v[170:171], v[6:7], s[2:3], v[50:51] op_sel_hi:[1,0,1]
	v_pk_fma_f32 v[172:173], v[8:9], s[2:3], v[52:53] op_sel_hi:[1,0,1]
	v_pk_fma_f32 v[174:175], v[10:11], s[2:3], v[54:55] op_sel_hi:[1,0,1]
	v_pk_fma_f32 v[176:177], v[12:13], s[2:3], v[62:63] op_sel_hi:[1,0,1]
	v_pk_fma_f32 v[178:179], v[14:15], s[2:3], v[64:65] op_sel_hi:[1,0,1]
	v_pk_fma_f32 v[180:181], v[16:17], s[2:3], v[66:67] op_sel_hi:[1,0,1]
	v_pk_fma_f32 v[162:163], v[18:19], s[2:3], v[162:163] op_sel_hi:[1,0,1]
	v_pk_fma_f32 v[160:161], v[20:21], s[2:3], v[160:161] op_sel_hi:[1,0,1]
	v_pk_fma_f32 v[158:159], v[22:23], s[2:3], v[158:159] op_sel_hi:[1,0,1]
	v_pk_fma_f32 v[156:157], v[24:25], s[2:3], v[156:157] op_sel_hi:[1,0,1]
	v_pk_fma_f32 v[154:155], v[26:27], s[2:3], v[154:155] op_sel_hi:[1,0,1]
	v_pk_fma_f32 v[152:153], v[28:29], s[2:3], v[152:153] op_sel_hi:[1,0,1]
	v_pk_fma_f32 v[150:151], v[30:31], s[2:3], v[150:151] op_sel_hi:[1,0,1]
	v_readlane_b32 s2, v241, 36
	v_readlane_b32 s3, v241, 37
	v_readlane_b32 s100, v241, 38
	v_readlane_b32 s101, v241, 39
	s_nop 1
	buffer_load_dwordx4 v[62:65], v129, s[44:47], s2 offen
	buffer_load_dwordx2 v[66:67], v210, s[44:47], s2 offen
	buffer_load_dwordx4 v[50:53], v129, s[44:47], s3 offen
	buffer_load_dwordx2 v[54:55], v210, s[44:47], s3 offen
	buffer_load_dwordx4 v[38:41], v129, s[44:47], s100 offen
	buffer_load_dwordx2 v[42:43], v210, s[44:47], s100 offen
	buffer_load_dwordx4 v[32:35], v129, s[44:47], s101 offen
	buffer_load_dwordx2 v[36:37], v210, s[44:47], s101 offen
	v_readlane_b32 s2, v131, 28
	s_waitcnt vmcnt(22)
	v_cvt_scalef32_pk32_f32_fp6 v[0:31], v[98:103], 1.0
	v_pk_fma_f32 v[98:99], v[0:1], s[2:3], v[164:165] op_sel_hi:[1,0,1]
	v_pk_fma_f32 v[100:101], v[2:3], s[2:3], v[166:167] op_sel_hi:[1,0,1]
	v_pk_fma_f32 v[102:103], v[4:5], s[2:3], v[168:169] op_sel_hi:[1,0,1]
	v_pk_fma_f32 v[164:165], v[6:7], s[2:3], v[170:171] op_sel_hi:[1,0,1]
	v_pk_fma_f32 v[166:167], v[8:9], s[2:3], v[172:173] op_sel_hi:[1,0,1]
	v_pk_fma_f32 v[168:169], v[10:11], s[2:3], v[174:175] op_sel_hi:[1,0,1]
	v_pk_fma_f32 v[170:171], v[12:13], s[2:3], v[176:177] op_sel_hi:[1,0,1]
	v_pk_fma_f32 v[172:173], v[14:15], s[2:3], v[178:179] op_sel_hi:[1,0,1]
	v_pk_fma_f32 v[174:175], v[16:17], s[2:3], v[180:181] op_sel_hi:[1,0,1]
	v_pk_fma_f32 v[162:163], v[18:19], s[2:3], v[162:163] op_sel_hi:[1,0,1]
	v_pk_fma_f32 v[160:161], v[20:21], s[2:3], v[160:161] op_sel_hi:[1,0,1]
	v_pk_fma_f32 v[158:159], v[22:23], s[2:3], v[158:159] op_sel_hi:[1,0,1]
	v_pk_fma_f32 v[156:157], v[24:25], s[2:3], v[156:157] op_sel_hi:[1,0,1]
	v_pk_fma_f32 v[154:155], v[26:27], s[2:3], v[154:155] op_sel_hi:[1,0,1]
	v_pk_fma_f32 v[152:153], v[28:29], s[2:3], v[152:153] op_sel_hi:[1,0,1]
	v_pk_fma_f32 v[150:151], v[30:31], s[2:3], v[150:151] op_sel_hi:[1,0,1]
	v_readlane_b32 s2, v131, 29
	s_waitcnt vmcnt(20)
	v_cvt_scalef32_pk32_f32_fp6 v[0:31], v[92:97], 1.0
	v_pk_fma_f32 v[92:93], v[0:1], s[2:3], v[98:99] op_sel_hi:[1,0,1]
	v_pk_fma_f32 v[94:95], v[2:3], s[2:3], v[100:101] op_sel_hi:[1,0,1]
	v_pk_fma_f32 v[96:97], v[4:5], s[2:3], v[102:103] op_sel_hi:[1,0,1]
	v_pk_fma_f32 v[98:99], v[6:7], s[2:3], v[164:165] op_sel_hi:[1,0,1]
	v_pk_fma_f32 v[100:101], v[8:9], s[2:3], v[166:167] op_sel_hi:[1,0,1]
	v_pk_fma_f32 v[102:103], v[10:11], s[2:3], v[168:169] op_sel_hi:[1,0,1]
	v_pk_fma_f32 v[164:165], v[12:13], s[2:3], v[170:171] op_sel_hi:[1,0,1]
	v_pk_fma_f32 v[166:167], v[14:15], s[2:3], v[172:173] op_sel_hi:[1,0,1]
	v_pk_fma_f32 v[168:169], v[16:17], s[2:3], v[174:175] op_sel_hi:[1,0,1]
	v_pk_fma_f32 v[162:163], v[18:19], s[2:3], v[162:163] op_sel_hi:[1,0,1]
	v_pk_fma_f32 v[160:161], v[20:21], s[2:3], v[160:161] op_sel_hi:[1,0,1]
	v_pk_fma_f32 v[158:159], v[22:23], s[2:3], v[158:159] op_sel_hi:[1,0,1]
	v_pk_fma_f32 v[156:157], v[24:25], s[2:3], v[156:157] op_sel_hi:[1,0,1]
	v_pk_fma_f32 v[154:155], v[26:27], s[2:3], v[154:155] op_sel_hi:[1,0,1]
	v_pk_fma_f32 v[152:153], v[28:29], s[2:3], v[152:153] op_sel_hi:[1,0,1]
	v_pk_fma_f32 v[150:151], v[30:31], s[2:3], v[150:151] op_sel_hi:[1,0,1]
	v_readlane_b32 s2, v131, 30
	s_waitcnt vmcnt(18)
	v_cvt_scalef32_pk32_f32_fp6 v[0:31], v[86:91], 1.0
	v_pk_fma_f32 v[86:87], v[0:1], s[2:3], v[92:93] op_sel_hi:[1,0,1]
	v_pk_fma_f32 v[88:89], v[2:3], s[2:3], v[94:95] op_sel_hi:[1,0,1]
	v_pk_fma_f32 v[90:91], v[4:5], s[2:3], v[96:97] op_sel_hi:[1,0,1]
	v_pk_fma_f32 v[92:93], v[6:7], s[2:3], v[98:99] op_sel_hi:[1,0,1]
	v_pk_fma_f32 v[94:95], v[8:9], s[2:3], v[100:101] op_sel_hi:[1,0,1]
	v_pk_fma_f32 v[96:97], v[10:11], s[2:3], v[102:103] op_sel_hi:[1,0,1]
	v_pk_fma_f32 v[98:99], v[12:13], s[2:3], v[164:165] op_sel_hi:[1,0,1]
	v_pk_fma_f32 v[100:101], v[14:15], s[2:3], v[166:167] op_sel_hi:[1,0,1]
	v_pk_fma_f32 v[102:103], v[16:17], s[2:3], v[168:169] op_sel_hi:[1,0,1]
	v_pk_fma_f32 v[162:163], v[18:19], s[2:3], v[162:163] op_sel_hi:[1,0,1]
	v_pk_fma_f32 v[160:161], v[20:21], s[2:3], v[160:161] op_sel_hi:[1,0,1]
	v_pk_fma_f32 v[158:159], v[22:23], s[2:3], v[158:159] op_sel_hi:[1,0,1]
	v_pk_fma_f32 v[156:157], v[24:25], s[2:3], v[156:157] op_sel_hi:[1,0,1]
	v_pk_fma_f32 v[154:155], v[26:27], s[2:3], v[154:155] op_sel_hi:[1,0,1]
	v_pk_fma_f32 v[152:153], v[28:29], s[2:3], v[152:153] op_sel_hi:[1,0,1]
	v_pk_fma_f32 v[150:151], v[30:31], s[2:3], v[150:151] op_sel_hi:[1,0,1]
	v_readlane_b32 s2, v131, 31
	s_waitcnt vmcnt(16)
	v_cvt_scalef32_pk32_f32_fp6 v[0:31], v[80:85], 1.0
	v_pk_fma_f32 v[180:181], v[0:1], s[2:3], v[86:87] op_sel_hi:[1,0,1]
	v_pk_fma_f32 v[178:179], v[2:3], s[2:3], v[88:89] op_sel_hi:[1,0,1]
	v_pk_fma_f32 v[176:177], v[4:5], s[2:3], v[90:91] op_sel_hi:[1,0,1]
	v_pk_fma_f32 v[174:175], v[6:7], s[2:3], v[92:93] op_sel_hi:[1,0,1]
	v_pk_fma_f32 v[172:173], v[8:9], s[2:3], v[94:95] op_sel_hi:[1,0,1]
	v_pk_fma_f32 v[170:171], v[10:11], s[2:3], v[96:97] op_sel_hi:[1,0,1]
	v_pk_fma_f32 v[168:169], v[12:13], s[2:3], v[98:99] op_sel_hi:[1,0,1]
	v_pk_fma_f32 v[166:167], v[14:15], s[2:3], v[100:101] op_sel_hi:[1,0,1]
	v_pk_fma_f32 v[164:165], v[16:17], s[2:3], v[102:103] op_sel_hi:[1,0,1]
	v_pk_fma_f32 v[162:163], v[18:19], s[2:3], v[162:163] op_sel_hi:[1,0,1]
	v_pk_fma_f32 v[160:161], v[20:21], s[2:3], v[160:161] op_sel_hi:[1,0,1]
	v_pk_fma_f32 v[158:159], v[22:23], s[2:3], v[158:159] op_sel_hi:[1,0,1]
	v_pk_fma_f32 v[156:157], v[24:25], s[2:3], v[156:157] op_sel_hi:[1,0,1]
	v_pk_fma_f32 v[154:155], v[26:27], s[2:3], v[154:155] op_sel_hi:[1,0,1]
	v_pk_fma_f32 v[152:153], v[28:29], s[2:3], v[152:153] op_sel_hi:[1,0,1]
	v_pk_fma_f32 v[150:151], v[30:31], s[2:3], v[150:151] op_sel_hi:[1,0,1]
	v_readlane_b32 s2, v241, 40
	v_readlane_b32 s3, v241, 41
	v_readlane_b32 s100, v241, 42
	v_readlane_b32 s101, v241, 43
	s_nop 1
	buffer_load_dwordx4 v[98:101], v129, s[44:47], s2 offen
	buffer_load_dwordx2 v[102:103], v210, s[44:47], s2 offen
	buffer_load_dwordx4 v[92:95], v129, s[44:47], s3 offen
	buffer_load_dwordx2 v[96:97], v210, s[44:47], s3 offen
	buffer_load_dwordx4 v[86:89], v129, s[44:47], s100 offen
	buffer_load_dwordx2 v[90:91], v210, s[44:47], s100 offen
	buffer_load_dwordx4 v[80:83], v129, s[44:47], s101 offen
	buffer_load_dwordx2 v[84:85], v210, s[44:47], s101 offen
	v_readlane_b32 s2, v131, 32
	s_waitcnt vmcnt(22)
	v_cvt_scalef32_pk32_f32_fp6 v[0:31], v[74:79], 1.0
	v_pk_fma_f32 v[74:75], v[0:1], s[2:3], v[180:181] op_sel_hi:[1,0,1]
	v_pk_fma_f32 v[76:77], v[2:3], s[2:3], v[178:179] op_sel_hi:[1,0,1]
	v_pk_fma_f32 v[78:79], v[4:5], s[2:3], v[176:177] op_sel_hi:[1,0,1]
	v_pk_fma_f32 v[174:175], v[6:7], s[2:3], v[174:175] op_sel_hi:[1,0,1]
	v_pk_fma_f32 v[172:173], v[8:9], s[2:3], v[172:173] op_sel_hi:[1,0,1]
	v_pk_fma_f32 v[170:171], v[10:11], s[2:3], v[170:171] op_sel_hi:[1,0,1]
	v_pk_fma_f32 v[168:169], v[12:13], s[2:3], v[168:169] op_sel_hi:[1,0,1]
	v_pk_fma_f32 v[166:167], v[14:15], s[2:3], v[166:167] op_sel_hi:[1,0,1]
	v_pk_fma_f32 v[164:165], v[16:17], s[2:3], v[164:165] op_sel_hi:[1,0,1]
	v_pk_fma_f32 v[162:163], v[18:19], s[2:3], v[162:163] op_sel_hi:[1,0,1]
	v_pk_fma_f32 v[160:161], v[20:21], s[2:3], v[160:161] op_sel_hi:[1,0,1]
	v_pk_fma_f32 v[158:159], v[22:23], s[2:3], v[158:159] op_sel_hi:[1,0,1]
	v_pk_fma_f32 v[156:157], v[24:25], s[2:3], v[156:157] op_sel_hi:[1,0,1]
	v_pk_fma_f32 v[154:155], v[26:27], s[2:3], v[154:155] op_sel_hi:[1,0,1]
	v_pk_fma_f32 v[152:153], v[28:29], s[2:3], v[152:153] op_sel_hi:[1,0,1]
	v_pk_fma_f32 v[150:151], v[30:31], s[2:3], v[150:151] op_sel_hi:[1,0,1]
	v_readlane_b32 s2, v131, 33
	s_waitcnt vmcnt(20)
	v_cvt_scalef32_pk32_f32_fp6 v[0:31], v[68:73], 1.0
	v_pk_fma_f32 v[68:69], v[0:1], s[2:3], v[74:75] op_sel_hi:[1,0,1]
	v_pk_fma_f32 v[70:71], v[2:3], s[2:3], v[76:77] op_sel_hi:[1,0,1]
	v_pk_fma_f32 v[72:73], v[4:5], s[2:3], v[78:79] op_sel_hi:[1,0,1]
	v_pk_fma_f32 v[74:75], v[6:7], s[2:3], v[174:175] op_sel_hi:[1,0,1]
	v_pk_fma_f32 v[76:77], v[8:9], s[2:3], v[172:173] op_sel_hi:[1,0,1]
	v_pk_fma_f32 v[78:79], v[10:11], s[2:3], v[170:171] op_sel_hi:[1,0,1]
	v_pk_fma_f32 v[168:169], v[12:13], s[2:3], v[168:169] op_sel_hi:[1,0,1]
	v_pk_fma_f32 v[166:167], v[14:15], s[2:3], v[166:167] op_sel_hi:[1,0,1]
	v_pk_fma_f32 v[164:165], v[16:17], s[2:3], v[164:165] op_sel_hi:[1,0,1]
	v_pk_fma_f32 v[162:163], v[18:19], s[2:3], v[162:163] op_sel_hi:[1,0,1]
	v_pk_fma_f32 v[160:161], v[20:21], s[2:3], v[160:161] op_sel_hi:[1,0,1]
	v_pk_fma_f32 v[158:159], v[22:23], s[2:3], v[158:159] op_sel_hi:[1,0,1]
	v_pk_fma_f32 v[156:157], v[24:25], s[2:3], v[156:157] op_sel_hi:[1,0,1]
	v_pk_fma_f32 v[154:155], v[26:27], s[2:3], v[154:155] op_sel_hi:[1,0,1]
	v_pk_fma_f32 v[152:153], v[28:29], s[2:3], v[152:153] op_sel_hi:[1,0,1]
	v_pk_fma_f32 v[150:151], v[30:31], s[2:3], v[150:151] op_sel_hi:[1,0,1]
	v_readlane_b32 s2, v131, 34
	s_waitcnt vmcnt(18)
	v_cvt_scalef32_pk32_f32_fp6 v[0:31], v[56:61], 1.0
	v_pk_fma_f32 v[56:57], v[0:1], s[2:3], v[68:69] op_sel_hi:[1,0,1]
	v_pk_fma_f32 v[58:59], v[2:3], s[2:3], v[70:71] op_sel_hi:[1,0,1]
	v_pk_fma_f32 v[60:61], v[4:5], s[2:3], v[72:73] op_sel_hi:[1,0,1]
	v_pk_fma_f32 v[68:69], v[6:7], s[2:3], v[74:75] op_sel_hi:[1,0,1]
	v_pk_fma_f32 v[70:71], v[8:9], s[2:3], v[76:77] op_sel_hi:[1,0,1]
	v_pk_fma_f32 v[72:73], v[10:11], s[2:3], v[78:79] op_sel_hi:[1,0,1]
	v_pk_fma_f32 v[74:75], v[12:13], s[2:3], v[168:169] op_sel_hi:[1,0,1]
	v_pk_fma_f32 v[76:77], v[14:15], s[2:3], v[166:167] op_sel_hi:[1,0,1]
	v_pk_fma_f32 v[78:79], v[16:17], s[2:3], v[164:165] op_sel_hi:[1,0,1]
	v_pk_fma_f32 v[162:163], v[18:19], s[2:3], v[162:163] op_sel_hi:[1,0,1]
	v_pk_fma_f32 v[160:161], v[20:21], s[2:3], v[160:161] op_sel_hi:[1,0,1]
	v_pk_fma_f32 v[158:159], v[22:23], s[2:3], v[158:159] op_sel_hi:[1,0,1]
	v_pk_fma_f32 v[156:157], v[24:25], s[2:3], v[156:157] op_sel_hi:[1,0,1]
	v_pk_fma_f32 v[154:155], v[26:27], s[2:3], v[154:155] op_sel_hi:[1,0,1]
	v_pk_fma_f32 v[152:153], v[28:29], s[2:3], v[152:153] op_sel_hi:[1,0,1]
	v_pk_fma_f32 v[150:151], v[30:31], s[2:3], v[150:151] op_sel_hi:[1,0,1]
	v_readlane_b32 s2, v131, 35
	s_waitcnt vmcnt(16)
	v_cvt_scalef32_pk32_f32_fp6 v[0:31], v[44:49], 1.0
	v_pk_fma_f32 v[164:165], v[0:1], s[2:3], v[56:57] op_sel_hi:[1,0,1]
	v_pk_fma_f32 v[166:167], v[2:3], s[2:3], v[58:59] op_sel_hi:[1,0,1]
	v_pk_fma_f32 v[168:169], v[4:5], s[2:3], v[60:61] op_sel_hi:[1,0,1]
	v_pk_fma_f32 v[170:171], v[6:7], s[2:3], v[68:69] op_sel_hi:[1,0,1]
	v_pk_fma_f32 v[172:173], v[8:9], s[2:3], v[70:71] op_sel_hi:[1,0,1]
	v_pk_fma_f32 v[174:175], v[10:11], s[2:3], v[72:73] op_sel_hi:[1,0,1]
	v_pk_fma_f32 v[176:177], v[12:13], s[2:3], v[74:75] op_sel_hi:[1,0,1]
	v_pk_fma_f32 v[178:179], v[14:15], s[2:3], v[76:77] op_sel_hi:[1,0,1]
	v_pk_fma_f32 v[180:181], v[16:17], s[2:3], v[78:79] op_sel_hi:[1,0,1]
	v_pk_fma_f32 v[162:163], v[18:19], s[2:3], v[162:163] op_sel_hi:[1,0,1]
	v_pk_fma_f32 v[160:161], v[20:21], s[2:3], v[160:161] op_sel_hi:[1,0,1]
	v_pk_fma_f32 v[158:159], v[22:23], s[2:3], v[158:159] op_sel_hi:[1,0,1]
	v_pk_fma_f32 v[156:157], v[24:25], s[2:3], v[156:157] op_sel_hi:[1,0,1]
	v_pk_fma_f32 v[154:155], v[26:27], s[2:3], v[154:155] op_sel_hi:[1,0,1]
	v_pk_fma_f32 v[152:153], v[28:29], s[2:3], v[152:153] op_sel_hi:[1,0,1]
	v_pk_fma_f32 v[150:151], v[30:31], s[2:3], v[150:151] op_sel_hi:[1,0,1]
	v_readlane_b32 s2, v241, 44
	v_readlane_b32 s3, v241, 45
	v_readlane_b32 s100, v241, 46
	v_readlane_b32 s101, v241, 47
	s_nop 1
	buffer_load_dwordx4 v[74:77], v129, s[44:47], s2 offen
	buffer_load_dwordx2 v[78:79], v210, s[44:47], s2 offen
	buffer_load_dwordx4 v[68:71], v129, s[44:47], s3 offen
	buffer_load_dwordx2 v[72:73], v210, s[44:47], s3 offen
	buffer_load_dwordx4 v[56:59], v129, s[44:47], s100 offen
	buffer_load_dwordx2 v[60:61], v210, s[44:47], s100 offen
	buffer_load_dwordx4 v[44:47], v129, s[44:47], s101 offen
	buffer_load_dwordx2 v[48:49], v210, s[44:47], s101 offen
	v_readlane_b32 s2, v131, 36
	s_waitcnt vmcnt(22)
	v_cvt_scalef32_pk32_f32_fp6 v[0:31], v[62:67], 1.0
	v_pk_fma_f32 v[62:63], v[0:1], s[2:3], v[164:165] op_sel_hi:[1,0,1]
	v_pk_fma_f32 v[64:65], v[2:3], s[2:3], v[166:167] op_sel_hi:[1,0,1]
	v_pk_fma_f32 v[66:67], v[4:5], s[2:3], v[168:169] op_sel_hi:[1,0,1]
	v_pk_fma_f32 v[164:165], v[6:7], s[2:3], v[170:171] op_sel_hi:[1,0,1]
	v_pk_fma_f32 v[166:167], v[8:9], s[2:3], v[172:173] op_sel_hi:[1,0,1]
	v_pk_fma_f32 v[168:169], v[10:11], s[2:3], v[174:175] op_sel_hi:[1,0,1]
	v_pk_fma_f32 v[170:171], v[12:13], s[2:3], v[176:177] op_sel_hi:[1,0,1]
	v_pk_fma_f32 v[172:173], v[14:15], s[2:3], v[178:179] op_sel_hi:[1,0,1]
	v_pk_fma_f32 v[174:175], v[16:17], s[2:3], v[180:181] op_sel_hi:[1,0,1]
	v_pk_fma_f32 v[162:163], v[18:19], s[2:3], v[162:163] op_sel_hi:[1,0,1]
	v_pk_fma_f32 v[160:161], v[20:21], s[2:3], v[160:161] op_sel_hi:[1,0,1]
	v_pk_fma_f32 v[158:159], v[22:23], s[2:3], v[158:159] op_sel_hi:[1,0,1]
	v_pk_fma_f32 v[156:157], v[24:25], s[2:3], v[156:157] op_sel_hi:[1,0,1]
	v_pk_fma_f32 v[154:155], v[26:27], s[2:3], v[154:155] op_sel_hi:[1,0,1]
	v_pk_fma_f32 v[152:153], v[28:29], s[2:3], v[152:153] op_sel_hi:[1,0,1]
	v_pk_fma_f32 v[150:151], v[30:31], s[2:3], v[150:151] op_sel_hi:[1,0,1]
	v_readlane_b32 s2, v131, 37
	s_waitcnt vmcnt(20)
	v_cvt_scalef32_pk32_f32_fp6 v[0:31], v[50:55], 1.0
	v_pk_fma_f32 v[50:51], v[0:1], s[2:3], v[62:63] op_sel_hi:[1,0,1]
	v_pk_fma_f32 v[52:53], v[2:3], s[2:3], v[64:65] op_sel_hi:[1,0,1]
	v_pk_fma_f32 v[54:55], v[4:5], s[2:3], v[66:67] op_sel_hi:[1,0,1]
	v_pk_fma_f32 v[62:63], v[6:7], s[2:3], v[164:165] op_sel_hi:[1,0,1]
	v_pk_fma_f32 v[64:65], v[8:9], s[2:3], v[166:167] op_sel_hi:[1,0,1]
	v_pk_fma_f32 v[66:67], v[10:11], s[2:3], v[168:169] op_sel_hi:[1,0,1]
	v_pk_fma_f32 v[164:165], v[12:13], s[2:3], v[170:171] op_sel_hi:[1,0,1]
	v_pk_fma_f32 v[166:167], v[14:15], s[2:3], v[172:173] op_sel_hi:[1,0,1]
	v_pk_fma_f32 v[168:169], v[16:17], s[2:3], v[174:175] op_sel_hi:[1,0,1]
	v_pk_fma_f32 v[162:163], v[18:19], s[2:3], v[162:163] op_sel_hi:[1,0,1]
	v_pk_fma_f32 v[160:161], v[20:21], s[2:3], v[160:161] op_sel_hi:[1,0,1]
	v_pk_fma_f32 v[158:159], v[22:23], s[2:3], v[158:159] op_sel_hi:[1,0,1]
	v_pk_fma_f32 v[156:157], v[24:25], s[2:3], v[156:157] op_sel_hi:[1,0,1]
	v_pk_fma_f32 v[154:155], v[26:27], s[2:3], v[154:155] op_sel_hi:[1,0,1]
	v_pk_fma_f32 v[152:153], v[28:29], s[2:3], v[152:153] op_sel_hi:[1,0,1]
	v_pk_fma_f32 v[150:151], v[30:31], s[2:3], v[150:151] op_sel_hi:[1,0,1]
	v_readlane_b32 s2, v131, 38
	s_waitcnt vmcnt(18)
	v_cvt_scalef32_pk32_f32_fp6 v[0:31], v[38:43], 1.0
	v_pk_fma_f32 v[38:39], v[0:1], s[2:3], v[50:51] op_sel_hi:[1,0,1]
	v_pk_fma_f32 v[40:41], v[2:3], s[2:3], v[52:53] op_sel_hi:[1,0,1]
	v_pk_fma_f32 v[42:43], v[4:5], s[2:3], v[54:55] op_sel_hi:[1,0,1]
	v_pk_fma_f32 v[50:51], v[6:7], s[2:3], v[62:63] op_sel_hi:[1,0,1]
	v_pk_fma_f32 v[52:53], v[8:9], s[2:3], v[64:65] op_sel_hi:[1,0,1]
	v_pk_fma_f32 v[54:55], v[10:11], s[2:3], v[66:67] op_sel_hi:[1,0,1]
	v_pk_fma_f32 v[62:63], v[12:13], s[2:3], v[164:165] op_sel_hi:[1,0,1]
	v_pk_fma_f32 v[64:65], v[14:15], s[2:3], v[166:167] op_sel_hi:[1,0,1]
	v_pk_fma_f32 v[66:67], v[16:17], s[2:3], v[168:169] op_sel_hi:[1,0,1]
	v_pk_fma_f32 v[162:163], v[18:19], s[2:3], v[162:163] op_sel_hi:[1,0,1]
	v_pk_fma_f32 v[160:161], v[20:21], s[2:3], v[160:161] op_sel_hi:[1,0,1]
	v_pk_fma_f32 v[158:159], v[22:23], s[2:3], v[158:159] op_sel_hi:[1,0,1]
	v_pk_fma_f32 v[156:157], v[24:25], s[2:3], v[156:157] op_sel_hi:[1,0,1]
	v_pk_fma_f32 v[154:155], v[26:27], s[2:3], v[154:155] op_sel_hi:[1,0,1]
	v_pk_fma_f32 v[152:153], v[28:29], s[2:3], v[152:153] op_sel_hi:[1,0,1]
	v_pk_fma_f32 v[150:151], v[30:31], s[2:3], v[150:151] op_sel_hi:[1,0,1]
	v_readlane_b32 s2, v131, 39
	s_waitcnt vmcnt(16)
	v_cvt_scalef32_pk32_f32_fp6 v[0:31], v[32:37], 1.0
	v_pk_fma_f32 v[164:165], v[0:1], s[2:3], v[38:39] op_sel_hi:[1,0,1]
	v_pk_fma_f32 v[166:167], v[2:3], s[2:3], v[40:41] op_sel_hi:[1,0,1]
	v_pk_fma_f32 v[168:169], v[4:5], s[2:3], v[42:43] op_sel_hi:[1,0,1]
	v_pk_fma_f32 v[170:171], v[6:7], s[2:3], v[50:51] op_sel_hi:[1,0,1]
	v_pk_fma_f32 v[172:173], v[8:9], s[2:3], v[52:53] op_sel_hi:[1,0,1]
	v_pk_fma_f32 v[174:175], v[10:11], s[2:3], v[54:55] op_sel_hi:[1,0,1]
	v_pk_fma_f32 v[176:177], v[12:13], s[2:3], v[62:63] op_sel_hi:[1,0,1]
	v_pk_fma_f32 v[178:179], v[14:15], s[2:3], v[64:65] op_sel_hi:[1,0,1]
	v_pk_fma_f32 v[180:181], v[16:17], s[2:3], v[66:67] op_sel_hi:[1,0,1]
	v_pk_fma_f32 v[162:163], v[18:19], s[2:3], v[162:163] op_sel_hi:[1,0,1]
	v_pk_fma_f32 v[160:161], v[20:21], s[2:3], v[160:161] op_sel_hi:[1,0,1]
	v_pk_fma_f32 v[158:159], v[22:23], s[2:3], v[158:159] op_sel_hi:[1,0,1]
	v_pk_fma_f32 v[156:157], v[24:25], s[2:3], v[156:157] op_sel_hi:[1,0,1]
	v_pk_fma_f32 v[154:155], v[26:27], s[2:3], v[154:155] op_sel_hi:[1,0,1]
	v_pk_fma_f32 v[152:153], v[28:29], s[2:3], v[152:153] op_sel_hi:[1,0,1]
	v_pk_fma_f32 v[150:151], v[30:31], s[2:3], v[150:151] op_sel_hi:[1,0,1]
	v_readlane_b32 s2, v241, 48
	v_readlane_b32 s3, v241, 49
	v_readlane_b32 s100, v241, 50
	v_readlane_b32 s101, v241, 51
	s_nop 1
	buffer_load_dwordx4 v[62:65], v129, s[44:47], s2 offen
	buffer_load_dwordx2 v[66:67], v210, s[44:47], s2 offen
	buffer_load_dwordx4 v[50:53], v129, s[44:47], s3 offen
	buffer_load_dwordx2 v[54:55], v210, s[44:47], s3 offen
	buffer_load_dwordx4 v[38:41], v129, s[44:47], s100 offen
	buffer_load_dwordx2 v[42:43], v210, s[44:47], s100 offen
	buffer_load_dwordx4 v[32:35], v129, s[44:47], s101 offen
	buffer_load_dwordx2 v[36:37], v210, s[44:47], s101 offen
	v_readlane_b32 s2, v131, 40
	s_waitcnt vmcnt(22)
	v_cvt_scalef32_pk32_f32_fp6 v[0:31], v[98:103], 1.0
	v_pk_fma_f32 v[98:99], v[0:1], s[2:3], v[164:165] op_sel_hi:[1,0,1]
	v_pk_fma_f32 v[100:101], v[2:3], s[2:3], v[166:167] op_sel_hi:[1,0,1]
	v_pk_fma_f32 v[102:103], v[4:5], s[2:3], v[168:169] op_sel_hi:[1,0,1]
	v_pk_fma_f32 v[164:165], v[6:7], s[2:3], v[170:171] op_sel_hi:[1,0,1]
	v_pk_fma_f32 v[166:167], v[8:9], s[2:3], v[172:173] op_sel_hi:[1,0,1]
	v_pk_fma_f32 v[168:169], v[10:11], s[2:3], v[174:175] op_sel_hi:[1,0,1]
	v_pk_fma_f32 v[170:171], v[12:13], s[2:3], v[176:177] op_sel_hi:[1,0,1]
	v_pk_fma_f32 v[172:173], v[14:15], s[2:3], v[178:179] op_sel_hi:[1,0,1]
	v_pk_fma_f32 v[174:175], v[16:17], s[2:3], v[180:181] op_sel_hi:[1,0,1]
	v_pk_fma_f32 v[162:163], v[18:19], s[2:3], v[162:163] op_sel_hi:[1,0,1]
	v_pk_fma_f32 v[160:161], v[20:21], s[2:3], v[160:161] op_sel_hi:[1,0,1]
	v_pk_fma_f32 v[158:159], v[22:23], s[2:3], v[158:159] op_sel_hi:[1,0,1]
	v_pk_fma_f32 v[156:157], v[24:25], s[2:3], v[156:157] op_sel_hi:[1,0,1]
	v_pk_fma_f32 v[154:155], v[26:27], s[2:3], v[154:155] op_sel_hi:[1,0,1]
	v_pk_fma_f32 v[152:153], v[28:29], s[2:3], v[152:153] op_sel_hi:[1,0,1]
	v_pk_fma_f32 v[150:151], v[30:31], s[2:3], v[150:151] op_sel_hi:[1,0,1]
	v_readlane_b32 s2, v131, 41
	s_waitcnt vmcnt(20)
	v_cvt_scalef32_pk32_f32_fp6 v[0:31], v[92:97], 1.0
	v_pk_fma_f32 v[92:93], v[0:1], s[2:3], v[98:99] op_sel_hi:[1,0,1]
	v_pk_fma_f32 v[94:95], v[2:3], s[2:3], v[100:101] op_sel_hi:[1,0,1]
	v_pk_fma_f32 v[96:97], v[4:5], s[2:3], v[102:103] op_sel_hi:[1,0,1]
	v_pk_fma_f32 v[98:99], v[6:7], s[2:3], v[164:165] op_sel_hi:[1,0,1]
	v_pk_fma_f32 v[100:101], v[8:9], s[2:3], v[166:167] op_sel_hi:[1,0,1]
	v_pk_fma_f32 v[102:103], v[10:11], s[2:3], v[168:169] op_sel_hi:[1,0,1]
	v_pk_fma_f32 v[164:165], v[12:13], s[2:3], v[170:171] op_sel_hi:[1,0,1]
	v_pk_fma_f32 v[166:167], v[14:15], s[2:3], v[172:173] op_sel_hi:[1,0,1]
	v_pk_fma_f32 v[168:169], v[16:17], s[2:3], v[174:175] op_sel_hi:[1,0,1]
	v_pk_fma_f32 v[162:163], v[18:19], s[2:3], v[162:163] op_sel_hi:[1,0,1]
	v_pk_fma_f32 v[160:161], v[20:21], s[2:3], v[160:161] op_sel_hi:[1,0,1]
	v_pk_fma_f32 v[158:159], v[22:23], s[2:3], v[158:159] op_sel_hi:[1,0,1]
	v_pk_fma_f32 v[156:157], v[24:25], s[2:3], v[156:157] op_sel_hi:[1,0,1]
	v_pk_fma_f32 v[154:155], v[26:27], s[2:3], v[154:155] op_sel_hi:[1,0,1]
	v_pk_fma_f32 v[152:153], v[28:29], s[2:3], v[152:153] op_sel_hi:[1,0,1]
	v_pk_fma_f32 v[150:151], v[30:31], s[2:3], v[150:151] op_sel_hi:[1,0,1]
	v_readlane_b32 s2, v131, 42
	s_waitcnt vmcnt(18)
	v_cvt_scalef32_pk32_f32_fp6 v[0:31], v[86:91], 1.0
	v_pk_fma_f32 v[86:87], v[0:1], s[2:3], v[92:93] op_sel_hi:[1,0,1]
	v_pk_fma_f32 v[88:89], v[2:3], s[2:3], v[94:95] op_sel_hi:[1,0,1]
	v_pk_fma_f32 v[90:91], v[4:5], s[2:3], v[96:97] op_sel_hi:[1,0,1]
	v_pk_fma_f32 v[92:93], v[6:7], s[2:3], v[98:99] op_sel_hi:[1,0,1]
	v_pk_fma_f32 v[94:95], v[8:9], s[2:3], v[100:101] op_sel_hi:[1,0,1]
	v_pk_fma_f32 v[96:97], v[10:11], s[2:3], v[102:103] op_sel_hi:[1,0,1]
	v_pk_fma_f32 v[98:99], v[12:13], s[2:3], v[164:165] op_sel_hi:[1,0,1]
	v_pk_fma_f32 v[100:101], v[14:15], s[2:3], v[166:167] op_sel_hi:[1,0,1]
	v_pk_fma_f32 v[102:103], v[16:17], s[2:3], v[168:169] op_sel_hi:[1,0,1]
	v_pk_fma_f32 v[162:163], v[18:19], s[2:3], v[162:163] op_sel_hi:[1,0,1]
	v_pk_fma_f32 v[160:161], v[20:21], s[2:3], v[160:161] op_sel_hi:[1,0,1]
	v_pk_fma_f32 v[158:159], v[22:23], s[2:3], v[158:159] op_sel_hi:[1,0,1]
	v_pk_fma_f32 v[156:157], v[24:25], s[2:3], v[156:157] op_sel_hi:[1,0,1]
	v_pk_fma_f32 v[154:155], v[26:27], s[2:3], v[154:155] op_sel_hi:[1,0,1]
	v_pk_fma_f32 v[152:153], v[28:29], s[2:3], v[152:153] op_sel_hi:[1,0,1]
	v_pk_fma_f32 v[150:151], v[30:31], s[2:3], v[150:151] op_sel_hi:[1,0,1]
	v_readlane_b32 s2, v131, 43
	s_waitcnt vmcnt(16)
	v_cvt_scalef32_pk32_f32_fp6 v[0:31], v[80:85], 1.0
	v_pk_fma_f32 v[180:181], v[0:1], s[2:3], v[86:87] op_sel_hi:[1,0,1]
	v_pk_fma_f32 v[178:179], v[2:3], s[2:3], v[88:89] op_sel_hi:[1,0,1]
	v_pk_fma_f32 v[176:177], v[4:5], s[2:3], v[90:91] op_sel_hi:[1,0,1]
	v_pk_fma_f32 v[174:175], v[6:7], s[2:3], v[92:93] op_sel_hi:[1,0,1]
	v_pk_fma_f32 v[172:173], v[8:9], s[2:3], v[94:95] op_sel_hi:[1,0,1]
	v_pk_fma_f32 v[170:171], v[10:11], s[2:3], v[96:97] op_sel_hi:[1,0,1]
	v_pk_fma_f32 v[168:169], v[12:13], s[2:3], v[98:99] op_sel_hi:[1,0,1]
	v_pk_fma_f32 v[166:167], v[14:15], s[2:3], v[100:101] op_sel_hi:[1,0,1]
	v_pk_fma_f32 v[164:165], v[16:17], s[2:3], v[102:103] op_sel_hi:[1,0,1]
	v_pk_fma_f32 v[162:163], v[18:19], s[2:3], v[162:163] op_sel_hi:[1,0,1]
	v_pk_fma_f32 v[160:161], v[20:21], s[2:3], v[160:161] op_sel_hi:[1,0,1]
	v_pk_fma_f32 v[158:159], v[22:23], s[2:3], v[158:159] op_sel_hi:[1,0,1]
	v_pk_fma_f32 v[156:157], v[24:25], s[2:3], v[156:157] op_sel_hi:[1,0,1]
	v_pk_fma_f32 v[154:155], v[26:27], s[2:3], v[154:155] op_sel_hi:[1,0,1]
	v_pk_fma_f32 v[152:153], v[28:29], s[2:3], v[152:153] op_sel_hi:[1,0,1]
	v_pk_fma_f32 v[150:151], v[30:31], s[2:3], v[150:151] op_sel_hi:[1,0,1]
	v_readlane_b32 s2, v241, 52
	v_readlane_b32 s3, v241, 53
	v_readlane_b32 s100, v241, 54
	v_readlane_b32 s101, v241, 55
	s_nop 1
	buffer_load_dwordx4 v[98:101], v129, s[44:47], s2 offen
	buffer_load_dwordx2 v[102:103], v210, s[44:47], s2 offen
	buffer_load_dwordx4 v[92:95], v129, s[44:47], s3 offen
	buffer_load_dwordx2 v[96:97], v210, s[44:47], s3 offen
	buffer_load_dwordx4 v[86:89], v129, s[44:47], s100 offen
	buffer_load_dwordx2 v[90:91], v210, s[44:47], s100 offen
	buffer_load_dwordx4 v[80:83], v129, s[44:47], s101 offen
	buffer_load_dwordx2 v[84:85], v210, s[44:47], s101 offen
	v_readlane_b32 s2, v131, 44
	s_waitcnt vmcnt(22)
	v_cvt_scalef32_pk32_f32_fp6 v[0:31], v[74:79], 1.0
	v_pk_fma_f32 v[74:75], v[0:1], s[2:3], v[180:181] op_sel_hi:[1,0,1]
	v_pk_fma_f32 v[76:77], v[2:3], s[2:3], v[178:179] op_sel_hi:[1,0,1]
	v_pk_fma_f32 v[78:79], v[4:5], s[2:3], v[176:177] op_sel_hi:[1,0,1]
	v_pk_fma_f32 v[174:175], v[6:7], s[2:3], v[174:175] op_sel_hi:[1,0,1]
	v_pk_fma_f32 v[172:173], v[8:9], s[2:3], v[172:173] op_sel_hi:[1,0,1]
	v_pk_fma_f32 v[170:171], v[10:11], s[2:3], v[170:171] op_sel_hi:[1,0,1]
	v_pk_fma_f32 v[168:169], v[12:13], s[2:3], v[168:169] op_sel_hi:[1,0,1]
	v_pk_fma_f32 v[166:167], v[14:15], s[2:3], v[166:167] op_sel_hi:[1,0,1]
	v_pk_fma_f32 v[164:165], v[16:17], s[2:3], v[164:165] op_sel_hi:[1,0,1]
	v_pk_fma_f32 v[162:163], v[18:19], s[2:3], v[162:163] op_sel_hi:[1,0,1]
	v_pk_fma_f32 v[160:161], v[20:21], s[2:3], v[160:161] op_sel_hi:[1,0,1]
	v_pk_fma_f32 v[158:159], v[22:23], s[2:3], v[158:159] op_sel_hi:[1,0,1]
	v_pk_fma_f32 v[156:157], v[24:25], s[2:3], v[156:157] op_sel_hi:[1,0,1]
	v_pk_fma_f32 v[154:155], v[26:27], s[2:3], v[154:155] op_sel_hi:[1,0,1]
	v_pk_fma_f32 v[152:153], v[28:29], s[2:3], v[152:153] op_sel_hi:[1,0,1]
	v_pk_fma_f32 v[150:151], v[30:31], s[2:3], v[150:151] op_sel_hi:[1,0,1]
	v_readlane_b32 s2, v131, 45
	s_waitcnt vmcnt(20)
	v_cvt_scalef32_pk32_f32_fp6 v[0:31], v[68:73], 1.0
	v_pk_fma_f32 v[68:69], v[0:1], s[2:3], v[74:75] op_sel_hi:[1,0,1]
	v_pk_fma_f32 v[70:71], v[2:3], s[2:3], v[76:77] op_sel_hi:[1,0,1]
	v_pk_fma_f32 v[72:73], v[4:5], s[2:3], v[78:79] op_sel_hi:[1,0,1]
	v_pk_fma_f32 v[74:75], v[6:7], s[2:3], v[174:175] op_sel_hi:[1,0,1]
	v_pk_fma_f32 v[76:77], v[8:9], s[2:3], v[172:173] op_sel_hi:[1,0,1]
	v_pk_fma_f32 v[78:79], v[10:11], s[2:3], v[170:171] op_sel_hi:[1,0,1]
	v_pk_fma_f32 v[168:169], v[12:13], s[2:3], v[168:169] op_sel_hi:[1,0,1]
	v_pk_fma_f32 v[166:167], v[14:15], s[2:3], v[166:167] op_sel_hi:[1,0,1]
	v_pk_fma_f32 v[164:165], v[16:17], s[2:3], v[164:165] op_sel_hi:[1,0,1]
	v_pk_fma_f32 v[162:163], v[18:19], s[2:3], v[162:163] op_sel_hi:[1,0,1]
	v_pk_fma_f32 v[160:161], v[20:21], s[2:3], v[160:161] op_sel_hi:[1,0,1]
	v_pk_fma_f32 v[158:159], v[22:23], s[2:3], v[158:159] op_sel_hi:[1,0,1]
	v_pk_fma_f32 v[156:157], v[24:25], s[2:3], v[156:157] op_sel_hi:[1,0,1]
	v_pk_fma_f32 v[154:155], v[26:27], s[2:3], v[154:155] op_sel_hi:[1,0,1]
	v_pk_fma_f32 v[152:153], v[28:29], s[2:3], v[152:153] op_sel_hi:[1,0,1]
	v_pk_fma_f32 v[150:151], v[30:31], s[2:3], v[150:151] op_sel_hi:[1,0,1]
	v_readlane_b32 s2, v131, 46
	s_waitcnt vmcnt(18)
	v_cvt_scalef32_pk32_f32_fp6 v[0:31], v[56:61], 1.0
	v_pk_fma_f32 v[56:57], v[0:1], s[2:3], v[68:69] op_sel_hi:[1,0,1]
	v_pk_fma_f32 v[58:59], v[2:3], s[2:3], v[70:71] op_sel_hi:[1,0,1]
	v_pk_fma_f32 v[60:61], v[4:5], s[2:3], v[72:73] op_sel_hi:[1,0,1]
	v_pk_fma_f32 v[68:69], v[6:7], s[2:3], v[74:75] op_sel_hi:[1,0,1]
	v_pk_fma_f32 v[70:71], v[8:9], s[2:3], v[76:77] op_sel_hi:[1,0,1]
	v_pk_fma_f32 v[72:73], v[10:11], s[2:3], v[78:79] op_sel_hi:[1,0,1]
	v_pk_fma_f32 v[74:75], v[12:13], s[2:3], v[168:169] op_sel_hi:[1,0,1]
	v_pk_fma_f32 v[76:77], v[14:15], s[2:3], v[166:167] op_sel_hi:[1,0,1]
	v_pk_fma_f32 v[78:79], v[16:17], s[2:3], v[164:165] op_sel_hi:[1,0,1]
	v_pk_fma_f32 v[162:163], v[18:19], s[2:3], v[162:163] op_sel_hi:[1,0,1]
	v_pk_fma_f32 v[160:161], v[20:21], s[2:3], v[160:161] op_sel_hi:[1,0,1]
	v_pk_fma_f32 v[158:159], v[22:23], s[2:3], v[158:159] op_sel_hi:[1,0,1]
	v_pk_fma_f32 v[156:157], v[24:25], s[2:3], v[156:157] op_sel_hi:[1,0,1]
	v_pk_fma_f32 v[154:155], v[26:27], s[2:3], v[154:155] op_sel_hi:[1,0,1]
	v_pk_fma_f32 v[152:153], v[28:29], s[2:3], v[152:153] op_sel_hi:[1,0,1]
	v_pk_fma_f32 v[150:151], v[30:31], s[2:3], v[150:151] op_sel_hi:[1,0,1]
	v_readlane_b32 s2, v131, 47
	s_waitcnt vmcnt(16)
	v_cvt_scalef32_pk32_f32_fp6 v[0:31], v[44:49], 1.0
	v_pk_fma_f32 v[164:165], v[0:1], s[2:3], v[56:57] op_sel_hi:[1,0,1]
	v_pk_fma_f32 v[166:167], v[2:3], s[2:3], v[58:59] op_sel_hi:[1,0,1]
	v_pk_fma_f32 v[168:169], v[4:5], s[2:3], v[60:61] op_sel_hi:[1,0,1]
	v_pk_fma_f32 v[170:171], v[6:7], s[2:3], v[68:69] op_sel_hi:[1,0,1]
	v_pk_fma_f32 v[172:173], v[8:9], s[2:3], v[70:71] op_sel_hi:[1,0,1]
	v_pk_fma_f32 v[174:175], v[10:11], s[2:3], v[72:73] op_sel_hi:[1,0,1]
	v_pk_fma_f32 v[176:177], v[12:13], s[2:3], v[74:75] op_sel_hi:[1,0,1]
	v_pk_fma_f32 v[178:179], v[14:15], s[2:3], v[76:77] op_sel_hi:[1,0,1]
	v_pk_fma_f32 v[180:181], v[16:17], s[2:3], v[78:79] op_sel_hi:[1,0,1]
	v_pk_fma_f32 v[162:163], v[18:19], s[2:3], v[162:163] op_sel_hi:[1,0,1]
	v_pk_fma_f32 v[160:161], v[20:21], s[2:3], v[160:161] op_sel_hi:[1,0,1]
	v_pk_fma_f32 v[158:159], v[22:23], s[2:3], v[158:159] op_sel_hi:[1,0,1]
	v_pk_fma_f32 v[156:157], v[24:25], s[2:3], v[156:157] op_sel_hi:[1,0,1]
	v_pk_fma_f32 v[154:155], v[26:27], s[2:3], v[154:155] op_sel_hi:[1,0,1]
	v_pk_fma_f32 v[152:153], v[28:29], s[2:3], v[152:153] op_sel_hi:[1,0,1]
	v_pk_fma_f32 v[150:151], v[30:31], s[2:3], v[150:151] op_sel_hi:[1,0,1]
	v_readlane_b32 s2, v241, 56
	v_readlane_b32 s3, v241, 57
	v_readlane_b32 s100, v241, 58
	v_readlane_b32 s101, v241, 59
	s_nop 1
	buffer_load_dwordx4 v[74:77], v129, s[44:47], s2 offen
	buffer_load_dwordx2 v[78:79], v210, s[44:47], s2 offen
	buffer_load_dwordx4 v[68:71], v129, s[44:47], s3 offen
	buffer_load_dwordx2 v[72:73], v210, s[44:47], s3 offen
	buffer_load_dwordx4 v[56:59], v129, s[44:47], s100 offen
	buffer_load_dwordx2 v[60:61], v210, s[44:47], s100 offen
	buffer_load_dwordx4 v[44:47], v129, s[44:47], s101 offen
	buffer_load_dwordx2 v[48:49], v210, s[44:47], s101 offen
	v_readlane_b32 s2, v131, 48
	s_waitcnt vmcnt(22)
	v_cvt_scalef32_pk32_f32_fp6 v[0:31], v[62:67], 1.0
	v_pk_fma_f32 v[62:63], v[0:1], s[2:3], v[164:165] op_sel_hi:[1,0,1]
	v_pk_fma_f32 v[64:65], v[2:3], s[2:3], v[166:167] op_sel_hi:[1,0,1]
	v_pk_fma_f32 v[66:67], v[4:5], s[2:3], v[168:169] op_sel_hi:[1,0,1]
	v_pk_fma_f32 v[164:165], v[6:7], s[2:3], v[170:171] op_sel_hi:[1,0,1]
	v_pk_fma_f32 v[166:167], v[8:9], s[2:3], v[172:173] op_sel_hi:[1,0,1]
	v_pk_fma_f32 v[168:169], v[10:11], s[2:3], v[174:175] op_sel_hi:[1,0,1]
	v_pk_fma_f32 v[170:171], v[12:13], s[2:3], v[176:177] op_sel_hi:[1,0,1]
	v_pk_fma_f32 v[172:173], v[14:15], s[2:3], v[178:179] op_sel_hi:[1,0,1]
	v_pk_fma_f32 v[174:175], v[16:17], s[2:3], v[180:181] op_sel_hi:[1,0,1]
	v_pk_fma_f32 v[162:163], v[18:19], s[2:3], v[162:163] op_sel_hi:[1,0,1]
	v_pk_fma_f32 v[160:161], v[20:21], s[2:3], v[160:161] op_sel_hi:[1,0,1]
	v_pk_fma_f32 v[158:159], v[22:23], s[2:3], v[158:159] op_sel_hi:[1,0,1]
	v_pk_fma_f32 v[156:157], v[24:25], s[2:3], v[156:157] op_sel_hi:[1,0,1]
	v_pk_fma_f32 v[154:155], v[26:27], s[2:3], v[154:155] op_sel_hi:[1,0,1]
	v_pk_fma_f32 v[152:153], v[28:29], s[2:3], v[152:153] op_sel_hi:[1,0,1]
	v_pk_fma_f32 v[150:151], v[30:31], s[2:3], v[150:151] op_sel_hi:[1,0,1]
	v_readlane_b32 s2, v131, 49
	s_waitcnt vmcnt(20)
	v_cvt_scalef32_pk32_f32_fp6 v[0:31], v[50:55], 1.0
	v_pk_fma_f32 v[50:51], v[0:1], s[2:3], v[62:63] op_sel_hi:[1,0,1]
	v_pk_fma_f32 v[52:53], v[2:3], s[2:3], v[64:65] op_sel_hi:[1,0,1]
	v_pk_fma_f32 v[54:55], v[4:5], s[2:3], v[66:67] op_sel_hi:[1,0,1]
	v_pk_fma_f32 v[62:63], v[6:7], s[2:3], v[164:165] op_sel_hi:[1,0,1]
	v_pk_fma_f32 v[64:65], v[8:9], s[2:3], v[166:167] op_sel_hi:[1,0,1]
	v_pk_fma_f32 v[66:67], v[10:11], s[2:3], v[168:169] op_sel_hi:[1,0,1]
	v_pk_fma_f32 v[164:165], v[12:13], s[2:3], v[170:171] op_sel_hi:[1,0,1]
	v_pk_fma_f32 v[166:167], v[14:15], s[2:3], v[172:173] op_sel_hi:[1,0,1]
	v_pk_fma_f32 v[168:169], v[16:17], s[2:3], v[174:175] op_sel_hi:[1,0,1]
	v_pk_fma_f32 v[162:163], v[18:19], s[2:3], v[162:163] op_sel_hi:[1,0,1]
	v_pk_fma_f32 v[160:161], v[20:21], s[2:3], v[160:161] op_sel_hi:[1,0,1]
	v_pk_fma_f32 v[158:159], v[22:23], s[2:3], v[158:159] op_sel_hi:[1,0,1]
	v_pk_fma_f32 v[156:157], v[24:25], s[2:3], v[156:157] op_sel_hi:[1,0,1]
	v_pk_fma_f32 v[154:155], v[26:27], s[2:3], v[154:155] op_sel_hi:[1,0,1]
	v_pk_fma_f32 v[152:153], v[28:29], s[2:3], v[152:153] op_sel_hi:[1,0,1]
	v_pk_fma_f32 v[150:151], v[30:31], s[2:3], v[150:151] op_sel_hi:[1,0,1]
	v_readlane_b32 s2, v131, 50
	s_waitcnt vmcnt(18)
	v_cvt_scalef32_pk32_f32_fp6 v[0:31], v[38:43], 1.0
	v_pk_fma_f32 v[38:39], v[0:1], s[2:3], v[50:51] op_sel_hi:[1,0,1]
	v_pk_fma_f32 v[40:41], v[2:3], s[2:3], v[52:53] op_sel_hi:[1,0,1]
	v_pk_fma_f32 v[42:43], v[4:5], s[2:3], v[54:55] op_sel_hi:[1,0,1]
	v_pk_fma_f32 v[50:51], v[6:7], s[2:3], v[62:63] op_sel_hi:[1,0,1]
	v_pk_fma_f32 v[52:53], v[8:9], s[2:3], v[64:65] op_sel_hi:[1,0,1]
	v_pk_fma_f32 v[54:55], v[10:11], s[2:3], v[66:67] op_sel_hi:[1,0,1]
	v_pk_fma_f32 v[62:63], v[12:13], s[2:3], v[164:165] op_sel_hi:[1,0,1]
	v_pk_fma_f32 v[64:65], v[14:15], s[2:3], v[166:167] op_sel_hi:[1,0,1]
	v_pk_fma_f32 v[66:67], v[16:17], s[2:3], v[168:169] op_sel_hi:[1,0,1]
	v_pk_fma_f32 v[162:163], v[18:19], s[2:3], v[162:163] op_sel_hi:[1,0,1]
	v_pk_fma_f32 v[160:161], v[20:21], s[2:3], v[160:161] op_sel_hi:[1,0,1]
	v_pk_fma_f32 v[158:159], v[22:23], s[2:3], v[158:159] op_sel_hi:[1,0,1]
	v_pk_fma_f32 v[156:157], v[24:25], s[2:3], v[156:157] op_sel_hi:[1,0,1]
	v_pk_fma_f32 v[154:155], v[26:27], s[2:3], v[154:155] op_sel_hi:[1,0,1]
	v_pk_fma_f32 v[152:153], v[28:29], s[2:3], v[152:153] op_sel_hi:[1,0,1]
	v_pk_fma_f32 v[150:151], v[30:31], s[2:3], v[150:151] op_sel_hi:[1,0,1]
	v_readlane_b32 s2, v131, 51
	s_waitcnt vmcnt(16)
	v_cvt_scalef32_pk32_f32_fp6 v[0:31], v[32:37], 1.0
	v_pk_fma_f32 v[164:165], v[0:1], s[2:3], v[38:39] op_sel_hi:[1,0,1]
	v_pk_fma_f32 v[166:167], v[2:3], s[2:3], v[40:41] op_sel_hi:[1,0,1]
	v_pk_fma_f32 v[168:169], v[4:5], s[2:3], v[42:43] op_sel_hi:[1,0,1]
	v_pk_fma_f32 v[170:171], v[6:7], s[2:3], v[50:51] op_sel_hi:[1,0,1]
	v_pk_fma_f32 v[172:173], v[8:9], s[2:3], v[52:53] op_sel_hi:[1,0,1]
	v_pk_fma_f32 v[174:175], v[10:11], s[2:3], v[54:55] op_sel_hi:[1,0,1]
	v_pk_fma_f32 v[176:177], v[12:13], s[2:3], v[62:63] op_sel_hi:[1,0,1]
	v_pk_fma_f32 v[178:179], v[14:15], s[2:3], v[64:65] op_sel_hi:[1,0,1]
	v_pk_fma_f32 v[180:181], v[16:17], s[2:3], v[66:67] op_sel_hi:[1,0,1]
	v_pk_fma_f32 v[162:163], v[18:19], s[2:3], v[162:163] op_sel_hi:[1,0,1]
	v_pk_fma_f32 v[160:161], v[20:21], s[2:3], v[160:161] op_sel_hi:[1,0,1]
	v_pk_fma_f32 v[158:159], v[22:23], s[2:3], v[158:159] op_sel_hi:[1,0,1]
	v_pk_fma_f32 v[156:157], v[24:25], s[2:3], v[156:157] op_sel_hi:[1,0,1]
	v_pk_fma_f32 v[154:155], v[26:27], s[2:3], v[154:155] op_sel_hi:[1,0,1]
	v_pk_fma_f32 v[152:153], v[28:29], s[2:3], v[152:153] op_sel_hi:[1,0,1]
	v_pk_fma_f32 v[150:151], v[30:31], s[2:3], v[150:151] op_sel_hi:[1,0,1]
	v_readlane_b32 s2, v241, 60
	v_readlane_b32 s3, v241, 61
	v_readlane_b32 s100, v241, 62
	v_readlane_b32 s101, v241, 63
	s_nop 1
	buffer_load_dwordx4 v[62:65], v129, s[44:47], s2 offen
	buffer_load_dwordx2 v[66:67], v210, s[44:47], s2 offen
	buffer_load_dwordx4 v[50:53], v129, s[44:47], s3 offen
	buffer_load_dwordx2 v[54:55], v210, s[44:47], s3 offen
	buffer_load_dwordx4 v[38:41], v129, s[44:47], s100 offen
	buffer_load_dwordx2 v[42:43], v210, s[44:47], s100 offen
	buffer_load_dwordx4 v[32:35], v129, s[44:47], s101 offen
	buffer_load_dwordx2 v[36:37], v210, s[44:47], s101 offen
	v_readlane_b32 s2, v131, 52
	s_waitcnt vmcnt(22)
	v_cvt_scalef32_pk32_f32_fp6 v[0:31], v[98:103], 1.0
	v_pk_fma_f32 v[98:99], v[0:1], s[2:3], v[164:165] op_sel_hi:[1,0,1]
	v_pk_fma_f32 v[100:101], v[2:3], s[2:3], v[166:167] op_sel_hi:[1,0,1]
	v_pk_fma_f32 v[102:103], v[4:5], s[2:3], v[168:169] op_sel_hi:[1,0,1]
	v_pk_fma_f32 v[164:165], v[6:7], s[2:3], v[170:171] op_sel_hi:[1,0,1]
	v_pk_fma_f32 v[166:167], v[8:9], s[2:3], v[172:173] op_sel_hi:[1,0,1]
	v_pk_fma_f32 v[168:169], v[10:11], s[2:3], v[174:175] op_sel_hi:[1,0,1]
	v_pk_fma_f32 v[170:171], v[12:13], s[2:3], v[176:177] op_sel_hi:[1,0,1]
	v_pk_fma_f32 v[172:173], v[14:15], s[2:3], v[178:179] op_sel_hi:[1,0,1]
	v_pk_fma_f32 v[174:175], v[16:17], s[2:3], v[180:181] op_sel_hi:[1,0,1]
	v_pk_fma_f32 v[162:163], v[18:19], s[2:3], v[162:163] op_sel_hi:[1,0,1]
	v_pk_fma_f32 v[160:161], v[20:21], s[2:3], v[160:161] op_sel_hi:[1,0,1]
	v_pk_fma_f32 v[158:159], v[22:23], s[2:3], v[158:159] op_sel_hi:[1,0,1]
	v_pk_fma_f32 v[156:157], v[24:25], s[2:3], v[156:157] op_sel_hi:[1,0,1]
	v_pk_fma_f32 v[154:155], v[26:27], s[2:3], v[154:155] op_sel_hi:[1,0,1]
	v_pk_fma_f32 v[152:153], v[28:29], s[2:3], v[152:153] op_sel_hi:[1,0,1]
	v_pk_fma_f32 v[150:151], v[30:31], s[2:3], v[150:151] op_sel_hi:[1,0,1]
	v_readlane_b32 s2, v131, 53
	s_waitcnt vmcnt(20)
	v_cvt_scalef32_pk32_f32_fp6 v[0:31], v[92:97], 1.0
	v_pk_fma_f32 v[92:93], v[0:1], s[2:3], v[98:99] op_sel_hi:[1,0,1]
	v_pk_fma_f32 v[94:95], v[2:3], s[2:3], v[100:101] op_sel_hi:[1,0,1]
	v_pk_fma_f32 v[96:97], v[4:5], s[2:3], v[102:103] op_sel_hi:[1,0,1]
	v_pk_fma_f32 v[98:99], v[6:7], s[2:3], v[164:165] op_sel_hi:[1,0,1]
	v_pk_fma_f32 v[100:101], v[8:9], s[2:3], v[166:167] op_sel_hi:[1,0,1]
	v_pk_fma_f32 v[102:103], v[10:11], s[2:3], v[168:169] op_sel_hi:[1,0,1]
	v_pk_fma_f32 v[164:165], v[12:13], s[2:3], v[170:171] op_sel_hi:[1,0,1]
	v_pk_fma_f32 v[166:167], v[14:15], s[2:3], v[172:173] op_sel_hi:[1,0,1]
	v_pk_fma_f32 v[168:169], v[16:17], s[2:3], v[174:175] op_sel_hi:[1,0,1]
	v_pk_fma_f32 v[162:163], v[18:19], s[2:3], v[162:163] op_sel_hi:[1,0,1]
	v_pk_fma_f32 v[160:161], v[20:21], s[2:3], v[160:161] op_sel_hi:[1,0,1]
	v_pk_fma_f32 v[158:159], v[22:23], s[2:3], v[158:159] op_sel_hi:[1,0,1]
	v_pk_fma_f32 v[156:157], v[24:25], s[2:3], v[156:157] op_sel_hi:[1,0,1]
	v_pk_fma_f32 v[154:155], v[26:27], s[2:3], v[154:155] op_sel_hi:[1,0,1]
	v_pk_fma_f32 v[152:153], v[28:29], s[2:3], v[152:153] op_sel_hi:[1,0,1]
	v_pk_fma_f32 v[150:151], v[30:31], s[2:3], v[150:151] op_sel_hi:[1,0,1]
	v_readlane_b32 s2, v131, 54
	s_waitcnt vmcnt(18)
	v_cvt_scalef32_pk32_f32_fp6 v[0:31], v[86:91], 1.0
	v_pk_fma_f32 v[86:87], v[0:1], s[2:3], v[92:93] op_sel_hi:[1,0,1]
	v_pk_fma_f32 v[88:89], v[2:3], s[2:3], v[94:95] op_sel_hi:[1,0,1]
	v_pk_fma_f32 v[90:91], v[4:5], s[2:3], v[96:97] op_sel_hi:[1,0,1]
	v_pk_fma_f32 v[92:93], v[6:7], s[2:3], v[98:99] op_sel_hi:[1,0,1]
	v_pk_fma_f32 v[94:95], v[8:9], s[2:3], v[100:101] op_sel_hi:[1,0,1]
	v_pk_fma_f32 v[96:97], v[10:11], s[2:3], v[102:103] op_sel_hi:[1,0,1]
	v_pk_fma_f32 v[98:99], v[12:13], s[2:3], v[164:165] op_sel_hi:[1,0,1]
	v_pk_fma_f32 v[100:101], v[14:15], s[2:3], v[166:167] op_sel_hi:[1,0,1]
	v_pk_fma_f32 v[102:103], v[16:17], s[2:3], v[168:169] op_sel_hi:[1,0,1]
	v_pk_fma_f32 v[162:163], v[18:19], s[2:3], v[162:163] op_sel_hi:[1,0,1]
	v_pk_fma_f32 v[160:161], v[20:21], s[2:3], v[160:161] op_sel_hi:[1,0,1]
	v_pk_fma_f32 v[158:159], v[22:23], s[2:3], v[158:159] op_sel_hi:[1,0,1]
	v_pk_fma_f32 v[156:157], v[24:25], s[2:3], v[156:157] op_sel_hi:[1,0,1]
	v_pk_fma_f32 v[154:155], v[26:27], s[2:3], v[154:155] op_sel_hi:[1,0,1]
	v_pk_fma_f32 v[152:153], v[28:29], s[2:3], v[152:153] op_sel_hi:[1,0,1]
	v_pk_fma_f32 v[150:151], v[30:31], s[2:3], v[150:151] op_sel_hi:[1,0,1]
	v_readlane_b32 s2, v131, 55
	s_waitcnt vmcnt(16)
	v_cvt_scalef32_pk32_f32_fp6 v[0:31], v[80:85], 1.0
	v_pk_fma_f32 v[180:181], v[0:1], s[2:3], v[86:87] op_sel_hi:[1,0,1]
	v_pk_fma_f32 v[178:179], v[2:3], s[2:3], v[88:89] op_sel_hi:[1,0,1]
	v_pk_fma_f32 v[176:177], v[4:5], s[2:3], v[90:91] op_sel_hi:[1,0,1]
	v_pk_fma_f32 v[174:175], v[6:7], s[2:3], v[92:93] op_sel_hi:[1,0,1]
	v_pk_fma_f32 v[172:173], v[8:9], s[2:3], v[94:95] op_sel_hi:[1,0,1]
	v_pk_fma_f32 v[170:171], v[10:11], s[2:3], v[96:97] op_sel_hi:[1,0,1]
	v_pk_fma_f32 v[168:169], v[12:13], s[2:3], v[98:99] op_sel_hi:[1,0,1]
	v_pk_fma_f32 v[166:167], v[14:15], s[2:3], v[100:101] op_sel_hi:[1,0,1]
	v_pk_fma_f32 v[164:165], v[16:17], s[2:3], v[102:103] op_sel_hi:[1,0,1]
	v_pk_fma_f32 v[162:163], v[18:19], s[2:3], v[162:163] op_sel_hi:[1,0,1]
	v_pk_fma_f32 v[160:161], v[20:21], s[2:3], v[160:161] op_sel_hi:[1,0,1]
	v_pk_fma_f32 v[158:159], v[22:23], s[2:3], v[158:159] op_sel_hi:[1,0,1]
	v_pk_fma_f32 v[156:157], v[24:25], s[2:3], v[156:157] op_sel_hi:[1,0,1]
	v_pk_fma_f32 v[154:155], v[26:27], s[2:3], v[154:155] op_sel_hi:[1,0,1]
	v_pk_fma_f32 v[152:153], v[28:29], s[2:3], v[152:153] op_sel_hi:[1,0,1]
	v_pk_fma_f32 v[150:151], v[30:31], s[2:3], v[150:151] op_sel_hi:[1,0,1]
	v_readlane_b32 s0, v131, 56
	s_waitcnt vmcnt(14)
	v_cvt_scalef32_pk32_f32_fp6 v[0:31], v[74:79], 1.0
	v_pk_fma_f32 v[74:75], v[0:1], s[0:1], v[180:181] op_sel_hi:[1,0,1]
	v_pk_fma_f32 v[76:77], v[2:3], s[0:1], v[178:179] op_sel_hi:[1,0,1]
	v_pk_fma_f32 v[78:79], v[4:5], s[0:1], v[176:177] op_sel_hi:[1,0,1]
	v_pk_fma_f32 v[80:81], v[6:7], s[0:1], v[174:175] op_sel_hi:[1,0,1]
	v_pk_fma_f32 v[82:83], v[8:9], s[0:1], v[172:173] op_sel_hi:[1,0,1]
	v_pk_fma_f32 v[84:85], v[10:11], s[0:1], v[170:171] op_sel_hi:[1,0,1]
	v_pk_fma_f32 v[86:87], v[12:13], s[0:1], v[168:169] op_sel_hi:[1,0,1]
	v_pk_fma_f32 v[88:89], v[14:15], s[0:1], v[166:167] op_sel_hi:[1,0,1]
	v_pk_fma_f32 v[90:91], v[16:17], s[0:1], v[164:165] op_sel_hi:[1,0,1]
	v_pk_fma_f32 v[92:93], v[18:19], s[0:1], v[162:163] op_sel_hi:[1,0,1]
	v_pk_fma_f32 v[94:95], v[20:21], s[0:1], v[160:161] op_sel_hi:[1,0,1]
	v_pk_fma_f32 v[96:97], v[22:23], s[0:1], v[158:159] op_sel_hi:[1,0,1]
	v_pk_fma_f32 v[98:99], v[24:25], s[0:1], v[156:157] op_sel_hi:[1,0,1]
	v_pk_fma_f32 v[100:101], v[26:27], s[0:1], v[154:155] op_sel_hi:[1,0,1]
	v_pk_fma_f32 v[102:103], v[28:29], s[0:1], v[152:153] op_sel_hi:[1,0,1]
	v_pk_fma_f32 v[150:151], v[30:31], s[0:1], v[150:151] op_sel_hi:[1,0,1]
	v_readlane_b32 s0, v131, 57
	s_waitcnt vmcnt(12)
	v_cvt_scalef32_pk32_f32_fp6 v[0:31], v[68:73], 1.0
	v_pk_fma_f32 v[68:69], v[0:1], s[0:1], v[74:75] op_sel_hi:[1,0,1]
	v_pk_fma_f32 v[70:71], v[2:3], s[0:1], v[76:77] op_sel_hi:[1,0,1]
	v_pk_fma_f32 v[72:73], v[4:5], s[0:1], v[78:79] op_sel_hi:[1,0,1]
	v_pk_fma_f32 v[74:75], v[6:7], s[0:1], v[80:81] op_sel_hi:[1,0,1]
	v_pk_fma_f32 v[76:77], v[8:9], s[0:1], v[82:83] op_sel_hi:[1,0,1]
	v_pk_fma_f32 v[78:79], v[10:11], s[0:1], v[84:85] op_sel_hi:[1,0,1]
	v_pk_fma_f32 v[80:81], v[12:13], s[0:1], v[86:87] op_sel_hi:[1,0,1]
	v_pk_fma_f32 v[82:83], v[14:15], s[0:1], v[88:89] op_sel_hi:[1,0,1]
	v_pk_fma_f32 v[84:85], v[16:17], s[0:1], v[90:91] op_sel_hi:[1,0,1]
	v_pk_fma_f32 v[86:87], v[18:19], s[0:1], v[92:93] op_sel_hi:[1,0,1]
	v_pk_fma_f32 v[88:89], v[20:21], s[0:1], v[94:95] op_sel_hi:[1,0,1]
	v_pk_fma_f32 v[90:91], v[22:23], s[0:1], v[96:97] op_sel_hi:[1,0,1]
	v_pk_fma_f32 v[92:93], v[24:25], s[0:1], v[98:99] op_sel_hi:[1,0,1]
	v_pk_fma_f32 v[94:95], v[26:27], s[0:1], v[100:101] op_sel_hi:[1,0,1]
	v_pk_fma_f32 v[96:97], v[28:29], s[0:1], v[102:103] op_sel_hi:[1,0,1]
	v_pk_fma_f32 v[98:99], v[30:31], s[0:1], v[150:151] op_sel_hi:[1,0,1]
	v_readlane_b32 s0, v131, 58
	s_waitcnt vmcnt(10)
	v_cvt_scalef32_pk32_f32_fp6 v[0:31], v[56:61], 1.0
	v_pk_fma_f32 v[56:57], v[0:1], s[0:1], v[68:69] op_sel_hi:[1,0,1]
	v_pk_fma_f32 v[58:59], v[2:3], s[0:1], v[70:71] op_sel_hi:[1,0,1]
	v_pk_fma_f32 v[60:61], v[4:5], s[0:1], v[72:73] op_sel_hi:[1,0,1]
	v_pk_fma_f32 v[68:69], v[6:7], s[0:1], v[74:75] op_sel_hi:[1,0,1]
	v_pk_fma_f32 v[70:71], v[8:9], s[0:1], v[76:77] op_sel_hi:[1,0,1]
	v_pk_fma_f32 v[72:73], v[10:11], s[0:1], v[78:79] op_sel_hi:[1,0,1]
	v_pk_fma_f32 v[74:75], v[12:13], s[0:1], v[80:81] op_sel_hi:[1,0,1]
	v_pk_fma_f32 v[76:77], v[14:15], s[0:1], v[82:83] op_sel_hi:[1,0,1]
	v_pk_fma_f32 v[78:79], v[16:17], s[0:1], v[84:85] op_sel_hi:[1,0,1]
	v_pk_fma_f32 v[80:81], v[18:19], s[0:1], v[86:87] op_sel_hi:[1,0,1]
	v_pk_fma_f32 v[82:83], v[20:21], s[0:1], v[88:89] op_sel_hi:[1,0,1]
	v_pk_fma_f32 v[84:85], v[22:23], s[0:1], v[90:91] op_sel_hi:[1,0,1]
	v_pk_fma_f32 v[86:87], v[24:25], s[0:1], v[92:93] op_sel_hi:[1,0,1]
	v_pk_fma_f32 v[88:89], v[26:27], s[0:1], v[94:95] op_sel_hi:[1,0,1]
	v_pk_fma_f32 v[90:91], v[28:29], s[0:1], v[96:97] op_sel_hi:[1,0,1]
	v_pk_fma_f32 v[92:93], v[30:31], s[0:1], v[98:99] op_sel_hi:[1,0,1]
	v_readlane_b32 s0, v131, 59
	s_waitcnt vmcnt(8)
	v_cvt_scalef32_pk32_f32_fp6 v[0:31], v[44:49], 1.0
	v_pk_fma_f32 v[46:47], v[2:3], s[0:1], v[58:59] op_sel_hi:[1,0,1]
	v_pk_fma_f32 v[44:45], v[0:1], s[0:1], v[56:57] op_sel_hi:[1,0,1]
	v_pk_fma_f32 v[48:49], v[4:5], s[0:1], v[60:61] op_sel_hi:[1,0,1]
	v_pk_fma_f32 v[56:57], v[6:7], s[0:1], v[68:69] op_sel_hi:[1,0,1]
	v_pk_fma_f32 v[58:59], v[8:9], s[0:1], v[70:71] op_sel_hi:[1,0,1]
	v_pk_fma_f32 v[60:61], v[10:11], s[0:1], v[72:73] op_sel_hi:[1,0,1]
	v_pk_fma_f32 v[68:69], v[12:13], s[0:1], v[74:75] op_sel_hi:[1,0,1]
	v_pk_fma_f32 v[70:71], v[14:15], s[0:1], v[76:77] op_sel_hi:[1,0,1]
	v_pk_fma_f32 v[72:73], v[16:17], s[0:1], v[78:79] op_sel_hi:[1,0,1]
	v_pk_fma_f32 v[74:75], v[18:19], s[0:1], v[80:81] op_sel_hi:[1,0,1]
	v_pk_fma_f32 v[76:77], v[20:21], s[0:1], v[82:83] op_sel_hi:[1,0,1]
	v_pk_fma_f32 v[78:79], v[22:23], s[0:1], v[84:85] op_sel_hi:[1,0,1]
	v_pk_fma_f32 v[80:81], v[24:25], s[0:1], v[86:87] op_sel_hi:[1,0,1]
	v_pk_fma_f32 v[82:83], v[26:27], s[0:1], v[88:89] op_sel_hi:[1,0,1]
	v_pk_fma_f32 v[84:85], v[28:29], s[0:1], v[90:91] op_sel_hi:[1,0,1]
	v_pk_fma_f32 v[86:87], v[30:31], s[0:1], v[92:93] op_sel_hi:[1,0,1]
	v_readlane_b32 s0, v131, 60
	s_waitcnt vmcnt(6)
	v_cvt_scalef32_pk32_f32_fp6 v[0:31], v[62:67], 1.0
	v_pk_fma_f32 v[44:45], v[0:1], s[0:1], v[44:45] op_sel_hi:[1,0,1]
	v_pk_fma_f32 v[46:47], v[2:3], s[0:1], v[46:47] op_sel_hi:[1,0,1]
	v_pk_fma_f32 v[48:49], v[4:5], s[0:1], v[48:49] op_sel_hi:[1,0,1]
	v_pk_fma_f32 v[56:57], v[6:7], s[0:1], v[56:57] op_sel_hi:[1,0,1]
	v_pk_fma_f32 v[58:59], v[8:9], s[0:1], v[58:59] op_sel_hi:[1,0,1]
	v_pk_fma_f32 v[60:61], v[10:11], s[0:1], v[60:61] op_sel_hi:[1,0,1]
	v_pk_fma_f32 v[62:63], v[12:13], s[0:1], v[68:69] op_sel_hi:[1,0,1]
	v_pk_fma_f32 v[64:65], v[14:15], s[0:1], v[70:71] op_sel_hi:[1,0,1]
	v_pk_fma_f32 v[66:67], v[16:17], s[0:1], v[72:73] op_sel_hi:[1,0,1]
	v_pk_fma_f32 v[68:69], v[18:19], s[0:1], v[74:75] op_sel_hi:[1,0,1]
	v_pk_fma_f32 v[70:71], v[20:21], s[0:1], v[76:77] op_sel_hi:[1,0,1]
	v_pk_fma_f32 v[72:73], v[22:23], s[0:1], v[78:79] op_sel_hi:[1,0,1]
	v_pk_fma_f32 v[74:75], v[24:25], s[0:1], v[80:81] op_sel_hi:[1,0,1]
	v_pk_fma_f32 v[76:77], v[26:27], s[0:1], v[82:83] op_sel_hi:[1,0,1]
	v_pk_fma_f32 v[78:79], v[28:29], s[0:1], v[84:85] op_sel_hi:[1,0,1]
	v_pk_fma_f32 v[80:81], v[30:31], s[0:1], v[86:87] op_sel_hi:[1,0,1]
	v_readlane_b32 s0, v131, 61
	s_waitcnt vmcnt(4)
	v_cvt_scalef32_pk32_f32_fp6 v[0:31], v[50:55], 1.0
	v_pk_fma_f32 v[44:45], v[0:1], s[0:1], v[44:45] op_sel_hi:[1,0,1]
	v_pk_fma_f32 v[46:47], v[2:3], s[0:1], v[46:47] op_sel_hi:[1,0,1]
	v_pk_fma_f32 v[48:49], v[4:5], s[0:1], v[48:49] op_sel_hi:[1,0,1]
	v_pk_fma_f32 v[50:51], v[6:7], s[0:1], v[56:57] op_sel_hi:[1,0,1]
	v_pk_fma_f32 v[52:53], v[8:9], s[0:1], v[58:59] op_sel_hi:[1,0,1]
	v_pk_fma_f32 v[54:55], v[10:11], s[0:1], v[60:61] op_sel_hi:[1,0,1]
	v_pk_fma_f32 v[56:57], v[12:13], s[0:1], v[62:63] op_sel_hi:[1,0,1]
	v_pk_fma_f32 v[58:59], v[14:15], s[0:1], v[64:65] op_sel_hi:[1,0,1]
	v_pk_fma_f32 v[60:61], v[16:17], s[0:1], v[66:67] op_sel_hi:[1,0,1]
	v_pk_fma_f32 v[62:63], v[18:19], s[0:1], v[68:69] op_sel_hi:[1,0,1]
	v_pk_fma_f32 v[64:65], v[20:21], s[0:1], v[70:71] op_sel_hi:[1,0,1]
	v_pk_fma_f32 v[66:67], v[22:23], s[0:1], v[72:73] op_sel_hi:[1,0,1]
	v_pk_fma_f32 v[68:69], v[24:25], s[0:1], v[74:75] op_sel_hi:[1,0,1]
	v_pk_fma_f32 v[70:71], v[26:27], s[0:1], v[76:77] op_sel_hi:[1,0,1]
	v_pk_fma_f32 v[72:73], v[28:29], s[0:1], v[78:79] op_sel_hi:[1,0,1]
	v_pk_fma_f32 v[74:75], v[30:31], s[0:1], v[80:81] op_sel_hi:[1,0,1]
	v_readlane_b32 s0, v131, 62
	s_waitcnt vmcnt(2)
	v_cvt_scalef32_pk32_f32_fp6 v[0:31], v[38:43], 1.0
	v_pk_fma_f32 v[38:39], v[0:1], s[0:1], v[44:45] op_sel_hi:[1,0,1]
	v_pk_fma_f32 v[40:41], v[2:3], s[0:1], v[46:47] op_sel_hi:[1,0,1]
	v_pk_fma_f32 v[42:43], v[4:5], s[0:1], v[48:49] op_sel_hi:[1,0,1]
	v_pk_fma_f32 v[44:45], v[6:7], s[0:1], v[50:51] op_sel_hi:[1,0,1]
	v_pk_fma_f32 v[46:47], v[8:9], s[0:1], v[52:53] op_sel_hi:[1,0,1]
	v_pk_fma_f32 v[48:49], v[10:11], s[0:1], v[54:55] op_sel_hi:[1,0,1]
	v_pk_fma_f32 v[50:51], v[12:13], s[0:1], v[56:57] op_sel_hi:[1,0,1]
	v_pk_fma_f32 v[52:53], v[14:15], s[0:1], v[58:59] op_sel_hi:[1,0,1]
	v_pk_fma_f32 v[54:55], v[16:17], s[0:1], v[60:61] op_sel_hi:[1,0,1]
	v_pk_fma_f32 v[56:57], v[18:19], s[0:1], v[62:63] op_sel_hi:[1,0,1]
	v_pk_fma_f32 v[58:59], v[20:21], s[0:1], v[64:65] op_sel_hi:[1,0,1]
	v_pk_fma_f32 v[62:63], v[22:23], s[0:1], v[66:67] op_sel_hi:[1,0,1]
	v_pk_fma_f32 v[64:65], v[24:25], s[0:1], v[68:69] op_sel_hi:[1,0,1]
	v_pk_fma_f32 v[66:67], v[26:27], s[0:1], v[70:71] op_sel_hi:[1,0,1]
	v_pk_fma_f32 v[68:69], v[28:29], s[0:1], v[72:73] op_sel_hi:[1,0,1]
	v_pk_fma_f32 v[70:71], v[30:31], s[0:1], v[74:75] op_sel_hi:[1,0,1]
	v_readlane_b32 s0, v131, 63
	s_waitcnt vmcnt(0)
	v_cvt_scalef32_pk32_f32_fp6 v[0:31], v[32:37], 1.0
	v_pk_fma_f32 v[34:35], v[0:1], s[0:1], v[38:39] op_sel_hi:[1,0,1]
	v_pk_fma_f32 v[32:33], v[2:3], s[0:1], v[40:41] op_sel_hi:[1,0,1]
	v_pk_fma_f32 v[38:39], v[4:5], s[0:1], v[42:43] op_sel_hi:[1,0,1]
	v_pk_fma_f32 v[36:37], v[6:7], s[0:1], v[44:45] op_sel_hi:[1,0,1]
	v_pk_fma_f32 v[42:43], v[8:9], s[0:1], v[46:47] op_sel_hi:[1,0,1]
	v_pk_fma_f32 v[40:41], v[10:11], s[0:1], v[48:49] op_sel_hi:[1,0,1]
	v_pk_fma_f32 v[48:49], v[12:13], s[0:1], v[50:51] op_sel_hi:[1,0,1]
	v_pk_fma_f32 v[46:47], v[14:15], s[0:1], v[52:53] op_sel_hi:[1,0,1]
	v_pk_fma_f32 v[50:51], v[18:19], s[0:1], v[56:57] op_sel_hi:[1,0,1]
	v_pk_fma_f32 v[54:55], v[16:17], s[0:1], v[54:55] op_sel_hi:[1,0,1]
	v_pk_fma_f32 v[60:61], v[20:21], s[0:1], v[58:59] op_sel_hi:[1,0,1]
	v_pk_fma_f32 v[56:57], v[22:23], s[0:1], v[62:63] op_sel_hi:[1,0,1]
	v_pk_fma_f32 v[44:45], v[24:25], s[0:1], v[64:65] op_sel_hi:[1,0,1]
	v_pk_fma_f32 v[64:65], v[26:27], s[0:1], v[66:67] op_sel_hi:[1,0,1]
	v_pk_fma_f32 v[18:19], v[28:29], s[0:1], v[68:69] op_sel_hi:[1,0,1]
	v_pk_fma_f32 v[24:25], v[30:31], s[0:1], v[70:71] op_sel_hi:[1,0,1]
	s_lshr_b32 s0, s58, 12
	s_ashr_i32 s59, s58, 31
	s_mul_i32 s4, s0, 0x3000
	s_lshl_b64 s[0:1], s[58:59], 12
	s_add_u32 s2, s71, s0
	v_lshlrev_b32_e32 v12, 2, v148
	s_addc_u32 s3, s74, s1
	v_ashrrev_i32_e32 v13, 31, v12
	v_lshlrev_b32_e32 v63, 3, v148
	v_lshl_add_u64 v[14:15], v[12:13], 1, s[2:3]
	v_add3_u32 v62, v201, s4, v63
	global_load_dwordx2 v[16:17], v[14:15], off
	ds_read2st64_b64 v[0:3], v62 offset1:1
	global_load_dwordx2 v[20:21], v[14:15], off offset:512
	global_load_dwordx2 v[22:23], v[14:15], off offset:1024
	ds_read2st64_b64 v[4:7], v62 offset0:2 offset1:3
	global_load_dwordx2 v[52:53], v[14:15], off offset:1536
	global_load_dwordx2 v[58:59], v[14:15], off offset:2048
	ds_read2st64_b64 v[8:11], v62 offset0:4 offset1:5
	global_load_dwordx2 v[66:67], v[14:15], off offset:2560
	global_load_dwordx2 v[68:69], v[14:15], off offset:3072
	global_load_dwordx2 v[26:27], v[14:15], off offset:3584
	ds_read2st64_b64 v[28:31], v62 offset0:6 offset1:7
	s_lshl_b64 s[2:3], s[58:59], 13
	s_add_u32 s4, s16, s2
	s_addc_u32 s5, s17, s3
	s_and_b64 vcc, exec, s[54:55]
	s_waitcnt lgkmcnt(0)
	v_lshlrev_b32_e32 v72, 16, v30
	v_and_b32_e32 v73, 0xffff0000, v30
	v_lshlrev_b32_e32 v30, 16, v31
	v_and_b32_e32 v31, 0xffff0000, v31
	v_pk_mul_f32 v[24:25], v[24:25], v[30:31]
	v_lshlrev_b32_e32 v30, 16, v28
	v_and_b32_e32 v31, 0xffff0000, v28
	v_pk_mul_f32 v[30:31], v[44:45], v[30:31]
	v_lshlrev_b32_e32 v28, 16, v29
	v_and_b32_e32 v29, 0xffff0000, v29
	v_pk_mul_f32 v[28:29], v[64:65], v[28:29]
	v_pk_mul_f32 v[18:19], v[18:19], v[72:73]
	s_waitcnt vmcnt(0)
	v_lshlrev_b32_e32 v70, 16, v26
	v_and_b32_e32 v71, 0xffff0000, v26
	v_lshlrev_b32_e32 v26, 16, v27
	v_and_b32_e32 v27, 0xffff0000, v27
	v_pk_fma_f32 v[24:25], v[26:27], s[38:39], v[24:25] op_sel_hi:[1,0,1]
	v_lshlrev_b32_e32 v26, 16, v68
	v_and_b32_e32 v27, 0xffff0000, v68
	v_pk_fma_f32 v[26:27], v[26:27], s[38:39], v[30:31] op_sel_hi:[1,0,1]
	v_lshlrev_b32_e32 v30, 16, v69
	v_and_b32_e32 v31, 0xffff0000, v69
	v_pk_fma_f32 v[44:45], v[30:31], s[38:39], v[28:29] op_sel_hi:[1,0,1]
	v_lshlrev_b32_e32 v30, 16, v10
	v_and_b32_e32 v31, 0xffff0000, v10
	v_lshlrev_b32_e32 v28, 16, v66
	v_and_b32_e32 v29, 0xffff0000, v66
	v_pk_mul_f32 v[30:31], v[60:61], v[30:31]
	v_lshlrev_b32_e32 v10, 16, v11
	v_and_b32_e32 v11, 0xffff0000, v11
	v_pk_fma_f32 v[28:29], v[28:29], s[38:39], v[30:31] op_sel_hi:[1,0,1]
	v_lshlrev_b32_e32 v30, 16, v67
	v_and_b32_e32 v31, 0xffff0000, v67
	v_pk_mul_f32 v[10:11], v[56:57], v[10:11]
	v_lshlrev_b32_e32 v56, 16, v8
	v_and_b32_e32 v57, 0xffff0000, v8
	v_pk_fma_f32 v[10:11], v[30:31], s[38:39], v[10:11] op_sel_hi:[1,0,1]
	v_lshlrev_b32_e32 v30, 16, v58
	v_and_b32_e32 v31, 0xffff0000, v58
	v_pk_mul_f32 v[54:55], v[54:55], v[56:57]
	v_lshlrev_b32_e32 v8, 16, v9
	v_and_b32_e32 v9, 0xffff0000, v9
	v_pk_fma_f32 v[30:31], v[30:31], s[38:39], v[54:55] op_sel_hi:[1,0,1]
	v_lshlrev_b32_e32 v54, 16, v59
	v_and_b32_e32 v55, 0xffff0000, v59
	v_pk_mul_f32 v[8:9], v[50:51], v[8:9]
	v_lshlrev_b32_e32 v50, 16, v52
	v_pk_fma_f32 v[8:9], v[54:55], s[38:39], v[8:9] op_sel_hi:[1,0,1]
	v_lshlrev_b32_e32 v54, 16, v6
	v_and_b32_e32 v55, 0xffff0000, v6
	v_and_b32_e32 v51, 0xffff0000, v52
	v_pk_mul_f32 v[48:49], v[48:49], v[54:55]
	v_lshlrev_b32_e32 v6, 16, v7
	v_and_b32_e32 v7, 0xffff0000, v7
	v_pk_fma_f32 v[48:49], v[50:51], s[38:39], v[48:49] op_sel_hi:[1,0,1]
	v_lshlrev_b32_e32 v50, 16, v53
	v_and_b32_e32 v51, 0xffff0000, v53
	v_pk_mul_f32 v[6:7], v[46:47], v[6:7]
	v_lshlrev_b32_e32 v46, 16, v22
	v_pk_fma_f32 v[6:7], v[50:51], s[38:39], v[6:7] op_sel_hi:[1,0,1]
	v_lshlrev_b32_e32 v50, 16, v4
	v_and_b32_e32 v51, 0xffff0000, v4
	v_lshlrev_b32_e32 v4, 16, v5
	v_and_b32_e32 v5, 0xffff0000, v5
	v_and_b32_e32 v47, 0xffff0000, v22
	v_lshlrev_b32_e32 v22, 16, v23
	v_and_b32_e32 v23, 0xffff0000, v23
	v_pk_mul_f32 v[4:5], v[40:41], v[4:5]
	v_lshlrev_b32_e32 v40, 16, v2
	v_and_b32_e32 v41, 0xffff0000, v2
	v_pk_fma_f32 v[4:5], v[22:23], s[38:39], v[4:5] op_sel_hi:[1,0,1]
	v_lshlrev_b32_e32 v22, 16, v20
	v_and_b32_e32 v23, 0xffff0000, v20
	v_pk_mul_f32 v[38:39], v[38:39], v[40:41]
	v_lshlrev_b32_e32 v40, 16, v0
	v_and_b32_e32 v41, 0xffff0000, v0
	v_pk_fma_f32 v[22:23], v[22:23], s[38:39], v[38:39] op_sel_hi:[1,0,1]
	v_lshlrev_b32_e32 v38, 16, v16
	v_and_b32_e32 v39, 0xffff0000, v16
	v_pk_mul_f32 v[34:35], v[34:35], v[40:41]
	v_lshlrev_b32_e32 v16, 16, v17
	v_pk_fma_f32 v[34:35], v[38:39], s[38:39], v[34:35] op_sel_hi:[1,0,1]
	v_and_b32_e32 v17, 0xffff0000, v17
	v_add_f32_e32 v0, 0, v34
	v_add_f32_e32 v38, v35, v0
	v_lshlrev_b32_e32 v0, 16, v1
	v_and_b32_e32 v1, 0xffff0000, v1
	v_pk_mul_f32 v[0:1], v[32:33], v[0:1]
	v_lshlrev_b32_e32 v2, 16, v3
	v_pk_fma_f32 v[0:1], v[16:17], s[38:39], v[0:1] op_sel_hi:[1,0,1]
	v_and_b32_e32 v3, 0xffff0000, v3
	v_add_f32_e32 v16, v0, v38
	v_add_f32_e32 v16, v1, v16
	v_lshlrev_b32_e32 v20, 16, v21
	v_and_b32_e32 v21, 0xffff0000, v21
	v_pk_mul_f32 v[2:3], v[36:37], v[2:3]
	v_add_f32_e32 v16, v22, v16
	v_pk_fma_f32 v[2:3], v[20:21], s[38:39], v[2:3] op_sel_hi:[1,0,1]
	v_add_f32_e32 v16, v23, v16
	v_pk_mul_f32 v[42:43], v[42:43], v[50:51]
	v_add_f32_e32 v16, v2, v16
	v_pk_fma_f32 v[52:53], v[46:47], s[38:39], v[42:43] op_sel_hi:[1,0,1]
	v_add_f32_e32 v16, v3, v16
	v_add_f32_e32 v16, v52, v16
	v_add_f32_e32 v16, v53, v16
	v_add_f32_e32 v16, v4, v16
	v_add_f32_e32 v16, v5, v16
	v_add_f32_e32 v16, v48, v16
	v_add_f32_e32 v16, v49, v16
	v_add_f32_e32 v16, v6, v16
	v_add_f32_e32 v16, v7, v16
	v_add_f32_e32 v16, v30, v16
	v_add_f32_e32 v16, v31, v16
	v_add_f32_e32 v16, v8, v16
	v_add_f32_e32 v16, v9, v16
	v_add_f32_e32 v16, v28, v16
	v_add_f32_e32 v16, v29, v16
	v_add_f32_e32 v16, v10, v16
	v_add_f32_e32 v16, v11, v16
	v_add_f32_e32 v16, v26, v16
	v_add_f32_e32 v16, v27, v16
	v_add_f32_e32 v16, v44, v16
	v_pk_fma_f32 v[18:19], v[70:71], s[38:39], v[18:19] op_sel_hi:[1,0,1]
	v_add_f32_e32 v16, v45, v16
	v_add_f32_e32 v16, v18, v16
	v_add_f32_e32 v16, v19, v16
	v_add_f32_e32 v16, v24, v16
	v_add_f32_e32 v16, v25, v16
	v_mov_b32_e32 v17, v105
	v_add_u32_e32 v50, v202, v63
	v_add_f32_dpp v16, v16, v16 quad_perm:[1,0,3,2] row_mask:0xf bank_mask:0xf bound_ctrl:1
	v_add_u32_e32 v51, v203, v63
	ds_read_b64 v[20:21], v50
	ds_read_b64 v[36:37], v51
	v_add_f32_dpp v16, v16, v16 quad_perm:[2,3,0,1] row_mask:0xf bank_mask:0xf bound_ctrl:1
	s_waitcnt lgkmcnt(1)
	v_lshlrev_b32_e32 v54, 16, v20
	v_add_f32_dpp v16, v16, v16 row_half_mirror row_mask:0xf bank_mask:0xf bound_ctrl:1
	s_waitcnt lgkmcnt(0)
	v_lshlrev_b32_e32 v56, 16, v36
	v_and_b32_e32 v57, 0xffff0000, v36
	v_add_f32_dpp v16, v16, v16 row_mirror row_mask:0xf bank_mask:0xf bound_ctrl:1
	v_lshlrev_b32_e32 v60, 16, v37
	v_and_b32_e32 v61, 0xffff0000, v37
	v_mov_b32_dpp v17, v16 row_bcast:15 row_mask:0xa bank_mask:0xf
	v_add_f32_e32 v16, v16, v17
	v_mov_b32_e32 v17, v105
	v_and_b32_e32 v55, 0xffff0000, v20
	v_lshlrev_b32_e32 v58, 16, v21
	v_mov_b32_dpp v17, v16 row_bcast:31 row_mask:0xc bank_mask:0xf
	v_add_f32_e32 v16, v16, v17
	v_and_b32_e32 v59, 0xffff0000, v21
	v_readlane_b32 s2, v16, 63
	s_nop 1
	v_mul_f32_e32 v64, s2, v187
	v_pk_add_f32 v[66:67], v[34:35], v[64:65] op_sel_hi:[1,0] neg_lo:[0,1] neg_hi:[0,1]
	v_pk_add_f32 v[70:71], v[0:1], v[64:65] op_sel_hi:[1,0] neg_lo:[0,1] neg_hi:[0,1]
	v_pk_mul_f32 v[68:69], v[66:67], v[66:67]
	v_pk_mul_f32 v[0:1], v[70:71], v[70:71]
	v_add_f32_e32 v63, v68, v69
	v_pk_add_f32 v[46:47], v[22:23], v[64:65] op_sel_hi:[1,0] neg_lo:[0,1] neg_hi:[0,1]
	v_add_f32_e32 v0, v0, v63
	v_pk_mul_f32 v[72:73], v[46:47], v[46:47]
	v_add_f32_e32 v0, v1, v0
	v_pk_add_f32 v[42:43], v[2:3], v[64:65] op_sel_hi:[1,0] neg_lo:[0,1] neg_hi:[0,1]
	v_add_f32_e32 v0, v72, v0
	v_pk_mul_f32 v[2:3], v[42:43], v[42:43]
	v_add_f32_e32 v0, v73, v0
	v_pk_add_f32 v[40:41], v[52:53], v[64:65] op_sel_hi:[1,0] neg_lo:[0,1] neg_hi:[0,1]
	v_add_f32_e32 v0, v2, v0
	v_pk_mul_f32 v[52:53], v[40:41], v[40:41]
	v_add_f32_e32 v0, v3, v0
	v_pk_add_f32 v[22:23], v[4:5], v[64:65] op_sel_hi:[1,0] neg_lo:[0,1] neg_hi:[0,1]
	v_add_f32_e32 v0, v52, v0
	v_pk_mul_f32 v[4:5], v[22:23], v[22:23]
	v_add_f32_e32 v0, v53, v0
	v_pk_add_f32 v[38:39], v[48:49], v[64:65] op_sel_hi:[1,0] neg_lo:[0,1] neg_hi:[0,1]
	v_add_f32_e32 v0, v4, v0
	v_pk_mul_f32 v[48:49], v[38:39], v[38:39]
	v_add_f32_e32 v0, v5, v0
	v_pk_add_f32 v[36:37], v[6:7], v[64:65] op_sel_hi:[1,0] neg_lo:[0,1] neg_hi:[0,1]
	v_add_f32_e32 v0, v48, v0
	v_pk_mul_f32 v[74:75], v[36:37], v[36:37]
	v_add_f32_e32 v0, v49, v0
	v_pk_add_f32 v[34:35], v[30:31], v[64:65] op_sel_hi:[1,0] neg_lo:[0,1] neg_hi:[0,1]
	v_add_f32_e32 v0, v74, v0
	v_pk_mul_f32 v[76:77], v[34:35], v[34:35]
	v_add_f32_e32 v0, v75, v0
	v_pk_add_f32 v[32:33], v[8:9], v[64:65] op_sel_hi:[1,0] neg_lo:[0,1] neg_hi:[0,1]
	v_add_f32_e32 v0, v76, v0
	v_pk_mul_f32 v[78:79], v[32:33], v[32:33]
	v_add_f32_e32 v0, v77, v0
	v_pk_add_f32 v[30:31], v[28:29], v[64:65] op_sel_hi:[1,0] neg_lo:[0,1] neg_hi:[0,1]
	v_add_f32_e32 v0, v78, v0
	v_pk_mul_f32 v[80:81], v[30:31], v[30:31]
	v_add_f32_e32 v0, v79, v0
	v_pk_add_f32 v[28:29], v[10:11], v[64:65] op_sel_hi:[1,0] neg_lo:[0,1] neg_hi:[0,1]
	v_add_f32_e32 v0, v80, v0
	v_pk_mul_f32 v[10:11], v[28:29], v[28:29]
	v_add_f32_e32 v0, v81, v0
	v_pk_add_f32 v[20:21], v[26:27], v[64:65] op_sel_hi:[1,0] neg_lo:[0,1] neg_hi:[0,1]
	v_add_f32_e32 v0, v10, v0
	v_pk_mul_f32 v[26:27], v[20:21], v[20:21]
	v_add_f32_e32 v0, v11, v0
	v_pk_add_f32 v[16:17], v[44:45], v[64:65] op_sel_hi:[1,0] neg_lo:[0,1] neg_hi:[0,1]
	v_add_f32_e32 v0, v26, v0
	v_pk_mul_f32 v[44:45], v[16:17], v[16:17]
	v_add_f32_e32 v0, v27, v0
	v_pk_add_f32 v[8:9], v[18:19], v[64:65] op_sel_hi:[1,0] neg_lo:[0,1] neg_hi:[0,1]
	v_add_f32_e32 v0, v44, v0
	v_pk_mul_f32 v[18:19], v[8:9], v[8:9]
	v_add_f32_e32 v0, v45, v0
	v_pk_add_f32 v[6:7], v[24:25], v[64:65] op_sel_hi:[1,0] neg_lo:[0,1] neg_hi:[0,1]
	v_add_f32_e32 v0, v18, v0
	v_pk_mul_f32 v[24:25], v[6:7], v[6:7]
	v_add_f32_e32 v0, v19, v0
	v_add_f32_e32 v0, v24, v0
	v_add_f32_e32 v0, v25, v0
	v_mov_b32_e32 v1, v105
	s_nop 0
	v_add_f32_dpp v0, v0, v0 quad_perm:[1,0,3,2] row_mask:0xf bank_mask:0xf bound_ctrl:1
	s_nop 1
	v_add_f32_dpp v0, v0, v0 quad_perm:[2,3,0,1] row_mask:0xf bank_mask:0xf bound_ctrl:1
	s_nop 1
	v_add_f32_dpp v0, v0, v0 row_half_mirror row_mask:0xf bank_mask:0xf bound_ctrl:1
	s_nop 1
	v_add_f32_dpp v0, v0, v0 row_mirror row_mask:0xf bank_mask:0xf bound_ctrl:1
	s_nop 1
	v_mov_b32_dpp v1, v0 row_bcast:15 row_mask:0xa bank_mask:0xf
	v_add_f32_e32 v0, v0, v1
	v_mov_b32_e32 v1, v105
	s_nop 1
	v_mov_b32_dpp v1, v0 row_bcast:31 row_mask:0xc bank_mask:0xf
	v_add_f32_e32 v0, v0, v1
	s_nop 0
	v_readlane_b32 s2, v0, 63
	s_nop 1
	v_fma_f32 v0, s2, v187, v183
	v_rsq_f32_e32 v10, v0
	s_mov_b64 s[2:3], -1
	v_pk_mul_f32 v[0:1], v[66:67], v[10:11] op_sel_hi:[1,0]
	v_pk_mul_f32 v[2:3], v[70:71], v[10:11] op_sel_hi:[1,0]
	v_pk_fma_f32 v[0:1], v[0:1], v[54:55], v[56:57]
	v_pk_fma_f32 v[2:3], v[2:3], v[58:59], v[60:61]
	s_cbranch_vccz .LBB0_1142
	ds_read2st64_b64 v[24:27], v62 offset0:8 offset1:16
	v_cvt_pk_bf16_f32 v4, v0, v1
	v_cvt_pk_bf16_f32 v5, v2, v3
	global_store_dwordx2 v[14:15], v[4:5], off
	s_mov_b64 s[2:3], 0
	s_waitcnt lgkmcnt(0)
	v_lshlrev_b32_e32 v18, 16, v26
	v_and_b32_e32 v19, 0xffff0000, v26
	v_lshlrev_b32_e32 v4, 16, v24
	v_and_b32_e32 v5, 0xffff0000, v24
	v_pk_add_f32 v[18:19], v[18:19], 1.0 op_sel_hi:[1,0]
	v_lshlrev_b32_e32 v24, 16, v27
	v_pk_fma_f32 v[4:5], v[0:1], v[18:19], v[4:5]
	v_lshlrev_b32_e32 v18, 16, v25
	v_and_b32_e32 v19, 0xffff0000, v25
	v_and_b32_e32 v25, 0xffff0000, v27
	v_pk_add_f32 v[24:25], v[24:25], 1.0 op_sel_hi:[1,0]
	v_cvt_pk_bf16_f32 v4, v4, v5
	v_pk_fma_f32 v[18:19], v[2:3], v[24:25], v[18:19]
	s_nop 0
	v_cvt_pk_bf16_f32 v5, v18, v19
